# all plain wide global stores made write-through (sc1) so grid-barrier L2 writebacks have less dirty data
# speedup vs baseline: 1.0003x; 1.0003x over previous
; #define LAS __attribute__((address_space(3)))
; __device__ __forceinline__ void t16_load(const float* W, int N, int mode, int item, int lane, f32x4 (&a)[4], f32x4 (&b)[4]) {
;     const int nblk = N / 32, kb = item / nblk, nb = item % nblk, k0 = 64 * kb, n0 = 32 * nb;
;     const int g = lane & 7, r = lane >> 3;
;     const float* p = W + (size_t)(k0 + 2 * r) * N + src_col(mode, n0 + 4 * g);
; #pragma unroll
;     for (int i = 0; i < 4; ++i) { a[i] = __builtin_nontemporal_load((const f32x4*)(p + (size_t)(16 * i) * N)); b[i] = __builtin_nontemporal_load((const f32x4*)(p + (size_t)(16 * i + 1) * N)); }
; }
; __device__ __forceinline__ void t16_store(const f32x4 (&a)[4], const f32x4 (&b)[4], int K, int N, bf16_t* WT, int item, LAS unsigned* scr, int lane) {
;     const int nblk = N / 32, kb = item / nblk, nb = item % nblk, k0 = 64 * kb, n0 = 32 * nb;
;     const int g = lane & 7, r = lane >> 3;
; #pragma unroll
;     for (int i = 0; i < 4; ++i)
; #pragma unroll
;         for (int j = 0; j < 4; ++j) scr[(4 * g + j) * 33 + r + 8 * i] = cvt_pk_bf16(a[i][j], b[i][j]);
;     asm volatile("s_waitcnt lgkmcnt(0)" ::: "memory");
;     const int c = lane & 7;
; #pragma unroll
;     for (int ii = 0; ii < 4; ++ii) { const int n = 8 * ii + (lane >> 3); const LAS unsigned* s = scr + n * 33 + 4 * c;
;         u32x4 o; o.x = s[0]; o.y = s[1]; o.z = s[2]; o.w = s[3];
;         *(u32x4*)(WT + (size_t)(n0 + n) * K + k0 + 8 * c) = o; }
;     asm volatile("s_waitcnt lgkmcnt(0)" ::: "memory");
; }
; __device__ __forceinline__ void p0_prologue(Frame& F, const Args& a) {
;     LAS unsigned* scr = (LAS unsigned*)(F.lds + F.wave * 4352);
;     const int gw = F.vcu * NWAVES + F.wave, NGW = F.G * NWAVES;
;     bf16_t* Win = (bf16_t*)(F.ws + WS_WIN);
;     constexpr int I_IN = (D / 64) * (INW / 32);
;     {
;         f32x4 A0[4], A1[4], B0[4], B1[4];
;         t16_load(a.in[2], INW, CM_WIN, gw < I_IN ? gw : I_IN - 1, F.lane, A0, A1);
;         for (int it = gw; it < I_IN; it += 2 * NGW) {
;             { const int n1 = it + NGW; t16_load(a.in[2], INW, CM_WIN, n1 < I_IN ? n1 : I_IN - 1, F.lane, B0, B1); }
;             t16_store(A0, A1, D, INW, Win, it, scr, F.lane);
;             { const int n2 = it + 2 * NGW; t16_load(a.in[2], INW, CM_WIN, n2 < I_IN ? n2 : I_IN - 1, F.lane, A0, A1); }
;             if (it + NGW < I_IN) t16_store(B0, B1, D, INW, Win, it + NGW, scr, F.lane);
;         }
.LBB0_15:
	v_lshl_or_b32 v35, s19, 6, v70
	v_mov_b64_e32 v[36:37], s[0:1]
	v_mad_i64_i32 v[36:37], s[16:17], v35, s3, v[36:37]
	v_ashrrev_i32_e32 v35, 31, v34
	s_waitcnt vmcnt(13)
	v_lshl_add_u64 v[58:59], v[34:35], 2, v[36:37]
	v_add_co_u32_e32 v42, vcc, 0xc000, v58
	s_waitcnt vmcnt(4)
	v_cvt_pk_bf16_f32 v22, v22, v18
	v_addc_co_u32_e32 v43, vcc, 0, v59, vcc
	v_add_co_u32_e32 v50, vcc, 0xc0000, v58
	v_cvt_pk_bf16_f32 v23, v23, v19
	s_nop 0
	v_addc_co_u32_e32 v51, vcc, 0, v59, vcc
	v_add_co_u32_e32 v52, vcc, 0xcc000, v58
	v_cvt_pk_bf16_f32 v24, v24, v20
	s_nop 0
	v_addc_co_u32_e32 v53, vcc, 0, v59, vcc
	v_add_co_u32_e32 v18, vcc, 0x180000, v58
	v_cvt_pk_bf16_f32 v25, v25, v21
	s_nop 0
	v_addc_co_u32_e32 v19, vcc, 0, v59, vcc
	v_add_co_u32_e32 v20, vcc, 0x18c000, v58
	global_load_dwordx4 v[34:37], v[58:59], off nt
	global_load_dwordx4 v[38:41], v[42:43], off nt
	v_addc_co_u32_e32 v21, vcc, 0, v59, vcc
	global_load_dwordx4 v[42:45], v[50:51], off nt
	global_load_dwordx4 v[46:49], v[52:53], off nt
	s_nop 0
	global_load_dwordx4 v[50:53], v[18:19], off nt
	global_load_dwordx4 v[54:57], v[20:21], off nt
	v_add_co_u32_e32 v18, vcc, 0x240000, v58
	s_waitcnt vmcnt(8)
	v_cvt_pk_bf16_f32 v2, v10, v2
	v_addc_co_u32_e32 v19, vcc, 0, v59, vcc
	v_add_co_u32_e32 v20, vcc, 0x24c000, v58
	v_cvt_pk_bf16_f32 v3, v11, v3
	s_nop 0
	v_addc_co_u32_e32 v21, vcc, 0, v59, vcc
	global_load_dwordx4 v[58:61], v[18:19], off nt
	global_load_dwordx4 v[62:65], v[20:21], off nt
	s_waitcnt vmcnt(9)
	v_cvt_pk_bf16_f32 v6, v26, v6
	ds_write2_b32 v77, v22, v2 offset1:8
	s_waitcnt vmcnt(8)
	v_cvt_pk_bf16_f32 v2, v30, v14
	v_cvt_pk_bf16_f32 v4, v12, v4
	v_cvt_pk_bf16_f32 v5, v13, v5
	v_cvt_pk_bf16_f32 v7, v27, v7
	s_mul_hi_i32 s16, s18, 0x2aaaaaab
	ds_write2_b32 v77, v23, v3 offset0:33 offset1:41
	ds_write2_b32 v77, v24, v4 offset0:66 offset1:74
	ds_write2_b32 v77, v25, v5 offset0:99 offset1:107
	ds_write2_b32 v77, v6, v2 offset0:16 offset1:24
	v_cvt_pk_bf16_f32 v2, v31, v15
	v_cvt_pk_bf16_f32 v8, v28, v8
	s_lshr_b32 s17, s16, 31
	s_ashr_i32 s16, s16, 6
	ds_write2_b32 v77, v7, v2 offset0:49 offset1:57
	v_cvt_pk_bf16_f32 v2, v32, v16
	v_cvt_pk_bf16_f32 v9, v29, v9
	s_add_i32 s17, s16, s17
	ds_write2_b32 v77, v8, v2 offset0:82 offset1:90
	v_cvt_pk_bf16_f32 v2, v33, v17
	s_lshl_b32 s16, s17, 6
	ds_write2_b32 v77, v9, v2 offset0:115 offset1:123
	s_mulk_i32 s17, 0x180
	s_sub_i32 s17, s18, s17
	s_waitcnt lgkmcnt(0)
	s_lshl_b32 s19, s17, 5
	ds_read2_b32 v[2:3], v78 offset1:1
	ds_read2_b32 v[4:5], v78 offset0:2 offset1:3
	v_or_b32_e32 v6, s19, v73
	s_ashr_i32 s17, s16, 31
	v_ashrrev_i32_e32 v7, 31, v6
	v_lshl_add_u64 v[10:11], s[16:17], 1, v[66:67]
	v_lshlrev_b64 v[6:7], 12, v[6:7]
	v_add_u32_e32 v79, 0x420, v78
	v_lshl_add_u64 v[12:13], v[10:11], 0, v[6:7]
	v_add_u32_e32 v80, 0x428, v78
	ds_read2_b32 v[6:7], v79 offset1:1
	ds_read2_b32 v[8:9], v80 offset1:1
	s_waitcnt lgkmcnt(2)
	global_store_dwordx4 v[12:13], v[2:5], off sc1
	v_add_u32_e32 v81, 0x840, v78
	v_add_u32_e32 v83, 0x848, v78
	v_or_b32_e32 v2, s19, v74
	v_ashrrev_i32_e32 v3, 31, v2
	v_lshlrev_b64 v[2:3], 12, v[2:3]
	v_lshl_add_u64 v[2:3], v[10:11], 0, v[2:3]
	s_waitcnt lgkmcnt(0)
	global_store_dwordx4 v[2:3], v[6:9], off sc1
	ds_read2_b32 v[2:3], v81 offset1:1
	ds_read2_b32 v[4:5], v83 offset1:1
	v_or_b32_e32 v6, s19, v75
	v_ashrrev_i32_e32 v7, 31, v6
	v_lshlrev_b64 v[6:7], 12, v[6:7]
	v_add_u32_e32 v84, 0xc60, v78
	v_lshl_add_u64 v[12:13], v[10:11], 0, v[6:7]
	v_add_u32_e32 v85, 0xc68, v78
	ds_read2_b32 v[6:7], v84 offset1:1
	ds_read2_b32 v[8:9], v85 offset1:1
	s_add_i32 s16, s13, s18
	s_waitcnt lgkmcnt(2)
	global_store_dwordx4 v[12:13], v[2:5], off sc1
	s_min_i32 s16, s16, 0x2fff
	s_mul_hi_i32 s17, s16, 0x2aaaaaab
	v_or_b32_e32 v2, s19, v76
	v_ashrrev_i32_e32 v3, 31, v2
	v_lshlrev_b64 v[2:3], 12, v[2:3]
	s_lshr_b32 s18, s17, 31
	s_ashr_i32 s17, s17, 6
	v_lshl_add_u64 v[2:3], v[10:11], 0, v[2:3]
	s_add_i32 s18, s17, s18
	s_waitcnt lgkmcnt(0)
	global_store_dwordx4 v[2:3], v[6:9], off sc1
	s_mul_i32 s17, s18, 0x180
	s_waitcnt lgkmcnt(0)
	s_sub_i32 s16, s16, s17
	s_lshl_b32 s19, s16, 5
	s_and_b32 s16, s16, 0x7ffffc0
	v_or_b32_e32 v3, s19, v69
	s_cmp_eq_u32 s16, 64
	s_mov_b64 s[16:17], -1
	s_cbranch_scc1 .LBB0_17
	v_lshlrev_b32_e32 v2, 1, v3
	v_and_b32_e32 v2, 24, v2
	v_or3_b32 v2, v71, v2, s19
	s_mov_b64 s[16:17], 0

; #define LAS __attribute__((address_space(3)))
; __device__ __forceinline__ unsigned cvt_pk_bf16(float lo, float hi) { f32x2 v = {lo, hi}; bf16x2_t b = __builtin_convertvector(v, bf16x2_t); return __builtin_bit_cast(unsigned, b); }
; __device__ __forceinline__ void t16_load(const float* W, int N, int mode, int item, int lane, f32x4 (&a)[4], f32x4 (&b)[4]) {
;     const int nblk = N / 32, kb = item / nblk, nb = item % nblk, k0 = 64 * kb, n0 = 32 * nb;
;     const int g = lane & 7, r = lane >> 3;
;     const float* p = W + (size_t)(k0 + 2 * r) * N + src_col(mode, n0 + 4 * g);
; #pragma unroll
;     for (int i = 0; i < 4; ++i) { a[i] = __builtin_nontemporal_load((const f32x4*)(p + (size_t)(16 * i) * N)); b[i] = __builtin_nontemporal_load((const f32x4*)(p + (size_t)(16 * i + 1) * N)); }
; }
; __device__ __forceinline__ void t16_store(const f32x4 (&a)[4], const f32x4 (&b)[4], int K, int N, bf16_t* WT, int item, LAS unsigned* scr, int lane) {
;     const int nblk = N / 32, kb = item / nblk, nb = item % nblk, k0 = 64 * kb, n0 = 32 * nb;
;     const int g = lane & 7, r = lane >> 3;
; #pragma unroll
;     for (int i = 0; i < 4; ++i)
; #pragma unroll
;         for (int j = 0; j < 4; ++j) scr[(4 * g + j) * 33 + r + 8 * i] = cvt_pk_bf16(a[i][j], b[i][j]);
;     asm volatile("s_waitcnt lgkmcnt(0)" ::: "memory");
;     const int c = lane & 7;
; #pragma unroll
;     for (int ii = 0; ii < 4; ++ii) { const int n = 8 * ii + (lane >> 3); const LAS unsigned* s = scr + n * 33 + 4 * c;
;         u32x4 o; o.x = s[0]; o.y = s[1]; o.z = s[2]; o.w = s[3];
;         *(u32x4*)(WT + (size_t)(n0 + n) * K + k0 + 8 * c) = o; }
;     asm volatile("s_waitcnt lgkmcnt(0)" ::: "memory");
; }
.LBB0_19:
	v_lshl_or_b32 v3, s18, 6, v70
	v_mov_b64_e32 v[4:5], s[0:1]
	v_mad_i64_i32 v[4:5], s[16:17], v3, s3, v[4:5]
	v_ashrrev_i32_e32 v3, 31, v2
	v_lshl_add_u64 v[14:15], v[2:3], 2, v[4:5]
	v_add_co_u32_e32 v2, vcc, 0xc000, v14
	s_nop 1
	v_addc_co_u32_e32 v3, vcc, 0, v15, vcc
	v_add_co_u32_e32 v6, vcc, 0xc0000, v14
	global_load_dwordx4 v[22:25], v[14:15], off nt
	global_load_dwordx4 v[18:21], v[2:3], off nt
	v_addc_co_u32_e32 v7, vcc, 0, v15, vcc
	v_add_co_u32_e32 v8, vcc, 0xcc000, v14
	s_nop 1
	v_addc_co_u32_e32 v9, vcc, 0, v15, vcc
	v_add_co_u32_e32 v16, vcc, 0x180000, v14
	global_load_dwordx4 v[10:13], v[6:7], off nt
	global_load_dwordx4 v[2:5], v[8:9], off nt
	v_addc_co_u32_e32 v17, vcc, 0, v15, vcc
	v_add_co_u32_e32 v30, vcc, 0x18c000, v14
	s_nop 1
	v_addc_co_u32_e32 v31, vcc, 0, v15, vcc
	v_add_co_u32_e32 v86, vcc, 0x240000, v14
	global_load_dwordx4 v[26:29], v[16:17], off nt
	global_load_dwordx4 v[6:9], v[30:31], off nt
	v_addc_co_u32_e32 v87, vcc, 0, v15, vcc
	v_add_co_u32_e32 v88, vcc, 0x24c000, v14
	s_nop 1
	v_addc_co_u32_e32 v89, vcc, 0, v15, vcc
	global_load_dwordx4 v[30:33], v[86:87], off nt
	global_load_dwordx4 v[14:17], v[88:89], off nt
	s_andn2_b64 vcc, exec, s[8:9]
	s_cbranch_vccnz .LBB0_10
	s_waitcnt vmcnt(18)
	v_cvt_pk_bf16_f32 v34, v34, v38
	s_waitcnt vmcnt(16)
	v_cvt_pk_bf16_f32 v38, v42, v46
	v_cvt_pk_bf16_f32 v35, v35, v39
	ds_write2_b32 v77, v34, v38 offset1:8
	v_cvt_pk_bf16_f32 v34, v43, v47
	v_cvt_pk_bf16_f32 v36, v36, v40
	ds_write2_b32 v77, v35, v34 offset0:33 offset1:41
	v_cvt_pk_bf16_f32 v34, v44, v48
	v_cvt_pk_bf16_f32 v37, v37, v41
	ds_write2_b32 v77, v36, v34 offset0:66 offset1:74
	v_cvt_pk_bf16_f32 v34, v45, v49
	ds_write2_b32 v77, v37, v34 offset0:99 offset1:107
	s_waitcnt vmcnt(14)
	v_cvt_pk_bf16_f32 v34, v50, v54
	s_waitcnt vmcnt(12)
	v_cvt_pk_bf16_f32 v38, v58, v62
	s_mul_hi_i32 s8, s15, 0x2aaaaaab
	v_cvt_pk_bf16_f32 v35, v51, v55
	ds_write2_b32 v77, v34, v38 offset0:16 offset1:24
	v_cvt_pk_bf16_f32 v34, v59, v63
	s_lshr_b32 s9, s8, 31
	s_ashr_i32 s8, s8, 6
	v_cvt_pk_bf16_f32 v36, v52, v56
	ds_write2_b32 v77, v35, v34 offset0:49 offset1:57
	v_cvt_pk_bf16_f32 v34, v60, v64
	s_add_i32 s9, s8, s9
	v_cvt_pk_bf16_f32 v37, v53, v57
	ds_write2_b32 v77, v36, v34 offset0:82 offset1:90
	v_cvt_pk_bf16_f32 v34, v61, v65
	s_lshl_b32 s8, s9, 6
	ds_write2_b32 v77, v37, v34 offset0:115 offset1:123
	s_mulk_i32 s9, 0x180
	s_sub_i32 s9, s15, s9
	s_waitcnt lgkmcnt(0)
	s_lshl_b32 s16, s9, 5
	ds_read2_b32 v[34:35], v78 offset1:1
	ds_read2_b32 v[36:37], v78 offset0:2 offset1:3
	v_or_b32_e32 v38, s16, v73
	s_ashr_i32 s9, s8, 31
	v_ashrrev_i32_e32 v39, 31, v38
	v_lshl_add_u64 v[42:43], s[8:9], 1, v[66:67]
	v_lshlrev_b64 v[38:39], 12, v[38:39]
	v_lshl_add_u64 v[44:45], v[42:43], 0, v[38:39]
	ds_read2_b32 v[38:39], v79 offset1:1
	ds_read2_b32 v[40:41], v80 offset1:1
	s_waitcnt lgkmcnt(2)
	global_store_dwordx4 v[44:45], v[34:37], off sc1
	s_nop 1
	v_or_b32_e32 v34, s16, v74
	v_ashrrev_i32_e32 v35, 31, v34
	v_lshlrev_b64 v[34:35], 12, v[34:35]
	v_lshl_add_u64 v[34:35], v[42:43], 0, v[34:35]
	s_waitcnt lgkmcnt(0)
	global_store_dwordx4 v[34:35], v[38:41], off sc1
	ds_read2_b32 v[34:35], v81 offset1:1
	ds_read2_b32 v[36:37], v83 offset1:1
	v_or_b32_e32 v38, s16, v75
	v_ashrrev_i32_e32 v39, 31, v38
	v_lshlrev_b64 v[38:39], 12, v[38:39]
	v_lshl_add_u64 v[44:45], v[42:43], 0, v[38:39]
	ds_read2_b32 v[38:39], v84 offset1:1
	ds_read2_b32 v[40:41], v85 offset1:1
	s_waitcnt lgkmcnt(2)
	global_store_dwordx4 v[44:45], v[34:37], off sc1
	s_nop 1
	v_or_b32_e32 v34, s16, v76
	v_ashrrev_i32_e32 v35, 31, v34
	v_lshlrev_b64 v[34:35], 12, v[34:35]
	v_lshl_add_u64 v[34:35], v[42:43], 0, v[34:35]
	s_waitcnt lgkmcnt(0)
	global_store_dwordx4 v[34:35], v[38:41], off sc1
	s_waitcnt lgkmcnt(0)
	s_branch .LBB0_10

; __device__ __forceinline__ unsigned cvt_pk_bf16(float lo, float hi) { f32x2 v = {lo, hi}; bf16x2_t b = __builtin_convertvector(v, bf16x2_t); return __builtin_bit_cast(unsigned, b); }
; __device__ __forceinline__ void p0_prologue(Frame& F, const Args& a) {
;     ...
;         for (int m = gw; m < T; m += NGW) {
;             f32x4 vn[8];
;             { const int mn = (m + NGW) < T ? (m + NGW) : T - 1; const f32x4* xr = (const f32x4*)(x + (size_t)mn * D) + F.lane;
; #pragma unroll
;               for (int j = 0; j < 8; ++j) vn[j] = __builtin_nontemporal_load(xr + 64 * j); }
;             float s = 0.f;
; #pragma unroll
;             for (int j = 0; j < 8; ++j) s += (vc[j].x * vc[j].x + vc[j].y * vc[j].y) + (vc[j].z * vc[j].z + vc[j].w * vc[j].w);
;             const float rstd = 1.0f / sqrtf(wave_sum(s) * (1.f / D) + EPS);
;             u32x2* o8 = (u32x2*)(H + (size_t)m * D) + F.lane;
; #pragma unroll
;             for (int j = 0; j < 8; ++j) { const f32x4 g = g1v[j]; u32x2 w; w.x = cvt_pk_bf16(vc[j].x * rstd * g.x, vc[j].y * rstd * g.y); w.y = cvt_pk_bf16(vc[j].z * rstd * g.z, vc[j].w * rstd * g.w); o8[64 * j] = w; }
.LBB0_27:
	s_waitcnt vmcnt(1)
	v_mov_b64_e32 v[114:115], v[40:41]
	s_waitcnt vmcnt(0)
	v_mov_b64_e32 v[118:119], v[36:37]
	v_mov_b64_e32 v[112:113], v[38:39]
	v_mov_b64_e32 v[116:117], v[34:35]
	v_mov_b32_e32 v36, v117
	v_mov_b32_e32 v37, v113
	v_mov_b32_e32 v35, v112
	v_pk_mul_f32 v[36:37], v[36:37], v[36:37]
	v_mov_b32_e32 v38, v119
	v_mov_b32_e32 v39, v115
	v_mov_b64_e32 v[110:111], v[44:45]
	v_pk_fma_f32 v[34:35], v[34:35], v[34:35], v[36:37]
	v_mov_b32_e32 v36, v118
	v_mov_b32_e32 v37, v114
	v_pk_mul_f32 v[38:39], v[38:39], v[38:39]
	v_mov_b64_e32 v[108:109], v[42:43]
	v_pk_fma_f32 v[36:37], v[36:37], v[36:37], v[38:39]
	v_pk_mul_f32 v[38:39], v[108:109], v[108:109]
	v_pk_add_f32 v[34:35], v[34:35], v[36:37]
	v_pk_mul_f32 v[36:37], v[110:111], v[110:111]
	v_mov_b64_e32 v[80:81], v[52:53]
	v_pk_mov_b32 v[40:41], v[38:39], v[36:37] op_sel:[1,0]
	v_mov_b32_e32 v39, v37
	v_mov_b64_e32 v[78:79], v[50:51]
	v_pk_add_f32 v[36:37], v[40:41], v[38:39]
	v_mov_b64_e32 v[106:107], v[48:49]
	v_mul_f32_e32 v38, v78, v78
	v_mul_f32_e32 v39, v79, v79
	v_pk_add_f32 v[34:35], v[34:35], v[34:35] op_sel:[0,1] op_sel_hi:[1,0]
	v_pk_add_f32 v[36:37], v[36:37], v[36:37] op_sel:[0,1] op_sel_hi:[1,0]
	v_mov_b64_e32 v[104:105], v[46:47]
	v_mov_b32_e32 v35, v38
	v_mov_b32_e32 v37, v39
	v_pk_add_f32 v[34:35], v[34:35], v[36:37]
	v_mul_f32_e32 v36, v105, v105
	v_mul_f32_e32 v38, v107, v107
	v_mul_f32_e32 v40, v80, v80
	v_mul_f32_e32 v41, v81, v81
	v_pk_fma_f32 v[36:37], v[104:105], v[104:105], v[36:37] op_sel_hi:[1,1,0]
	v_pk_fma_f32 v[38:39], v[106:107], v[106:107], v[38:39] op_sel_hi:[1,1,0]
	v_mov_b64_e32 v[76:77], v[56:57]
	v_mov_b32_e32 v37, v40
	v_mov_b32_e32 v39, v41
	v_mov_b64_e32 v[74:75], v[54:55]
	v_pk_add_f32 v[36:37], v[36:37], v[38:39]
	v_pk_mul_f32 v[38:39], v[74:75], v[74:75]
	v_pk_add_f32 v[34:35], v[34:35], v[36:37]
	v_pk_mul_f32 v[36:37], v[76:77], v[76:77]
	v_mov_b64_e32 v[68:69], v[64:65]
	v_pk_mov_b32 v[40:41], v[38:39], v[36:37] op_sel:[1,0]
	v_mov_b32_e32 v39, v37
	v_mov_b64_e32 v[66:67], v[62:63]
	v_pk_add_f32 v[36:37], v[40:41], v[38:39]
	v_mov_b64_e32 v[72:73], v[60:61]
	v_mul_f32_e32 v38, v66, v66
	v_mul_f32_e32 v39, v67, v67
	v_pk_add_f32 v[34:35], v[34:35], v[34:35] op_sel:[0,1] op_sel_hi:[1,0]
	v_pk_add_f32 v[36:37], v[36:37], v[36:37] op_sel:[0,1] op_sel_hi:[1,0]
	v_mov_b64_e32 v[70:71], v[58:59]
	v_mov_b32_e32 v35, v38
	v_mov_b32_e32 v37, v39
	v_pk_add_f32 v[34:35], v[34:35], v[36:37]
	v_mul_f32_e32 v36, v71, v71
	v_mul_f32_e32 v38, v73, v73
	v_mul_f32_e32 v40, v68, v68
	v_mul_f32_e32 v41, v69, v69
	v_pk_fma_f32 v[36:37], v[70:71], v[70:71], v[36:37] op_sel_hi:[1,1,0]
	v_pk_fma_f32 v[38:39], v[72:73], v[72:73], v[38:39] op_sel_hi:[1,1,0]
	v_mov_b32_e32 v37, v40
	v_mov_b32_e32 v39, v41
	v_pk_add_f32 v[36:37], v[36:37], v[38:39]
	s_add_i32 s12, s12, s14
	v_pk_add_f32 v[34:35], v[34:35], v[36:37]
	s_min_i32 s4, s12, 0x3fff
	v_add_f32_e32 v34, v34, v35
	ds_bpermute_b32 v35, v92, v34
	s_ashr_i32 s5, s4, 31
	s_waitcnt lgkmcnt(0)
	v_add_f32_e32 v34, v34, v35
	ds_bpermute_b32 v35, v93, v34
	s_waitcnt lgkmcnt(0)
	v_add_f32_e32 v34, v34, v35
	ds_bpermute_b32 v35, v94, v34
	s_waitcnt lgkmcnt(0)
	v_add_f32_e32 v34, v34, v35
	ds_bpermute_b32 v35, v95, v34
	s_waitcnt lgkmcnt(0)
	v_add_f32_e32 v34, v34, v35
	ds_bpermute_b32 v35, v96, v34
	s_waitcnt lgkmcnt(0)
	v_add_f32_e32 v34, v34, v35
	ds_bpermute_b32 v35, v97, v34
	s_waitcnt lgkmcnt(0)
	v_add_f32_e32 v34, v34, v35
	v_fmamk_f32 v34, v34, 0x3a000000, v1
	v_mul_f32_e32 v35, 0x4f800000, v34
	v_cmp_gt_f32_e32 vcc, s13, v34
	s_nop 1
	v_cndmask_b32_e32 v34, v34, v35, vcc
	v_sqrt_f32_e32 v35, v34
	s_nop 0
	v_add_u32_e32 v36, -1, v35
	v_fma_f32 v37, -v36, v35, v34
	v_cmp_ge_f32_e64 s[0:1], 0, v37
	v_add_u32_e32 v37, 1, v35
	s_nop 0
	v_cndmask_b32_e64 v36, v35, v36, s[0:1]
	v_fma_f32 v35, -v37, v35, v34
	v_cmp_lt_f32_e64 s[0:1], 0, v35
	s_nop 1
	v_cndmask_b32_e64 v35, v36, v37, s[0:1]
	v_mul_f32_e32 v36, 0x37800000, v35
	s_lshl_b64 s[0:1], s[4:5], 13
	v_cndmask_b32_e32 v35, v35, v36, vcc
	v_cmp_class_f32_e32 vcc, v34, v85
	v_lshl_add_u64 v[120:121], v[86:87], 0, s[0:1]
	s_nop 0
	v_cndmask_b32_e32 v82, v35, v34, vcc
	v_add_co_u32_e32 v122, vcc, s3, v120
	global_load_dwordx4 v[34:37], v[120:121], off nt
	global_load_dwordx4 v[38:41], v[120:121], off offset:1024 nt
	v_addc_co_u32_e32 v123, vcc, 0, v121, vcc
	global_load_dwordx4 v[42:45], v[120:121], off offset:2048 nt
	global_load_dwordx4 v[46:49], v[120:121], off offset:3072 nt
	global_load_dwordx4 v[50:53], v[122:123], off nt
	global_load_dwordx4 v[54:57], v[122:123], off offset:1024 nt
	global_load_dwordx4 v[58:61], v[122:123], off offset:2048 nt
	global_load_dwordx4 v[62:65], v[122:123], off offset:3072 nt
	v_div_scale_f32 v120, s[0:1], v82, v82, 1.0
	v_rcp_f32_e32 v121, v120
	s_nop 0
	v_fma_f32 v122, -v120, v121, 1.0
	v_fmac_f32_e32 v121, v122, v121
	v_div_scale_f32 v122, vcc, 1.0, v82, 1.0
	v_mul_f32_e32 v123, v122, v121
	v_fma_f32 v124, -v120, v123, v122
	v_fmac_f32_e32 v123, v124, v121
	v_fma_f32 v120, -v120, v123, v122
	v_div_fmas_f32 v120, v120, v121, v123
	v_div_fixup_f32 v82, v120, v82, 1.0
	v_pk_mul_f32 v[116:117], v[116:117], v[82:83] op_sel_hi:[1,0]
	v_pk_mul_f32 v[118:119], v[118:119], v[82:83] op_sel_hi:[1,0]
	v_lshl_add_u64 v[120:121], s[94:95], 0, v[90:91]
	v_pk_mul_f32 v[116:117], v[30:31], v[116:117]
	v_pk_mul_f32 v[118:119], v[32:33], v[118:119]
	v_cvt_pk_bf16_f32 v116, v116, v117
	v_cvt_pk_bf16_f32 v117, v118, v119
	v_add_co_u32_e32 v118, vcc, s15, v120
	v_pk_mul_f32 v[112:113], v[112:113], v[82:83] op_sel_hi:[1,0]
	v_pk_mul_f32 v[114:115], v[114:115], v[82:83] op_sel_hi:[1,0]
	v_pk_mul_f32 v[108:109], v[108:109], v[82:83] op_sel_hi:[1,0]
; __device__ __forceinline__ unsigned cvt_pk_bf16(float lo, float hi) { f32x2 v = {lo, hi}; bf16x2_t b = __builtin_convertvector(v, bf16x2_t); return __builtin_bit_cast(unsigned, b); }
; #define ROPE_ENTRY() do { if (ridx < T * 64) { const int pos = ridx >> 6, i_ = ridx & 63; double ang = (double)pos * invf[i_]; const double k_ = rint(ang * 0.15915494309189535); ang = ang - k_ * 6.283185307179586; \
;         const float af = (float)ang; rc[ridx] = cosf(af); rs[ridx] = sinf(af); } ridx += F.G * NTHREADS; } while (0)
; __device__ __forceinline__ void p0_prologue(Frame& F, const Args& a) {
;     ...
;             u32x2* o8 = (u32x2*)(H + (size_t)m * D) + F.lane;
; #pragma unroll
;             for (int j = 0; j < 8; ++j) { const f32x4 g = g1v[j]; u32x2 w; w.x = cvt_pk_bf16(vc[j].x * rstd * g.x, vc[j].y * rstd * g.y); w.y = cvt_pk_bf16(vc[j].z * rstd * g.z, vc[j].w * rstd * g.w); o8[64 * j] = w; }
; #pragma unroll
;             for (int j = 0; j < 8; ++j) vc[j] = vn[j];
;             ROPE_ENTRY();
	v_pk_mul_f32 v[110:111], v[110:111], v[82:83] op_sel_hi:[1,0]
	v_pk_mul_f32 v[104:105], v[104:105], v[82:83] op_sel_hi:[1,0]
	v_pk_mul_f32 v[106:107], v[106:107], v[82:83] op_sel_hi:[1,0]
	v_pk_mul_f32 v[78:79], v[78:79], v[82:83] op_sel_hi:[1,0]
	v_pk_mul_f32 v[80:81], v[80:81], v[82:83] op_sel_hi:[1,0]
	v_pk_mul_f32 v[74:75], v[74:75], v[82:83] op_sel_hi:[1,0]
	v_pk_mul_f32 v[76:77], v[76:77], v[82:83] op_sel_hi:[1,0]
	v_pk_mul_f32 v[70:71], v[70:71], v[82:83] op_sel_hi:[1,0]
	v_pk_mul_f32 v[72:73], v[72:73], v[82:83] op_sel_hi:[1,0]
	v_pk_mul_f32 v[66:67], v[66:67], v[82:83] op_sel_hi:[1,0]
	v_pk_mul_f32 v[68:69], v[68:69], v[82:83] op_sel_hi:[1,0]
	v_addc_co_u32_e32 v119, vcc, 0, v121, vcc
	v_pk_mul_f32 v[112:113], v[26:27], v[112:113]
	v_pk_mul_f32 v[114:115], v[28:29], v[114:115]
	v_pk_mul_f32 v[108:109], v[22:23], v[108:109]
	v_pk_mul_f32 v[110:111], v[24:25], v[110:111]
	v_pk_mul_f32 v[104:105], v[18:19], v[104:105]
	v_pk_mul_f32 v[106:107], v[20:21], v[106:107]
	v_pk_mul_f32 v[78:79], v[14:15], v[78:79]
	v_pk_mul_f32 v[80:81], v[16:17], v[80:81]
	v_pk_mul_f32 v[74:75], v[10:11], v[74:75]
	v_pk_mul_f32 v[76:77], v[12:13], v[76:77]
	v_pk_mul_f32 v[70:71], v[6:7], v[70:71]
	v_pk_mul_f32 v[72:73], v[8:9], v[72:73]
	v_pk_mul_f32 v[66:67], v[2:3], v[66:67]
	v_pk_mul_f32 v[68:69], v[4:5], v[68:69]
	v_cvt_pk_bf16_f32 v112, v112, v113
	v_cvt_pk_bf16_f32 v113, v114, v115
	v_cvt_pk_bf16_f32 v108, v108, v109
	v_cvt_pk_bf16_f32 v109, v110, v111
	v_cvt_pk_bf16_f32 v104, v104, v105
	v_cvt_pk_bf16_f32 v105, v106, v107
	v_cvt_pk_bf16_f32 v78, v78, v79
	v_cvt_pk_bf16_f32 v79, v80, v81
	v_cvt_pk_bf16_f32 v74, v74, v75
	v_cvt_pk_bf16_f32 v75, v76, v77
	v_cvt_pk_bf16_f32 v70, v70, v71
	v_cvt_pk_bf16_f32 v71, v72, v73
	v_cvt_pk_bf16_f32 v66, v66, v67
	v_cvt_pk_bf16_f32 v67, v68, v69
	v_cmp_gt_i32_e32 vcc, s17, v84
	global_store_dwordx2 v[118:119], v[116:117], off sc1
	global_store_dwordx2 v[118:119], v[112:113], off offset:512 sc1
	global_store_dwordx2 v[118:119], v[108:109], off offset:1024 sc1
	global_store_dwordx2 v[118:119], v[104:105], off offset:1536 sc1
	global_store_dwordx2 v[118:119], v[78:79], off offset:2048 sc1
	global_store_dwordx2 v[118:119], v[74:75], off offset:2560 sc1
	global_store_dwordx2 v[118:119], v[70:71], off offset:3072 sc1
	global_store_dwordx2 v[118:119], v[66:67], off offset:3584 sc1
	s_and_saveexec_b64 s[26:27], vcc
	s_cbranch_execz .LBB0_26
	ds_read_b64 v[66:67], v98 offset:40960
	v_ashrrev_i32_e32 v68, 6, v84
	v_cvt_f64_i32_e32 v[68:69], v68
	s_waitcnt lgkmcnt(0)
	v_mul_f64 v[66:67], v[66:67], v[68:69]
	v_mul_f64 v[68:69], v[66:67], s[22:23]
	v_rndne_f64_e32 v[68:69], v[68:69]
	v_fmac_f64_e32 v[66:67], s[24:25], v[68:69]
	v_cvt_f32_f64_e32 v68, v[66:67]
	v_and_b32_e32 v69, 0x7fffffff, v68
	v_lshrrev_b32_e32 v66, 23, v69
	v_and_b32_e32 v67, 0x7fffff, v69
	v_cmp_nlt_f32_e64 s[8:9], |v68|, s30
	v_add_u32_e32 v71, 0xffffff88, v66
	v_or_b32_e32 v70, 0x800000, v67
	s_and_saveexec_b64 s[0:1], s[8:9]
	s_xor_b64 s[28:29], exec, s[0:1]
	s_cbranch_execz .LBB0_30
	v_cmp_lt_u32_e32 vcc, 63, v71
	s_nop 1
	v_cndmask_b32_e32 v66, 0, v101, vcc
	v_add_u32_e32 v66, v66, v71
	v_cmp_lt_u32_e64 s[0:1], 31, v66
	s_nop 1
	v_cndmask_b32_e64 v67, 0, v102, s[0:1]
	v_add_u32_e32 v66, v67, v66
	v_cmp_lt_u32_e64 s[4:5], 31, v66
	s_nop 1
	v_cndmask_b32_e64 v67, 0, v102, s[4:5]
	v_add_u32_e32 v106, v67, v66
	v_mad_u64_u32 v[66:67], s[6:7], v70, s31, 0
	v_mov_b32_e32 v82, v67
	v_mad_u64_u32 v[72:73], s[6:7], v70, s33, v[82:83]
	v_mov_b32_e32 v82, v73
	v_mad_u64_u32 v[74:75], s[6:7], v70, s34, v[82:83]
	v_mov_b32_e32 v82, v75
	v_mad_u64_u32 v[76:77], s[6:7], v70, s35, v[82:83]
	v_mov_b32_e32 v82, v77
	v_mad_u64_u32 v[78:79], s[6:7], v70, s36, v[82:83]
	v_mov_b32_e32 v82, v79
	v_mad_u64_u32 v[80:81], s[6:7], v70, s37, v[82:83]
	v_mov_b32_e32 v82, v81
	v_mad_u64_u32 v[104:105], s[6:7], v70, s38, v[82:83]
	v_cndmask_b32_e32 v67, v80, v76, vcc
	v_cndmask_b32_e32 v73, v104, v78, vcc
	v_cndmask_b32_e32 v77, v105, v80, vcc
	v_cndmask_b32_e64 v75, v73, v67, s[0:1]
	v_cndmask_b32_e64 v73, v77, v73, s[0:1]
	v_cndmask_b32_e32 v77, v78, v74, vcc
	v_cndmask_b32_e64 v67, v67, v77, s[0:1]
	v_cndmask_b32_e32 v72, v76, v72, vcc
	v_cndmask_b32_e64 v73, v73, v75, s[4:5]
	v_cndmask_b32_e64 v75, v75, v67, s[4:5]
	v_sub_u32_e32 v78, 32, v106
	v_cndmask_b32_e64 v76, v77, v72, s[0:1]
	v_alignbit_b32 v79, v73, v75, v78
	v_cmp_eq_u32_e64 s[6:7], 0, v106
	v_cndmask_b32_e64 v67, v67, v76, s[4:5]
	v_alignbit_b32 v77, v75, v67, v78
	v_cndmask_b32_e64 v73, v79, v73, s[6:7]
	v_cndmask_b32_e32 v66, v74, v66, vcc
	v_cndmask_b32_e64 v75, v77, v75, s[6:7]
	v_bfe_u32 v80, v73, 29, 1
	v_cndmask_b32_e64 v66, v72, v66, s[0:1]
	v_alignbit_b32 v77, v73, v75, 30
	v_sub_u32_e32 v81, 0, v80
	v_cndmask_b32_e64 v66, v76, v66, s[4:5]
	v_xor_b32_e32 v77, v77, v81
	v_alignbit_b32 v72, v67, v66, v78
	v_cndmask_b32_e64 v67, v72, v67, s[6:7]
	v_ffbh_u32_e32 v74, v77
	v_alignbit_b32 v72, v75, v67, 30
	v_min_u32_e32 v74, 32, v74
	v_alignbit_b32 v66, v67, v66, 30
	v_xor_b32_e32 v72, v72, v81
	v_sub_u32_e32 v75, 31, v74
	v_xor_b32_e32 v66, v66, v81
	v_alignbit_b32 v76, v77, v72, v75
	v_alignbit_b32 v66, v72, v66, v75
	v_alignbit_b32 v67, v76, v66, 9
	v_ffbh_u32_e32 v72, v67
	v_min_u32_e32 v72, 32, v72
	v_lshrrev_b32_e32 v79, 29, v73
	v_not_b32_e32 v75, v72
	v_alignbit_b32 v66, v67, v66, v75
	v_lshlrev_b32_e32 v67, 31, v79
	v_or_b32_e32 v75, 0x33000000, v67
	v_add_lshl_u32 v72, v72, v74, 23
	v_lshrrev_b32_e32 v66, 9, v66
	v_sub_u32_e32 v72, v75, v72
	v_or_b32_e32 v67, 0.5, v67
	v_lshlrev_b32_e32 v74, 23, v74
	v_or_b32_e32 v66, v72, v66
	v_lshrrev_b32_e32 v72, 9, v76
	v_sub_u32_e32 v67, v67, v74
	v_or_b32_e32 v67, v72, v67
	v_mul_f32_e32 v72, 0x3fc90fda, v67
	v_fma_f32 v74, v67, s39, -v72
	v_fmac_f32_e32 v74, 0x33a22168, v67
	v_fmac_f32_e32 v74, 0x3fc90fda, v66
	v_lshrrev_b32_e32 v66, 30, v73
	v_add_f32_e32 v67, v72, v74
	v_add_u32_e32 v66, v80, v66

; __device__ __forceinline__ unsigned cvt_pk_bf16(float lo, float hi) { f32x2 v = {lo, hi}; bf16x2_t b = __builtin_convertvector(v, bf16x2_t); return __builtin_bit_cast(unsigned, b); }
; __device__ __forceinline__ float sigmoid_f(float x) { return __builtin_amdgcn_rcpf(1.0f + __expf(-x)); }
;     __device__ __forceinline__ void operator()(const AccT& acc, const pg8::Unit& u, int wr, int wc, int fr, int fq) const {
;     ...
;             const int kind = (pn - 16) >> 3;
;             bf16_t* dst = (bf16_t*)(ws + (kind == 0 ? WS_RV : kind == 1 ? WS_RG : kind == 2 ? WS_GA : WS_GR)); const int col0 = ((pn - 16) & 7) * 256 + wc * 32 + 8 * fq;
; #pragma unroll
;             for (int ai = 0; ai < 2; ++ai)
; #pragma unroll
;                 for (int m = 0; m < 4; ++m) { const int row = row0 + ai * 128 + m * 16;
; #pragma unroll
;                     for (int bj = 0; bj < 2; ++bj) { f32x4 v0 = acc[ai][bj][m][0], v1 = acc[ai][bj][m][1];
;                         if (kind == 1) {
; #pragma unroll
;                             for (int j = 0; j < 4; ++j) { v0[j] = v0[j] * sigmoid_f(v0[j]); v1[j] = v1[j] * sigmoid_f(v1[j]); } }
;                         else if (kind >= 2) {
; #pragma unroll
;                             for (int j = 0; j < 4; ++j) { v0[j] = sigmoid_f(v0[j]); v1[j] = sigmoid_f(v1[j]); } }
;                         u32x4 w; w.x = cvt_pk_bf16(v0[0], v0[1]); w.y = cvt_pk_bf16(v0[2], v0[3]); w.z = cvt_pk_bf16(v1[0], v1[1]); w.w = cvt_pk_bf16(v1[2], v1[3]);
;                         if (kind >= 1) __builtin_nontemporal_store(w, (u32x4*)(dst + (size_t)row * D + col0 + bj * 128));
;                         else *(u32x4*)(dst + (size_t)row * D + col0 + bj * 128) = w; } }
.LBB0_152:
	s_cmp_eq_u32 s4, 2
	s_cselect_b32 s4, s76, 0x4c600000
	s_and_b64 s[54:55], s[54:55], exec
	s_cselect_b32 s4, 0x44600000, s4
	s_and_b64 s[12:13], s[12:13], exec
	s_cselect_b32 s4, 0x40600000, s4
	s_add_u32 s12, s94, s4
	s_addc_u32 s13, s95, 0
	s_lshl_b32 s4, s52, 8
	s_and_b32 s4, s4, 0x700
	v_or_b32_e32 v130, s4, v162
	v_lshlrev_b32_e32 v130, 1, v130
	v_ashrrev_i32_e32 v143, 31, v142
	v_lshl_add_u64 v[144:145], s[12:13], 0, v[130:131]
	v_lshlrev_b64 v[146:147], 12, v[142:143]
	v_cndmask_b32_e64 v130, 0, 1, s[0:1]
	v_lshl_add_u64 v[146:147], v[144:145], 0, v[146:147]
	v_cvt_pk_bf16_f32 v148, v148, v149
	v_cvt_pk_bf16_f32 v149, v152, v153
	v_cvt_pk_bf16_f32 v150, v150, v151
	v_cvt_pk_bf16_f32 v151, v154, v155
	v_cmp_ne_u32_e64 s[12:13], 1, v130
	s_andn2_b64 vcc, exec, s[0:1]
	s_mov_b64 s[0:1], -1
	global_store_dwordx4 v[146:147], v[148:151], off sc1
	s_cbranch_vccnz .LBB0_156
	s_and_b64 vcc, exec, s[10:11]
	v_mov_b32_e32 v155, v117
	v_mov_b32_e32 v154, v116
	v_mov_b32_e32 v151, v115
	v_mov_b32_e32 v150, v114
	v_mov_b32_e32 v153, v121
	v_mov_b32_e32 v152, v120
	v_mov_b32_e32 v149, v119
	v_mov_b32_e32 v148, v118
	s_cbranch_vccnz .LBB0_155
	v_mul_f32_e32 v130, 0xbfb8aa3b, v118
	v_exp_f32_e32 v130, v130
	v_mul_f32_e32 v141, 0xbfb8aa3b, v114
	v_exp_f32_e32 v141, v141
	v_mul_f32_e32 v149, 0xbfb8aa3b, v115
	v_add_f32_e32 v130, 1.0, v130
	v_rcp_f32_e32 v148, v130
	v_mul_f32_e32 v130, 0xbfb8aa3b, v119
	v_exp_f32_e32 v130, v130
	v_exp_f32_e32 v151, v149
	v_add_f32_e32 v141, 1.0, v141
	v_rcp_f32_e32 v150, v141
	v_add_f32_e32 v130, 1.0, v130
	v_mul_f32_e32 v141, 0xbfb8aa3b, v120
	v_rcp_f32_e32 v149, v130
	v_add_f32_e32 v130, 1.0, v151
	v_exp_f32_e32 v141, v141
	v_mul_f32_e32 v151, 0xbfb8aa3b, v116
	v_exp_f32_e32 v153, v151
	v_rcp_f32_e32 v151, v130
	v_add_f32_e32 v130, 1.0, v141
	v_mul_f32_e32 v141, 0xbfb8aa3b, v121
	v_rcp_f32_e32 v152, v130
	v_add_f32_e32 v130, 1.0, v153
	v_exp_f32_e32 v141, v141
	v_mul_f32_e32 v153, 0xbfb8aa3b, v117
	v_exp_f32_e32 v155, v153
	v_rcp_f32_e32 v154, v130
	v_add_f32_e32 v130, 1.0, v141
	v_rcp_f32_e32 v153, v130
	v_add_f32_e32 v130, 1.0, v155
	v_rcp_f32_e32 v155, v130

; __device__ __forceinline__ unsigned cvt_pk_bf16(float lo, float hi) { f32x2 v = {lo, hi}; bf16x2_t b = __builtin_convertvector(v, bf16x2_t); return __builtin_bit_cast(unsigned, b); }
; __device__ __forceinline__ float sigmoid_f(float x) { return __builtin_amdgcn_rcpf(1.0f + __expf(-x)); }
;     __device__ __forceinline__ void operator()(const AccT& acc, const pg8::Unit& u, int wr, int wc, int fr, int fq) const {
;     ...
;             const int kind = (pn - 16) >> 3;
;             bf16_t* dst = (bf16_t*)(ws + (kind == 0 ? WS_RV : kind == 1 ? WS_RG : kind == 2 ? WS_GA : WS_GR)); const int col0 = ((pn - 16) & 7) * 256 + wc * 32 + 8 * fq;
; #pragma unroll
;             for (int ai = 0; ai < 2; ++ai)
; #pragma unroll
;                 for (int m = 0; m < 4; ++m) { const int row = row0 + ai * 128 + m * 16;
; #pragma unroll
;                     for (int bj = 0; bj < 2; ++bj) { f32x4 v0 = acc[ai][bj][m][0], v1 = acc[ai][bj][m][1];
;                         if (kind == 1) {
; #pragma unroll
;                             for (int j = 0; j < 4; ++j) { v0[j] = v0[j] * sigmoid_f(v0[j]); v1[j] = v1[j] * sigmoid_f(v1[j]); } }
;                         else if (kind >= 2) {
; #pragma unroll
;                             for (int j = 0; j < 4; ++j) { v0[j] = sigmoid_f(v0[j]); v1[j] = sigmoid_f(v1[j]); } }
;                         u32x4 w; w.x = cvt_pk_bf16(v0[0], v0[1]); w.y = cvt_pk_bf16(v0[2], v0[3]); w.z = cvt_pk_bf16(v1[0], v1[1]); w.w = cvt_pk_bf16(v1[2], v1[3]);
;                         if (kind >= 1) __builtin_nontemporal_store(w, (u32x4*)(dst + (size_t)row * D + col0 + bj * 128));
;                         else *(u32x4*)(dst + (size_t)row * D + col0 + bj * 128) = w; } }
.LBB0_158:
	v_cvt_pk_bf16_f32 v148, v148, v149
	v_cvt_pk_bf16_f32 v149, v152, v153
	v_cvt_pk_bf16_f32 v150, v150, v151
	v_cvt_pk_bf16_f32 v151, v154, v155
	s_and_b64 vcc, exec, s[12:13]
	s_mov_b64 s[0:1], -1
	global_store_dwordx4 v[146:147], v[148:151], off offset:256 sc1
	s_cbranch_vccnz .LBB0_162
	s_and_b64 vcc, exec, s[10:11]
	v_mov_b32_e32 v155, v109
	v_mov_b32_e32 v154, v108
	v_mov_b32_e32 v151, v107
	v_mov_b32_e32 v150, v106
	v_mov_b32_e32 v153, v113
	v_mov_b32_e32 v152, v112
	v_mov_b32_e32 v149, v111
	v_mov_b32_e32 v148, v110
	s_cbranch_vccnz .LBB0_161
	v_mul_f32_e32 v130, 0xbfb8aa3b, v110
	v_exp_f32_e32 v130, v130
	v_mul_f32_e32 v141, 0xbfb8aa3b, v106
	v_exp_f32_e32 v141, v141
	v_mul_f32_e32 v146, 0xbfb8aa3b, v107
	v_add_f32_e32 v130, 1.0, v130
	v_rcp_f32_e32 v148, v130
	v_mul_f32_e32 v130, 0xbfb8aa3b, v111
	v_exp_f32_e32 v130, v130
	v_exp_f32_e32 v146, v146
	v_add_f32_e32 v141, 1.0, v141
	v_rcp_f32_e32 v150, v141
	v_add_f32_e32 v130, 1.0, v130
	v_mul_f32_e32 v141, 0xbfb8aa3b, v112
	v_rcp_f32_e32 v149, v130
	v_add_f32_e32 v130, 1.0, v146
	v_exp_f32_e32 v141, v141
	v_mul_f32_e32 v146, 0xbfb8aa3b, v108
	v_exp_f32_e32 v146, v146
	v_rcp_f32_e32 v151, v130
	v_add_f32_e32 v130, 1.0, v141
	v_mul_f32_e32 v141, 0xbfb8aa3b, v113
	v_rcp_f32_e32 v152, v130
	v_add_f32_e32 v130, 1.0, v146
	v_exp_f32_e32 v141, v141
	v_mul_f32_e32 v146, 0xbfb8aa3b, v109
	v_exp_f32_e32 v146, v146
	v_rcp_f32_e32 v154, v130
	v_add_f32_e32 v130, 1.0, v141
	v_rcp_f32_e32 v153, v130
	v_add_f32_e32 v130, 1.0, v146
	v_rcp_f32_e32 v155, v130

; __device__ __forceinline__ unsigned cvt_pk_bf16(float lo, float hi) { f32x2 v = {lo, hi}; bf16x2_t b = __builtin_convertvector(v, bf16x2_t); return __builtin_bit_cast(unsigned, b); }
; __device__ __forceinline__ float sigmoid_f(float x) { return __builtin_amdgcn_rcpf(1.0f + __expf(-x)); }
;     __device__ __forceinline__ void operator()(const AccT& acc, const pg8::Unit& u, int wr, int wc, int fr, int fq) const {
;     ...
;             const int kind = (pn - 16) >> 3;
;             bf16_t* dst = (bf16_t*)(ws + (kind == 0 ? WS_RV : kind == 1 ? WS_RG : kind == 2 ? WS_GA : WS_GR)); const int col0 = ((pn - 16) & 7) * 256 + wc * 32 + 8 * fq;
; #pragma unroll
;             for (int ai = 0; ai < 2; ++ai)
; #pragma unroll
;                 for (int m = 0; m < 4; ++m) { const int row = row0 + ai * 128 + m * 16;
; #pragma unroll
;                     for (int bj = 0; bj < 2; ++bj) { f32x4 v0 = acc[ai][bj][m][0], v1 = acc[ai][bj][m][1];
;                         if (kind == 1) {
; #pragma unroll
;                             for (int j = 0; j < 4; ++j) { v0[j] = v0[j] * sigmoid_f(v0[j]); v1[j] = v1[j] * sigmoid_f(v1[j]); } }
;                         else if (kind >= 2) {
; #pragma unroll
;                             for (int j = 0; j < 4; ++j) { v0[j] = sigmoid_f(v0[j]); v1[j] = sigmoid_f(v1[j]); } }
;                         u32x4 w; w.x = cvt_pk_bf16(v0[0], v0[1]); w.y = cvt_pk_bf16(v0[2], v0[3]); w.z = cvt_pk_bf16(v1[0], v1[1]); w.w = cvt_pk_bf16(v1[2], v1[3]);
;                         if (kind >= 1) __builtin_nontemporal_store(w, (u32x4*)(dst + (size_t)row * D + col0 + bj * 128));
;                         else *(u32x4*)(dst + (size_t)row * D + col0 + bj * 128) = w; } }
.LBB0_164:
	v_or_b32_e32 v146, 16, v142
	v_ashrrev_i32_e32 v147, 31, v146
	v_lshlrev_b64 v[146:147], 12, v[146:147]
	v_lshl_add_u64 v[146:147], v[144:145], 0, v[146:147]
	v_cvt_pk_bf16_f32 v148, v148, v149
	v_cvt_pk_bf16_f32 v149, v152, v153
	v_cvt_pk_bf16_f32 v150, v150, v151
	v_cvt_pk_bf16_f32 v151, v154, v155
	s_and_b64 vcc, exec, s[12:13]
	s_mov_b64 s[0:1], -1
	global_store_dwordx4 v[146:147], v[148:151], off sc1
	s_cbranch_vccnz .LBB0_168
	s_and_b64 vcc, exec, s[10:11]
	v_mov_b32_e32 v155, v101
	v_mov_b32_e32 v154, v100
	v_mov_b32_e32 v151, v99
	v_mov_b32_e32 v150, v98
	v_mov_b32_e32 v153, v105
	v_mov_b32_e32 v152, v104
	v_mov_b32_e32 v149, v103
	v_mov_b32_e32 v148, v102
	s_cbranch_vccnz .LBB0_167
	v_mul_f32_e32 v130, 0xbfb8aa3b, v102
	v_exp_f32_e32 v130, v130
	v_mul_f32_e32 v141, 0xbfb8aa3b, v98
	v_exp_f32_e32 v141, v141
	v_mul_f32_e32 v149, 0xbfb8aa3b, v99
	v_add_f32_e32 v130, 1.0, v130
	v_rcp_f32_e32 v148, v130
	v_mul_f32_e32 v130, 0xbfb8aa3b, v103
	v_exp_f32_e32 v130, v130
	v_exp_f32_e32 v151, v149
	v_add_f32_e32 v141, 1.0, v141
	v_rcp_f32_e32 v150, v141
	v_add_f32_e32 v130, 1.0, v130
	v_mul_f32_e32 v141, 0xbfb8aa3b, v104
	v_rcp_f32_e32 v149, v130
	v_add_f32_e32 v130, 1.0, v151
	v_exp_f32_e32 v141, v141
	v_mul_f32_e32 v151, 0xbfb8aa3b, v100
	v_exp_f32_e32 v153, v151
	v_rcp_f32_e32 v151, v130
	v_add_f32_e32 v130, 1.0, v141
	v_mul_f32_e32 v141, 0xbfb8aa3b, v105
	v_rcp_f32_e32 v152, v130
	v_add_f32_e32 v130, 1.0, v153
	v_exp_f32_e32 v141, v141
	v_mul_f32_e32 v153, 0xbfb8aa3b, v101
	v_exp_f32_e32 v155, v153
	v_rcp_f32_e32 v154, v130
	v_add_f32_e32 v130, 1.0, v141
	v_rcp_f32_e32 v153, v130
	v_add_f32_e32 v130, 1.0, v155
	v_rcp_f32_e32 v155, v130

; __device__ __forceinline__ unsigned cvt_pk_bf16(float lo, float hi) { f32x2 v = {lo, hi}; bf16x2_t b = __builtin_convertvector(v, bf16x2_t); return __builtin_bit_cast(unsigned, b); }
; __device__ __forceinline__ float sigmoid_f(float x) { return __builtin_amdgcn_rcpf(1.0f + __expf(-x)); }
;     __device__ __forceinline__ void operator()(const AccT& acc, const pg8::Unit& u, int wr, int wc, int fr, int fq) const {
;     ...
;             const int kind = (pn - 16) >> 3;
;             bf16_t* dst = (bf16_t*)(ws + (kind == 0 ? WS_RV : kind == 1 ? WS_RG : kind == 2 ? WS_GA : WS_GR)); const int col0 = ((pn - 16) & 7) * 256 + wc * 32 + 8 * fq;
; #pragma unroll
;             for (int ai = 0; ai < 2; ++ai)
; #pragma unroll
;                 for (int m = 0; m < 4; ++m) { const int row = row0 + ai * 128 + m * 16;
; #pragma unroll
;                     for (int bj = 0; bj < 2; ++bj) { f32x4 v0 = acc[ai][bj][m][0], v1 = acc[ai][bj][m][1];
;                         if (kind == 1) {
; #pragma unroll
;                             for (int j = 0; j < 4; ++j) { v0[j] = v0[j] * sigmoid_f(v0[j]); v1[j] = v1[j] * sigmoid_f(v1[j]); } }
;                         else if (kind >= 2) {
; #pragma unroll
;                             for (int j = 0; j < 4; ++j) { v0[j] = sigmoid_f(v0[j]); v1[j] = sigmoid_f(v1[j]); } }
;                         u32x4 w; w.x = cvt_pk_bf16(v0[0], v0[1]); w.y = cvt_pk_bf16(v0[2], v0[3]); w.z = cvt_pk_bf16(v1[0], v1[1]); w.w = cvt_pk_bf16(v1[2], v1[3]);
;                         if (kind >= 1) __builtin_nontemporal_store(w, (u32x4*)(dst + (size_t)row * D + col0 + bj * 128));
;                         else *(u32x4*)(dst + (size_t)row * D + col0 + bj * 128) = w; } }
.LBB0_170:
	v_cvt_pk_bf16_f32 v148, v148, v149
	v_cvt_pk_bf16_f32 v149, v152, v153
	v_cvt_pk_bf16_f32 v150, v150, v151
	v_cvt_pk_bf16_f32 v151, v154, v155
	s_and_b64 vcc, exec, s[12:13]
	s_mov_b64 s[0:1], -1
	global_store_dwordx4 v[146:147], v[148:151], off offset:256 sc1
	s_cbranch_vccnz .LBB0_174
	s_and_b64 vcc, exec, s[10:11]
	v_mov_b32_e32 v155, v93
	v_mov_b32_e32 v154, v92
	v_mov_b32_e32 v151, v91
	v_mov_b32_e32 v150, v90
	v_mov_b32_e32 v153, v97
	v_mov_b32_e32 v152, v96
	v_mov_b32_e32 v149, v95
	v_mov_b32_e32 v148, v94
	s_cbranch_vccnz .LBB0_173
	v_mul_f32_e32 v130, 0xbfb8aa3b, v94
	v_exp_f32_e32 v130, v130
	v_mul_f32_e32 v141, 0xbfb8aa3b, v90
	v_exp_f32_e32 v141, v141
	v_mul_f32_e32 v146, 0xbfb8aa3b, v91
	v_add_f32_e32 v130, 1.0, v130
	v_rcp_f32_e32 v148, v130
	v_mul_f32_e32 v130, 0xbfb8aa3b, v95
	v_exp_f32_e32 v130, v130
	v_exp_f32_e32 v146, v146
	v_add_f32_e32 v141, 1.0, v141
	v_rcp_f32_e32 v150, v141
	v_add_f32_e32 v130, 1.0, v130
	v_mul_f32_e32 v141, 0xbfb8aa3b, v96
	v_rcp_f32_e32 v149, v130
	v_add_f32_e32 v130, 1.0, v146
	v_exp_f32_e32 v141, v141
	v_mul_f32_e32 v146, 0xbfb8aa3b, v92
	v_exp_f32_e32 v146, v146
	v_rcp_f32_e32 v151, v130
	v_add_f32_e32 v130, 1.0, v141
	v_mul_f32_e32 v141, 0xbfb8aa3b, v97
	v_rcp_f32_e32 v152, v130
	v_add_f32_e32 v130, 1.0, v146
	v_exp_f32_e32 v141, v141
	v_mul_f32_e32 v146, 0xbfb8aa3b, v93
	v_exp_f32_e32 v146, v146
	v_rcp_f32_e32 v154, v130
	v_add_f32_e32 v130, 1.0, v141
	v_rcp_f32_e32 v153, v130
	v_add_f32_e32 v130, 1.0, v146
	v_rcp_f32_e32 v155, v130

; __device__ __forceinline__ unsigned cvt_pk_bf16(float lo, float hi) { f32x2 v = {lo, hi}; bf16x2_t b = __builtin_convertvector(v, bf16x2_t); return __builtin_bit_cast(unsigned, b); }
; __device__ __forceinline__ float sigmoid_f(float x) { return __builtin_amdgcn_rcpf(1.0f + __expf(-x)); }
;     __device__ __forceinline__ void operator()(const AccT& acc, const pg8::Unit& u, int wr, int wc, int fr, int fq) const {
;     ...
;             const int kind = (pn - 16) >> 3;
;             bf16_t* dst = (bf16_t*)(ws + (kind == 0 ? WS_RV : kind == 1 ? WS_RG : kind == 2 ? WS_GA : WS_GR)); const int col0 = ((pn - 16) & 7) * 256 + wc * 32 + 8 * fq;
; #pragma unroll
;             for (int ai = 0; ai < 2; ++ai)
; #pragma unroll
;                 for (int m = 0; m < 4; ++m) { const int row = row0 + ai * 128 + m * 16;
; #pragma unroll
;                     for (int bj = 0; bj < 2; ++bj) { f32x4 v0 = acc[ai][bj][m][0], v1 = acc[ai][bj][m][1];
;                         if (kind == 1) {
; #pragma unroll
;                             for (int j = 0; j < 4; ++j) { v0[j] = v0[j] * sigmoid_f(v0[j]); v1[j] = v1[j] * sigmoid_f(v1[j]); } }
;                         else if (kind >= 2) {
; #pragma unroll
;                             for (int j = 0; j < 4; ++j) { v0[j] = sigmoid_f(v0[j]); v1[j] = sigmoid_f(v1[j]); } }
;                         u32x4 w; w.x = cvt_pk_bf16(v0[0], v0[1]); w.y = cvt_pk_bf16(v0[2], v0[3]); w.z = cvt_pk_bf16(v1[0], v1[1]); w.w = cvt_pk_bf16(v1[2], v1[3]);
;                         if (kind >= 1) __builtin_nontemporal_store(w, (u32x4*)(dst + (size_t)row * D + col0 + bj * 128));
;                         else *(u32x4*)(dst + (size_t)row * D + col0 + bj * 128) = w; } }
.LBB0_176:
	v_or_b32_e32 v146, 32, v142
	v_ashrrev_i32_e32 v147, 31, v146
	v_lshlrev_b64 v[146:147], 12, v[146:147]
	v_lshl_add_u64 v[146:147], v[144:145], 0, v[146:147]
	v_cvt_pk_bf16_f32 v148, v148, v149
	v_cvt_pk_bf16_f32 v149, v152, v153
	v_cvt_pk_bf16_f32 v150, v150, v151
	v_cvt_pk_bf16_f32 v151, v154, v155
	s_and_b64 vcc, exec, s[12:13]
	s_mov_b64 s[0:1], -1
	global_store_dwordx4 v[146:147], v[148:151], off sc1
	s_cbranch_vccnz .LBB0_180
	s_and_b64 vcc, exec, s[10:11]
	v_mov_b32_e32 v155, v85
	v_mov_b32_e32 v154, v84
	v_mov_b32_e32 v151, v83
	v_mov_b32_e32 v150, v82
	v_mov_b32_e32 v153, v89
	v_mov_b32_e32 v152, v88
	v_mov_b32_e32 v149, v87
	v_mov_b32_e32 v148, v86
	s_cbranch_vccnz .LBB0_179
	v_mul_f32_e32 v130, 0xbfb8aa3b, v86
	v_exp_f32_e32 v130, v130
	v_mul_f32_e32 v141, 0xbfb8aa3b, v82
	v_exp_f32_e32 v141, v141
	v_mul_f32_e32 v149, 0xbfb8aa3b, v83
	v_add_f32_e32 v130, 1.0, v130
	v_rcp_f32_e32 v148, v130
	v_mul_f32_e32 v130, 0xbfb8aa3b, v87
	v_exp_f32_e32 v130, v130
	v_exp_f32_e32 v151, v149
	v_add_f32_e32 v141, 1.0, v141
	v_rcp_f32_e32 v150, v141
	v_add_f32_e32 v130, 1.0, v130
	v_mul_f32_e32 v141, 0xbfb8aa3b, v88
	v_rcp_f32_e32 v149, v130
	v_add_f32_e32 v130, 1.0, v151
	v_exp_f32_e32 v141, v141
	v_mul_f32_e32 v151, 0xbfb8aa3b, v84
	v_exp_f32_e32 v153, v151
	v_rcp_f32_e32 v151, v130
	v_add_f32_e32 v130, 1.0, v141
	v_mul_f32_e32 v141, 0xbfb8aa3b, v89
	v_rcp_f32_e32 v152, v130
	v_add_f32_e32 v130, 1.0, v153
	v_exp_f32_e32 v141, v141
	v_mul_f32_e32 v153, 0xbfb8aa3b, v85
	v_exp_f32_e32 v155, v153
	v_rcp_f32_e32 v154, v130
	v_add_f32_e32 v130, 1.0, v141
	v_rcp_f32_e32 v153, v130
	v_add_f32_e32 v130, 1.0, v155
	v_rcp_f32_e32 v155, v130

; __device__ __forceinline__ unsigned cvt_pk_bf16(float lo, float hi) { f32x2 v = {lo, hi}; bf16x2_t b = __builtin_convertvector(v, bf16x2_t); return __builtin_bit_cast(unsigned, b); }
; __device__ __forceinline__ float sigmoid_f(float x) { return __builtin_amdgcn_rcpf(1.0f + __expf(-x)); }
;     __device__ __forceinline__ void operator()(const AccT& acc, const pg8::Unit& u, int wr, int wc, int fr, int fq) const {
;     ...
;             const int kind = (pn - 16) >> 3;
;             bf16_t* dst = (bf16_t*)(ws + (kind == 0 ? WS_RV : kind == 1 ? WS_RG : kind == 2 ? WS_GA : WS_GR)); const int col0 = ((pn - 16) & 7) * 256 + wc * 32 + 8 * fq;
; #pragma unroll
;             for (int ai = 0; ai < 2; ++ai)
; #pragma unroll
;                 for (int m = 0; m < 4; ++m) { const int row = row0 + ai * 128 + m * 16;
; #pragma unroll
;                     for (int bj = 0; bj < 2; ++bj) { f32x4 v0 = acc[ai][bj][m][0], v1 = acc[ai][bj][m][1];
;                         if (kind == 1) {
; #pragma unroll
;                             for (int j = 0; j < 4; ++j) { v0[j] = v0[j] * sigmoid_f(v0[j]); v1[j] = v1[j] * sigmoid_f(v1[j]); } }
;                         else if (kind >= 2) {
; #pragma unroll
;                             for (int j = 0; j < 4; ++j) { v0[j] = sigmoid_f(v0[j]); v1[j] = sigmoid_f(v1[j]); } }
;                         u32x4 w; w.x = cvt_pk_bf16(v0[0], v0[1]); w.y = cvt_pk_bf16(v0[2], v0[3]); w.z = cvt_pk_bf16(v1[0], v1[1]); w.w = cvt_pk_bf16(v1[2], v1[3]);
;                         if (kind >= 1) __builtin_nontemporal_store(w, (u32x4*)(dst + (size_t)row * D + col0 + bj * 128));
;                         else *(u32x4*)(dst + (size_t)row * D + col0 + bj * 128) = w; } }
.LBB0_182:
	v_cvt_pk_bf16_f32 v148, v148, v149
	v_cvt_pk_bf16_f32 v149, v152, v153
	v_cvt_pk_bf16_f32 v150, v150, v151
	v_cvt_pk_bf16_f32 v151, v154, v155
	s_and_b64 vcc, exec, s[12:13]
	s_mov_b64 s[0:1], -1
	global_store_dwordx4 v[146:147], v[148:151], off offset:256 sc1
	s_cbranch_vccnz .LBB0_186
	s_and_b64 vcc, exec, s[10:11]
	v_mov_b32_e32 v155, v77
	v_mov_b32_e32 v154, v76
	v_mov_b32_e32 v151, v75
	v_mov_b32_e32 v150, v74
	v_mov_b32_e32 v153, v81
	v_mov_b32_e32 v152, v80
	v_mov_b32_e32 v149, v79
	v_mov_b32_e32 v148, v78
	s_cbranch_vccnz .LBB0_185
	v_mul_f32_e32 v130, 0xbfb8aa3b, v78
	v_exp_f32_e32 v130, v130
	v_mul_f32_e32 v141, 0xbfb8aa3b, v74
	v_exp_f32_e32 v141, v141
	v_mul_f32_e32 v146, 0xbfb8aa3b, v75
	v_add_f32_e32 v130, 1.0, v130
	v_rcp_f32_e32 v148, v130
	v_mul_f32_e32 v130, 0xbfb8aa3b, v79
	v_exp_f32_e32 v130, v130
	v_exp_f32_e32 v146, v146
	v_add_f32_e32 v141, 1.0, v141
	v_rcp_f32_e32 v150, v141
	v_add_f32_e32 v130, 1.0, v130
	v_mul_f32_e32 v141, 0xbfb8aa3b, v80
	v_rcp_f32_e32 v149, v130
	v_add_f32_e32 v130, 1.0, v146
	v_exp_f32_e32 v141, v141
	v_mul_f32_e32 v146, 0xbfb8aa3b, v76
	v_exp_f32_e32 v146, v146
	v_rcp_f32_e32 v151, v130
	v_add_f32_e32 v130, 1.0, v141
	v_mul_f32_e32 v141, 0xbfb8aa3b, v81
	v_rcp_f32_e32 v152, v130
	v_add_f32_e32 v130, 1.0, v146
	v_exp_f32_e32 v141, v141
	v_mul_f32_e32 v146, 0xbfb8aa3b, v77
	v_exp_f32_e32 v146, v146
	v_rcp_f32_e32 v154, v130
	v_add_f32_e32 v130, 1.0, v141
	v_rcp_f32_e32 v153, v130
	v_add_f32_e32 v130, 1.0, v146
	v_rcp_f32_e32 v155, v130

; __device__ __forceinline__ unsigned cvt_pk_bf16(float lo, float hi) { f32x2 v = {lo, hi}; bf16x2_t b = __builtin_convertvector(v, bf16x2_t); return __builtin_bit_cast(unsigned, b); }
; __device__ __forceinline__ float sigmoid_f(float x) { return __builtin_amdgcn_rcpf(1.0f + __expf(-x)); }
;     __device__ __forceinline__ void operator()(const AccT& acc, const pg8::Unit& u, int wr, int wc, int fr, int fq) const {
;     ...
;             const int kind = (pn - 16) >> 3;
;             bf16_t* dst = (bf16_t*)(ws + (kind == 0 ? WS_RV : kind == 1 ? WS_RG : kind == 2 ? WS_GA : WS_GR)); const int col0 = ((pn - 16) & 7) * 256 + wc * 32 + 8 * fq;
; #pragma unroll
;             for (int ai = 0; ai < 2; ++ai)
; #pragma unroll
;                 for (int m = 0; m < 4; ++m) { const int row = row0 + ai * 128 + m * 16;
; #pragma unroll
;                     for (int bj = 0; bj < 2; ++bj) { f32x4 v0 = acc[ai][bj][m][0], v1 = acc[ai][bj][m][1];
;                         if (kind == 1) {
; #pragma unroll
;                             for (int j = 0; j < 4; ++j) { v0[j] = v0[j] * sigmoid_f(v0[j]); v1[j] = v1[j] * sigmoid_f(v1[j]); } }
;                         else if (kind >= 2) {
; #pragma unroll
;                             for (int j = 0; j < 4; ++j) { v0[j] = sigmoid_f(v0[j]); v1[j] = sigmoid_f(v1[j]); } }
;                         u32x4 w; w.x = cvt_pk_bf16(v0[0], v0[1]); w.y = cvt_pk_bf16(v0[2], v0[3]); w.z = cvt_pk_bf16(v1[0], v1[1]); w.w = cvt_pk_bf16(v1[2], v1[3]);
;                         if (kind >= 1) __builtin_nontemporal_store(w, (u32x4*)(dst + (size_t)row * D + col0 + bj * 128));
;                         else *(u32x4*)(dst + (size_t)row * D + col0 + bj * 128) = w; } }
.LBB0_188:
	v_or_b32_e32 v146, 48, v142
	v_ashrrev_i32_e32 v147, 31, v146
	v_lshlrev_b64 v[146:147], 12, v[146:147]
	v_lshl_add_u64 v[146:147], v[144:145], 0, v[146:147]
	v_cvt_pk_bf16_f32 v148, v148, v149
	v_cvt_pk_bf16_f32 v149, v152, v153
	v_cvt_pk_bf16_f32 v150, v150, v151
	v_cvt_pk_bf16_f32 v151, v154, v155
	s_and_b64 vcc, exec, s[12:13]
	s_mov_b64 s[0:1], -1
	global_store_dwordx4 v[146:147], v[148:151], off sc1
	s_cbranch_vccnz .LBB0_192
	s_and_b64 vcc, exec, s[10:11]
	v_mov_b32_e32 v155, v69
	v_mov_b32_e32 v154, v68
	v_mov_b32_e32 v151, v67
	v_mov_b32_e32 v150, v66
	v_mov_b32_e32 v153, v73
	v_mov_b32_e32 v152, v72
	v_mov_b32_e32 v149, v71
	v_mov_b32_e32 v148, v70
	s_cbranch_vccnz .LBB0_191
	v_mul_f32_e32 v130, 0xbfb8aa3b, v70
	v_exp_f32_e32 v130, v130
	v_mul_f32_e32 v141, 0xbfb8aa3b, v66
	v_exp_f32_e32 v141, v141
	v_mul_f32_e32 v149, 0xbfb8aa3b, v67
	v_add_f32_e32 v130, 1.0, v130
	v_rcp_f32_e32 v148, v130
	v_mul_f32_e32 v130, 0xbfb8aa3b, v71
	v_exp_f32_e32 v130, v130
	v_exp_f32_e32 v151, v149
	v_add_f32_e32 v141, 1.0, v141
	v_rcp_f32_e32 v150, v141
	v_add_f32_e32 v130, 1.0, v130
	v_mul_f32_e32 v141, 0xbfb8aa3b, v72
	v_rcp_f32_e32 v149, v130
	v_add_f32_e32 v130, 1.0, v151
	v_exp_f32_e32 v141, v141
	v_mul_f32_e32 v151, 0xbfb8aa3b, v68
	v_exp_f32_e32 v153, v151
	v_rcp_f32_e32 v151, v130
	v_add_f32_e32 v130, 1.0, v141
	v_mul_f32_e32 v141, 0xbfb8aa3b, v73
	v_rcp_f32_e32 v152, v130
	v_add_f32_e32 v130, 1.0, v153
	v_exp_f32_e32 v141, v141
	v_mul_f32_e32 v153, 0xbfb8aa3b, v69
	v_exp_f32_e32 v155, v153
	v_rcp_f32_e32 v154, v130
	v_add_f32_e32 v130, 1.0, v141
	v_rcp_f32_e32 v153, v130
	v_add_f32_e32 v130, 1.0, v155
	v_rcp_f32_e32 v155, v130

; __device__ __forceinline__ unsigned cvt_pk_bf16(float lo, float hi) { f32x2 v = {lo, hi}; bf16x2_t b = __builtin_convertvector(v, bf16x2_t); return __builtin_bit_cast(unsigned, b); }
; __device__ __forceinline__ float sigmoid_f(float x) { return __builtin_amdgcn_rcpf(1.0f + __expf(-x)); }
;     __device__ __forceinline__ void operator()(const AccT& acc, const pg8::Unit& u, int wr, int wc, int fr, int fq) const {
;     ...
;             const int kind = (pn - 16) >> 3;
;             bf16_t* dst = (bf16_t*)(ws + (kind == 0 ? WS_RV : kind == 1 ? WS_RG : kind == 2 ? WS_GA : WS_GR)); const int col0 = ((pn - 16) & 7) * 256 + wc * 32 + 8 * fq;
; #pragma unroll
;             for (int ai = 0; ai < 2; ++ai)
; #pragma unroll
;                 for (int m = 0; m < 4; ++m) { const int row = row0 + ai * 128 + m * 16;
; #pragma unroll
;                     for (int bj = 0; bj < 2; ++bj) { f32x4 v0 = acc[ai][bj][m][0], v1 = acc[ai][bj][m][1];
;                         if (kind == 1) {
; #pragma unroll
;                             for (int j = 0; j < 4; ++j) { v0[j] = v0[j] * sigmoid_f(v0[j]); v1[j] = v1[j] * sigmoid_f(v1[j]); } }
;                         else if (kind >= 2) {
; #pragma unroll
;                             for (int j = 0; j < 4; ++j) { v0[j] = sigmoid_f(v0[j]); v1[j] = sigmoid_f(v1[j]); } }
;                         u32x4 w; w.x = cvt_pk_bf16(v0[0], v0[1]); w.y = cvt_pk_bf16(v0[2], v0[3]); w.z = cvt_pk_bf16(v1[0], v1[1]); w.w = cvt_pk_bf16(v1[2], v1[3]);
;                         if (kind >= 1) __builtin_nontemporal_store(w, (u32x4*)(dst + (size_t)row * D + col0 + bj * 128));
;                         else *(u32x4*)(dst + (size_t)row * D + col0 + bj * 128) = w; } }
.LBB0_194:
	v_cvt_pk_bf16_f32 v148, v148, v149
	v_cvt_pk_bf16_f32 v149, v152, v153
	v_cvt_pk_bf16_f32 v150, v150, v151
	v_cvt_pk_bf16_f32 v151, v154, v155
	s_and_b64 vcc, exec, s[12:13]
	s_mov_b64 s[0:1], -1
	global_store_dwordx4 v[146:147], v[148:151], off offset:256 sc1
	s_cbranch_vccnz .LBB0_198
	s_and_b64 vcc, exec, s[10:11]
	v_mov_b32_e32 v155, v61
	v_mov_b32_e32 v154, v60
	v_mov_b32_e32 v151, v59
	v_mov_b32_e32 v150, v58
	v_mov_b32_e32 v153, v65
	v_mov_b32_e32 v152, v64
	v_mov_b32_e32 v149, v63
	v_mov_b32_e32 v148, v62
	s_cbranch_vccnz .LBB0_197
	v_mul_f32_e32 v130, 0xbfb8aa3b, v62
	v_exp_f32_e32 v130, v130
	v_mul_f32_e32 v141, 0xbfb8aa3b, v58
	v_exp_f32_e32 v141, v141
	v_mul_f32_e32 v146, 0xbfb8aa3b, v59
	v_add_f32_e32 v130, 1.0, v130
	v_rcp_f32_e32 v148, v130
	v_mul_f32_e32 v130, 0xbfb8aa3b, v63
	v_exp_f32_e32 v130, v130
	v_exp_f32_e32 v146, v146
	v_add_f32_e32 v141, 1.0, v141
	v_rcp_f32_e32 v150, v141
	v_add_f32_e32 v130, 1.0, v130
	v_mul_f32_e32 v141, 0xbfb8aa3b, v64
	v_rcp_f32_e32 v149, v130
	v_add_f32_e32 v130, 1.0, v146
	v_exp_f32_e32 v141, v141
	v_mul_f32_e32 v146, 0xbfb8aa3b, v60
	v_exp_f32_e32 v146, v146
	v_rcp_f32_e32 v151, v130
	v_add_f32_e32 v130, 1.0, v141
	v_mul_f32_e32 v141, 0xbfb8aa3b, v65
	v_rcp_f32_e32 v152, v130
	v_add_f32_e32 v130, 1.0, v146
	v_exp_f32_e32 v141, v141
	v_mul_f32_e32 v146, 0xbfb8aa3b, v61
	v_exp_f32_e32 v146, v146
	v_rcp_f32_e32 v154, v130
	v_add_f32_e32 v130, 1.0, v141
	v_rcp_f32_e32 v153, v130
	v_add_f32_e32 v130, 1.0, v146
	v_rcp_f32_e32 v155, v130

; __device__ __forceinline__ unsigned cvt_pk_bf16(float lo, float hi) { f32x2 v = {lo, hi}; bf16x2_t b = __builtin_convertvector(v, bf16x2_t); return __builtin_bit_cast(unsigned, b); }
; __device__ __forceinline__ float sigmoid_f(float x) { return __builtin_amdgcn_rcpf(1.0f + __expf(-x)); }
;     __device__ __forceinline__ void operator()(const AccT& acc, const pg8::Unit& u, int wr, int wc, int fr, int fq) const {
;     ...
;             const int kind = (pn - 16) >> 3;
;             bf16_t* dst = (bf16_t*)(ws + (kind == 0 ? WS_RV : kind == 1 ? WS_RG : kind == 2 ? WS_GA : WS_GR)); const int col0 = ((pn - 16) & 7) * 256 + wc * 32 + 8 * fq;
; #pragma unroll
;             for (int ai = 0; ai < 2; ++ai)
; #pragma unroll
;                 for (int m = 0; m < 4; ++m) { const int row = row0 + ai * 128 + m * 16;
; #pragma unroll
;                     for (int bj = 0; bj < 2; ++bj) { f32x4 v0 = acc[ai][bj][m][0], v1 = acc[ai][bj][m][1];
;                         if (kind == 1) {
; #pragma unroll
;                             for (int j = 0; j < 4; ++j) { v0[j] = v0[j] * sigmoid_f(v0[j]); v1[j] = v1[j] * sigmoid_f(v1[j]); } }
;                         else if (kind >= 2) {
; #pragma unroll
;                             for (int j = 0; j < 4; ++j) { v0[j] = sigmoid_f(v0[j]); v1[j] = sigmoid_f(v1[j]); } }
;                         u32x4 w; w.x = cvt_pk_bf16(v0[0], v0[1]); w.y = cvt_pk_bf16(v0[2], v0[3]); w.z = cvt_pk_bf16(v1[0], v1[1]); w.w = cvt_pk_bf16(v1[2], v1[3]);
;                         if (kind >= 1) __builtin_nontemporal_store(w, (u32x4*)(dst + (size_t)row * D + col0 + bj * 128));
;                         else *(u32x4*)(dst + (size_t)row * D + col0 + bj * 128) = w; } }
.LBB0_200:
	v_lshlrev_b64 v[146:147], 12, v[142:143]
	v_lshl_add_u64 v[146:147], v[144:145], 0, v[146:147]
	v_cvt_pk_bf16_f32 v148, v148, v149
	v_cvt_pk_bf16_f32 v149, v152, v153
	v_add_co_u32_e32 v152, vcc, 0x80000, v146
	v_cvt_pk_bf16_f32 v150, v150, v151
	s_nop 0
	v_addc_co_u32_e32 v153, vcc, 0, v147, vcc
	v_cvt_pk_bf16_f32 v151, v154, v155
	s_and_b64 vcc, exec, s[12:13]
	s_mov_b64 s[0:1], -1
	global_store_dwordx4 v[152:153], v[148:151], off sc1
	s_cbranch_vccnz .LBB0_204
	s_and_b64 vcc, exec, s[10:11]
	v_mov_b32_e32 v155, v53
	v_mov_b32_e32 v154, v52
	v_mov_b32_e32 v151, v51
	v_mov_b32_e32 v150, v50
	v_mov_b32_e32 v153, v57
	v_mov_b32_e32 v152, v56
	v_mov_b32_e32 v149, v55
	v_mov_b32_e32 v148, v54
	s_cbranch_vccnz .LBB0_203
	v_mul_f32_e32 v130, 0xbfb8aa3b, v54
	v_exp_f32_e32 v130, v130
	v_mul_f32_e32 v141, 0xbfb8aa3b, v50
	v_exp_f32_e32 v141, v141
	v_mul_f32_e32 v149, 0xbfb8aa3b, v51
	v_add_f32_e32 v130, 1.0, v130
	v_rcp_f32_e32 v148, v130
	v_mul_f32_e32 v130, 0xbfb8aa3b, v55
	v_exp_f32_e32 v130, v130
	v_exp_f32_e32 v151, v149
	v_add_f32_e32 v141, 1.0, v141
	v_rcp_f32_e32 v150, v141
	v_add_f32_e32 v130, 1.0, v130
	v_mul_f32_e32 v141, 0xbfb8aa3b, v56
	v_rcp_f32_e32 v149, v130
	v_add_f32_e32 v130, 1.0, v151
	v_exp_f32_e32 v141, v141
	v_mul_f32_e32 v151, 0xbfb8aa3b, v52
	v_exp_f32_e32 v153, v151
	v_rcp_f32_e32 v151, v130
	v_add_f32_e32 v130, 1.0, v141
	v_mul_f32_e32 v141, 0xbfb8aa3b, v57
	v_rcp_f32_e32 v152, v130
	v_add_f32_e32 v130, 1.0, v153
	v_exp_f32_e32 v141, v141
	v_mul_f32_e32 v153, 0xbfb8aa3b, v53
	v_exp_f32_e32 v155, v153
	v_rcp_f32_e32 v154, v130
	v_add_f32_e32 v130, 1.0, v141
	v_rcp_f32_e32 v153, v130
	v_add_f32_e32 v130, 1.0, v155
	v_rcp_f32_e32 v155, v130

; __device__ __forceinline__ unsigned cvt_pk_bf16(float lo, float hi) { f32x2 v = {lo, hi}; bf16x2_t b = __builtin_convertvector(v, bf16x2_t); return __builtin_bit_cast(unsigned, b); }
; __device__ __forceinline__ float sigmoid_f(float x) { return __builtin_amdgcn_rcpf(1.0f + __expf(-x)); }
;     __device__ __forceinline__ void operator()(const AccT& acc, const pg8::Unit& u, int wr, int wc, int fr, int fq) const {
;     ...
;             const int kind = (pn - 16) >> 3;
;             bf16_t* dst = (bf16_t*)(ws + (kind == 0 ? WS_RV : kind == 1 ? WS_RG : kind == 2 ? WS_GA : WS_GR)); const int col0 = ((pn - 16) & 7) * 256 + wc * 32 + 8 * fq;
; #pragma unroll
;             for (int ai = 0; ai < 2; ++ai)
; #pragma unroll
;                 for (int m = 0; m < 4; ++m) { const int row = row0 + ai * 128 + m * 16;
; #pragma unroll
;                     for (int bj = 0; bj < 2; ++bj) { f32x4 v0 = acc[ai][bj][m][0], v1 = acc[ai][bj][m][1];
;                         if (kind == 1) {
; #pragma unroll
;                             for (int j = 0; j < 4; ++j) { v0[j] = v0[j] * sigmoid_f(v0[j]); v1[j] = v1[j] * sigmoid_f(v1[j]); } }
;                         else if (kind >= 2) {
; #pragma unroll
;                             for (int j = 0; j < 4; ++j) { v0[j] = sigmoid_f(v0[j]); v1[j] = sigmoid_f(v1[j]); } }
;                         u32x4 w; w.x = cvt_pk_bf16(v0[0], v0[1]); w.y = cvt_pk_bf16(v0[2], v0[3]); w.z = cvt_pk_bf16(v1[0], v1[1]); w.w = cvt_pk_bf16(v1[2], v1[3]);
;                         if (kind >= 1) __builtin_nontemporal_store(w, (u32x4*)(dst + (size_t)row * D + col0 + bj * 128));
;                         else *(u32x4*)(dst + (size_t)row * D + col0 + bj * 128) = w; } }
.LBB0_206:
	v_lshl_add_u64 v[170:171], v[146:147], 0, s[16:17]
	v_cvt_pk_bf16_f32 v146, v148, v149
	v_cvt_pk_bf16_f32 v147, v152, v153
	v_cvt_pk_bf16_f32 v148, v150, v151
	v_cvt_pk_bf16_f32 v149, v154, v155
	s_and_b64 vcc, exec, s[12:13]
	s_mov_b64 s[0:1], -1
	global_store_dwordx4 v[170:171], v[146:149], off offset:256 sc1
	s_cbranch_vccnz .LBB0_210
	s_and_b64 vcc, exec, s[10:11]
	v_mov_b32_e32 v155, v45
	v_mov_b32_e32 v154, v44
	v_mov_b32_e32 v151, v43
	v_mov_b32_e32 v150, v42
	v_mov_b32_e32 v153, v49
	v_mov_b32_e32 v152, v48
	v_mov_b32_e32 v149, v47
	v_mov_b32_e32 v148, v46
	s_cbranch_vccnz .LBB0_209
	v_mul_f32_e32 v130, 0xbfb8aa3b, v46
	v_exp_f32_e32 v130, v130
	v_mul_f32_e32 v141, 0xbfb8aa3b, v42
	v_exp_f32_e32 v141, v141
	v_mul_f32_e32 v146, 0xbfb8aa3b, v43
	v_add_f32_e32 v130, 1.0, v130
	v_rcp_f32_e32 v148, v130
	v_mul_f32_e32 v130, 0xbfb8aa3b, v47
	v_exp_f32_e32 v130, v130
	v_exp_f32_e32 v146, v146
	v_add_f32_e32 v141, 1.0, v141
	v_rcp_f32_e32 v150, v141
	v_add_f32_e32 v130, 1.0, v130
	v_mul_f32_e32 v141, 0xbfb8aa3b, v48
	v_rcp_f32_e32 v149, v130
	v_add_f32_e32 v130, 1.0, v146
	v_exp_f32_e32 v141, v141
	v_mul_f32_e32 v146, 0xbfb8aa3b, v44
	v_exp_f32_e32 v146, v146
	v_rcp_f32_e32 v151, v130
	v_add_f32_e32 v130, 1.0, v141
	v_mul_f32_e32 v141, 0xbfb8aa3b, v49
	v_rcp_f32_e32 v152, v130
	v_add_f32_e32 v130, 1.0, v146
	v_exp_f32_e32 v141, v141
	v_mul_f32_e32 v146, 0xbfb8aa3b, v45
	v_exp_f32_e32 v146, v146
	v_rcp_f32_e32 v154, v130
	v_add_f32_e32 v130, 1.0, v141
	v_rcp_f32_e32 v153, v130
	v_add_f32_e32 v130, 1.0, v146
	v_rcp_f32_e32 v155, v130

; __device__ __forceinline__ unsigned cvt_pk_bf16(float lo, float hi) { f32x2 v = {lo, hi}; bf16x2_t b = __builtin_convertvector(v, bf16x2_t); return __builtin_bit_cast(unsigned, b); }
; __device__ __forceinline__ float sigmoid_f(float x) { return __builtin_amdgcn_rcpf(1.0f + __expf(-x)); }
;     __device__ __forceinline__ void operator()(const AccT& acc, const pg8::Unit& u, int wr, int wc, int fr, int fq) const {
;     ...
;             const int kind = (pn - 16) >> 3;
;             bf16_t* dst = (bf16_t*)(ws + (kind == 0 ? WS_RV : kind == 1 ? WS_RG : kind == 2 ? WS_GA : WS_GR)); const int col0 = ((pn - 16) & 7) * 256 + wc * 32 + 8 * fq;
; #pragma unroll
;             for (int ai = 0; ai < 2; ++ai)
; #pragma unroll
;                 for (int m = 0; m < 4; ++m) { const int row = row0 + ai * 128 + m * 16;
; #pragma unroll
;                     for (int bj = 0; bj < 2; ++bj) { f32x4 v0 = acc[ai][bj][m][0], v1 = acc[ai][bj][m][1];
;                         if (kind == 1) {
; #pragma unroll
;                             for (int j = 0; j < 4; ++j) { v0[j] = v0[j] * sigmoid_f(v0[j]); v1[j] = v1[j] * sigmoid_f(v1[j]); } }
;                         else if (kind >= 2) {
; #pragma unroll
;                             for (int j = 0; j < 4; ++j) { v0[j] = sigmoid_f(v0[j]); v1[j] = sigmoid_f(v1[j]); } }
;                         u32x4 w; w.x = cvt_pk_bf16(v0[0], v0[1]); w.y = cvt_pk_bf16(v0[2], v0[3]); w.z = cvt_pk_bf16(v1[0], v1[1]); w.w = cvt_pk_bf16(v1[2], v1[3]);
;                         if (kind >= 1) __builtin_nontemporal_store(w, (u32x4*)(dst + (size_t)row * D + col0 + bj * 128));
;                         else *(u32x4*)(dst + (size_t)row * D + col0 + bj * 128) = w; } }
.LBB0_212:
	v_lshlrev_b64 v[146:147], 12, v[142:143]
	v_lshl_add_u64 v[146:147], v[144:145], 0, v[146:147]
	v_cvt_pk_bf16_f32 v148, v148, v149
	v_cvt_pk_bf16_f32 v149, v152, v153
	v_add_co_u32_e32 v152, vcc, 0x90000, v146
	v_cvt_pk_bf16_f32 v150, v150, v151
	s_nop 0
	v_addc_co_u32_e32 v153, vcc, 0, v147, vcc
	v_cvt_pk_bf16_f32 v151, v154, v155
	s_and_b64 vcc, exec, s[12:13]
	s_mov_b64 s[0:1], -1
	global_store_dwordx4 v[152:153], v[148:151], off sc1
	s_cbranch_vccnz .LBB0_216
	s_and_b64 vcc, exec, s[10:11]
	v_mov_b32_e32 v155, v37
	v_mov_b32_e32 v154, v36
	v_mov_b32_e32 v151, v35
	v_mov_b32_e32 v150, v34
	v_mov_b32_e32 v153, v41
	v_mov_b32_e32 v152, v40
	v_mov_b32_e32 v149, v39
	v_mov_b32_e32 v148, v38
	s_cbranch_vccnz .LBB0_215
	v_mul_f32_e32 v130, 0xbfb8aa3b, v38
	v_exp_f32_e32 v130, v130
	v_mul_f32_e32 v141, 0xbfb8aa3b, v34
	v_exp_f32_e32 v141, v141
	v_mul_f32_e32 v149, 0xbfb8aa3b, v35
	v_add_f32_e32 v130, 1.0, v130
	v_rcp_f32_e32 v148, v130
	v_mul_f32_e32 v130, 0xbfb8aa3b, v39
	v_exp_f32_e32 v130, v130
	v_exp_f32_e32 v151, v149
	v_add_f32_e32 v141, 1.0, v141
	v_rcp_f32_e32 v150, v141
	v_add_f32_e32 v130, 1.0, v130
	v_mul_f32_e32 v141, 0xbfb8aa3b, v40
	v_rcp_f32_e32 v149, v130
	v_add_f32_e32 v130, 1.0, v151
	v_exp_f32_e32 v141, v141
	v_mul_f32_e32 v151, 0xbfb8aa3b, v36
	v_exp_f32_e32 v153, v151
	v_rcp_f32_e32 v151, v130
	v_add_f32_e32 v130, 1.0, v141
	v_mul_f32_e32 v141, 0xbfb8aa3b, v41
	v_rcp_f32_e32 v152, v130
	v_add_f32_e32 v130, 1.0, v153
	v_exp_f32_e32 v141, v141
	v_mul_f32_e32 v153, 0xbfb8aa3b, v37
	v_exp_f32_e32 v155, v153
	v_rcp_f32_e32 v154, v130
	v_add_f32_e32 v130, 1.0, v141
	v_rcp_f32_e32 v153, v130
	v_add_f32_e32 v130, 1.0, v155
	v_rcp_f32_e32 v155, v130

; __device__ __forceinline__ unsigned cvt_pk_bf16(float lo, float hi) { f32x2 v = {lo, hi}; bf16x2_t b = __builtin_convertvector(v, bf16x2_t); return __builtin_bit_cast(unsigned, b); }
; __device__ __forceinline__ float sigmoid_f(float x) { return __builtin_amdgcn_rcpf(1.0f + __expf(-x)); }
;     __device__ __forceinline__ void operator()(const AccT& acc, const pg8::Unit& u, int wr, int wc, int fr, int fq) const {
;     ...
;             const int kind = (pn - 16) >> 3;
;             bf16_t* dst = (bf16_t*)(ws + (kind == 0 ? WS_RV : kind == 1 ? WS_RG : kind == 2 ? WS_GA : WS_GR)); const int col0 = ((pn - 16) & 7) * 256 + wc * 32 + 8 * fq;
; #pragma unroll
;             for (int ai = 0; ai < 2; ++ai)
; #pragma unroll
;                 for (int m = 0; m < 4; ++m) { const int row = row0 + ai * 128 + m * 16;
; #pragma unroll
;                     for (int bj = 0; bj < 2; ++bj) { f32x4 v0 = acc[ai][bj][m][0], v1 = acc[ai][bj][m][1];
;                         if (kind == 1) {
; #pragma unroll
;                             for (int j = 0; j < 4; ++j) { v0[j] = v0[j] * sigmoid_f(v0[j]); v1[j] = v1[j] * sigmoid_f(v1[j]); } }
;                         else if (kind >= 2) {
; #pragma unroll
;                             for (int j = 0; j < 4; ++j) { v0[j] = sigmoid_f(v0[j]); v1[j] = sigmoid_f(v1[j]); } }
;                         u32x4 w; w.x = cvt_pk_bf16(v0[0], v0[1]); w.y = cvt_pk_bf16(v0[2], v0[3]); w.z = cvt_pk_bf16(v1[0], v1[1]); w.w = cvt_pk_bf16(v1[2], v1[3]);
;                         if (kind >= 1) __builtin_nontemporal_store(w, (u32x4*)(dst + (size_t)row * D + col0 + bj * 128));
;                         else *(u32x4*)(dst + (size_t)row * D + col0 + bj * 128) = w; } }
.LBB0_218:
	v_lshl_add_u64 v[170:171], v[146:147], 0, s[22:23]
	v_cvt_pk_bf16_f32 v146, v148, v149
	v_cvt_pk_bf16_f32 v147, v152, v153
	v_cvt_pk_bf16_f32 v148, v150, v151
	v_cvt_pk_bf16_f32 v149, v154, v155
	s_and_b64 vcc, exec, s[12:13]
	s_mov_b64 s[0:1], -1
	global_store_dwordx4 v[170:171], v[146:149], off offset:256 sc1
	s_cbranch_vccnz .LBB0_222
	s_and_b64 vcc, exec, s[10:11]
	v_mov_b32_e32 v155, v29
	v_mov_b32_e32 v154, v28
	v_mov_b32_e32 v151, v27
	v_mov_b32_e32 v150, v26
	v_mov_b32_e32 v153, v33
	v_mov_b32_e32 v152, v32
	v_mov_b32_e32 v149, v31
	v_mov_b32_e32 v148, v30
	s_cbranch_vccnz .LBB0_221
	v_mul_f32_e32 v130, 0xbfb8aa3b, v30
	v_exp_f32_e32 v130, v130
	v_mul_f32_e32 v141, 0xbfb8aa3b, v26
	v_exp_f32_e32 v141, v141
	v_mul_f32_e32 v146, 0xbfb8aa3b, v27
	v_add_f32_e32 v130, 1.0, v130
	v_rcp_f32_e32 v148, v130
	v_mul_f32_e32 v130, 0xbfb8aa3b, v31
	v_exp_f32_e32 v130, v130
	v_exp_f32_e32 v146, v146
	v_add_f32_e32 v141, 1.0, v141
	v_rcp_f32_e32 v150, v141
	v_add_f32_e32 v130, 1.0, v130
	v_mul_f32_e32 v141, 0xbfb8aa3b, v32
	v_rcp_f32_e32 v149, v130
	v_add_f32_e32 v130, 1.0, v146
	v_exp_f32_e32 v141, v141
	v_mul_f32_e32 v146, 0xbfb8aa3b, v28
	v_exp_f32_e32 v146, v146
	v_rcp_f32_e32 v151, v130
	v_add_f32_e32 v130, 1.0, v141
	v_mul_f32_e32 v141, 0xbfb8aa3b, v33
	v_rcp_f32_e32 v152, v130
	v_add_f32_e32 v130, 1.0, v146
	v_exp_f32_e32 v141, v141
	v_mul_f32_e32 v146, 0xbfb8aa3b, v29
	v_exp_f32_e32 v146, v146
	v_rcp_f32_e32 v154, v130
	v_add_f32_e32 v130, 1.0, v141
	v_rcp_f32_e32 v153, v130
	v_add_f32_e32 v130, 1.0, v146
	v_rcp_f32_e32 v155, v130

; __device__ __forceinline__ unsigned cvt_pk_bf16(float lo, float hi) { f32x2 v = {lo, hi}; bf16x2_t b = __builtin_convertvector(v, bf16x2_t); return __builtin_bit_cast(unsigned, b); }
; __device__ __forceinline__ float sigmoid_f(float x) { return __builtin_amdgcn_rcpf(1.0f + __expf(-x)); }
;     __device__ __forceinline__ void operator()(const AccT& acc, const pg8::Unit& u, int wr, int wc, int fr, int fq) const {
;     ...
;             const int kind = (pn - 16) >> 3;
;             bf16_t* dst = (bf16_t*)(ws + (kind == 0 ? WS_RV : kind == 1 ? WS_RG : kind == 2 ? WS_GA : WS_GR)); const int col0 = ((pn - 16) & 7) * 256 + wc * 32 + 8 * fq;
; #pragma unroll
;             for (int ai = 0; ai < 2; ++ai)
; #pragma unroll
;                 for (int m = 0; m < 4; ++m) { const int row = row0 + ai * 128 + m * 16;
; #pragma unroll
;                     for (int bj = 0; bj < 2; ++bj) { f32x4 v0 = acc[ai][bj][m][0], v1 = acc[ai][bj][m][1];
;                         if (kind == 1) {
; #pragma unroll
;                             for (int j = 0; j < 4; ++j) { v0[j] = v0[j] * sigmoid_f(v0[j]); v1[j] = v1[j] * sigmoid_f(v1[j]); } }
;                         else if (kind >= 2) {
; #pragma unroll
;                             for (int j = 0; j < 4; ++j) { v0[j] = sigmoid_f(v0[j]); v1[j] = sigmoid_f(v1[j]); } }
;                         u32x4 w; w.x = cvt_pk_bf16(v0[0], v0[1]); w.y = cvt_pk_bf16(v0[2], v0[3]); w.z = cvt_pk_bf16(v1[0], v1[1]); w.w = cvt_pk_bf16(v1[2], v1[3]);
;                         if (kind >= 1) __builtin_nontemporal_store(w, (u32x4*)(dst + (size_t)row * D + col0 + bj * 128));
;                         else *(u32x4*)(dst + (size_t)row * D + col0 + bj * 128) = w; } }
.LBB0_224:
	v_lshlrev_b64 v[146:147], 12, v[142:143]
	v_lshl_add_u64 v[146:147], v[144:145], 0, v[146:147]
	v_cvt_pk_bf16_f32 v148, v148, v149
	v_cvt_pk_bf16_f32 v149, v152, v153
	v_add_co_u32_e32 v152, vcc, 0xa0000, v146
	v_cvt_pk_bf16_f32 v150, v150, v151
	s_nop 0
	v_addc_co_u32_e32 v153, vcc, 0, v147, vcc
	v_cvt_pk_bf16_f32 v151, v154, v155
	s_and_b64 vcc, exec, s[12:13]
	s_mov_b64 s[0:1], -1
	global_store_dwordx4 v[152:153], v[148:151], off sc1
	s_cbranch_vccnz .LBB0_228
	s_and_b64 vcc, exec, s[10:11]
	v_mov_b32_e32 v155, v21
	v_mov_b32_e32 v154, v20
	v_mov_b32_e32 v151, v19
	v_mov_b32_e32 v150, v18
	v_mov_b32_e32 v153, v25
	v_mov_b32_e32 v152, v24
	v_mov_b32_e32 v149, v23
	v_mov_b32_e32 v148, v22
	s_cbranch_vccnz .LBB0_227
	v_mul_f32_e32 v130, 0xbfb8aa3b, v22
	v_exp_f32_e32 v130, v130
	v_mul_f32_e32 v141, 0xbfb8aa3b, v18
	v_exp_f32_e32 v141, v141
	v_mul_f32_e32 v149, 0xbfb8aa3b, v19
	v_add_f32_e32 v130, 1.0, v130
	v_rcp_f32_e32 v148, v130
	v_mul_f32_e32 v130, 0xbfb8aa3b, v23
	v_exp_f32_e32 v130, v130
	v_exp_f32_e32 v151, v149
	v_add_f32_e32 v141, 1.0, v141
	v_rcp_f32_e32 v150, v141
	v_add_f32_e32 v130, 1.0, v130
	v_mul_f32_e32 v141, 0xbfb8aa3b, v24
	v_rcp_f32_e32 v149, v130
	v_add_f32_e32 v130, 1.0, v151
	v_exp_f32_e32 v141, v141
	v_mul_f32_e32 v151, 0xbfb8aa3b, v20
	v_exp_f32_e32 v153, v151
	v_rcp_f32_e32 v151, v130
	v_add_f32_e32 v130, 1.0, v141
	v_mul_f32_e32 v141, 0xbfb8aa3b, v25
	v_rcp_f32_e32 v152, v130
	v_add_f32_e32 v130, 1.0, v153
	v_exp_f32_e32 v141, v141
	v_mul_f32_e32 v153, 0xbfb8aa3b, v21
	v_exp_f32_e32 v155, v153
	v_rcp_f32_e32 v154, v130
	v_add_f32_e32 v130, 1.0, v141
	v_rcp_f32_e32 v153, v130
	v_add_f32_e32 v130, 1.0, v155
	v_rcp_f32_e32 v155, v130

; __device__ __forceinline__ unsigned cvt_pk_bf16(float lo, float hi) { f32x2 v = {lo, hi}; bf16x2_t b = __builtin_convertvector(v, bf16x2_t); return __builtin_bit_cast(unsigned, b); }
; __device__ __forceinline__ float sigmoid_f(float x) { return __builtin_amdgcn_rcpf(1.0f + __expf(-x)); }
;     __device__ __forceinline__ void operator()(const AccT& acc, const pg8::Unit& u, int wr, int wc, int fr, int fq) const {
;     ...
;             const int kind = (pn - 16) >> 3;
;             bf16_t* dst = (bf16_t*)(ws + (kind == 0 ? WS_RV : kind == 1 ? WS_RG : kind == 2 ? WS_GA : WS_GR)); const int col0 = ((pn - 16) & 7) * 256 + wc * 32 + 8 * fq;
; #pragma unroll
;             for (int ai = 0; ai < 2; ++ai)
; #pragma unroll
;                 for (int m = 0; m < 4; ++m) { const int row = row0 + ai * 128 + m * 16;
; #pragma unroll
;                     for (int bj = 0; bj < 2; ++bj) { f32x4 v0 = acc[ai][bj][m][0], v1 = acc[ai][bj][m][1];
;                         if (kind == 1) {
; #pragma unroll
;                             for (int j = 0; j < 4; ++j) { v0[j] = v0[j] * sigmoid_f(v0[j]); v1[j] = v1[j] * sigmoid_f(v1[j]); } }
;                         else if (kind >= 2) {
; #pragma unroll
;                             for (int j = 0; j < 4; ++j) { v0[j] = sigmoid_f(v0[j]); v1[j] = sigmoid_f(v1[j]); } }
;                         u32x4 w; w.x = cvt_pk_bf16(v0[0], v0[1]); w.y = cvt_pk_bf16(v0[2], v0[3]); w.z = cvt_pk_bf16(v1[0], v1[1]); w.w = cvt_pk_bf16(v1[2], v1[3]);
;                         if (kind >= 1) __builtin_nontemporal_store(w, (u32x4*)(dst + (size_t)row * D + col0 + bj * 128));
;                         else *(u32x4*)(dst + (size_t)row * D + col0 + bj * 128) = w; } }
.LBB0_230:
	v_lshl_add_u64 v[170:171], v[146:147], 0, s[24:25]
	v_cvt_pk_bf16_f32 v146, v148, v149
	v_cvt_pk_bf16_f32 v147, v152, v153
	v_cvt_pk_bf16_f32 v148, v150, v151
	v_cvt_pk_bf16_f32 v149, v154, v155
	s_and_b64 vcc, exec, s[12:13]
	s_mov_b64 s[0:1], -1
	global_store_dwordx4 v[170:171], v[146:149], off offset:256 sc1
	s_cbranch_vccnz .LBB0_234
	s_and_b64 vcc, exec, s[10:11]
	v_mov_b32_e32 v153, v13
	v_mov_b32_e32 v152, v12
	v_mov_b32_e32 v149, v11
	v_mov_b32_e32 v148, v10
	v_mov_b32_e32 v151, v17
	v_mov_b32_e32 v150, v16
	v_mov_b32_e32 v147, v15
	v_mov_b32_e32 v146, v14
	s_cbranch_vccnz .LBB0_233
	v_mul_f32_e32 v130, 0xbfb8aa3b, v14
	v_exp_f32_e32 v130, v130
	v_mul_f32_e32 v141, 0xbfb8aa3b, v10
	v_exp_f32_e32 v141, v141
	v_mul_f32_e32 v147, 0xbfb8aa3b, v11
	v_add_f32_e32 v130, 1.0, v130
	v_rcp_f32_e32 v146, v130
	v_mul_f32_e32 v130, 0xbfb8aa3b, v15
	v_exp_f32_e32 v130, v130
	v_exp_f32_e32 v149, v147
	v_add_f32_e32 v141, 1.0, v141
	v_rcp_f32_e32 v148, v141
	v_add_f32_e32 v130, 1.0, v130
	v_mul_f32_e32 v141, 0xbfb8aa3b, v16
	v_rcp_f32_e32 v147, v130
	v_add_f32_e32 v130, 1.0, v149
	v_exp_f32_e32 v141, v141
	v_mul_f32_e32 v149, 0xbfb8aa3b, v12
	v_exp_f32_e32 v151, v149
	v_rcp_f32_e32 v149, v130
	v_add_f32_e32 v130, 1.0, v141
	v_mul_f32_e32 v141, 0xbfb8aa3b, v17
	v_rcp_f32_e32 v150, v130
	v_add_f32_e32 v130, 1.0, v151
	v_exp_f32_e32 v141, v141
	v_mul_f32_e32 v151, 0xbfb8aa3b, v13
	v_exp_f32_e32 v153, v151
	v_rcp_f32_e32 v152, v130
	v_add_f32_e32 v130, 1.0, v141
	v_rcp_f32_e32 v151, v130
	v_add_f32_e32 v130, 1.0, v153
	v_rcp_f32_e32 v153, v130

; __device__ __forceinline__ unsigned cvt_pk_bf16(float lo, float hi) { f32x2 v = {lo, hi}; bf16x2_t b = __builtin_convertvector(v, bf16x2_t); return __builtin_bit_cast(unsigned, b); }
; __device__ __forceinline__ float sigmoid_f(float x) { return __builtin_amdgcn_rcpf(1.0f + __expf(-x)); }
;     __device__ __forceinline__ void operator()(const AccT& acc, const pg8::Unit& u, int wr, int wc, int fr, int fq) const {
;     ...
;             const int kind = (pn - 16) >> 3;
;             bf16_t* dst = (bf16_t*)(ws + (kind == 0 ? WS_RV : kind == 1 ? WS_RG : kind == 2 ? WS_GA : WS_GR)); const int col0 = ((pn - 16) & 7) * 256 + wc * 32 + 8 * fq;
; #pragma unroll
;             for (int ai = 0; ai < 2; ++ai)
; #pragma unroll
;                 for (int m = 0; m < 4; ++m) { const int row = row0 + ai * 128 + m * 16;
; #pragma unroll
;                     for (int bj = 0; bj < 2; ++bj) { f32x4 v0 = acc[ai][bj][m][0], v1 = acc[ai][bj][m][1];
;                         if (kind == 1) {
; #pragma unroll
;                             for (int j = 0; j < 4; ++j) { v0[j] = v0[j] * sigmoid_f(v0[j]); v1[j] = v1[j] * sigmoid_f(v1[j]); } }
;                         else if (kind >= 2) {
; #pragma unroll
;                             for (int j = 0; j < 4; ++j) { v0[j] = sigmoid_f(v0[j]); v1[j] = sigmoid_f(v1[j]); } }
;                         u32x4 w; w.x = cvt_pk_bf16(v0[0], v0[1]); w.y = cvt_pk_bf16(v0[2], v0[3]); w.z = cvt_pk_bf16(v1[0], v1[1]); w.w = cvt_pk_bf16(v1[2], v1[3]);
;                         if (kind >= 1) __builtin_nontemporal_store(w, (u32x4*)(dst + (size_t)row * D + col0 + bj * 128));
;                         else *(u32x4*)(dst + (size_t)row * D + col0 + bj * 128) = w; } }
.LBB0_236:
	v_lshlrev_b64 v[154:155], 12, v[142:143]
	v_lshl_add_u64 v[144:145], v[144:145], 0, v[154:155]
	v_cvt_pk_bf16_f32 v146, v146, v147
	v_cvt_pk_bf16_f32 v147, v150, v151
	v_add_co_u32_e32 v150, vcc, 0xb0000, v144
	v_cvt_pk_bf16_f32 v148, v148, v149
	s_nop 0
	v_addc_co_u32_e32 v151, vcc, 0, v145, vcc
	v_cvt_pk_bf16_f32 v149, v152, v153
	s_and_b64 vcc, exec, s[12:13]
	s_mov_b64 s[0:1], -1
	global_store_dwordx4 v[150:151], v[146:149], off sc1
	s_cbranch_vccnz .LBB0_240
	s_and_b64 vcc, exec, s[10:11]
	v_mov_b32_e32 v153, v5
	v_mov_b32_e32 v152, v4
	v_mov_b32_e32 v149, v3
	v_mov_b32_e32 v148, v2
	v_mov_b32_e32 v151, v9
	v_mov_b32_e32 v150, v8
	v_mov_b32_e32 v147, v7
	v_mov_b32_e32 v146, v6
	s_cbranch_vccnz .LBB0_239
	v_mul_f32_e32 v130, 0xbfb8aa3b, v6
	v_exp_f32_e32 v130, v130
	v_mul_f32_e32 v141, 0xbfb8aa3b, v2
	v_exp_f32_e32 v141, v141
	v_mul_f32_e32 v143, 0xbfb8aa3b, v3
	v_add_f32_e32 v130, 1.0, v130
	v_rcp_f32_e32 v146, v130
	v_mul_f32_e32 v130, 0xbfb8aa3b, v7
	v_exp_f32_e32 v130, v130
	v_exp_f32_e32 v143, v143
	v_add_f32_e32 v141, 1.0, v141
	v_rcp_f32_e32 v148, v141
	v_add_f32_e32 v130, 1.0, v130
	v_mul_f32_e32 v141, 0xbfb8aa3b, v8
	v_rcp_f32_e32 v147, v130
	v_add_f32_e32 v130, 1.0, v143
	v_exp_f32_e32 v141, v141
	v_mul_f32_e32 v143, 0xbfb8aa3b, v4
	v_exp_f32_e32 v143, v143
	v_rcp_f32_e32 v149, v130
	v_add_f32_e32 v130, 1.0, v141
	v_mul_f32_e32 v141, 0xbfb8aa3b, v9
	v_rcp_f32_e32 v150, v130
	v_add_f32_e32 v130, 1.0, v143
	v_exp_f32_e32 v141, v141
	v_mul_f32_e32 v143, 0xbfb8aa3b, v5
	v_exp_f32_e32 v143, v143
	v_rcp_f32_e32 v152, v130
	v_add_f32_e32 v130, 1.0, v141
	v_rcp_f32_e32 v151, v130
	v_add_f32_e32 v130, 1.0, v143
	v_rcp_f32_e32 v153, v130

; __device__ __forceinline__ unsigned cvt_pk_bf16(float lo, float hi) { f32x2 v = {lo, hi}; bf16x2_t b = __builtin_convertvector(v, bf16x2_t); return __builtin_bit_cast(unsigned, b); }
;     __device__ __forceinline__ void operator()(const AccT& acc, const pg8::Unit& u, int wr, int wc, int fr, int fq) const {
;     ...
;             bf16_t* dst = (bf16_t*)(ws + (pn < 12 ? WS_Q : WS_K)); const float sc = pn < 12 ? 1.0f : 0.08838834764831845f;
;             const float* rc = (const float*)(ws + WS_ROPEC); const float* rs = (const float*)(ws + WS_ROPES);
;             const int dd = 16 * wc + 4 * fq;
; #pragma unroll
;             for (int ai = 0; ai < 2; ++ai) {
;                 f32x4 cc[4], ss[4];
; #pragma unroll
;                 for (int m = 0; m < 4; ++m) { const int row = row0 + ai * 128 + m * 16; cc[m] = *(const f32x4*)(rc + (size_t)row * 64 + dd); ss[m] = *(const f32x4*)(rs + (size_t)row * 64 + dd); }
; #pragma unroll
;                 for (int m = 0; m < 4; ++m) { const int row = row0 + ai * 128 + m * 16;
;                     const f32x4 c = cc[m] * sc, s = ss[m] * sc;
; #pragma unroll
;                     for (int bj = 0; bj < 2; ++bj) { const f32x4 t1 = acc[ai][bj][m][0], t2 = acc[ai][bj][m][1];
;                         const f32x4 o1 = t1 * c - t2 * s, o2 = t2 * c + t1 * s;
;                         bf16_t* p = dst + (size_t)row * QKW + (pn & 3) * 256 + bj * 128 + dd;
;                         u32x2 w1, w2; w1.x = cvt_pk_bf16(o1[0], o1[1]); w1.y = cvt_pk_bf16(o1[2], o1[3]); w2.x = cvt_pk_bf16(o2[0], o2[1]); w2.y = cvt_pk_bf16(o2[2], o2[3]);
;                         if (pn < 12) { __builtin_nontemporal_store(w1, (u32x2*)p); __builtin_nontemporal_store(w2, (u32x2*)(p + 64)); }
;                         else { *(u32x2*)p = w1; *(u32x2*)(p + 64) = w2; } } } }
;     ...
;                         u32x4 w; w.x = cvt_pk_bf16(v0[0], v0[1]); w.y = cvt_pk_bf16(v0[2], v0[3]); w.z = cvt_pk_bf16(v1[0], v1[1]); w.w = cvt_pk_bf16(v1[2], v1[3]);
;                         if (kind >= 1) __builtin_nontemporal_store(w, (u32x4*)(dst + (size_t)row * D + col0 + bj * 128));
;                         else *(u32x4*)(dst + (size_t)row * D + col0 + bj * 128) = w; } }
.LBB0_242:
	v_lshl_add_u64 v[154:155], v[144:145], 0, s[26:27]
	v_cvt_pk_bf16_f32 v144, v146, v147
	v_cvt_pk_bf16_f32 v145, v150, v151
	v_cvt_pk_bf16_f32 v146, v148, v149
	v_cvt_pk_bf16_f32 v147, v152, v153
	global_store_dwordx4 v[154:155], v[144:147], off offset:256 sc1
	s_mov_b64 s[0:1], 0
.LBB0_243:
	s_and_b64 vcc, exec, s[0:1]
	s_cbranch_vccz .LBB0_245
	v_ashrrev_i32_e32 v143, 31, v142
	v_lshlrev_b64 v[144:145], 8, v[142:143]
	v_lshl_add_u64 v[146:147], v[132:133], 0, v[144:145]
	v_lshl_add_u64 v[144:145], v[134:135], 0, v[144:145]
	global_load_dwordx4 v[146:149], v[146:147], off
	v_or_b32_e32 v194, 48, v142
	global_load_dwordx4 v[150:153], v[144:145], off
	v_or_b32_e32 v144, 16, v142
	v_ashrrev_i32_e32 v145, 31, v144
	v_lshlrev_b64 v[154:155], 8, v[144:145]
	v_lshl_add_u64 v[170:171], v[132:133], 0, v[154:155]
	v_lshl_add_u64 v[154:155], v[134:135], 0, v[154:155]
	global_load_dwordx4 v[174:177], v[154:155], off
	v_or_b32_e32 v154, 32, v142
	global_load_dwordx4 v[170:173], v[170:171], off
	v_ashrrev_i32_e32 v155, 31, v154
	v_lshlrev_b64 v[182:183], 8, v[154:155]
	v_lshlrev_b64 v[198:199], 11, v[144:145]
	v_lshl_add_u64 v[144:145], v[132:133], 0, v[182:183]
	global_load_dwordx4 v[178:181], v[144:145], off
	v_lshl_add_u64 v[144:145], v[134:135], 0, v[182:183]
	global_load_dwordx4 v[182:185], v[144:145], off
	v_ashrrev_i32_e32 v195, 31, v194
	v_lshlrev_b64 v[186:187], 8, v[194:195]
	v_lshl_add_u64 v[144:145], v[132:133], 0, v[186:187]
	v_lshl_add_u64 v[190:191], v[134:135], 0, v[186:187]
	global_load_dwordx4 v[186:189], v[144:145], off
	s_nop 0
	global_load_dwordx4 v[190:193], v[190:191], off
	s_cmp_lt_u32 s52, 12
	s_cselect_b64 s[0:1], -1, 0
	v_cndmask_b32_e64 v130, v168, 1.0, s[0:1]
	s_and_b64 s[0:1], s[0:1], exec
	s_cselect_b32 s0, s77, 0x3e600000
	s_add_u32 s0, s94, s0
	s_addc_u32 s1, s95, 0
	s_lshl_b32 s4, s52, 9
	s_and_b32 s4, s4, 0x600
	s_add_u32 s0, s0, s4
	v_mov_b32_e32 v141, v131
	s_addc_u32 s1, s1, 0
	v_lshlrev_b64 v[196:197], 11, v[142:143]
	v_lshl_add_u64 v[144:145], s[0:1], 0, v[140:141]
	v_lshl_add_u64 v[196:197], v[144:145], 0, v[196:197]
	v_lshl_add_u64 v[198:199], v[144:145], 0, v[198:199]
	v_lshlrev_b64 v[154:155], 11, v[154:155]
	v_lshl_add_u64 v[154:155], v[144:145], 0, v[154:155]
	s_waitcnt vmcnt(7)
	v_pk_mul_f32 v[146:147], v[130:131], v[146:147] op_sel_hi:[0,1]
	v_pk_mul_f32 v[148:149], v[130:131], v[148:149] op_sel_hi:[0,1]
	s_waitcnt vmcnt(6)
	v_pk_mul_f32 v[152:153], v[130:131], v[152:153] op_sel_hi:[0,1]
	v_pk_mul_f32 v[150:151], v[130:131], v[150:151] op_sel_hi:[0,1]
	v_pk_mul_f32 v[200:201], v[122:123], v[150:151]
	v_pk_mul_f32 v[202:203], v[124:125], v[152:153]
	v_pk_mul_f32 v[204:205], v[126:127], v[150:151]
	v_pk_mul_f32 v[206:207], v[128:129], v[152:153]
	v_pk_mul_f32 v[208:209], v[114:115], v[150:151]
	v_pk_mul_f32 v[210:211], v[116:117], v[152:153]
	v_pk_mul_f32 v[150:151], v[118:119], v[150:151]
	v_pk_mul_f32 v[152:153], v[120:121], v[152:153]
	s_waitcnt vmcnt(5)
	v_pk_mul_f32 v[176:177], v[130:131], v[176:177] op_sel_hi:[0,1]
	v_pk_mul_f32 v[174:175], v[130:131], v[174:175] op_sel_hi:[0,1]
	s_waitcnt vmcnt(4)
	v_pk_mul_f32 v[172:173], v[130:131], v[172:173] op_sel_hi:[0,1]
	v_pk_mul_f32 v[170:171], v[130:131], v[170:171] op_sel_hi:[0,1]
	v_pk_fma_f32 v[202:203], v[128:129], v[148:149], v[202:203] neg_lo:[0,0,1] neg_hi:[0,0,1]
	v_pk_fma_f32 v[200:201], v[126:127], v[146:147], v[200:201] neg_lo:[0,0,1] neg_hi:[0,0,1]
	v_pk_fma_f32 v[206:207], v[124:125], v[148:149], v[206:207]
	v_pk_fma_f32 v[204:205], v[122:123], v[146:147], v[204:205]
	v_pk_fma_f32 v[210:211], v[120:121], v[148:149], v[210:211] neg_lo:[0,0,1] neg_hi:[0,0,1]
	v_pk_fma_f32 v[208:209], v[118:119], v[146:147], v[208:209] neg_lo:[0,0,1] neg_hi:[0,0,1]
	v_pk_fma_f32 v[148:149], v[116:117], v[148:149], v[152:153]
	v_pk_fma_f32 v[146:147], v[114:115], v[146:147], v[150:151]
	v_pk_mul_f32 v[150:151], v[108:109], v[176:177]
	v_pk_mul_f32 v[152:153], v[106:107], v[174:175]
	v_pk_mul_f32 v[212:213], v[112:113], v[176:177]
	v_pk_mul_f32 v[214:215], v[110:111], v[174:175]
	v_cvt_pk_bf16_f32 v200, v200, v201
	v_cvt_pk_bf16_f32 v201, v202, v203
	v_cvt_pk_bf16_f32 v203, v206, v207
	v_cvt_pk_bf16_f32 v146, v146, v147
	v_cvt_pk_bf16_f32 v147, v148, v149
	v_pk_fma_f32 v[148:149], v[112:113], v[172:173], v[150:151] neg_lo:[0,0,1] neg_hi:[0,0,1]
	v_pk_fma_f32 v[150:151], v[110:111], v[170:171], v[152:153] neg_lo:[0,0,1] neg_hi:[0,0,1]
	v_pk_fma_f32 v[152:153], v[108:109], v[172:173], v[212:213]
	v_pk_fma_f32 v[206:207], v[106:107], v[170:171], v[214:215]
	v_cvt_pk_bf16_f32 v202, v204, v205
	v_cvt_pk_bf16_f32 v204, v208, v209
	v_cvt_pk_bf16_f32 v205, v210, v211
	global_store_dwordx2 v[196:197], v[200:201], off sc1
	global_store_dwordx2 v[196:197], v[202:203], off offset:128 sc1
	global_store_dwordx2 v[196:197], v[204:205], off offset:256 sc1
	global_store_dwordx2 v[196:197], v[146:147], off offset:384 sc1
	v_cvt_pk_bf16_f32 v146, v150, v151
	v_cvt_pk_bf16_f32 v147, v148, v149
	v_cvt_pk_bf16_f32 v148, v206, v207
	v_cvt_pk_bf16_f32 v149, v152, v153
	global_store_dwordx2 v[198:199], v[146:147], off sc1
	global_store_dwordx2 v[198:199], v[148:149], off offset:128 sc1
	v_pk_mul_f32 v[146:147], v[100:101], v[176:177]
	v_pk_mul_f32 v[148:149], v[98:99], v[174:175]
	v_pk_mul_f32 v[150:151], v[104:105], v[176:177]
	v_pk_mul_f32 v[152:153], v[102:103], v[174:175]
	v_pk_fma_f32 v[146:147], v[104:105], v[172:173], v[146:147] neg_lo:[0,0,1] neg_hi:[0,0,1]
	v_pk_fma_f32 v[148:149], v[102:103], v[170:171], v[148:149] neg_lo:[0,0,1] neg_hi:[0,0,1]
	v_pk_fma_f32 v[150:151], v[100:101], v[172:173], v[150:151]
	v_pk_fma_f32 v[152:153], v[98:99], v[170:171], v[152:153]
	v_cvt_pk_bf16_f32 v148, v148, v149
	v_cvt_pk_bf16_f32 v149, v146, v147
	v_cvt_pk_bf16_f32 v146, v152, v153
	v_cvt_pk_bf16_f32 v147, v150, v151
	s_waitcnt vmcnt(8)
; __device__ __forceinline__ unsigned cvt_pk_bf16(float lo, float hi) { f32x2 v = {lo, hi}; bf16x2_t b = __builtin_convertvector(v, bf16x2_t); return __builtin_bit_cast(unsigned, b); }
;     __device__ __forceinline__ void operator()(const AccT& acc, const pg8::Unit& u, int wr, int wc, int fr, int fq) const {
;     ...
;                 for (int m = 0; m < 4; ++m) { const int row = row0 + ai * 128 + m * 16; cc[m] = *(const f32x4*)(rc + (size_t)row * 64 + dd); ss[m] = *(const f32x4*)(rs + (size_t)row * 64 + dd); }
; #pragma unroll
;                 for (int m = 0; m < 4; ++m) { const int row = row0 + ai * 128 + m * 16;
;                     const f32x4 c = cc[m] * sc, s = ss[m] * sc;
; #pragma unroll
;                     for (int bj = 0; bj < 2; ++bj) { const f32x4 t1 = acc[ai][bj][m][0], t2 = acc[ai][bj][m][1];
;                         const f32x4 o1 = t1 * c - t2 * s, o2 = t2 * c + t1 * s;
;                         bf16_t* p = dst + (size_t)row * QKW + (pn & 3) * 256 + bj * 128 + dd;
;                         u32x2 w1, w2; w1.x = cvt_pk_bf16(o1[0], o1[1]); w1.y = cvt_pk_bf16(o1[2], o1[3]); w2.x = cvt_pk_bf16(o2[0], o2[1]); w2.y = cvt_pk_bf16(o2[2], o2[3]);
;                         if (pn < 12) { __builtin_nontemporal_store(w1, (u32x2*)p); __builtin_nontemporal_store(w2, (u32x2*)(p + 64)); }
;                         else { *(u32x2*)p = w1; *(u32x2*)(p + 64) = w2; } } } }
	v_pk_mul_f32 v[150:151], v[130:131], v[184:185] op_sel_hi:[0,1]
	v_pk_mul_f32 v[152:153], v[130:131], v[182:183] op_sel_hi:[0,1]
	global_store_dwordx2 v[198:199], v[148:149], off offset:256 sc1
	global_store_dwordx2 v[198:199], v[146:147], off offset:384 sc1
	v_pk_mul_f32 v[146:147], v[130:131], v[180:181] op_sel_hi:[0,1]
	v_pk_mul_f32 v[148:149], v[130:131], v[178:179] op_sel_hi:[0,1]
	v_pk_mul_f32 v[170:171], v[92:93], v[150:151]
	v_pk_mul_f32 v[172:173], v[90:91], v[152:153]
	v_pk_mul_f32 v[174:175], v[96:97], v[150:151]
	v_pk_mul_f32 v[176:177], v[94:95], v[152:153]
	v_pk_fma_f32 v[170:171], v[96:97], v[146:147], v[170:171] neg_lo:[0,0,1] neg_hi:[0,0,1]
	v_pk_fma_f32 v[172:173], v[94:95], v[148:149], v[172:173] neg_lo:[0,0,1] neg_hi:[0,0,1]
	v_pk_fma_f32 v[174:175], v[92:93], v[146:147], v[174:175]
	v_pk_fma_f32 v[176:177], v[90:91], v[148:149], v[176:177]
	v_cvt_pk_bf16_f32 v172, v172, v173
	v_cvt_pk_bf16_f32 v173, v170, v171
	v_cvt_pk_bf16_f32 v170, v176, v177
	v_cvt_pk_bf16_f32 v171, v174, v175
	global_store_dwordx2 v[154:155], v[172:173], off sc1
	global_store_dwordx2 v[154:155], v[170:171], off offset:128 sc1
	v_pk_mul_f32 v[170:171], v[84:85], v[150:151]
	v_pk_mul_f32 v[172:173], v[82:83], v[152:153]
	v_pk_fma_f32 v[170:171], v[88:89], v[146:147], v[170:171] neg_lo:[0,0,1] neg_hi:[0,0,1]
	v_pk_fma_f32 v[172:173], v[86:87], v[148:149], v[172:173] neg_lo:[0,0,1] neg_hi:[0,0,1]
	v_pk_mul_f32 v[150:151], v[88:89], v[150:151]
	v_pk_mul_f32 v[152:153], v[86:87], v[152:153]
	v_pk_fma_f32 v[146:147], v[84:85], v[146:147], v[150:151]
	v_pk_fma_f32 v[148:149], v[82:83], v[148:149], v[152:153]
	v_cvt_pk_bf16_f32 v150, v172, v173
	v_cvt_pk_bf16_f32 v151, v170, v171
	v_cvt_pk_bf16_f32 v148, v148, v149
	v_cvt_pk_bf16_f32 v149, v146, v147
	global_store_dwordx2 v[154:155], v[150:151], off offset:256 sc1
	global_store_dwordx2 v[154:155], v[148:149], off offset:384 sc1
	s_waitcnt vmcnt(12)
	v_pk_mul_f32 v[150:151], v[130:131], v[192:193] op_sel_hi:[0,1]
	v_pk_mul_f32 v[152:153], v[130:131], v[190:191] op_sel_hi:[0,1]
	v_pk_mul_f32 v[146:147], v[130:131], v[188:189] op_sel_hi:[0,1]
	v_pk_mul_f32 v[148:149], v[130:131], v[186:187] op_sel_hi:[0,1]
	v_pk_mul_f32 v[170:171], v[76:77], v[150:151]
	v_pk_mul_f32 v[172:173], v[74:75], v[152:153]
	v_pk_mul_f32 v[174:175], v[80:81], v[150:151]
	v_pk_mul_f32 v[176:177], v[78:79], v[152:153]
	v_lshlrev_b64 v[154:155], 11, v[194:195]
	v_pk_fma_f32 v[170:171], v[80:81], v[146:147], v[170:171] neg_lo:[0,0,1] neg_hi:[0,0,1]
	v_pk_fma_f32 v[172:173], v[78:79], v[148:149], v[172:173] neg_lo:[0,0,1] neg_hi:[0,0,1]
	v_pk_fma_f32 v[174:175], v[76:77], v[146:147], v[174:175]
	v_pk_fma_f32 v[176:177], v[74:75], v[148:149], v[176:177]
	v_lshl_add_u64 v[154:155], v[144:145], 0, v[154:155]
	v_cvt_pk_bf16_f32 v172, v172, v173
	v_cvt_pk_bf16_f32 v173, v170, v171
	v_cvt_pk_bf16_f32 v170, v176, v177
	v_cvt_pk_bf16_f32 v171, v174, v175
	global_store_dwordx2 v[154:155], v[172:173], off sc1
	global_store_dwordx2 v[154:155], v[170:171], off offset:128 sc1
	v_pk_mul_f32 v[170:171], v[68:69], v[150:151]
	v_pk_mul_f32 v[172:173], v[66:67], v[152:153]
	v_pk_fma_f32 v[170:171], v[72:73], v[146:147], v[170:171] neg_lo:[0,0,1] neg_hi:[0,0,1]
	v_pk_fma_f32 v[172:173], v[70:71], v[148:149], v[172:173] neg_lo:[0,0,1] neg_hi:[0,0,1]
	v_pk_mul_f32 v[150:151], v[72:73], v[150:151]
	v_pk_mul_f32 v[152:153], v[70:71], v[152:153]
	v_pk_fma_f32 v[146:147], v[68:69], v[146:147], v[150:151]
	v_pk_fma_f32 v[148:149], v[66:67], v[148:149], v[152:153]
	v_cvt_pk_bf16_f32 v150, v172, v173
	v_cvt_pk_bf16_f32 v151, v170, v171
	v_cvt_pk_bf16_f32 v148, v148, v149
	v_cvt_pk_bf16_f32 v149, v146, v147
	global_store_dwordx2 v[154:155], v[150:151], off offset:256 sc1
	global_store_dwordx2 v[154:155], v[148:149], off offset:384 sc1
	v_add_u32_e32 v154, 0x80, v142
	v_ashrrev_i32_e32 v155, 31, v154
	v_lshlrev_b64 v[150:151], 8, v[154:155]
	v_lshl_add_u64 v[146:147], v[132:133], 0, v[150:151]
	v_lshl_add_u64 v[150:151], v[134:135], 0, v[150:151]
	global_load_dwordx4 v[146:149], v[146:147], off
	v_add_u32_e32 v194, 0x90, v142
	global_load_dwordx4 v[150:153], v[150:151], off
	v_ashrrev_i32_e32 v195, 31, v194
	v_lshlrev_b64 v[174:175], 8, v[194:195]
	v_lshl_add_u64 v[170:171], v[132:133], 0, v[174:175]
	v_lshl_add_u64 v[174:175], v[134:135], 0, v[174:175]
	global_load_dwordx4 v[170:173], v[170:171], off
	v_add_u32_e32 v196, 0xa0, v142
	global_load_dwordx4 v[174:177], v[174:175], off
	v_ashrrev_i32_e32 v197, 31, v196
	v_lshlrev_b64 v[182:183], 8, v[196:197]
	v_lshl_add_u64 v[178:179], v[132:133], 0, v[182:183]
	v_lshl_add_u64 v[182:183], v[134:135], 0, v[182:183]
	global_load_dwordx4 v[178:181], v[178:179], off
	v_add_u32_e32 v198, 0xb0, v142
	global_load_dwordx4 v[182:185], v[182:183], off
	v_ashrrev_i32_e32 v199, 31, v198
	v_lshlrev_b64 v[186:187], 8, v[198:199]
	v_lshl_add_u64 v[188:189], v[132:133], 0, v[186:187]
	v_lshl_add_u64 v[190:191], v[134:135], 0, v[186:187]
	global_load_dwordx4 v[186:189], v[188:189], off
	s_nop 0
	global_load_dwordx4 v[190:193], v[190:191], off
	v_lshlrev_b64 v[154:155], 11, v[154:155]
	v_lshl_add_u64 v[154:155], v[144:145], 0, v[154:155]
	s_waitcnt vmcnt(7)
	v_pk_mul_f32 v[148:149], v[130:131], v[148:149] op_sel_hi:[0,1]
	v_pk_mul_f32 v[146:147], v[130:131], v[146:147] op_sel_hi:[0,1]
	s_waitcnt vmcnt(6)
; __device__ __forceinline__ unsigned cvt_pk_bf16(float lo, float hi) { f32x2 v = {lo, hi}; bf16x2_t b = __builtin_convertvector(v, bf16x2_t); return __builtin_bit_cast(unsigned, b); }
;     __device__ __forceinline__ void operator()(const AccT& acc, const pg8::Unit& u, int wr, int wc, int fr, int fq) const {
;     ...
;                 for (int m = 0; m < 4; ++m) { const int row = row0 + ai * 128 + m * 16; cc[m] = *(const f32x4*)(rc + (size_t)row * 64 + dd); ss[m] = *(const f32x4*)(rs + (size_t)row * 64 + dd); }
; #pragma unroll
;                 for (int m = 0; m < 4; ++m) { const int row = row0 + ai * 128 + m * 16;
;                     const f32x4 c = cc[m] * sc, s = ss[m] * sc;
; #pragma unroll
;                     for (int bj = 0; bj < 2; ++bj) { const f32x4 t1 = acc[ai][bj][m][0], t2 = acc[ai][bj][m][1];
;                         const f32x4 o1 = t1 * c - t2 * s, o2 = t2 * c + t1 * s;
;                         bf16_t* p = dst + (size_t)row * QKW + (pn & 3) * 256 + bj * 128 + dd;
;                         u32x2 w1, w2; w1.x = cvt_pk_bf16(o1[0], o1[1]); w1.y = cvt_pk_bf16(o1[2], o1[3]); w2.x = cvt_pk_bf16(o2[0], o2[1]); w2.y = cvt_pk_bf16(o2[2], o2[3]);
;                         if (pn < 12) { __builtin_nontemporal_store(w1, (u32x2*)p); __builtin_nontemporal_store(w2, (u32x2*)(p + 64)); }
;                         else { *(u32x2*)p = w1; *(u32x2*)(p + 64) = w2; } } } }
	v_pk_mul_f32 v[152:153], v[130:131], v[152:153] op_sel_hi:[0,1]
	v_pk_mul_f32 v[150:151], v[130:131], v[150:151] op_sel_hi:[0,1]
	v_pk_mul_f32 v[200:201], v[60:61], v[152:153]
	v_pk_mul_f32 v[202:203], v[58:59], v[150:151]
	v_pk_mul_f32 v[204:205], v[64:65], v[152:153]
	v_pk_mul_f32 v[206:207], v[62:63], v[150:151]
	v_pk_fma_f32 v[200:201], v[64:65], v[148:149], v[200:201] neg_lo:[0,0,1] neg_hi:[0,0,1]
	v_pk_fma_f32 v[202:203], v[62:63], v[146:147], v[202:203] neg_lo:[0,0,1] neg_hi:[0,0,1]
	v_pk_fma_f32 v[204:205], v[60:61], v[148:149], v[204:205]
	v_pk_fma_f32 v[206:207], v[58:59], v[146:147], v[206:207]
	v_cvt_pk_bf16_f32 v202, v202, v203
	v_cvt_pk_bf16_f32 v203, v200, v201
	v_cvt_pk_bf16_f32 v200, v206, v207
	v_cvt_pk_bf16_f32 v201, v204, v205
	global_store_dwordx2 v[154:155], v[202:203], off sc1
	global_store_dwordx2 v[154:155], v[200:201], off offset:128 sc1
	v_pk_mul_f32 v[200:201], v[52:53], v[152:153]
	v_pk_mul_f32 v[202:203], v[50:51], v[150:151]
	v_pk_fma_f32 v[200:201], v[56:57], v[148:149], v[200:201] neg_lo:[0,0,1] neg_hi:[0,0,1]
	v_pk_fma_f32 v[202:203], v[54:55], v[146:147], v[202:203] neg_lo:[0,0,1] neg_hi:[0,0,1]
	v_pk_mul_f32 v[152:153], v[56:57], v[152:153]
	v_pk_mul_f32 v[150:151], v[54:55], v[150:151]
	v_pk_fma_f32 v[148:149], v[52:53], v[148:149], v[152:153]
	v_pk_fma_f32 v[146:147], v[50:51], v[146:147], v[150:151]
	v_cvt_pk_bf16_f32 v150, v202, v203
	v_cvt_pk_bf16_f32 v151, v200, v201
	v_cvt_pk_bf16_f32 v146, v146, v147
	v_cvt_pk_bf16_f32 v147, v148, v149
	global_store_dwordx2 v[154:155], v[150:151], off offset:256 sc1
	global_store_dwordx2 v[154:155], v[146:147], off offset:384 sc1
	s_waitcnt vmcnt(8)
	v_pk_mul_f32 v[150:151], v[130:131], v[176:177] op_sel_hi:[0,1]
	v_pk_mul_f32 v[152:153], v[130:131], v[174:175] op_sel_hi:[0,1]
	v_pk_mul_f32 v[146:147], v[130:131], v[172:173] op_sel_hi:[0,1]
	v_pk_mul_f32 v[148:149], v[130:131], v[170:171] op_sel_hi:[0,1]
	v_pk_mul_f32 v[170:171], v[44:45], v[150:151]
	v_pk_mul_f32 v[172:173], v[42:43], v[152:153]
	v_pk_mul_f32 v[174:175], v[48:49], v[150:151]
	v_pk_mul_f32 v[176:177], v[46:47], v[152:153]
	v_lshlrev_b64 v[154:155], 11, v[194:195]
	v_pk_fma_f32 v[170:171], v[48:49], v[146:147], v[170:171] neg_lo:[0,0,1] neg_hi:[0,0,1]
	v_pk_fma_f32 v[172:173], v[46:47], v[148:149], v[172:173] neg_lo:[0,0,1] neg_hi:[0,0,1]
	v_pk_fma_f32 v[174:175], v[44:45], v[146:147], v[174:175]
	v_pk_fma_f32 v[176:177], v[42:43], v[148:149], v[176:177]
	v_lshl_add_u64 v[154:155], v[144:145], 0, v[154:155]
	v_cvt_pk_bf16_f32 v172, v172, v173
	v_cvt_pk_bf16_f32 v173, v170, v171
	v_cvt_pk_bf16_f32 v170, v176, v177
	v_cvt_pk_bf16_f32 v171, v174, v175
	global_store_dwordx2 v[154:155], v[172:173], off sc1
	global_store_dwordx2 v[154:155], v[170:171], off offset:128 sc1
	v_pk_mul_f32 v[170:171], v[36:37], v[150:151]
	v_pk_mul_f32 v[172:173], v[34:35], v[152:153]
	v_pk_fma_f32 v[170:171], v[40:41], v[146:147], v[170:171] neg_lo:[0,0,1] neg_hi:[0,0,1]
	v_pk_fma_f32 v[172:173], v[38:39], v[148:149], v[172:173] neg_lo:[0,0,1] neg_hi:[0,0,1]
	v_pk_mul_f32 v[150:151], v[40:41], v[150:151]
	v_pk_mul_f32 v[152:153], v[38:39], v[152:153]
	v_pk_fma_f32 v[146:147], v[36:37], v[146:147], v[150:151]
	v_pk_fma_f32 v[148:149], v[34:35], v[148:149], v[152:153]
	v_cvt_pk_bf16_f32 v150, v172, v173
	v_cvt_pk_bf16_f32 v151, v170, v171
	v_cvt_pk_bf16_f32 v148, v148, v149
	v_cvt_pk_bf16_f32 v149, v146, v147
	global_store_dwordx2 v[154:155], v[150:151], off offset:256 sc1
	global_store_dwordx2 v[154:155], v[148:149], off offset:384 sc1
	s_waitcnt vmcnt(10)
; __device__ __forceinline__ unsigned cvt_pk_bf16(float lo, float hi) { f32x2 v = {lo, hi}; bf16x2_t b = __builtin_convertvector(v, bf16x2_t); return __builtin_bit_cast(unsigned, b); }
;     __device__ __forceinline__ void operator()(const AccT& acc, const pg8::Unit& u, int wr, int wc, int fr, int fq) const {
;     ...
;                 for (int m = 0; m < 4; ++m) { const int row = row0 + ai * 128 + m * 16; cc[m] = *(const f32x4*)(rc + (size_t)row * 64 + dd); ss[m] = *(const f32x4*)(rs + (size_t)row * 64 + dd); }
; #pragma unroll
;                 for (int m = 0; m < 4; ++m) { const int row = row0 + ai * 128 + m * 16;
;                     const f32x4 c = cc[m] * sc, s = ss[m] * sc;
; #pragma unroll
;                     for (int bj = 0; bj < 2; ++bj) { const f32x4 t1 = acc[ai][bj][m][0], t2 = acc[ai][bj][m][1];
;                         const f32x4 o1 = t1 * c - t2 * s, o2 = t2 * c + t1 * s;
;                         bf16_t* p = dst + (size_t)row * QKW + (pn & 3) * 256 + bj * 128 + dd;
;                         u32x2 w1, w2; w1.x = cvt_pk_bf16(o1[0], o1[1]); w1.y = cvt_pk_bf16(o1[2], o1[3]); w2.x = cvt_pk_bf16(o2[0], o2[1]); w2.y = cvt_pk_bf16(o2[2], o2[3]);
;                         if (pn < 12) { __builtin_nontemporal_store(w1, (u32x2*)p); __builtin_nontemporal_store(w2, (u32x2*)(p + 64)); }
;                         else { *(u32x2*)p = w1; *(u32x2*)(p + 64) = w2; } } } }
	v_pk_mul_f32 v[150:151], v[130:131], v[184:185] op_sel_hi:[0,1]
	v_pk_mul_f32 v[152:153], v[130:131], v[182:183] op_sel_hi:[0,1]
	v_pk_mul_f32 v[146:147], v[130:131], v[180:181] op_sel_hi:[0,1]
	v_pk_mul_f32 v[148:149], v[130:131], v[178:179] op_sel_hi:[0,1]
	v_pk_mul_f32 v[170:171], v[28:29], v[150:151]
	v_pk_mul_f32 v[172:173], v[26:27], v[152:153]
	v_pk_mul_f32 v[174:175], v[32:33], v[150:151]
	v_pk_mul_f32 v[176:177], v[30:31], v[152:153]
	v_lshlrev_b64 v[154:155], 11, v[196:197]
	v_pk_fma_f32 v[170:171], v[32:33], v[146:147], v[170:171] neg_lo:[0,0,1] neg_hi:[0,0,1]
	v_pk_fma_f32 v[172:173], v[30:31], v[148:149], v[172:173] neg_lo:[0,0,1] neg_hi:[0,0,1]
	v_pk_fma_f32 v[174:175], v[28:29], v[146:147], v[174:175]
	v_pk_fma_f32 v[176:177], v[26:27], v[148:149], v[176:177]
	v_lshl_add_u64 v[154:155], v[144:145], 0, v[154:155]
	v_cvt_pk_bf16_f32 v172, v172, v173
	v_cvt_pk_bf16_f32 v173, v170, v171
	v_cvt_pk_bf16_f32 v170, v176, v177
	v_cvt_pk_bf16_f32 v171, v174, v175
	global_store_dwordx2 v[154:155], v[172:173], off sc1
	global_store_dwordx2 v[154:155], v[170:171], off offset:128 sc1
	v_pk_mul_f32 v[170:171], v[20:21], v[150:151]
	v_pk_mul_f32 v[172:173], v[18:19], v[152:153]
	v_pk_fma_f32 v[170:171], v[24:25], v[146:147], v[170:171] neg_lo:[0,0,1] neg_hi:[0,0,1]
	v_pk_fma_f32 v[172:173], v[22:23], v[148:149], v[172:173] neg_lo:[0,0,1] neg_hi:[0,0,1]
	v_pk_mul_f32 v[150:151], v[24:25], v[150:151]
	v_pk_mul_f32 v[152:153], v[22:23], v[152:153]
	v_pk_fma_f32 v[146:147], v[20:21], v[146:147], v[150:151]
	v_pk_fma_f32 v[148:149], v[18:19], v[148:149], v[152:153]
	v_cvt_pk_bf16_f32 v150, v172, v173
	v_cvt_pk_bf16_f32 v151, v170, v171
	v_cvt_pk_bf16_f32 v148, v148, v149
	v_cvt_pk_bf16_f32 v149, v146, v147
	global_store_dwordx2 v[154:155], v[150:151], off offset:256 sc1
	global_store_dwordx2 v[154:155], v[148:149], off offset:384 sc1
	s_waitcnt vmcnt(12)
	v_pk_mul_f32 v[150:151], v[130:131], v[192:193] op_sel_hi:[0,1]
	v_pk_mul_f32 v[152:153], v[130:131], v[190:191] op_sel_hi:[0,1]
	v_lshlrev_b64 v[154:155], 11, v[198:199]
	v_pk_mul_f32 v[146:147], v[130:131], v[188:189] op_sel_hi:[0,1]
	v_pk_mul_f32 v[148:149], v[130:131], v[186:187] op_sel_hi:[0,1]
	v_lshl_add_u64 v[144:145], v[144:145], 0, v[154:155]
	v_pk_mul_f32 v[154:155], v[12:13], v[150:151]
	v_pk_mul_f32 v[170:171], v[10:11], v[152:153]
	v_pk_mul_f32 v[172:173], v[16:17], v[150:151]
	v_pk_mul_f32 v[174:175], v[14:15], v[152:153]
	v_pk_fma_f32 v[154:155], v[16:17], v[146:147], v[154:155] neg_lo:[0,0,1] neg_hi:[0,0,1]
	v_pk_fma_f32 v[170:171], v[14:15], v[148:149], v[170:171] neg_lo:[0,0,1] neg_hi:[0,0,1]
	v_pk_fma_f32 v[172:173], v[12:13], v[146:147], v[172:173]
	v_pk_fma_f32 v[174:175], v[10:11], v[148:149], v[174:175]
	v_cvt_pk_bf16_f32 v170, v170, v171
	v_cvt_pk_bf16_f32 v171, v154, v155
	v_cvt_pk_bf16_f32 v154, v174, v175
	v_cvt_pk_bf16_f32 v155, v172, v173
	global_store_dwordx2 v[144:145], v[170:171], off sc1
	global_store_dwordx2 v[144:145], v[154:155], off offset:128 sc1
	v_pk_mul_f32 v[154:155], v[4:5], v[150:151]
	v_pk_mul_f32 v[170:171], v[2:3], v[152:153]
	v_pk_fma_f32 v[154:155], v[8:9], v[146:147], v[154:155] neg_lo:[0,0,1] neg_hi:[0,0,1]
	v_pk_fma_f32 v[170:171], v[6:7], v[148:149], v[170:171] neg_lo:[0,0,1] neg_hi:[0,0,1]
	v_pk_mul_f32 v[150:151], v[8:9], v[150:151]
	v_pk_mul_f32 v[152:153], v[6:7], v[152:153]
	v_pk_fma_f32 v[146:147], v[4:5], v[146:147], v[150:151]
	v_pk_fma_f32 v[148:149], v[2:3], v[148:149], v[152:153]
	v_cvt_pk_bf16_f32 v150, v170, v171
	v_cvt_pk_bf16_f32 v151, v154, v155
	v_cvt_pk_bf16_f32 v148, v148, v149
	v_cvt_pk_bf16_f32 v149, v146, v147
	global_store_dwordx2 v[144:145], v[150:151], off offset:256 sc1
	global_store_dwordx2 v[144:145], v[148:149], off offset:384 sc1

; __device__ __forceinline__ unsigned cvt_pk_bf16(float lo, float hi) { f32x2 v = {lo, hi}; bf16x2_t b = __builtin_convertvector(v, bf16x2_t); return __builtin_bit_cast(unsigned, b); }
; __device__ __forceinline__ f32x4 gelu4(f32x4 v) { f32x2 a = gelu_pk((f32x2){v[0], v[1]}), b = gelu_pk((f32x2){v[2], v[3]}); return (f32x4){a.x, a.y, b.x, b.y}; }
; __device__ __forceinline__ f32x2 gelu_pk(f32x2 v) {
;     const f32x2 av = __builtin_elementwise_abs(v), d = av * 0.2316418882f + 1.0f;
;     f32x2 t; t.x = __builtin_amdgcn_rcpf(d.x); t.y = __builtin_amdgcn_rcpf(d.y);
;     f32x2 q = t * 0.5307027145f + (-0.7265760135f); q = q * t + 0.7107068705f; q = q * t + (-0.142248368f); q = q * t + 0.127414796f; q = q * t;
;     const f32x2 s = (v * v) * (-0.72134752044f);
;     f32x2 e; e.x = __builtin_amdgcn_exp2f(s.x); e.y = __builtin_amdgcn_exp2f(s.y);
;     const f32x2 m = v * (q * e), r = v - m;
;     f32x2 o; o.x = v.x < 0.f ? m.x : r.x; o.y = v.y < 0.f ? m.y : r.y; return o;
;     __device__ __forceinline__ void operator()(const AccT& acc, const pg8::Unit& u, int wr, int wc, int fr, int fq) const {
;     ...
;             for (int ai = 0; ai < 2; ++ai)
; #pragma unroll
;                 for (int m = 0; m < 4; ++m) { const int row = row0 + ai * 128 + m * 16; float s = 0.f, q = 0.f;
; #pragma unroll
;                     for (int bj = 0; bj < 2; ++bj) { const f32x4 v0 = gelu4(acc[ai][bj][m][0]), v1 = gelu4(acc[ai][bj][m][1]);
;                         s += (v0[0] + v0[1]) + (v0[2] + v0[3]) + (v1[0] + v1[1]) + (v1[2] + v1[3]);
;                         q += (v0[0] * v0[0] + v0[1] * v0[1]) + (v0[2] * v0[2] + v0[3] * v0[3]) + (v1[0] * v1[0] + v1[1] * v1[1]) + (v1[2] * v1[2] + v1[3] * v1[3]);
;                         u32x4 w; w.x = cvt_pk_bf16(v0[0], v0[1]); w.y = cvt_pk_bf16(v0[2], v0[3]); w.z = cvt_pk_bf16(v1[0], v1[1]); w.w = cvt_pk_bf16(v1[2], v1[3]);
;                         *(u32x4*)(dst + (size_t)row * GW + col0 + bj * 128) = w; }
;                     if (pn >= 4) { s += __shfl_xor(s, 16); s += __shfl_xor(s, 32); q += __shfl_xor(q, 16); q += __shfl_xor(q, 32);
;                         if (fq == 0) *(f32x2*)(vstat + (size_t)row * 32 + ((pn - 4) * 4 + wc) * 2) = (f32x2){s, q}; } }
.LBB0_246:
	v_and_b32_e32 v147, 0x7fffffff, v127
	v_and_b32_e32 v146, 0x7fffffff, v126
	v_pk_fma_f32 v[146:147], v[146:147], s[28:29], 1.0 op_sel_hi:[1,0,0]
	v_mov_b64_e32 v[148:149], s[34:35]
	v_rcp_f32_e32 v150, v146
	v_rcp_f32_e32 v151, v147
	v_pk_mul_f32 v[154:155], v[126:127], v[126:127]
	v_and_b32_e32 v171, 0x7fffffff, v129
	v_pk_mul_f32 v[154:155], v[154:155], s[42:43] op_sel_hi:[1,0]
	v_pk_fma_f32 v[152:153], v[150:151], s[30:31], v[148:149] op_sel_hi:[1,0,0]
	v_and_b32_e32 v170, 0x7fffffff, v128
	v_pk_fma_f32 v[152:153], v[150:151], v[152:153], s[36:37] op_sel_hi:[1,1,0]
	v_exp_f32_e32 v154, v154
	v_exp_f32_e32 v155, v155
	v_pk_fma_f32 v[170:171], v[170:171], s[28:29], 1.0 op_sel_hi:[1,0,0]
	v_pk_fma_f32 v[152:153], v[150:151], v[152:153], s[38:39] op_sel_hi:[1,1,0]
	v_rcp_f32_e32 v170, v170
	v_rcp_f32_e32 v171, v171
	v_pk_fma_f32 v[152:153], v[150:151], v[152:153], s[40:41] op_sel_hi:[1,1,0]
	s_cmp_lt_i32 s52, 4
	v_pk_mul_f32 v[150:151], v[150:151], v[152:153]
	v_pk_mul_f32 v[152:153], v[128:129], v[128:129]
	v_pk_mul_f32 v[150:151], v[154:155], v[150:151]
	s_cselect_b64 s[0:1], -1, 0
	v_pk_mul_f32 v[154:155], v[126:127], v[150:151]
	v_pk_fma_f32 v[174:175], v[126:127], v[150:151], v[126:127] neg_lo:[1,0,0] neg_hi:[1,0,0]
	v_pk_fma_f32 v[150:151], v[170:171], s[30:31], v[148:149] op_sel_hi:[1,0,0]
	v_pk_mul_f32 v[152:153], v[152:153], s[42:43] op_sel_hi:[1,0]
	v_pk_fma_f32 v[150:151], v[170:171], v[150:151], s[36:37] op_sel_hi:[1,1,0]
	s_and_b64 vcc, s[0:1], exec
	v_pk_fma_f32 v[150:151], v[170:171], v[150:151], s[38:39] op_sel_hi:[1,1,0]
	v_exp_f32_e32 v152, v152
	v_pk_fma_f32 v[150:151], v[170:171], v[150:151], s[40:41] op_sel_hi:[1,1,0]
	v_exp_f32_e32 v153, v153
	v_pk_mul_f32 v[150:151], v[170:171], v[150:151]
	v_and_b32_e32 v171, 0x7fffffff, v123
	v_and_b32_e32 v170, 0x7fffffff, v122
	v_pk_fma_f32 v[170:171], v[170:171], s[28:29], 1.0 op_sel_hi:[1,0,0]
	s_cselect_b32 s0, s78, 0x3a600000
	v_rcp_f32_e32 v170, v170
	v_rcp_f32_e32 v171, v171
	s_add_u32 s0, s94, s0
	s_addc_u32 s1, s95, 0
	s_lshl_b32 s4, s52, 8
	s_and_b32 s4, s4, 0x300
	v_pk_mul_f32 v[150:151], v[152:153], v[150:151]
	v_pk_mul_f32 v[152:153], v[122:123], v[122:123]
	v_or_b32_e32 v130, s4, v162
	v_pk_mul_f32 v[176:177], v[128:129], v[150:151]
	v_pk_fma_f32 v[178:179], v[128:129], v[150:151], v[128:129] neg_lo:[1,0,0] neg_hi:[1,0,0]
	v_pk_fma_f32 v[150:151], v[170:171], s[30:31], v[148:149] op_sel_hi:[1,0,0]
	v_pk_mul_f32 v[152:153], v[152:153], s[42:43] op_sel_hi:[1,0]
	v_lshlrev_b32_e32 v130, 1, v130
	s_cmp_gt_i32 s52, 3
	v_pk_fma_f32 v[150:151], v[170:171], v[150:151], s[36:37] op_sel_hi:[1,1,0]
	v_exp_f32_e32 v152, v152
	v_exp_f32_e32 v153, v153
	v_lshl_add_u64 v[144:145], s[0:1], 0, v[130:131]
	s_cselect_b64 s[54:55], -1, 0
	s_lshl_b32 s0, s52, 3
	v_pk_fma_f32 v[150:151], v[170:171], v[150:151], s[38:39] op_sel_hi:[1,1,0]
	v_and_b32_e32 v173, 0x7fffffff, v125
	v_and_b32_e32 v172, 0x7fffffff, v124
	s_add_i32 s4, s74, s0
	v_pk_fma_f32 v[150:151], v[170:171], v[150:151], s[40:41] op_sel_hi:[1,1,0]
	v_pk_fma_f32 v[172:173], v[172:173], s[28:29], 1.0 op_sel_hi:[1,0,0]
	s_lshl_b64 s[0:1], s[4:5], 2
	v_pk_mul_f32 v[150:151], v[170:171], v[150:151]
	v_rcp_f32_e32 v172, v172
	v_rcp_f32_e32 v173, v173
	s_add_u32 s12, s62, s0
	v_pk_mul_f32 v[150:151], v[152:153], v[150:151]
	s_addc_u32 s13, s63, s1
	v_pk_mul_f32 v[152:153], v[122:123], v[150:151]
	v_pk_fma_f32 v[150:151], v[122:123], v[150:151], v[122:123] neg_lo:[1,0,0] neg_hi:[1,0,0]
	v_cmp_gt_f32_e64 s[0:1], 0, v123
	v_pk_mul_f32 v[170:171], v[124:125], v[124:125]
	v_pk_mul_f32 v[180:181], v[118:119], v[118:119]
	v_cndmask_b32_e64 v123, v151, v153, s[0:1]
	v_cmp_gt_f32_e64 s[0:1], 0, v122
	v_pk_mul_f32 v[180:181], v[180:181], s[42:43] op_sel_hi:[1,0]
	v_and_b32_e32 v183, 0x7fffffff, v121
	v_cndmask_b32_e64 v122, v150, v152, s[0:1]
	v_pk_fma_f32 v[150:151], v[172:173], s[30:31], v[148:149] op_sel_hi:[1,0,0]
	v_pk_mul_f32 v[152:153], v[170:171], s[42:43] op_sel_hi:[1,0]
	v_pk_fma_f32 v[150:151], v[172:173], v[150:151], s[36:37] op_sel_hi:[1,1,0]
	v_exp_f32_e32 v152, v152
	v_exp_f32_e32 v153, v153
	v_pk_fma_f32 v[150:151], v[172:173], v[150:151], s[38:39] op_sel_hi:[1,1,0]
	v_and_b32_e32 v182, 0x7fffffff, v120
	v_pk_fma_f32 v[150:151], v[172:173], v[150:151], s[40:41] op_sel_hi:[1,1,0]
	v_exp_f32_e32 v180, v180
	v_pk_mul_f32 v[150:151], v[172:173], v[150:151]
	v_exp_f32_e32 v181, v181
	v_pk_mul_f32 v[150:151], v[152:153], v[150:151]
	v_pk_fma_f32 v[182:183], v[182:183], s[28:29], 1.0 op_sel_hi:[1,0,0]
	v_pk_mul_f32 v[170:171], v[124:125], v[150:151]
	v_pk_fma_f32 v[172:173], v[124:125], v[150:151], v[124:125] neg_lo:[1,0,0] neg_hi:[1,0,0]
	v_and_b32_e32 v151, 0x7fffffff, v119
	v_and_b32_e32 v150, 0x7fffffff, v118
	v_pk_fma_f32 v[150:151], v[150:151], s[28:29], 1.0 op_sel_hi:[1,0,0]
	v_rcp_f32_e32 v182, v182
	v_rcp_f32_e32 v150, v150
	v_rcp_f32_e32 v151, v151
	v_rcp_f32_e32 v183, v183
	v_cmp_gt_f32_e64 s[0:1], 0, v124
	v_ashrrev_i32_e32 v143, 31, v142
	v_pk_fma_f32 v[152:153], v[150:151], s[30:31], v[148:149] op_sel_hi:[1,0,0]
	v_cndmask_b32_e64 v124, v172, v170, s[0:1]
	v_pk_fma_f32 v[152:153], v[150:151], v[152:153], s[36:37] op_sel_hi:[1,1,0]
	v_cmp_gt_f32_e64 s[0:1], 0, v120
	v_pk_fma_f32 v[152:153], v[150:151], v[152:153], s[38:39] op_sel_hi:[1,1,0]
	v_lshlrev_b64 v[146:147], 11, v[142:143]
	v_pk_fma_f32 v[152:153], v[150:151], v[152:153], s[40:41] op_sel_hi:[1,1,0]
	v_lshl_add_u64 v[146:147], v[144:145], 0, v[146:147]
	v_pk_mul_f32 v[150:151], v[150:151], v[152:153]
	v_pk_mul_f32 v[152:153], v[120:121], v[120:121]
	v_pk_mul_f32 v[150:151], v[180:181], v[150:151]
	v_pk_mul_f32 v[152:153], v[152:153], s[42:43] op_sel_hi:[1,0]
; __device__ __forceinline__ unsigned cvt_pk_bf16(float lo, float hi) { f32x2 v = {lo, hi}; bf16x2_t b = __builtin_convertvector(v, bf16x2_t); return __builtin_bit_cast(unsigned, b); }
; __device__ __forceinline__ f32x4 gelu4(f32x4 v) { f32x2 a = gelu_pk((f32x2){v[0], v[1]}), b = gelu_pk((f32x2){v[2], v[3]}); return (f32x4){a.x, a.y, b.x, b.y}; }
;     __device__ __forceinline__ void operator()(const AccT& acc, const pg8::Unit& u, int wr, int wc, int fr, int fq) const {
;     ...
;             for (int ai = 0; ai < 2; ++ai)
; #pragma unroll
;                 for (int m = 0; m < 4; ++m) { const int row = row0 + ai * 128 + m * 16; float s = 0.f, q = 0.f;
; #pragma unroll
;                     for (int bj = 0; bj < 2; ++bj) { const f32x4 v0 = gelu4(acc[ai][bj][m][0]), v1 = gelu4(acc[ai][bj][m][1]);
;                         s += (v0[0] + v0[1]) + (v0[2] + v0[3]) + (v1[0] + v1[1]) + (v1[2] + v1[3]);
;                         q += (v0[0] * v0[0] + v0[1] * v0[1]) + (v0[2] * v0[2] + v0[3] * v0[3]) + (v1[0] * v1[0] + v1[1] * v1[1]) + (v1[2] * v1[2] + v1[3] * v1[3]);
;                         u32x4 w; w.x = cvt_pk_bf16(v0[0], v0[1]); w.y = cvt_pk_bf16(v0[2], v0[3]); w.z = cvt_pk_bf16(v1[0], v1[1]); w.w = cvt_pk_bf16(v1[2], v1[3]);
;                         *(u32x4*)(dst + (size_t)row * GW + col0 + bj * 128) = w; }
;                     if (pn >= 4) { s += __shfl_xor(s, 16); s += __shfl_xor(s, 32); q += __shfl_xor(q, 16); q += __shfl_xor(q, 32);
;                         if (fq == 0) *(f32x2*)(vstat + (size_t)row * 32 + ((pn - 4) * 4 + wc) * 2) = (f32x2){s, q}; } }
	v_pk_mul_f32 v[180:181], v[118:119], v[150:151]
	v_pk_fma_f32 v[184:185], v[118:119], v[150:151], v[118:119] neg_lo:[1,0,0] neg_hi:[1,0,0]
	v_pk_fma_f32 v[150:151], v[182:183], s[30:31], v[148:149] op_sel_hi:[1,0,0]
	v_exp_f32_e32 v152, v152
	v_pk_fma_f32 v[150:151], v[182:183], v[150:151], s[36:37] op_sel_hi:[1,1,0]
	v_exp_f32_e32 v153, v153
	v_pk_fma_f32 v[150:151], v[182:183], v[150:151], s[38:39] op_sel_hi:[1,1,0]
	v_cvt_pk_bf16_f32 v172, v122, v123
	v_pk_fma_f32 v[150:151], v[182:183], v[150:151], s[40:41] op_sel_hi:[1,1,0]
	s_nop 0
	v_pk_mul_f32 v[150:151], v[182:183], v[150:151]
	s_nop 0
	v_pk_mul_f32 v[150:151], v[152:153], v[150:151]
	s_nop 0
	v_pk_mul_f32 v[152:153], v[120:121], v[150:151]
	v_pk_fma_f32 v[182:183], v[120:121], v[150:151], v[120:121] neg_lo:[1,0,0] neg_hi:[1,0,0]
	v_and_b32_e32 v151, 0x7fffffff, v115
	v_and_b32_e32 v150, 0x7fffffff, v114
	v_pk_fma_f32 v[150:151], v[150:151], s[28:29], 1.0 op_sel_hi:[1,0,0]
	s_nop 0
	v_rcp_f32_e32 v186, v150
	v_rcp_f32_e32 v187, v151
	v_cndmask_b32_e64 v151, v182, v152, s[0:1]
	v_cmp_gt_f32_e64 s[0:1], 0, v121
	s_nop 1
	v_cndmask_b32_e64 v121, v183, v153, s[0:1]
	v_pk_mul_f32 v[182:183], v[114:115], v[114:115]
	v_pk_fma_f32 v[152:153], v[186:187], s[30:31], v[148:149] op_sel_hi:[1,0,0]
	v_pk_mul_f32 v[182:183], v[182:183], s[42:43] op_sel_hi:[1,0]
	v_pk_fma_f32 v[152:153], v[186:187], v[152:153], s[36:37] op_sel_hi:[1,1,0]
	v_exp_f32_e32 v182, v182
	v_exp_f32_e32 v183, v183
	v_pk_fma_f32 v[152:153], v[186:187], v[152:153], s[38:39] op_sel_hi:[1,1,0]
	v_cmp_gt_f32_e64 s[0:1], 0, v126
	v_pk_fma_f32 v[152:153], v[186:187], v[152:153], s[40:41] op_sel_hi:[1,1,0]
	s_nop 0
	v_pk_mul_f32 v[152:153], v[186:187], v[152:153]
	v_pk_mul_f32 v[186:187], v[116:117], v[116:117]
	v_pk_mul_f32 v[152:153], v[182:183], v[152:153]
	s_nop 0
	v_pk_mul_f32 v[182:183], v[114:115], v[152:153]
	v_pk_fma_f32 v[188:189], v[114:115], v[152:153], v[114:115] neg_lo:[1,0,0] neg_hi:[1,0,0]
	v_cndmask_b32_e64 v152, v174, v154, s[0:1]
	v_cmp_gt_f32_e64 s[0:1], 0, v118
	v_and_b32_e32 v174, 0x7fffffff, v116
	s_nop 0
	v_cndmask_b32_e64 v153, v184, v180, s[0:1]
	v_cmp_gt_f32_e64 s[0:1], 0, v127
	s_nop 1
	v_cndmask_b32_e64 v154, v175, v155, s[0:1]
	v_cmp_gt_f32_e64 s[0:1], 0, v128
	v_and_b32_e32 v175, 0x7fffffff, v117
	v_pk_fma_f32 v[174:175], v[174:175], s[28:29], 1.0 op_sel_hi:[1,0,0]
	v_cndmask_b32_e64 v126, v178, v176, s[0:1]
	v_cmp_gt_f32_e64 s[0:1], 0, v119
	v_rcp_f32_e32 v174, v174
	v_rcp_f32_e32 v175, v175
	v_cndmask_b32_e64 v127, v185, v181, s[0:1]
	v_cmp_gt_f32_e64 s[0:1], 0, v129
	v_cvt_pk_bf16_f32 v170, v152, v154
	v_pk_fma_f32 v[148:149], v[174:175], s[30:31], v[148:149] op_sel_hi:[1,0,0]
	v_cndmask_b32_e64 v128, v179, v177, s[0:1]
	v_cmp_gt_f32_e64 s[0:1], 0, v114
	v_pk_fma_f32 v[148:149], v[174:175], v[148:149], s[36:37] op_sel_hi:[1,1,0]
	s_nop 0
	v_cndmask_b32_e64 v118, v188, v182, s[0:1]
	v_cmp_gt_f32_e64 s[0:1], 0, v125
	v_pk_fma_f32 v[148:149], v[174:175], v[148:149], s[38:39] op_sel_hi:[1,1,0]
	s_nop 0
	v_cndmask_b32_e64 v119, v173, v171, s[0:1]
	v_cvt_pk_bf16_f32 v171, v126, v128
	v_cvt_pk_bf16_f32 v173, v124, v119
	global_store_dwordx4 v[146:147], v[170:173], off sc1
	v_pk_fma_f32 v[148:149], v[174:175], v[148:149], s[40:41] op_sel_hi:[1,1,0]
	v_cmp_gt_f32_e64 s[0:1], 0, v115
	v_pk_mul_f32 v[170:171], v[186:187], s[42:43] op_sel_hi:[1,0]
	v_pk_mul_f32 v[148:149], v[174:175], v[148:149]
	v_exp_f32_e32 v170, v170
	v_exp_f32_e32 v171, v171
	v_cndmask_b32_e64 v114, v189, v183, s[0:1]
	v_cmp_gt_f32_e64 s[0:1], 0, v117
	v_cvt_pk_bf16_f32 v172, v118, v114
	v_pk_mul_f32 v[148:149], v[170:171], v[148:149]
	s_nop 0
	v_pk_mul_f32 v[170:171], v[116:117], v[148:149]
	v_pk_fma_f32 v[148:149], v[116:117], v[148:149], v[116:117] neg_lo:[1,0,0] neg_hi:[1,0,0]
	s_nop 0
	v_cndmask_b32_e64 v117, v149, v171, s[0:1]
	v_cmp_gt_f32_e64 s[0:1], 0, v116
	v_cvt_pk_bf16_f32 v171, v151, v121
	s_nop 0
	v_cndmask_b32_e64 v116, v148, v170, s[0:1]
	v_cvt_pk_bf16_f32 v170, v153, v127
	v_cvt_pk_bf16_f32 v173, v116, v117
	global_store_dwordx4 v[146:147], v[170:173], off offset:256 sc1
	s_cbranch_vccnz .LBB0_250
	v_mov_b32_e32 v155, v153
	v_mov_b32_e32 v115, v119
	v_mov_b32_e32 v129, v127
	v_pk_add_f32 v[146:147], v[118:119], v[114:115]
	v_pk_mul_f32 v[148:149], v[118:119], v[114:115]
	v_mov_b32_e32 v170, v154
	v_pk_add_f32 v[174:175], v[152:153], v[154:155]
	v_pk_mul_f32 v[154:155], v[152:153], v[154:155]
	v_mov_b32_e32 v147, v149
	v_mov_b32_e32 v149, v126
	v_mov_b32_e32 v171, v128
	v_mov_b32_e32 v175, v155
	v_pk_add_f32 v[154:155], v[126:127], v[128:129]
	v_pk_mul_f32 v[128:129], v[126:127], v[128:129]
	v_and_b32_e32 v126, 64, v169
	v_xor_b32_e32 v125, 16, v169
	v_add_u32_e32 v126, 64, v126
	v_mov_b32_e32 v148, v152
	v_pk_mul_f32 v[170:171], v[170:171], v[170:171]
	v_mul_f32_e32 v120, v122, v122
	v_cmp_lt_i32_e32 vcc, v125, v126
	v_pk_fma_f32 v[148:149], v[148:149], v[148:149], v[170:171]
	v_pk_fma_f32 v[170:171], v[122:123], v[122:123], v[120:121] op_sel_hi:[1,1,0]
	v_mul_f32_e32 v120, v116, v116
	v_mov_b32_e32 v155, v129
	v_mul_f32_e32 v129, v151, v151
	v_mul_f32_e32 v177, v121, v121
	v_pk_mul_f32 v[178:179], v[118:119], v[118:119]
	v_pk_mul_f32 v[114:115], v[114:115], v[114:115]
	v_cndmask_b32_e32 v125, v169, v125, vcc
	v_mov_b32_e32 v128, v122
	v_mov_b32_e32 v176, v123
	v_pk_fma_f32 v[172:173], v[116:117], v[116:117], v[120:121] op_sel_hi:[1,1,0]
	v_mov_b32_e32 v150, v153
	v_mov_b32_e32 v120, v127
	v_lshlrev_b32_e32 v127, 2, v125
	v_mov_b32_e32 v125, v178
	v_pk_mov_b32 v[114:115], v[118:119], v[114:115] op_sel:[1,0]
	v_pk_add_f32 v[118:119], v[174:175], v[154:155]
	v_pk_add_f32 v[122:123], v[128:129], v[176:177]
	v_pk_add_f32 v[120:121], v[150:151], v[120:121]
	v_pk_add_f32 v[114:115], v[124:125], v[114:115]
	v_pk_add_f32 v[118:119], v[118:119], v[122:123]
	v_mul_f32_e32 v130, v124, v124
	v_pk_add_f32 v[148:149], v[148:149], v[148:149] op_sel_hi:[0,1]
	v_pk_add_f32 v[114:115], v[118:119], v[114:115]
	v_pk_add_f32 v[118:119], v[120:121], v[120:121] op_sel:[0,1] op_sel_hi:[1,0]
	v_mov_b32_e32 v148, v116
	v_mov_b32_e32 v170, v117
	v_mov_b32_e32 v119, v130
	v_mov_b32_e32 v172, v131
	v_pk_add_f32 v[116:117], v[148:149], v[170:171]
	v_pk_add_f32 v[118:119], v[118:119], v[146:147]
	v_pk_add_f32 v[114:115], v[114:115], v[172:173]
	v_pk_add_f32 v[116:117], v[118:119], v[116:117]
	v_xor_b32_e32 v118, 32, v169
	v_pk_add_f32 v[114:115], v[116:117], v[114:115]
	ds_bpermute_b32 v116, v127, v114
	ds_bpermute_b32 v117, v127, v115
	v_cmp_lt_i32_e32 vcc, v118, v126
	s_waitcnt lgkmcnt(0)
	v_pk_add_f32 v[114:115], v[114:115], v[116:117]
	v_cndmask_b32_e32 v118, v169, v118, vcc
	v_lshlrev_b32_e32 v118, 2, v118
	ds_bpermute_b32 v116, v118, v114
	ds_bpermute_b32 v117, v118, v115
	s_and_saveexec_b64 s[0:1], s[6:7]
	s_cbranch_execz .LBB0_249
	s_waitcnt lgkmcnt(0)
	v_pk_add_f32 v[114:115], v[114:115], v[116:117]
	v_lshlrev_b64 v[116:117], 7, v[142:143]
	v_lshl_add_u64 v[116:117], s[12:13], 0, v[116:117]
	global_store_dwordx2 v[116:117], v[114:115], off sc1

; __device__ __forceinline__ f32x4 gelu4(f32x4 v) { f32x2 a = gelu_pk((f32x2){v[0], v[1]}), b = gelu_pk((f32x2){v[2], v[3]}); return (f32x4){a.x, a.y, b.x, b.y}; }
; __device__ __forceinline__ f32x2 gelu_pk(f32x2 v) {
;     const f32x2 av = __builtin_elementwise_abs(v), d = av * 0.2316418882f + 1.0f;
;     f32x2 t; t.x = __builtin_amdgcn_rcpf(d.x); t.y = __builtin_amdgcn_rcpf(d.y);
;     f32x2 q = t * 0.5307027145f + (-0.7265760135f); q = q * t + 0.7107068705f; q = q * t + (-0.142248368f); q = q * t + 0.127414796f; q = q * t;
;     const f32x2 s = (v * v) * (-0.72134752044f);
;     f32x2 e; e.x = __builtin_amdgcn_exp2f(s.x); e.y = __builtin_amdgcn_exp2f(s.y);
;     const f32x2 m = v * (q * e), r = v - m;
;     f32x2 o; o.x = v.x < 0.f ? m.x : r.x; o.y = v.y < 0.f ? m.y : r.y; return o;
;     __device__ __forceinline__ void operator()(const AccT& acc, const pg8::Unit& u, int wr, int wc, int fr, int fq) const {
;     ...
;             for (int ai = 0; ai < 2; ++ai)
; #pragma unroll
;                 for (int m = 0; m < 4; ++m) { const int row = row0 + ai * 128 + m * 16; float s = 0.f, q = 0.f;
; #pragma unroll
;                     for (int bj = 0; bj < 2; ++bj) { const f32x4 v0 = gelu4(acc[ai][bj][m][0]), v1 = gelu4(acc[ai][bj][m][1]);
;                         s += (v0[0] + v0[1]) + (v0[2] + v0[3]) + (v1[0] + v1[1]) + (v1[2] + v1[3]);
;                         q += (v0[0] * v0[0] + v0[1] * v0[1]) + (v0[2] * v0[2] + v0[3] * v0[3]) + (v1[0] * v1[0] + v1[1] * v1[1]) + (v1[2] * v1[2] + v1[3] * v1[3]);
.LBB0_250:
	s_waitcnt lgkmcnt(0)
	v_and_b32_e32 v117, 0x7fffffff, v111
	v_and_b32_e32 v116, 0x7fffffff, v110
	v_pk_fma_f32 v[116:117], v[116:117], s[28:29], 1.0 op_sel_hi:[1,0,0]
	v_mov_b64_e32 v[118:119], s[34:35]
	v_rcp_f32_e32 v120, v116
	v_rcp_f32_e32 v121, v117
	v_pk_mul_f32 v[124:125], v[110:111], v[110:111]
	v_and_b32_e32 v127, 0x7fffffff, v113
	v_pk_mul_f32 v[124:125], v[124:125], s[42:43] op_sel_hi:[1,0]
	v_pk_fma_f32 v[122:123], v[120:121], s[30:31], v[118:119] op_sel_hi:[1,0,0]
	v_and_b32_e32 v126, 0x7fffffff, v112
	v_pk_fma_f32 v[122:123], v[120:121], v[122:123], s[36:37] op_sel_hi:[1,1,0]
	v_exp_f32_e32 v124, v124
	v_exp_f32_e32 v125, v125
	v_pk_fma_f32 v[126:127], v[126:127], s[28:29], 1.0 op_sel_hi:[1,0,0]
	v_pk_fma_f32 v[122:123], v[120:121], v[122:123], s[38:39] op_sel_hi:[1,1,0]
	v_rcp_f32_e32 v126, v126
	v_rcp_f32_e32 v127, v127
	v_pk_fma_f32 v[122:123], v[120:121], v[122:123], s[40:41] op_sel_hi:[1,1,0]
	v_and_b32_e32 v129, 0x7fffffff, v109
	v_pk_mul_f32 v[120:121], v[120:121], v[122:123]
	v_pk_mul_f32 v[122:123], v[112:113], v[112:113]
	v_pk_mul_f32 v[120:121], v[124:125], v[120:121]
	v_pk_mul_f32 v[122:123], v[122:123], s[42:43] op_sel_hi:[1,0]
	v_pk_mul_f32 v[124:125], v[110:111], v[120:121]
	v_pk_fma_f32 v[146:147], v[110:111], v[120:121], v[110:111] neg_lo:[1,0,0] neg_hi:[1,0,0]
	v_pk_fma_f32 v[120:121], v[126:127], s[30:31], v[118:119] op_sel_hi:[1,0,0]
	v_exp_f32_e32 v122, v122
	v_pk_fma_f32 v[120:121], v[126:127], v[120:121], s[36:37] op_sel_hi:[1,1,0]
	v_exp_f32_e32 v123, v123
	v_pk_fma_f32 v[120:121], v[126:127], v[120:121], s[38:39] op_sel_hi:[1,1,0]
	v_and_b32_e32 v128, 0x7fffffff, v108
	v_pk_fma_f32 v[120:121], v[126:127], v[120:121], s[40:41] op_sel_hi:[1,1,0]
	v_pk_fma_f32 v[128:129], v[128:129], s[28:29], 1.0 op_sel_hi:[1,0,0]
	v_pk_mul_f32 v[120:121], v[126:127], v[120:121]
	v_and_b32_e32 v127, 0x7fffffff, v107
	v_and_b32_e32 v126, 0x7fffffff, v106
	v_pk_fma_f32 v[126:127], v[126:127], s[28:29], 1.0 op_sel_hi:[1,0,0]
	v_pk_mul_f32 v[120:121], v[122:123], v[120:121]
	v_rcp_f32_e32 v126, v126
	v_rcp_f32_e32 v127, v127
	v_pk_mul_f32 v[122:123], v[106:107], v[106:107]
	v_pk_mul_f32 v[148:149], v[112:113], v[120:121]
	v_pk_fma_f32 v[150:151], v[112:113], v[120:121], v[112:113] neg_lo:[1,0,0] neg_hi:[1,0,0]
	v_pk_fma_f32 v[120:121], v[126:127], s[30:31], v[118:119] op_sel_hi:[1,0,0]
	v_pk_mul_f32 v[122:123], v[122:123], s[42:43] op_sel_hi:[1,0]
	v_pk_fma_f32 v[120:121], v[126:127], v[120:121], s[36:37] op_sel_hi:[1,1,0]
	v_exp_f32_e32 v122, v122
	v_exp_f32_e32 v123, v123
	v_pk_fma_f32 v[120:121], v[126:127], v[120:121], s[38:39] op_sel_hi:[1,1,0]
	v_rcp_f32_e32 v128, v128
	v_pk_fma_f32 v[120:121], v[126:127], v[120:121], s[40:41] op_sel_hi:[1,1,0]
	v_rcp_f32_e32 v129, v129
	v_pk_mul_f32 v[120:121], v[126:127], v[120:121]
	v_cmp_gt_f32_e32 vcc, 0, v107
	v_pk_mul_f32 v[120:121], v[122:123], v[120:121]
	v_pk_mul_f32 v[126:127], v[108:109], v[108:109]
	v_pk_mul_f32 v[122:123], v[106:107], v[120:121]
	v_pk_fma_f32 v[120:121], v[106:107], v[120:121], v[106:107] neg_lo:[1,0,0] neg_hi:[1,0,0]
	v_pk_mul_f32 v[152:153], v[102:103], v[102:103]
	v_cndmask_b32_e32 v107, v121, v123, vcc
	v_cmp_gt_f32_e32 vcc, 0, v106
	v_pk_mul_f32 v[152:153], v[152:153], s[42:43] op_sel_hi:[1,0]
	v_and_b32_e32 v155, 0x7fffffff, v105
	v_cndmask_b32_e32 v106, v120, v122, vcc
	v_pk_fma_f32 v[120:121], v[128:129], s[30:31], v[118:119] op_sel_hi:[1,0,0]
	v_pk_mul_f32 v[122:123], v[126:127], s[42:43] op_sel_hi:[1,0]
	v_pk_fma_f32 v[120:121], v[128:129], v[120:121], s[36:37] op_sel_hi:[1,1,0]
	v_exp_f32_e32 v122, v122
	v_exp_f32_e32 v123, v123
	v_pk_fma_f32 v[120:121], v[128:129], v[120:121], s[38:39] op_sel_hi:[1,1,0]
	v_and_b32_e32 v154, 0x7fffffff, v104
	v_pk_fma_f32 v[120:121], v[128:129], v[120:121], s[40:41] op_sel_hi:[1,1,0]
	v_exp_f32_e32 v152, v152
	v_pk_mul_f32 v[120:121], v[128:129], v[120:121]
	v_exp_f32_e32 v153, v153
	v_pk_mul_f32 v[120:121], v[122:123], v[120:121]
	v_pk_fma_f32 v[154:155], v[154:155], s[28:29], 1.0 op_sel_hi:[1,0,0]
	v_pk_mul_f32 v[126:127], v[108:109], v[120:121]
	v_pk_fma_f32 v[128:129], v[108:109], v[120:121], v[108:109] neg_lo:[1,0,0] neg_hi:[1,0,0]
	v_and_b32_e32 v121, 0x7fffffff, v103
	v_and_b32_e32 v120, 0x7fffffff, v102
	v_pk_fma_f32 v[120:121], v[120:121], s[28:29], 1.0 op_sel_hi:[1,0,0]
	v_rcp_f32_e32 v154, v154
	v_rcp_f32_e32 v120, v120
	v_rcp_f32_e32 v121, v121
	v_rcp_f32_e32 v155, v155
	v_cmp_gt_f32_e32 vcc, 0, v108
	v_or_b32_e32 v114, 16, v142
	v_pk_fma_f32 v[122:123], v[120:121], s[30:31], v[118:119] op_sel_hi:[1,0,0]
	v_cndmask_b32_e32 v108, v128, v126, vcc
	v_pk_fma_f32 v[122:123], v[120:121], v[122:123], s[36:37] op_sel_hi:[1,1,0]
	v_cmp_gt_f32_e32 vcc, 0, v104
	v_pk_fma_f32 v[122:123], v[120:121], v[122:123], s[38:39] op_sel_hi:[1,1,0]
	v_ashrrev_i32_e32 v115, 31, v114
	v_pk_fma_f32 v[122:123], v[120:121], v[122:123], s[40:41] op_sel_hi:[1,1,0]
	v_lshlrev_b64 v[116:117], 11, v[114:115]
	v_pk_mul_f32 v[120:121], v[120:121], v[122:123]
	v_pk_mul_f32 v[122:123], v[104:105], v[104:105]
	v_pk_mul_f32 v[120:121], v[152:153], v[120:121]
	v_pk_mul_f32 v[122:123], v[122:123], s[42:43] op_sel_hi:[1,0]
	v_pk_mul_f32 v[152:153], v[102:103], v[120:121]
	v_pk_fma_f32 v[170:171], v[102:103], v[120:121], v[102:103] neg_lo:[1,0,0] neg_hi:[1,0,0]
	v_pk_fma_f32 v[120:121], v[154:155], s[30:31], v[118:119] op_sel_hi:[1,0,0]
	v_exp_f32_e32 v122, v122
	v_pk_fma_f32 v[120:121], v[154:155], v[120:121], s[36:37] op_sel_hi:[1,1,0]
	v_exp_f32_e32 v123, v123
	v_pk_fma_f32 v[120:121], v[154:155], v[120:121], s[38:39] op_sel_hi:[1,1,0]
	v_lshl_add_u64 v[116:117], v[144:145], 0, v[116:117]
; __device__ __forceinline__ unsigned cvt_pk_bf16(float lo, float hi) { f32x2 v = {lo, hi}; bf16x2_t b = __builtin_convertvector(v, bf16x2_t); return __builtin_bit_cast(unsigned, b); }
; __device__ __forceinline__ f32x4 gelu4(f32x4 v) { f32x2 a = gelu_pk((f32x2){v[0], v[1]}), b = gelu_pk((f32x2){v[2], v[3]}); return (f32x4){a.x, a.y, b.x, b.y}; }
;     __device__ __forceinline__ void operator()(const AccT& acc, const pg8::Unit& u, int wr, int wc, int fr, int fq) const {
;     ...
;             for (int ai = 0; ai < 2; ++ai)
; #pragma unroll
;                 for (int m = 0; m < 4; ++m) { const int row = row0 + ai * 128 + m * 16; float s = 0.f, q = 0.f;
; #pragma unroll
;                     for (int bj = 0; bj < 2; ++bj) { const f32x4 v0 = gelu4(acc[ai][bj][m][0]), v1 = gelu4(acc[ai][bj][m][1]);
;                         s += (v0[0] + v0[1]) + (v0[2] + v0[3]) + (v1[0] + v1[1]) + (v1[2] + v1[3]);
;                         q += (v0[0] * v0[0] + v0[1] * v0[1]) + (v0[2] * v0[2] + v0[3] * v0[3]) + (v1[0] * v1[0] + v1[1] * v1[1]) + (v1[2] * v1[2] + v1[3] * v1[3]);
;                         u32x4 w; w.x = cvt_pk_bf16(v0[0], v0[1]); w.y = cvt_pk_bf16(v0[2], v0[3]); w.z = cvt_pk_bf16(v1[0], v1[1]); w.w = cvt_pk_bf16(v1[2], v1[3]);
;                         *(u32x4*)(dst + (size_t)row * GW + col0 + bj * 128) = w; }
;                     if (pn >= 4) { s += __shfl_xor(s, 16); s += __shfl_xor(s, 32); q += __shfl_xor(q, 16); q += __shfl_xor(q, 32);
;                         if (fq == 0) *(f32x2*)(vstat + (size_t)row * 32 + ((pn - 4) * 4 + wc) * 2) = (f32x2){s, q}; } }
	v_pk_fma_f32 v[120:121], v[154:155], v[120:121], s[40:41] op_sel_hi:[1,1,0]
	v_cvt_pk_bf16_f32 v128, v106, v107
	v_pk_mul_f32 v[120:121], v[154:155], v[120:121]
	s_nop 0
	v_pk_mul_f32 v[120:121], v[122:123], v[120:121]
	s_nop 0
	v_pk_mul_f32 v[122:123], v[104:105], v[120:121]
	v_pk_fma_f32 v[154:155], v[104:105], v[120:121], v[104:105] neg_lo:[1,0,0] neg_hi:[1,0,0]
	v_and_b32_e32 v121, 0x7fffffff, v99
	v_and_b32_e32 v120, 0x7fffffff, v98
	v_pk_fma_f32 v[120:121], v[120:121], s[28:29], 1.0 op_sel_hi:[1,0,0]
	v_cndmask_b32_e64 v104, 0, 1, s[54:55]
	v_rcp_f32_e32 v172, v120
	v_rcp_f32_e32 v173, v121
	v_cndmask_b32_e32 v121, v154, v122, vcc
	v_cmp_gt_f32_e32 vcc, 0, v105
	v_cmp_ne_u32_e64 s[10:11], 1, v104
	s_nop 0
	v_cndmask_b32_e32 v105, v155, v123, vcc
	v_pk_mul_f32 v[154:155], v[98:99], v[98:99]
	v_pk_fma_f32 v[122:123], v[172:173], s[30:31], v[118:119] op_sel_hi:[1,0,0]
	v_pk_mul_f32 v[154:155], v[154:155], s[42:43] op_sel_hi:[1,0]
	v_pk_fma_f32 v[122:123], v[172:173], v[122:123], s[36:37] op_sel_hi:[1,1,0]
	v_exp_f32_e32 v154, v154
	v_exp_f32_e32 v155, v155
	v_pk_fma_f32 v[122:123], v[172:173], v[122:123], s[38:39] op_sel_hi:[1,1,0]
	v_cmp_gt_f32_e32 vcc, 0, v110
	v_pk_fma_f32 v[122:123], v[172:173], v[122:123], s[40:41] op_sel_hi:[1,1,0]
	s_nop 0
	v_pk_mul_f32 v[122:123], v[172:173], v[122:123]
	v_pk_mul_f32 v[172:173], v[100:101], v[100:101]
	v_pk_mul_f32 v[122:123], v[154:155], v[122:123]
	s_nop 0
	v_pk_mul_f32 v[154:155], v[98:99], v[122:123]
	v_pk_fma_f32 v[174:175], v[98:99], v[122:123], v[98:99] neg_lo:[1,0,0] neg_hi:[1,0,0]
	v_cndmask_b32_e32 v122, v146, v124, vcc
	v_cmp_gt_f32_e32 vcc, 0, v102
	v_and_b32_e32 v146, 0x7fffffff, v100
	s_nop 0
	v_cndmask_b32_e32 v123, v170, v152, vcc
	v_cmp_gt_f32_e32 vcc, 0, v111
	s_nop 1
	v_cndmask_b32_e32 v124, v147, v125, vcc
	v_cmp_gt_f32_e32 vcc, 0, v112
	v_and_b32_e32 v147, 0x7fffffff, v101
	v_pk_fma_f32 v[146:147], v[146:147], s[28:29], 1.0 op_sel_hi:[1,0,0]
	v_cndmask_b32_e32 v110, v150, v148, vcc
	v_cmp_gt_f32_e32 vcc, 0, v103
	v_rcp_f32_e32 v146, v146
	v_rcp_f32_e32 v147, v147
	v_cndmask_b32_e32 v111, v171, v153, vcc
	v_cmp_gt_f32_e32 vcc, 0, v113
	v_cvt_pk_bf16_f32 v126, v122, v124
	v_pk_fma_f32 v[118:119], v[146:147], s[30:31], v[118:119] op_sel_hi:[1,0,0]
	v_cndmask_b32_e32 v112, v151, v149, vcc
	v_cmp_gt_f32_e32 vcc, 0, v98
	v_pk_fma_f32 v[118:119], v[146:147], v[118:119], s[36:37] op_sel_hi:[1,1,0]
	s_nop 0
	v_cndmask_b32_e32 v102, v174, v154, vcc
	v_cmp_gt_f32_e32 vcc, 0, v109
	v_pk_fma_f32 v[118:119], v[146:147], v[118:119], s[38:39] op_sel_hi:[1,1,0]
	s_nop 0
	v_cndmask_b32_e32 v103, v129, v127, vcc
	v_cvt_pk_bf16_f32 v127, v110, v112
	v_cvt_pk_bf16_f32 v129, v108, v103
	global_store_dwordx4 v[116:117], v[126:129], off sc1
	v_pk_fma_f32 v[118:119], v[146:147], v[118:119], s[40:41] op_sel_hi:[1,1,0]
	v_cmp_gt_f32_e32 vcc, 0, v99
	v_pk_mul_f32 v[126:127], v[172:173], s[42:43] op_sel_hi:[1,0]
	v_pk_mul_f32 v[118:119], v[146:147], v[118:119]
	v_exp_f32_e32 v126, v126
	v_exp_f32_e32 v127, v127
	v_cndmask_b32_e32 v98, v175, v155, vcc
	v_cmp_gt_f32_e32 vcc, 0, v101
	v_cvt_pk_bf16_f32 v128, v102, v98
	v_pk_mul_f32 v[118:119], v[126:127], v[118:119]
	s_nop 0
	v_pk_mul_f32 v[126:127], v[100:101], v[118:119]
	v_pk_fma_f32 v[118:119], v[100:101], v[118:119], v[100:101] neg_lo:[1,0,0] neg_hi:[1,0,0]
	s_nop 0
	v_cndmask_b32_e32 v101, v119, v127, vcc
	v_cmp_gt_f32_e32 vcc, 0, v100
	v_cvt_pk_bf16_f32 v127, v121, v105
	s_nop 0
	v_cndmask_b32_e32 v100, v118, v126, vcc
	v_cvt_pk_bf16_f32 v126, v123, v111
	v_cvt_pk_bf16_f32 v129, v100, v101
	s_andn2_b64 vcc, exec, s[54:55]
	global_store_dwordx4 v[116:117], v[126:129], off offset:256 sc1
	s_cbranch_vccnz .LBB0_254
	v_mov_b32_e32 v125, v123
	v_mov_b32_e32 v99, v103
	v_mov_b32_e32 v113, v111
	v_pk_add_f32 v[116:117], v[102:103], v[98:99]
	v_pk_mul_f32 v[118:119], v[102:103], v[98:99]
	v_mov_b32_e32 v126, v124
	v_pk_add_f32 v[146:147], v[122:123], v[124:125]
	v_pk_mul_f32 v[124:125], v[122:123], v[124:125]
	v_mov_b32_e32 v117, v119
	v_mov_b32_e32 v119, v110
	v_mov_b32_e32 v127, v112
	v_mov_b32_e32 v147, v125
	v_pk_add_f32 v[124:125], v[110:111], v[112:113]
	v_pk_mul_f32 v[112:113], v[110:111], v[112:113]
	v_and_b32_e32 v110, 64, v169
	v_xor_b32_e32 v109, 16, v169
	v_add_u32_e32 v110, 64, v110
	v_mov_b32_e32 v118, v122
	v_pk_mul_f32 v[126:127], v[126:127], v[126:127]
	v_mul_f32_e32 v104, v106, v106
	v_cmp_lt_i32_e32 vcc, v109, v110
	v_pk_fma_f32 v[118:119], v[118:119], v[118:119], v[126:127]
	v_pk_fma_f32 v[126:127], v[106:107], v[106:107], v[104:105] op_sel_hi:[1,1,0]
	v_mul_f32_e32 v104, v100, v100
	v_mov_b32_e32 v125, v113
	v_mul_f32_e32 v113, v121, v121
	v_mul_f32_e32 v149, v105, v105
	v_pk_mul_f32 v[150:151], v[102:103], v[102:103]
	v_pk_mul_f32 v[98:99], v[98:99], v[98:99]
	v_cndmask_b32_e32 v109, v169, v109, vcc
	v_mov_b32_e32 v112, v106
	v_mov_b32_e32 v148, v107
	v_pk_fma_f32 v[128:129], v[100:101], v[100:101], v[104:105] op_sel_hi:[1,1,0]
	v_mov_b32_e32 v120, v123
	v_mov_b32_e32 v104, v111
	v_lshlrev_b32_e32 v111, 2, v109
	v_mov_b32_e32 v109, v150
	v_pk_mov_b32 v[98:99], v[102:103], v[98:99] op_sel:[1,0]
	v_pk_add_f32 v[102:103], v[146:147], v[124:125]
	v_pk_add_f32 v[106:107], v[112:113], v[148:149]
	v_pk_add_f32 v[104:105], v[120:121], v[104:105]
	v_pk_add_f32 v[98:99], v[108:109], v[98:99]
	v_pk_add_f32 v[102:103], v[102:103], v[106:107]
	v_mul_f32_e32 v130, v108, v108
	v_pk_add_f32 v[118:119], v[118:119], v[118:119] op_sel_hi:[0,1]
	v_pk_add_f32 v[98:99], v[102:103], v[98:99]
	v_pk_add_f32 v[102:103], v[104:105], v[104:105] op_sel:[0,1] op_sel_hi:[1,0]
	v_mov_b32_e32 v118, v100
	v_mov_b32_e32 v126, v101
	v_mov_b32_e32 v103, v130
	v_mov_b32_e32 v128, v131
	v_pk_add_f32 v[100:101], v[118:119], v[126:127]
	v_pk_add_f32 v[102:103], v[102:103], v[116:117]
	v_pk_add_f32 v[98:99], v[98:99], v[128:129]
	v_pk_add_f32 v[100:101], v[102:103], v[100:101]
	v_xor_b32_e32 v102, 32, v169
	v_pk_add_f32 v[98:99], v[100:101], v[98:99]
	ds_bpermute_b32 v100, v111, v98
	ds_bpermute_b32 v101, v111, v99
	v_cmp_lt_i32_e32 vcc, v102, v110
	s_waitcnt lgkmcnt(0)
	v_pk_add_f32 v[98:99], v[98:99], v[100:101]
	v_cndmask_b32_e32 v102, v169, v102, vcc
	v_lshlrev_b32_e32 v102, 2, v102
	ds_bpermute_b32 v100, v102, v98
	ds_bpermute_b32 v101, v102, v99
	s_and_saveexec_b64 s[0:1], s[6:7]
	s_cbranch_execz .LBB0_253
	s_waitcnt lgkmcnt(0)
	v_pk_add_f32 v[98:99], v[98:99], v[100:101]
	v_lshlrev_b64 v[100:101], 7, v[114:115]
	v_lshl_add_u64 v[100:101], s[12:13], 0, v[100:101]
	global_store_dwordx2 v[100:101], v[98:99], off sc1

; __device__ __forceinline__ f32x4 gelu4(f32x4 v) { f32x2 a = gelu_pk((f32x2){v[0], v[1]}), b = gelu_pk((f32x2){v[2], v[3]}); return (f32x4){a.x, a.y, b.x, b.y}; }
; __device__ __forceinline__ f32x2 gelu_pk(f32x2 v) {
;     const f32x2 av = __builtin_elementwise_abs(v), d = av * 0.2316418882f + 1.0f;
;     f32x2 t; t.x = __builtin_amdgcn_rcpf(d.x); t.y = __builtin_amdgcn_rcpf(d.y);
;     f32x2 q = t * 0.5307027145f + (-0.7265760135f); q = q * t + 0.7107068705f; q = q * t + (-0.142248368f); q = q * t + 0.127414796f; q = q * t;
;     const f32x2 s = (v * v) * (-0.72134752044f);
;     f32x2 e; e.x = __builtin_amdgcn_exp2f(s.x); e.y = __builtin_amdgcn_exp2f(s.y);
;     const f32x2 m = v * (q * e), r = v - m;
;     f32x2 o; o.x = v.x < 0.f ? m.x : r.x; o.y = v.y < 0.f ? m.y : r.y; return o;
;     __device__ __forceinline__ void operator()(const AccT& acc, const pg8::Unit& u, int wr, int wc, int fr, int fq) const {
;     ...
;             for (int ai = 0; ai < 2; ++ai)
; #pragma unroll
;                 for (int m = 0; m < 4; ++m) { const int row = row0 + ai * 128 + m * 16; float s = 0.f, q = 0.f;
; #pragma unroll
;                     for (int bj = 0; bj < 2; ++bj) { const f32x4 v0 = gelu4(acc[ai][bj][m][0]), v1 = gelu4(acc[ai][bj][m][1]);
;                         s += (v0[0] + v0[1]) + (v0[2] + v0[3]) + (v1[0] + v1[1]) + (v1[2] + v1[3]);
;                         q += (v0[0] * v0[0] + v0[1] * v0[1]) + (v0[2] * v0[2] + v0[3] * v0[3]) + (v1[0] * v1[0] + v1[1] * v1[1]) + (v1[2] * v1[2] + v1[3] * v1[3]);
.LBB0_254:
	s_waitcnt lgkmcnt(0)
	v_and_b32_e32 v101, 0x7fffffff, v95
	v_and_b32_e32 v100, 0x7fffffff, v94
	v_pk_fma_f32 v[100:101], v[100:101], s[28:29], 1.0 op_sel_hi:[1,0,0]
	v_mov_b64_e32 v[102:103], s[34:35]
	v_rcp_f32_e32 v104, v100
	v_rcp_f32_e32 v105, v101
	v_pk_mul_f32 v[108:109], v[94:95], v[94:95]
	v_and_b32_e32 v111, 0x7fffffff, v97
	v_pk_mul_f32 v[108:109], v[108:109], s[42:43] op_sel_hi:[1,0]
	v_pk_fma_f32 v[106:107], v[104:105], s[30:31], v[102:103] op_sel_hi:[1,0,0]
	v_and_b32_e32 v110, 0x7fffffff, v96
	v_pk_fma_f32 v[106:107], v[104:105], v[106:107], s[36:37] op_sel_hi:[1,1,0]
	v_exp_f32_e32 v108, v108
	v_exp_f32_e32 v109, v109
	v_pk_fma_f32 v[110:111], v[110:111], s[28:29], 1.0 op_sel_hi:[1,0,0]
	v_pk_fma_f32 v[106:107], v[104:105], v[106:107], s[38:39] op_sel_hi:[1,1,0]
	v_rcp_f32_e32 v110, v110
	v_rcp_f32_e32 v111, v111
	v_pk_fma_f32 v[106:107], v[104:105], v[106:107], s[40:41] op_sel_hi:[1,1,0]
	v_and_b32_e32 v113, 0x7fffffff, v93
	v_pk_mul_f32 v[104:105], v[104:105], v[106:107]
	v_pk_mul_f32 v[106:107], v[96:97], v[96:97]
	v_pk_mul_f32 v[104:105], v[108:109], v[104:105]
	v_pk_mul_f32 v[106:107], v[106:107], s[42:43] op_sel_hi:[1,0]
	v_pk_mul_f32 v[108:109], v[94:95], v[104:105]
	v_pk_fma_f32 v[114:115], v[94:95], v[104:105], v[94:95] neg_lo:[1,0,0] neg_hi:[1,0,0]
	v_pk_fma_f32 v[104:105], v[110:111], s[30:31], v[102:103] op_sel_hi:[1,0,0]
	v_exp_f32_e32 v106, v106
	v_pk_fma_f32 v[104:105], v[110:111], v[104:105], s[36:37] op_sel_hi:[1,1,0]
	v_exp_f32_e32 v107, v107
	v_pk_fma_f32 v[104:105], v[110:111], v[104:105], s[38:39] op_sel_hi:[1,1,0]
	v_and_b32_e32 v112, 0x7fffffff, v92
	v_pk_fma_f32 v[104:105], v[110:111], v[104:105], s[40:41] op_sel_hi:[1,1,0]
	v_pk_fma_f32 v[112:113], v[112:113], s[28:29], 1.0 op_sel_hi:[1,0,0]
	v_pk_mul_f32 v[104:105], v[110:111], v[104:105]
	v_and_b32_e32 v111, 0x7fffffff, v91
	v_and_b32_e32 v110, 0x7fffffff, v90
	v_pk_fma_f32 v[110:111], v[110:111], s[28:29], 1.0 op_sel_hi:[1,0,0]
	v_pk_mul_f32 v[104:105], v[106:107], v[104:105]
	v_rcp_f32_e32 v110, v110
	v_rcp_f32_e32 v111, v111
	v_pk_mul_f32 v[106:107], v[90:91], v[90:91]
	v_pk_mul_f32 v[116:117], v[96:97], v[104:105]
	v_pk_fma_f32 v[118:119], v[96:97], v[104:105], v[96:97] neg_lo:[1,0,0] neg_hi:[1,0,0]
	v_pk_fma_f32 v[104:105], v[110:111], s[30:31], v[102:103] op_sel_hi:[1,0,0]
	v_pk_mul_f32 v[106:107], v[106:107], s[42:43] op_sel_hi:[1,0]
	v_pk_fma_f32 v[104:105], v[110:111], v[104:105], s[36:37] op_sel_hi:[1,1,0]
	v_exp_f32_e32 v106, v106
	v_exp_f32_e32 v107, v107
	v_pk_fma_f32 v[104:105], v[110:111], v[104:105], s[38:39] op_sel_hi:[1,1,0]
	v_rcp_f32_e32 v112, v112
	v_pk_fma_f32 v[104:105], v[110:111], v[104:105], s[40:41] op_sel_hi:[1,1,0]
	v_rcp_f32_e32 v113, v113
	v_pk_mul_f32 v[104:105], v[110:111], v[104:105]
	v_cmp_gt_f32_e32 vcc, 0, v91
	v_pk_mul_f32 v[104:105], v[106:107], v[104:105]
	v_pk_mul_f32 v[110:111], v[92:93], v[92:93]
	v_pk_mul_f32 v[106:107], v[90:91], v[104:105]
	v_pk_fma_f32 v[104:105], v[90:91], v[104:105], v[90:91] neg_lo:[1,0,0] neg_hi:[1,0,0]
	v_pk_mul_f32 v[120:121], v[86:87], v[86:87]
	v_cndmask_b32_e32 v91, v105, v107, vcc
	v_cmp_gt_f32_e32 vcc, 0, v90
	v_pk_mul_f32 v[120:121], v[120:121], s[42:43] op_sel_hi:[1,0]
	v_and_b32_e32 v123, 0x7fffffff, v89
	v_cndmask_b32_e32 v90, v104, v106, vcc
	v_pk_fma_f32 v[104:105], v[112:113], s[30:31], v[102:103] op_sel_hi:[1,0,0]
	v_pk_mul_f32 v[106:107], v[110:111], s[42:43] op_sel_hi:[1,0]
	v_pk_fma_f32 v[104:105], v[112:113], v[104:105], s[36:37] op_sel_hi:[1,1,0]
	v_exp_f32_e32 v106, v106
	v_exp_f32_e32 v107, v107
	v_pk_fma_f32 v[104:105], v[112:113], v[104:105], s[38:39] op_sel_hi:[1,1,0]
	v_and_b32_e32 v122, 0x7fffffff, v88
	v_pk_fma_f32 v[104:105], v[112:113], v[104:105], s[40:41] op_sel_hi:[1,1,0]
	v_exp_f32_e32 v120, v120
	v_pk_mul_f32 v[104:105], v[112:113], v[104:105]
	v_exp_f32_e32 v121, v121
	v_pk_mul_f32 v[104:105], v[106:107], v[104:105]
	v_pk_fma_f32 v[122:123], v[122:123], s[28:29], 1.0 op_sel_hi:[1,0,0]
	v_pk_mul_f32 v[110:111], v[92:93], v[104:105]
	v_pk_fma_f32 v[112:113], v[92:93], v[104:105], v[92:93] neg_lo:[1,0,0] neg_hi:[1,0,0]
	v_and_b32_e32 v105, 0x7fffffff, v87
	v_and_b32_e32 v104, 0x7fffffff, v86
	v_pk_fma_f32 v[104:105], v[104:105], s[28:29], 1.0 op_sel_hi:[1,0,0]
	v_rcp_f32_e32 v122, v122
	v_rcp_f32_e32 v104, v104
	v_rcp_f32_e32 v105, v105
	v_rcp_f32_e32 v123, v123
	v_cmp_gt_f32_e32 vcc, 0, v92
	v_or_b32_e32 v98, 32, v142
	v_pk_fma_f32 v[106:107], v[104:105], s[30:31], v[102:103] op_sel_hi:[1,0,0]
	v_cndmask_b32_e32 v92, v112, v110, vcc
	v_pk_fma_f32 v[106:107], v[104:105], v[106:107], s[36:37] op_sel_hi:[1,1,0]
	v_cmp_gt_f32_e32 vcc, 0, v88
	v_pk_fma_f32 v[106:107], v[104:105], v[106:107], s[38:39] op_sel_hi:[1,1,0]
	v_ashrrev_i32_e32 v99, 31, v98
	v_pk_fma_f32 v[106:107], v[104:105], v[106:107], s[40:41] op_sel_hi:[1,1,0]
	v_lshlrev_b64 v[100:101], 11, v[98:99]
	v_pk_mul_f32 v[104:105], v[104:105], v[106:107]
	v_pk_mul_f32 v[106:107], v[88:89], v[88:89]
	v_pk_mul_f32 v[104:105], v[120:121], v[104:105]
	v_pk_mul_f32 v[106:107], v[106:107], s[42:43] op_sel_hi:[1,0]
	v_pk_mul_f32 v[120:121], v[86:87], v[104:105]
	v_pk_fma_f32 v[124:125], v[86:87], v[104:105], v[86:87] neg_lo:[1,0,0] neg_hi:[1,0,0]
	v_pk_fma_f32 v[104:105], v[122:123], s[30:31], v[102:103] op_sel_hi:[1,0,0]
	v_exp_f32_e32 v106, v106
	v_pk_fma_f32 v[104:105], v[122:123], v[104:105], s[36:37] op_sel_hi:[1,1,0]
	v_exp_f32_e32 v107, v107
	v_pk_fma_f32 v[104:105], v[122:123], v[104:105], s[38:39] op_sel_hi:[1,1,0]
	v_lshl_add_u64 v[100:101], v[144:145], 0, v[100:101]
	v_pk_fma_f32 v[104:105], v[122:123], v[104:105], s[40:41] op_sel_hi:[1,1,0]
	v_cvt_pk_bf16_f32 v112, v90, v91
; __device__ __forceinline__ unsigned cvt_pk_bf16(float lo, float hi) { f32x2 v = {lo, hi}; bf16x2_t b = __builtin_convertvector(v, bf16x2_t); return __builtin_bit_cast(unsigned, b); }
; __device__ __forceinline__ f32x4 gelu4(f32x4 v) { f32x2 a = gelu_pk((f32x2){v[0], v[1]}), b = gelu_pk((f32x2){v[2], v[3]}); return (f32x4){a.x, a.y, b.x, b.y}; }
;     __device__ __forceinline__ void operator()(const AccT& acc, const pg8::Unit& u, int wr, int wc, int fr, int fq) const {
;     ...
;             for (int ai = 0; ai < 2; ++ai)
; #pragma unroll
;                 for (int m = 0; m < 4; ++m) { const int row = row0 + ai * 128 + m * 16; float s = 0.f, q = 0.f;
; #pragma unroll
;                     for (int bj = 0; bj < 2; ++bj) { const f32x4 v0 = gelu4(acc[ai][bj][m][0]), v1 = gelu4(acc[ai][bj][m][1]);
;                         s += (v0[0] + v0[1]) + (v0[2] + v0[3]) + (v1[0] + v1[1]) + (v1[2] + v1[3]);
;                         q += (v0[0] * v0[0] + v0[1] * v0[1]) + (v0[2] * v0[2] + v0[3] * v0[3]) + (v1[0] * v1[0] + v1[1] * v1[1]) + (v1[2] * v1[2] + v1[3] * v1[3]);
;                         u32x4 w; w.x = cvt_pk_bf16(v0[0], v0[1]); w.y = cvt_pk_bf16(v0[2], v0[3]); w.z = cvt_pk_bf16(v1[0], v1[1]); w.w = cvt_pk_bf16(v1[2], v1[3]);
;                         *(u32x4*)(dst + (size_t)row * GW + col0 + bj * 128) = w; }
;                     if (pn >= 4) { s += __shfl_xor(s, 16); s += __shfl_xor(s, 32); q += __shfl_xor(q, 16); q += __shfl_xor(q, 32);
;                         if (fq == 0) *(f32x2*)(vstat + (size_t)row * 32 + ((pn - 4) * 4 + wc) * 2) = (f32x2){s, q}; } }
	v_pk_mul_f32 v[104:105], v[122:123], v[104:105]
	s_nop 0
	v_pk_mul_f32 v[104:105], v[106:107], v[104:105]
	s_nop 0
	v_pk_mul_f32 v[106:107], v[88:89], v[104:105]
	v_pk_fma_f32 v[122:123], v[88:89], v[104:105], v[88:89] neg_lo:[1,0,0] neg_hi:[1,0,0]
	v_and_b32_e32 v105, 0x7fffffff, v83
	v_and_b32_e32 v104, 0x7fffffff, v82
	v_pk_fma_f32 v[104:105], v[104:105], s[28:29], 1.0 op_sel_hi:[1,0,0]
	s_nop 0
	v_rcp_f32_e32 v126, v104
	v_rcp_f32_e32 v127, v105
	v_cndmask_b32_e32 v105, v122, v106, vcc
	v_cmp_gt_f32_e32 vcc, 0, v89
	s_nop 1
	v_cndmask_b32_e32 v89, v123, v107, vcc
	v_pk_mul_f32 v[122:123], v[82:83], v[82:83]
	v_pk_fma_f32 v[106:107], v[126:127], s[30:31], v[102:103] op_sel_hi:[1,0,0]
	v_pk_mul_f32 v[122:123], v[122:123], s[42:43] op_sel_hi:[1,0]
	v_pk_fma_f32 v[106:107], v[126:127], v[106:107], s[36:37] op_sel_hi:[1,1,0]
	v_exp_f32_e32 v122, v122
	v_exp_f32_e32 v123, v123
	v_pk_fma_f32 v[106:107], v[126:127], v[106:107], s[38:39] op_sel_hi:[1,1,0]
	v_cmp_gt_f32_e32 vcc, 0, v94
	v_pk_fma_f32 v[106:107], v[126:127], v[106:107], s[40:41] op_sel_hi:[1,1,0]
	s_nop 0
	v_pk_mul_f32 v[106:107], v[126:127], v[106:107]
	v_pk_mul_f32 v[126:127], v[84:85], v[84:85]
	v_pk_mul_f32 v[106:107], v[122:123], v[106:107]
	s_nop 0
	v_pk_mul_f32 v[122:123], v[82:83], v[106:107]
	v_pk_fma_f32 v[128:129], v[82:83], v[106:107], v[82:83] neg_lo:[1,0,0] neg_hi:[1,0,0]
	v_cndmask_b32_e32 v106, v114, v108, vcc
	v_cmp_gt_f32_e32 vcc, 0, v86
	v_and_b32_e32 v114, 0x7fffffff, v84
	s_nop 0
	v_cndmask_b32_e32 v107, v124, v120, vcc
	v_cmp_gt_f32_e32 vcc, 0, v95
	s_nop 1
	v_cndmask_b32_e32 v108, v115, v109, vcc
	v_cmp_gt_f32_e32 vcc, 0, v96
	v_and_b32_e32 v115, 0x7fffffff, v85
	v_pk_fma_f32 v[114:115], v[114:115], s[28:29], 1.0 op_sel_hi:[1,0,0]
	v_cndmask_b32_e32 v94, v118, v116, vcc
	v_cmp_gt_f32_e32 vcc, 0, v87
	v_rcp_f32_e32 v114, v114
	v_rcp_f32_e32 v115, v115
	v_cndmask_b32_e32 v95, v125, v121, vcc
	v_cmp_gt_f32_e32 vcc, 0, v97
	v_cvt_pk_bf16_f32 v110, v106, v108
	v_pk_fma_f32 v[102:103], v[114:115], s[30:31], v[102:103] op_sel_hi:[1,0,0]
	v_cndmask_b32_e32 v96, v119, v117, vcc
	v_cmp_gt_f32_e32 vcc, 0, v82
	v_pk_fma_f32 v[102:103], v[114:115], v[102:103], s[36:37] op_sel_hi:[1,1,0]
	s_nop 0
	v_cndmask_b32_e32 v86, v128, v122, vcc
	v_cmp_gt_f32_e32 vcc, 0, v93
	v_pk_fma_f32 v[102:103], v[114:115], v[102:103], s[38:39] op_sel_hi:[1,1,0]
	s_nop 0
	v_cndmask_b32_e32 v87, v113, v111, vcc
	v_cvt_pk_bf16_f32 v111, v94, v96
	v_cvt_pk_bf16_f32 v113, v92, v87
	global_store_dwordx4 v[100:101], v[110:113], off sc1
	v_pk_fma_f32 v[102:103], v[114:115], v[102:103], s[40:41] op_sel_hi:[1,1,0]
	v_cmp_gt_f32_e32 vcc, 0, v83
	v_pk_mul_f32 v[110:111], v[126:127], s[42:43] op_sel_hi:[1,0]
	v_pk_mul_f32 v[102:103], v[114:115], v[102:103]
	v_exp_f32_e32 v110, v110
	v_exp_f32_e32 v111, v111
	v_cndmask_b32_e32 v82, v129, v123, vcc
	v_cmp_gt_f32_e32 vcc, 0, v85
	v_cvt_pk_bf16_f32 v112, v86, v82
	v_pk_mul_f32 v[102:103], v[110:111], v[102:103]
	s_nop 0
	v_pk_mul_f32 v[110:111], v[84:85], v[102:103]
	v_pk_fma_f32 v[102:103], v[84:85], v[102:103], v[84:85] neg_lo:[1,0,0] neg_hi:[1,0,0]
	s_nop 0
	v_cndmask_b32_e32 v85, v103, v111, vcc
	v_cmp_gt_f32_e32 vcc, 0, v84
	v_cvt_pk_bf16_f32 v111, v105, v89
	s_nop 0
	v_cndmask_b32_e32 v84, v102, v110, vcc
	v_cvt_pk_bf16_f32 v110, v107, v95
	v_cvt_pk_bf16_f32 v113, v84, v85
	s_and_b64 vcc, exec, s[10:11]
	global_store_dwordx4 v[100:101], v[110:113], off offset:256 sc1
	s_cbranch_vccnz .LBB0_258
	v_mov_b32_e32 v109, v107
	v_mov_b32_e32 v83, v87
	v_mov_b32_e32 v97, v95
	v_pk_add_f32 v[100:101], v[86:87], v[82:83]
	v_pk_mul_f32 v[102:103], v[86:87], v[82:83]
	v_mov_b32_e32 v110, v108
	v_pk_add_f32 v[114:115], v[106:107], v[108:109]
	v_pk_mul_f32 v[108:109], v[106:107], v[108:109]
	v_mov_b32_e32 v101, v103
	v_mov_b32_e32 v103, v94
	v_mov_b32_e32 v111, v96
	v_mov_b32_e32 v115, v109
	v_pk_add_f32 v[108:109], v[94:95], v[96:97]
	v_pk_mul_f32 v[96:97], v[94:95], v[96:97]
	v_and_b32_e32 v94, 64, v169
	v_xor_b32_e32 v93, 16, v169
	v_add_u32_e32 v94, 64, v94
	v_mov_b32_e32 v102, v106
	v_pk_mul_f32 v[110:111], v[110:111], v[110:111]
	v_mul_f32_e32 v88, v90, v90
	v_cmp_lt_i32_e32 vcc, v93, v94
	v_pk_fma_f32 v[102:103], v[102:103], v[102:103], v[110:111]
	v_pk_fma_f32 v[110:111], v[90:91], v[90:91], v[88:89] op_sel_hi:[1,1,0]
	v_mul_f32_e32 v88, v84, v84
	v_mov_b32_e32 v109, v97
	v_mul_f32_e32 v97, v105, v105
	v_mul_f32_e32 v117, v89, v89
	v_pk_mul_f32 v[118:119], v[86:87], v[86:87]
	v_pk_mul_f32 v[82:83], v[82:83], v[82:83]
	v_cndmask_b32_e32 v93, v169, v93, vcc
	v_mov_b32_e32 v96, v90
	v_mov_b32_e32 v116, v91
	v_pk_fma_f32 v[112:113], v[84:85], v[84:85], v[88:89] op_sel_hi:[1,1,0]
	v_mov_b32_e32 v104, v107
	v_mov_b32_e32 v88, v95
	v_lshlrev_b32_e32 v95, 2, v93
	v_mov_b32_e32 v93, v118
	v_pk_mov_b32 v[82:83], v[86:87], v[82:83] op_sel:[1,0]
	v_pk_add_f32 v[86:87], v[114:115], v[108:109]
	v_pk_add_f32 v[90:91], v[96:97], v[116:117]
	v_pk_add_f32 v[88:89], v[104:105], v[88:89]
	v_pk_add_f32 v[82:83], v[92:93], v[82:83]
	v_pk_add_f32 v[86:87], v[86:87], v[90:91]
	v_mul_f32_e32 v120, v92, v92
	v_pk_add_f32 v[102:103], v[102:103], v[102:103] op_sel_hi:[0,1]
	v_pk_add_f32 v[82:83], v[86:87], v[82:83]
	v_pk_add_f32 v[86:87], v[88:89], v[88:89] op_sel:[0,1] op_sel_hi:[1,0]
	v_mov_b32_e32 v102, v84
	v_mov_b32_e32 v110, v85
	v_mov_b32_e32 v87, v120
	v_mov_b32_e32 v112, v131
	v_pk_add_f32 v[84:85], v[102:103], v[110:111]
	v_pk_add_f32 v[86:87], v[86:87], v[100:101]
	v_pk_add_f32 v[82:83], v[82:83], v[112:113]
	v_pk_add_f32 v[84:85], v[86:87], v[84:85]
	v_xor_b32_e32 v86, 32, v169
	v_pk_add_f32 v[82:83], v[84:85], v[82:83]
	ds_bpermute_b32 v84, v95, v82
	ds_bpermute_b32 v85, v95, v83
	v_cmp_lt_i32_e32 vcc, v86, v94
	s_waitcnt lgkmcnt(0)
	v_pk_add_f32 v[82:83], v[82:83], v[84:85]
	v_cndmask_b32_e32 v86, v169, v86, vcc
	v_lshlrev_b32_e32 v86, 2, v86
	ds_bpermute_b32 v84, v86, v82
	ds_bpermute_b32 v85, v86, v83
	s_and_saveexec_b64 s[0:1], s[6:7]
	s_cbranch_execz .LBB0_257
	s_waitcnt lgkmcnt(0)
	v_pk_add_f32 v[82:83], v[82:83], v[84:85]
	v_lshlrev_b64 v[84:85], 7, v[98:99]
	v_lshl_add_u64 v[84:85], s[12:13], 0, v[84:85]
	global_store_dwordx2 v[84:85], v[82:83], off sc1

; __device__ __forceinline__ f32x4 gelu4(f32x4 v) { f32x2 a = gelu_pk((f32x2){v[0], v[1]}), b = gelu_pk((f32x2){v[2], v[3]}); return (f32x4){a.x, a.y, b.x, b.y}; }
; __device__ __forceinline__ f32x2 gelu_pk(f32x2 v) {
;     const f32x2 av = __builtin_elementwise_abs(v), d = av * 0.2316418882f + 1.0f;
;     f32x2 t; t.x = __builtin_amdgcn_rcpf(d.x); t.y = __builtin_amdgcn_rcpf(d.y);
;     f32x2 q = t * 0.5307027145f + (-0.7265760135f); q = q * t + 0.7107068705f; q = q * t + (-0.142248368f); q = q * t + 0.127414796f; q = q * t;
;     const f32x2 s = (v * v) * (-0.72134752044f);
;     f32x2 e; e.x = __builtin_amdgcn_exp2f(s.x); e.y = __builtin_amdgcn_exp2f(s.y);
;     const f32x2 m = v * (q * e), r = v - m;
;     f32x2 o; o.x = v.x < 0.f ? m.x : r.x; o.y = v.y < 0.f ? m.y : r.y; return o;
;     __device__ __forceinline__ void operator()(const AccT& acc, const pg8::Unit& u, int wr, int wc, int fr, int fq) const {
;     ...
;             for (int ai = 0; ai < 2; ++ai)
; #pragma unroll
;                 for (int m = 0; m < 4; ++m) { const int row = row0 + ai * 128 + m * 16; float s = 0.f, q = 0.f;
; #pragma unroll
;                     for (int bj = 0; bj < 2; ++bj) { const f32x4 v0 = gelu4(acc[ai][bj][m][0]), v1 = gelu4(acc[ai][bj][m][1]);
;                         s += (v0[0] + v0[1]) + (v0[2] + v0[3]) + (v1[0] + v1[1]) + (v1[2] + v1[3]);
;                         q += (v0[0] * v0[0] + v0[1] * v0[1]) + (v0[2] * v0[2] + v0[3] * v0[3]) + (v1[0] * v1[0] + v1[1] * v1[1]) + (v1[2] * v1[2] + v1[3] * v1[3]);
.LBB0_258:
	s_waitcnt lgkmcnt(0)
	v_and_b32_e32 v85, 0x7fffffff, v79
	v_and_b32_e32 v84, 0x7fffffff, v78
	v_pk_fma_f32 v[84:85], v[84:85], s[28:29], 1.0 op_sel_hi:[1,0,0]
	v_mov_b64_e32 v[86:87], s[34:35]
	v_rcp_f32_e32 v88, v84
	v_rcp_f32_e32 v89, v85
	v_pk_mul_f32 v[92:93], v[78:79], v[78:79]
	v_and_b32_e32 v95, 0x7fffffff, v81
	v_pk_mul_f32 v[92:93], v[92:93], s[42:43] op_sel_hi:[1,0]
	v_pk_fma_f32 v[90:91], v[88:89], s[30:31], v[86:87] op_sel_hi:[1,0,0]
	v_and_b32_e32 v94, 0x7fffffff, v80
	v_pk_fma_f32 v[90:91], v[88:89], v[90:91], s[36:37] op_sel_hi:[1,1,0]
	v_exp_f32_e32 v92, v92
	v_exp_f32_e32 v93, v93
	v_pk_fma_f32 v[94:95], v[94:95], s[28:29], 1.0 op_sel_hi:[1,0,0]
	v_pk_fma_f32 v[90:91], v[88:89], v[90:91], s[38:39] op_sel_hi:[1,1,0]
	v_rcp_f32_e32 v94, v94
	v_rcp_f32_e32 v95, v95
	v_pk_fma_f32 v[90:91], v[88:89], v[90:91], s[40:41] op_sel_hi:[1,1,0]
	v_and_b32_e32 v97, 0x7fffffff, v77
	v_pk_mul_f32 v[88:89], v[88:89], v[90:91]
	v_pk_mul_f32 v[90:91], v[80:81], v[80:81]
	v_pk_mul_f32 v[88:89], v[92:93], v[88:89]
	v_pk_mul_f32 v[90:91], v[90:91], s[42:43] op_sel_hi:[1,0]
	v_pk_mul_f32 v[92:93], v[78:79], v[88:89]
	v_pk_fma_f32 v[98:99], v[78:79], v[88:89], v[78:79] neg_lo:[1,0,0] neg_hi:[1,0,0]
	v_pk_fma_f32 v[88:89], v[94:95], s[30:31], v[86:87] op_sel_hi:[1,0,0]
	v_exp_f32_e32 v90, v90
	v_pk_fma_f32 v[88:89], v[94:95], v[88:89], s[36:37] op_sel_hi:[1,1,0]
	v_exp_f32_e32 v91, v91
	v_pk_fma_f32 v[88:89], v[94:95], v[88:89], s[38:39] op_sel_hi:[1,1,0]
	v_and_b32_e32 v96, 0x7fffffff, v76
	v_pk_fma_f32 v[88:89], v[94:95], v[88:89], s[40:41] op_sel_hi:[1,1,0]
	v_pk_fma_f32 v[96:97], v[96:97], s[28:29], 1.0 op_sel_hi:[1,0,0]
	v_pk_mul_f32 v[88:89], v[94:95], v[88:89]
	v_and_b32_e32 v95, 0x7fffffff, v75
	v_and_b32_e32 v94, 0x7fffffff, v74
	v_pk_fma_f32 v[94:95], v[94:95], s[28:29], 1.0 op_sel_hi:[1,0,0]
	v_pk_mul_f32 v[88:89], v[90:91], v[88:89]
	v_rcp_f32_e32 v94, v94
	v_rcp_f32_e32 v95, v95
	v_pk_mul_f32 v[90:91], v[74:75], v[74:75]
	v_pk_mul_f32 v[100:101], v[80:81], v[88:89]
	v_pk_fma_f32 v[102:103], v[80:81], v[88:89], v[80:81] neg_lo:[1,0,0] neg_hi:[1,0,0]
	v_pk_fma_f32 v[88:89], v[94:95], s[30:31], v[86:87] op_sel_hi:[1,0,0]
	v_pk_mul_f32 v[90:91], v[90:91], s[42:43] op_sel_hi:[1,0]
	v_pk_fma_f32 v[88:89], v[94:95], v[88:89], s[36:37] op_sel_hi:[1,1,0]
	v_exp_f32_e32 v90, v90
	v_exp_f32_e32 v91, v91
	v_pk_fma_f32 v[88:89], v[94:95], v[88:89], s[38:39] op_sel_hi:[1,1,0]
	v_rcp_f32_e32 v96, v96
	v_pk_fma_f32 v[88:89], v[94:95], v[88:89], s[40:41] op_sel_hi:[1,1,0]
	v_rcp_f32_e32 v97, v97
	v_pk_mul_f32 v[88:89], v[94:95], v[88:89]
	v_cmp_gt_f32_e32 vcc, 0, v75
	v_pk_mul_f32 v[88:89], v[90:91], v[88:89]
	v_pk_mul_f32 v[94:95], v[76:77], v[76:77]
	v_pk_mul_f32 v[90:91], v[74:75], v[88:89]
	v_pk_fma_f32 v[88:89], v[74:75], v[88:89], v[74:75] neg_lo:[1,0,0] neg_hi:[1,0,0]
	v_pk_mul_f32 v[104:105], v[70:71], v[70:71]
	v_cndmask_b32_e32 v75, v89, v91, vcc
	v_cmp_gt_f32_e32 vcc, 0, v74
	v_pk_mul_f32 v[104:105], v[104:105], s[42:43] op_sel_hi:[1,0]
	v_and_b32_e32 v107, 0x7fffffff, v73
	v_cndmask_b32_e32 v74, v88, v90, vcc
	v_pk_fma_f32 v[88:89], v[96:97], s[30:31], v[86:87] op_sel_hi:[1,0,0]
	v_pk_mul_f32 v[90:91], v[94:95], s[42:43] op_sel_hi:[1,0]
	v_pk_fma_f32 v[88:89], v[96:97], v[88:89], s[36:37] op_sel_hi:[1,1,0]
	v_exp_f32_e32 v90, v90
	v_exp_f32_e32 v91, v91
	v_pk_fma_f32 v[88:89], v[96:97], v[88:89], s[38:39] op_sel_hi:[1,1,0]
	v_and_b32_e32 v106, 0x7fffffff, v72
	v_pk_fma_f32 v[88:89], v[96:97], v[88:89], s[40:41] op_sel_hi:[1,1,0]
	v_exp_f32_e32 v104, v104
	v_pk_mul_f32 v[88:89], v[96:97], v[88:89]
	v_exp_f32_e32 v105, v105
	v_pk_mul_f32 v[88:89], v[90:91], v[88:89]
	v_pk_fma_f32 v[106:107], v[106:107], s[28:29], 1.0 op_sel_hi:[1,0,0]
	v_pk_mul_f32 v[94:95], v[76:77], v[88:89]
	v_pk_fma_f32 v[96:97], v[76:77], v[88:89], v[76:77] neg_lo:[1,0,0] neg_hi:[1,0,0]
	v_and_b32_e32 v89, 0x7fffffff, v71
	v_and_b32_e32 v88, 0x7fffffff, v70
	v_pk_fma_f32 v[88:89], v[88:89], s[28:29], 1.0 op_sel_hi:[1,0,0]
	v_rcp_f32_e32 v106, v106
	v_rcp_f32_e32 v88, v88
	v_rcp_f32_e32 v89, v89
	v_rcp_f32_e32 v107, v107
	v_cmp_gt_f32_e32 vcc, 0, v76
	v_or_b32_e32 v82, 48, v142
	v_pk_fma_f32 v[90:91], v[88:89], s[30:31], v[86:87] op_sel_hi:[1,0,0]
	v_cndmask_b32_e32 v76, v96, v94, vcc
	v_pk_fma_f32 v[90:91], v[88:89], v[90:91], s[36:37] op_sel_hi:[1,1,0]
	v_cmp_gt_f32_e32 vcc, 0, v72
	v_pk_fma_f32 v[90:91], v[88:89], v[90:91], s[38:39] op_sel_hi:[1,1,0]
	v_ashrrev_i32_e32 v83, 31, v82
	v_pk_fma_f32 v[90:91], v[88:89], v[90:91], s[40:41] op_sel_hi:[1,1,0]
	v_lshlrev_b64 v[84:85], 11, v[82:83]
	v_pk_mul_f32 v[88:89], v[88:89], v[90:91]
	v_pk_mul_f32 v[90:91], v[72:73], v[72:73]
	v_pk_mul_f32 v[88:89], v[104:105], v[88:89]
	v_pk_mul_f32 v[90:91], v[90:91], s[42:43] op_sel_hi:[1,0]
	v_pk_mul_f32 v[104:105], v[70:71], v[88:89]
	v_pk_fma_f32 v[108:109], v[70:71], v[88:89], v[70:71] neg_lo:[1,0,0] neg_hi:[1,0,0]
	v_pk_fma_f32 v[88:89], v[106:107], s[30:31], v[86:87] op_sel_hi:[1,0,0]
	v_exp_f32_e32 v90, v90
	v_pk_fma_f32 v[88:89], v[106:107], v[88:89], s[36:37] op_sel_hi:[1,1,0]
	v_exp_f32_e32 v91, v91
	v_pk_fma_f32 v[88:89], v[106:107], v[88:89], s[38:39] op_sel_hi:[1,1,0]
	v_lshl_add_u64 v[84:85], v[144:145], 0, v[84:85]
	v_pk_fma_f32 v[88:89], v[106:107], v[88:89], s[40:41] op_sel_hi:[1,1,0]
	v_cvt_pk_bf16_f32 v96, v74, v75
	v_pk_mul_f32 v[88:89], v[106:107], v[88:89]
	s_nop 0
	v_pk_mul_f32 v[88:89], v[90:91], v[88:89]
	s_nop 0
	v_pk_mul_f32 v[90:91], v[72:73], v[88:89]
	v_pk_fma_f32 v[106:107], v[72:73], v[88:89], v[72:73] neg_lo:[1,0,0] neg_hi:[1,0,0]
	v_and_b32_e32 v89, 0x7fffffff, v67
	v_and_b32_e32 v88, 0x7fffffff, v66
; __device__ __forceinline__ unsigned cvt_pk_bf16(float lo, float hi) { f32x2 v = {lo, hi}; bf16x2_t b = __builtin_convertvector(v, bf16x2_t); return __builtin_bit_cast(unsigned, b); }
; __device__ __forceinline__ f32x4 gelu4(f32x4 v) { f32x2 a = gelu_pk((f32x2){v[0], v[1]}), b = gelu_pk((f32x2){v[2], v[3]}); return (f32x4){a.x, a.y, b.x, b.y}; }
;     __device__ __forceinline__ void operator()(const AccT& acc, const pg8::Unit& u, int wr, int wc, int fr, int fq) const {
;     ...
;             for (int ai = 0; ai < 2; ++ai)
; #pragma unroll
;                 for (int m = 0; m < 4; ++m) { const int row = row0 + ai * 128 + m * 16; float s = 0.f, q = 0.f;
; #pragma unroll
;                     for (int bj = 0; bj < 2; ++bj) { const f32x4 v0 = gelu4(acc[ai][bj][m][0]), v1 = gelu4(acc[ai][bj][m][1]);
;                         s += (v0[0] + v0[1]) + (v0[2] + v0[3]) + (v1[0] + v1[1]) + (v1[2] + v1[3]);
;                         q += (v0[0] * v0[0] + v0[1] * v0[1]) + (v0[2] * v0[2] + v0[3] * v0[3]) + (v1[0] * v1[0] + v1[1] * v1[1]) + (v1[2] * v1[2] + v1[3] * v1[3]);
;                         u32x4 w; w.x = cvt_pk_bf16(v0[0], v0[1]); w.y = cvt_pk_bf16(v0[2], v0[3]); w.z = cvt_pk_bf16(v1[0], v1[1]); w.w = cvt_pk_bf16(v1[2], v1[3]);
;                         *(u32x4*)(dst + (size_t)row * GW + col0 + bj * 128) = w; }
;                     if (pn >= 4) { s += __shfl_xor(s, 16); s += __shfl_xor(s, 32); q += __shfl_xor(q, 16); q += __shfl_xor(q, 32);
;                         if (fq == 0) *(f32x2*)(vstat + (size_t)row * 32 + ((pn - 4) * 4 + wc) * 2) = (f32x2){s, q}; } }
	v_pk_fma_f32 v[88:89], v[88:89], s[28:29], 1.0 op_sel_hi:[1,0,0]
	s_nop 0
	v_rcp_f32_e32 v110, v88
	v_rcp_f32_e32 v111, v89
	v_cndmask_b32_e32 v89, v106, v90, vcc
	v_cmp_gt_f32_e32 vcc, 0, v73
	s_nop 1
	v_cndmask_b32_e32 v73, v107, v91, vcc
	v_pk_mul_f32 v[106:107], v[66:67], v[66:67]
	v_pk_fma_f32 v[90:91], v[110:111], s[30:31], v[86:87] op_sel_hi:[1,0,0]
	v_pk_mul_f32 v[106:107], v[106:107], s[42:43] op_sel_hi:[1,0]
	v_pk_fma_f32 v[90:91], v[110:111], v[90:91], s[36:37] op_sel_hi:[1,1,0]
	v_exp_f32_e32 v106, v106
	v_exp_f32_e32 v107, v107
	v_pk_fma_f32 v[90:91], v[110:111], v[90:91], s[38:39] op_sel_hi:[1,1,0]
	v_cmp_gt_f32_e32 vcc, 0, v78
	v_pk_fma_f32 v[90:91], v[110:111], v[90:91], s[40:41] op_sel_hi:[1,1,0]
	s_nop 0
	v_pk_mul_f32 v[90:91], v[110:111], v[90:91]
	v_pk_mul_f32 v[110:111], v[68:69], v[68:69]
	v_pk_mul_f32 v[90:91], v[106:107], v[90:91]
	s_nop 0
	v_pk_mul_f32 v[106:107], v[66:67], v[90:91]
	v_pk_fma_f32 v[112:113], v[66:67], v[90:91], v[66:67] neg_lo:[1,0,0] neg_hi:[1,0,0]
	v_cndmask_b32_e32 v90, v98, v92, vcc
	v_cmp_gt_f32_e32 vcc, 0, v70
	v_and_b32_e32 v98, 0x7fffffff, v68
	s_nop 0
	v_cndmask_b32_e32 v91, v108, v104, vcc
	v_cmp_gt_f32_e32 vcc, 0, v79
	s_nop 1
	v_cndmask_b32_e32 v92, v99, v93, vcc
	v_cmp_gt_f32_e32 vcc, 0, v80
	v_and_b32_e32 v99, 0x7fffffff, v69
	v_pk_fma_f32 v[98:99], v[98:99], s[28:29], 1.0 op_sel_hi:[1,0,0]
	v_cndmask_b32_e32 v78, v102, v100, vcc
	v_cmp_gt_f32_e32 vcc, 0, v71
	v_rcp_f32_e32 v98, v98
	v_rcp_f32_e32 v99, v99
	v_cndmask_b32_e32 v79, v109, v105, vcc
	v_cmp_gt_f32_e32 vcc, 0, v81
	v_cvt_pk_bf16_f32 v94, v90, v92
	v_pk_fma_f32 v[86:87], v[98:99], s[30:31], v[86:87] op_sel_hi:[1,0,0]
	v_cndmask_b32_e32 v80, v103, v101, vcc
	v_cmp_gt_f32_e32 vcc, 0, v66
	v_pk_fma_f32 v[86:87], v[98:99], v[86:87], s[36:37] op_sel_hi:[1,1,0]
	s_nop 0
	v_cndmask_b32_e32 v70, v112, v106, vcc
	v_cmp_gt_f32_e32 vcc, 0, v77
	v_pk_fma_f32 v[86:87], v[98:99], v[86:87], s[38:39] op_sel_hi:[1,1,0]
	s_nop 0
	v_cndmask_b32_e32 v71, v97, v95, vcc
	v_cvt_pk_bf16_f32 v95, v78, v80
	v_cvt_pk_bf16_f32 v97, v76, v71
	global_store_dwordx4 v[84:85], v[94:97], off sc1
	v_pk_fma_f32 v[86:87], v[98:99], v[86:87], s[40:41] op_sel_hi:[1,1,0]
	v_cmp_gt_f32_e32 vcc, 0, v67
	v_pk_mul_f32 v[94:95], v[110:111], s[42:43] op_sel_hi:[1,0]
	v_pk_mul_f32 v[86:87], v[98:99], v[86:87]
	v_exp_f32_e32 v94, v94
	v_exp_f32_e32 v95, v95
	v_cndmask_b32_e32 v66, v113, v107, vcc
	v_cmp_gt_f32_e32 vcc, 0, v69
	v_cvt_pk_bf16_f32 v96, v70, v66
	v_pk_mul_f32 v[86:87], v[94:95], v[86:87]
	s_nop 0
	v_pk_mul_f32 v[94:95], v[68:69], v[86:87]
	v_pk_fma_f32 v[86:87], v[68:69], v[86:87], v[68:69] neg_lo:[1,0,0] neg_hi:[1,0,0]
	s_nop 0
	v_cndmask_b32_e32 v69, v87, v95, vcc
	v_cmp_gt_f32_e32 vcc, 0, v68
	v_cvt_pk_bf16_f32 v95, v89, v73
	s_nop 0
	v_cndmask_b32_e32 v68, v86, v94, vcc
	v_cvt_pk_bf16_f32 v94, v91, v79
	v_cvt_pk_bf16_f32 v97, v68, v69
	s_and_b64 vcc, exec, s[10:11]
	global_store_dwordx4 v[84:85], v[94:97], off offset:256 sc1
	s_cbranch_vccnz .LBB0_262
	v_mov_b32_e32 v93, v91
	v_mov_b32_e32 v67, v71
	v_mov_b32_e32 v81, v79
	v_pk_add_f32 v[84:85], v[70:71], v[66:67]
	v_pk_mul_f32 v[86:87], v[70:71], v[66:67]
	v_mov_b32_e32 v94, v92
	v_pk_add_f32 v[98:99], v[90:91], v[92:93]
	v_pk_mul_f32 v[92:93], v[90:91], v[92:93]
	v_mov_b32_e32 v85, v87
	v_mov_b32_e32 v87, v78
	v_mov_b32_e32 v95, v80
	v_mov_b32_e32 v99, v93
	v_pk_add_f32 v[92:93], v[78:79], v[80:81]
	v_pk_mul_f32 v[80:81], v[78:79], v[80:81]
	v_and_b32_e32 v78, 64, v169
	v_xor_b32_e32 v77, 16, v169
	v_add_u32_e32 v78, 64, v78
	v_mov_b32_e32 v86, v90
	v_pk_mul_f32 v[94:95], v[94:95], v[94:95]
	v_mul_f32_e32 v72, v74, v74
	v_cmp_lt_i32_e32 vcc, v77, v78
	v_pk_fma_f32 v[86:87], v[86:87], v[86:87], v[94:95]
	v_pk_fma_f32 v[94:95], v[74:75], v[74:75], v[72:73] op_sel_hi:[1,1,0]
	v_mul_f32_e32 v72, v68, v68
	v_mov_b32_e32 v93, v81
	v_mul_f32_e32 v81, v89, v89
	v_mul_f32_e32 v101, v73, v73
	v_pk_mul_f32 v[102:103], v[70:71], v[70:71]
	v_pk_mul_f32 v[66:67], v[66:67], v[66:67]
	v_cndmask_b32_e32 v77, v169, v77, vcc
	v_mov_b32_e32 v80, v74
	v_mov_b32_e32 v100, v75
	v_pk_fma_f32 v[96:97], v[68:69], v[68:69], v[72:73] op_sel_hi:[1,1,0]
	v_mov_b32_e32 v88, v91
	v_mov_b32_e32 v72, v79
	v_lshlrev_b32_e32 v79, 2, v77
	v_mov_b32_e32 v77, v102
	v_pk_mov_b32 v[66:67], v[70:71], v[66:67] op_sel:[1,0]
	v_pk_add_f32 v[70:71], v[98:99], v[92:93]
	v_pk_add_f32 v[74:75], v[80:81], v[100:101]
	v_pk_add_f32 v[72:73], v[88:89], v[72:73]
	v_pk_add_f32 v[66:67], v[76:77], v[66:67]
	v_pk_add_f32 v[70:71], v[70:71], v[74:75]
	v_mul_f32_e32 v104, v76, v76
	v_pk_add_f32 v[86:87], v[86:87], v[86:87] op_sel_hi:[0,1]
	v_pk_add_f32 v[66:67], v[70:71], v[66:67]
	v_pk_add_f32 v[70:71], v[72:73], v[72:73] op_sel:[0,1] op_sel_hi:[1,0]
	v_mov_b32_e32 v86, v68
	v_mov_b32_e32 v94, v69
	v_mov_b32_e32 v71, v104
	v_mov_b32_e32 v96, v131
	v_pk_add_f32 v[68:69], v[86:87], v[94:95]
	v_pk_add_f32 v[70:71], v[70:71], v[84:85]
	v_pk_add_f32 v[66:67], v[66:67], v[96:97]
	v_pk_add_f32 v[68:69], v[70:71], v[68:69]
	v_xor_b32_e32 v70, 32, v169
	v_pk_add_f32 v[66:67], v[68:69], v[66:67]
	ds_bpermute_b32 v68, v79, v66
	ds_bpermute_b32 v69, v79, v67
	v_cmp_lt_i32_e32 vcc, v70, v78
	s_waitcnt lgkmcnt(0)
	v_pk_add_f32 v[66:67], v[66:67], v[68:69]
	v_cndmask_b32_e32 v70, v169, v70, vcc
	v_lshlrev_b32_e32 v70, 2, v70
	ds_bpermute_b32 v68, v70, v66
	ds_bpermute_b32 v69, v70, v67
	s_and_saveexec_b64 s[0:1], s[6:7]
	s_cbranch_execz .LBB0_261
	s_waitcnt lgkmcnt(0)
	v_pk_add_f32 v[66:67], v[66:67], v[68:69]
	v_lshlrev_b64 v[68:69], 7, v[82:83]
	v_lshl_add_u64 v[68:69], s[12:13], 0, v[68:69]
	global_store_dwordx2 v[68:69], v[66:67], off sc1

; __device__ __forceinline__ f32x4 gelu4(f32x4 v) { f32x2 a = gelu_pk((f32x2){v[0], v[1]}), b = gelu_pk((f32x2){v[2], v[3]}); return (f32x4){a.x, a.y, b.x, b.y}; }
; __device__ __forceinline__ f32x2 gelu_pk(f32x2 v) {
;     const f32x2 av = __builtin_elementwise_abs(v), d = av * 0.2316418882f + 1.0f;
;     f32x2 t; t.x = __builtin_amdgcn_rcpf(d.x); t.y = __builtin_amdgcn_rcpf(d.y);
;     f32x2 q = t * 0.5307027145f + (-0.7265760135f); q = q * t + 0.7107068705f; q = q * t + (-0.142248368f); q = q * t + 0.127414796f; q = q * t;
;     const f32x2 s = (v * v) * (-0.72134752044f);
;     f32x2 e; e.x = __builtin_amdgcn_exp2f(s.x); e.y = __builtin_amdgcn_exp2f(s.y);
;     const f32x2 m = v * (q * e), r = v - m;
;     f32x2 o; o.x = v.x < 0.f ? m.x : r.x; o.y = v.y < 0.f ? m.y : r.y; return o;
;     __device__ __forceinline__ void operator()(const AccT& acc, const pg8::Unit& u, int wr, int wc, int fr, int fq) const {
;     ...
;             for (int ai = 0; ai < 2; ++ai)
; #pragma unroll
;                 for (int m = 0; m < 4; ++m) { const int row = row0 + ai * 128 + m * 16; float s = 0.f, q = 0.f;
; #pragma unroll
;                     for (int bj = 0; bj < 2; ++bj) { const f32x4 v0 = gelu4(acc[ai][bj][m][0]), v1 = gelu4(acc[ai][bj][m][1]);
;                         s += (v0[0] + v0[1]) + (v0[2] + v0[3]) + (v1[0] + v1[1]) + (v1[2] + v1[3]);
;                         q += (v0[0] * v0[0] + v0[1] * v0[1]) + (v0[2] * v0[2] + v0[3] * v0[3]) + (v1[0] * v1[0] + v1[1] * v1[1]) + (v1[2] * v1[2] + v1[3] * v1[3]);
.LBB0_262:
	s_waitcnt lgkmcnt(0)
	v_and_b32_e32 v69, 0x7fffffff, v63
	v_and_b32_e32 v68, 0x7fffffff, v62
	v_pk_fma_f32 v[68:69], v[68:69], s[28:29], 1.0 op_sel_hi:[1,0,0]
	v_mov_b64_e32 v[70:71], s[34:35]
	v_rcp_f32_e32 v72, v68
	v_rcp_f32_e32 v73, v69
	v_pk_mul_f32 v[76:77], v[62:63], v[62:63]
	v_and_b32_e32 v79, 0x7fffffff, v65
	v_pk_mul_f32 v[76:77], v[76:77], s[42:43] op_sel_hi:[1,0]
	v_pk_fma_f32 v[74:75], v[72:73], s[30:31], v[70:71] op_sel_hi:[1,0,0]
	v_and_b32_e32 v78, 0x7fffffff, v64
	v_pk_fma_f32 v[74:75], v[72:73], v[74:75], s[36:37] op_sel_hi:[1,1,0]
	v_exp_f32_e32 v76, v76
	v_exp_f32_e32 v77, v77
	v_pk_fma_f32 v[78:79], v[78:79], s[28:29], 1.0 op_sel_hi:[1,0,0]
	v_pk_fma_f32 v[74:75], v[72:73], v[74:75], s[38:39] op_sel_hi:[1,1,0]
	v_rcp_f32_e32 v78, v78
	v_rcp_f32_e32 v79, v79
	v_pk_fma_f32 v[74:75], v[72:73], v[74:75], s[40:41] op_sel_hi:[1,1,0]
	v_and_b32_e32 v81, 0x7fffffff, v61
	v_pk_mul_f32 v[72:73], v[72:73], v[74:75]
	v_pk_mul_f32 v[74:75], v[64:65], v[64:65]
	v_pk_mul_f32 v[72:73], v[76:77], v[72:73]
	v_pk_mul_f32 v[74:75], v[74:75], s[42:43] op_sel_hi:[1,0]
	v_pk_mul_f32 v[76:77], v[62:63], v[72:73]
	v_pk_fma_f32 v[82:83], v[62:63], v[72:73], v[62:63] neg_lo:[1,0,0] neg_hi:[1,0,0]
	v_pk_fma_f32 v[72:73], v[78:79], s[30:31], v[70:71] op_sel_hi:[1,0,0]
	v_exp_f32_e32 v74, v74
	v_pk_fma_f32 v[72:73], v[78:79], v[72:73], s[36:37] op_sel_hi:[1,1,0]
	v_exp_f32_e32 v75, v75
	v_pk_fma_f32 v[72:73], v[78:79], v[72:73], s[38:39] op_sel_hi:[1,1,0]
	v_and_b32_e32 v80, 0x7fffffff, v60
	v_pk_fma_f32 v[72:73], v[78:79], v[72:73], s[40:41] op_sel_hi:[1,1,0]
	v_pk_fma_f32 v[80:81], v[80:81], s[28:29], 1.0 op_sel_hi:[1,0,0]
	v_pk_mul_f32 v[72:73], v[78:79], v[72:73]
	v_and_b32_e32 v79, 0x7fffffff, v59
	v_and_b32_e32 v78, 0x7fffffff, v58
	v_pk_fma_f32 v[78:79], v[78:79], s[28:29], 1.0 op_sel_hi:[1,0,0]
	v_pk_mul_f32 v[72:73], v[74:75], v[72:73]
	v_rcp_f32_e32 v78, v78
	v_rcp_f32_e32 v79, v79
	v_pk_mul_f32 v[74:75], v[58:59], v[58:59]
	v_pk_mul_f32 v[84:85], v[64:65], v[72:73]
	v_pk_fma_f32 v[86:87], v[64:65], v[72:73], v[64:65] neg_lo:[1,0,0] neg_hi:[1,0,0]
	v_pk_fma_f32 v[72:73], v[78:79], s[30:31], v[70:71] op_sel_hi:[1,0,0]
	v_pk_mul_f32 v[74:75], v[74:75], s[42:43] op_sel_hi:[1,0]
	v_pk_fma_f32 v[72:73], v[78:79], v[72:73], s[36:37] op_sel_hi:[1,1,0]
	v_exp_f32_e32 v74, v74
	v_exp_f32_e32 v75, v75
	v_pk_fma_f32 v[72:73], v[78:79], v[72:73], s[38:39] op_sel_hi:[1,1,0]
	v_rcp_f32_e32 v80, v80
	v_pk_fma_f32 v[72:73], v[78:79], v[72:73], s[40:41] op_sel_hi:[1,1,0]
	v_rcp_f32_e32 v81, v81
	v_pk_mul_f32 v[72:73], v[78:79], v[72:73]
	v_cmp_gt_f32_e32 vcc, 0, v59
	v_pk_mul_f32 v[72:73], v[74:75], v[72:73]
	v_pk_mul_f32 v[78:79], v[60:61], v[60:61]
	v_pk_mul_f32 v[74:75], v[58:59], v[72:73]
	v_pk_fma_f32 v[72:73], v[58:59], v[72:73], v[58:59] neg_lo:[1,0,0] neg_hi:[1,0,0]
	v_pk_mul_f32 v[88:89], v[54:55], v[54:55]
	v_cndmask_b32_e32 v59, v73, v75, vcc
	v_cmp_gt_f32_e32 vcc, 0, v58
	v_pk_mul_f32 v[88:89], v[88:89], s[42:43] op_sel_hi:[1,0]
	v_and_b32_e32 v91, 0x7fffffff, v57
	v_cndmask_b32_e32 v58, v72, v74, vcc
	v_pk_fma_f32 v[72:73], v[80:81], s[30:31], v[70:71] op_sel_hi:[1,0,0]
	v_pk_mul_f32 v[74:75], v[78:79], s[42:43] op_sel_hi:[1,0]
	v_pk_fma_f32 v[72:73], v[80:81], v[72:73], s[36:37] op_sel_hi:[1,1,0]
	v_exp_f32_e32 v74, v74
	v_exp_f32_e32 v75, v75
	v_pk_fma_f32 v[72:73], v[80:81], v[72:73], s[38:39] op_sel_hi:[1,1,0]
	v_and_b32_e32 v90, 0x7fffffff, v56
	v_pk_fma_f32 v[72:73], v[80:81], v[72:73], s[40:41] op_sel_hi:[1,1,0]
	v_exp_f32_e32 v88, v88
	v_pk_mul_f32 v[72:73], v[80:81], v[72:73]
	v_exp_f32_e32 v89, v89
	v_pk_mul_f32 v[72:73], v[74:75], v[72:73]
	v_pk_fma_f32 v[90:91], v[90:91], s[28:29], 1.0 op_sel_hi:[1,0,0]
	v_pk_mul_f32 v[78:79], v[60:61], v[72:73]
	v_pk_fma_f32 v[80:81], v[60:61], v[72:73], v[60:61] neg_lo:[1,0,0] neg_hi:[1,0,0]
	v_and_b32_e32 v73, 0x7fffffff, v55
	v_and_b32_e32 v72, 0x7fffffff, v54
	v_pk_fma_f32 v[72:73], v[72:73], s[28:29], 1.0 op_sel_hi:[1,0,0]
	v_rcp_f32_e32 v90, v90
	v_rcp_f32_e32 v72, v72
	v_rcp_f32_e32 v73, v73
	v_rcp_f32_e32 v91, v91
	v_cmp_gt_f32_e32 vcc, 0, v60
	v_add_u32_e32 v66, 0x80, v142
	v_pk_fma_f32 v[74:75], v[72:73], s[30:31], v[70:71] op_sel_hi:[1,0,0]
	v_cndmask_b32_e32 v60, v80, v78, vcc
	v_pk_fma_f32 v[74:75], v[72:73], v[74:75], s[36:37] op_sel_hi:[1,1,0]
	v_cmp_gt_f32_e32 vcc, 0, v56
	v_pk_fma_f32 v[74:75], v[72:73], v[74:75], s[38:39] op_sel_hi:[1,1,0]
	v_ashrrev_i32_e32 v67, 31, v66
	v_pk_fma_f32 v[74:75], v[72:73], v[74:75], s[40:41] op_sel_hi:[1,1,0]
	v_lshlrev_b64 v[68:69], 11, v[66:67]
	v_pk_mul_f32 v[72:73], v[72:73], v[74:75]
	v_pk_mul_f32 v[74:75], v[56:57], v[56:57]
	v_pk_mul_f32 v[72:73], v[88:89], v[72:73]
	v_pk_mul_f32 v[74:75], v[74:75], s[42:43] op_sel_hi:[1,0]
	v_pk_mul_f32 v[88:89], v[54:55], v[72:73]
	v_pk_fma_f32 v[92:93], v[54:55], v[72:73], v[54:55] neg_lo:[1,0,0] neg_hi:[1,0,0]
	v_pk_fma_f32 v[72:73], v[90:91], s[30:31], v[70:71] op_sel_hi:[1,0,0]
	v_exp_f32_e32 v74, v74
	v_pk_fma_f32 v[72:73], v[90:91], v[72:73], s[36:37] op_sel_hi:[1,1,0]
	v_exp_f32_e32 v75, v75
	v_pk_fma_f32 v[72:73], v[90:91], v[72:73], s[38:39] op_sel_hi:[1,1,0]
	v_lshl_add_u64 v[68:69], v[144:145], 0, v[68:69]
	v_pk_fma_f32 v[72:73], v[90:91], v[72:73], s[40:41] op_sel_hi:[1,1,0]
	v_cvt_pk_bf16_f32 v80, v58, v59
	v_pk_mul_f32 v[72:73], v[90:91], v[72:73]
	s_nop 0
	v_pk_mul_f32 v[72:73], v[74:75], v[72:73]
	s_nop 0
	v_pk_mul_f32 v[74:75], v[56:57], v[72:73]
	v_pk_fma_f32 v[90:91], v[56:57], v[72:73], v[56:57] neg_lo:[1,0,0] neg_hi:[1,0,0]
	v_and_b32_e32 v73, 0x7fffffff, v51
	v_and_b32_e32 v72, 0x7fffffff, v50
; __device__ __forceinline__ unsigned cvt_pk_bf16(float lo, float hi) { f32x2 v = {lo, hi}; bf16x2_t b = __builtin_convertvector(v, bf16x2_t); return __builtin_bit_cast(unsigned, b); }
; __device__ __forceinline__ f32x4 gelu4(f32x4 v) { f32x2 a = gelu_pk((f32x2){v[0], v[1]}), b = gelu_pk((f32x2){v[2], v[3]}); return (f32x4){a.x, a.y, b.x, b.y}; }
;     __device__ __forceinline__ void operator()(const AccT& acc, const pg8::Unit& u, int wr, int wc, int fr, int fq) const {
;     ...
;             for (int ai = 0; ai < 2; ++ai)
; #pragma unroll
;                 for (int m = 0; m < 4; ++m) { const int row = row0 + ai * 128 + m * 16; float s = 0.f, q = 0.f;
; #pragma unroll
;                     for (int bj = 0; bj < 2; ++bj) { const f32x4 v0 = gelu4(acc[ai][bj][m][0]), v1 = gelu4(acc[ai][bj][m][1]);
;                         s += (v0[0] + v0[1]) + (v0[2] + v0[3]) + (v1[0] + v1[1]) + (v1[2] + v1[3]);
;                         q += (v0[0] * v0[0] + v0[1] * v0[1]) + (v0[2] * v0[2] + v0[3] * v0[3]) + (v1[0] * v1[0] + v1[1] * v1[1]) + (v1[2] * v1[2] + v1[3] * v1[3]);
;                         u32x4 w; w.x = cvt_pk_bf16(v0[0], v0[1]); w.y = cvt_pk_bf16(v0[2], v0[3]); w.z = cvt_pk_bf16(v1[0], v1[1]); w.w = cvt_pk_bf16(v1[2], v1[3]);
;                         *(u32x4*)(dst + (size_t)row * GW + col0 + bj * 128) = w; }
;                     if (pn >= 4) { s += __shfl_xor(s, 16); s += __shfl_xor(s, 32); q += __shfl_xor(q, 16); q += __shfl_xor(q, 32);
;                         if (fq == 0) *(f32x2*)(vstat + (size_t)row * 32 + ((pn - 4) * 4 + wc) * 2) = (f32x2){s, q}; } }
	v_pk_fma_f32 v[72:73], v[72:73], s[28:29], 1.0 op_sel_hi:[1,0,0]
	s_nop 0
	v_rcp_f32_e32 v94, v72
	v_rcp_f32_e32 v95, v73
	v_cndmask_b32_e32 v73, v90, v74, vcc
	v_cmp_gt_f32_e32 vcc, 0, v57
	s_nop 1
	v_cndmask_b32_e32 v57, v91, v75, vcc
	v_pk_mul_f32 v[90:91], v[50:51], v[50:51]
	v_pk_fma_f32 v[74:75], v[94:95], s[30:31], v[70:71] op_sel_hi:[1,0,0]
	v_pk_mul_f32 v[90:91], v[90:91], s[42:43] op_sel_hi:[1,0]
	v_pk_fma_f32 v[74:75], v[94:95], v[74:75], s[36:37] op_sel_hi:[1,1,0]
	v_exp_f32_e32 v90, v90
	v_exp_f32_e32 v91, v91
	v_pk_fma_f32 v[74:75], v[94:95], v[74:75], s[38:39] op_sel_hi:[1,1,0]
	v_cmp_gt_f32_e32 vcc, 0, v62
	v_pk_fma_f32 v[74:75], v[94:95], v[74:75], s[40:41] op_sel_hi:[1,1,0]
	s_nop 0
	v_pk_mul_f32 v[74:75], v[94:95], v[74:75]
	v_pk_mul_f32 v[94:95], v[52:53], v[52:53]
	v_pk_mul_f32 v[74:75], v[90:91], v[74:75]
	s_nop 0
	v_pk_mul_f32 v[90:91], v[50:51], v[74:75]
	v_pk_fma_f32 v[96:97], v[50:51], v[74:75], v[50:51] neg_lo:[1,0,0] neg_hi:[1,0,0]
	v_cndmask_b32_e32 v74, v82, v76, vcc
	v_cmp_gt_f32_e32 vcc, 0, v54
	v_and_b32_e32 v82, 0x7fffffff, v52
	s_nop 0
	v_cndmask_b32_e32 v75, v92, v88, vcc
	v_cmp_gt_f32_e32 vcc, 0, v63
	s_nop 1
	v_cndmask_b32_e32 v76, v83, v77, vcc
	v_cmp_gt_f32_e32 vcc, 0, v64
	v_and_b32_e32 v83, 0x7fffffff, v53
	v_pk_fma_f32 v[82:83], v[82:83], s[28:29], 1.0 op_sel_hi:[1,0,0]
	v_cndmask_b32_e32 v62, v86, v84, vcc
	v_cmp_gt_f32_e32 vcc, 0, v55
	v_rcp_f32_e32 v82, v82
	v_rcp_f32_e32 v83, v83
	v_cndmask_b32_e32 v63, v93, v89, vcc
	v_cmp_gt_f32_e32 vcc, 0, v65
	v_cvt_pk_bf16_f32 v78, v74, v76
	v_pk_fma_f32 v[70:71], v[82:83], s[30:31], v[70:71] op_sel_hi:[1,0,0]
	v_cndmask_b32_e32 v64, v87, v85, vcc
	v_cmp_gt_f32_e32 vcc, 0, v50
	v_pk_fma_f32 v[70:71], v[82:83], v[70:71], s[36:37] op_sel_hi:[1,1,0]
	s_nop 0
	v_cndmask_b32_e32 v54, v96, v90, vcc
	v_cmp_gt_f32_e32 vcc, 0, v61
	v_pk_fma_f32 v[70:71], v[82:83], v[70:71], s[38:39] op_sel_hi:[1,1,0]
	s_nop 0
	v_cndmask_b32_e32 v55, v81, v79, vcc
	v_cvt_pk_bf16_f32 v79, v62, v64
	v_cvt_pk_bf16_f32 v81, v60, v55
	global_store_dwordx4 v[68:69], v[78:81], off sc1
	v_pk_fma_f32 v[70:71], v[82:83], v[70:71], s[40:41] op_sel_hi:[1,1,0]
	v_cmp_gt_f32_e32 vcc, 0, v51
	v_pk_mul_f32 v[78:79], v[94:95], s[42:43] op_sel_hi:[1,0]
	v_pk_mul_f32 v[70:71], v[82:83], v[70:71]
	v_exp_f32_e32 v78, v78
	v_exp_f32_e32 v79, v79
	v_cndmask_b32_e32 v50, v97, v91, vcc
	v_cmp_gt_f32_e32 vcc, 0, v53
	v_cvt_pk_bf16_f32 v80, v54, v50
	v_pk_mul_f32 v[70:71], v[78:79], v[70:71]
	s_nop 0
	v_pk_mul_f32 v[78:79], v[52:53], v[70:71]
	v_pk_fma_f32 v[70:71], v[52:53], v[70:71], v[52:53] neg_lo:[1,0,0] neg_hi:[1,0,0]
	s_nop 0
	v_cndmask_b32_e32 v53, v71, v79, vcc
	v_cmp_gt_f32_e32 vcc, 0, v52
	v_cvt_pk_bf16_f32 v79, v73, v57
	s_nop 0
	v_cndmask_b32_e32 v52, v70, v78, vcc
	v_cvt_pk_bf16_f32 v78, v75, v63
	v_cvt_pk_bf16_f32 v81, v52, v53
	s_and_b64 vcc, exec, s[10:11]
	global_store_dwordx4 v[68:69], v[78:81], off offset:256 sc1
	s_cbranch_vccnz .LBB0_266
	v_mov_b32_e32 v77, v75
	v_mov_b32_e32 v51, v55
	v_mov_b32_e32 v65, v63
	v_pk_add_f32 v[68:69], v[54:55], v[50:51]
	v_pk_mul_f32 v[70:71], v[54:55], v[50:51]
	v_mov_b32_e32 v78, v76
	v_pk_add_f32 v[82:83], v[74:75], v[76:77]
	v_pk_mul_f32 v[76:77], v[74:75], v[76:77]
	v_mov_b32_e32 v69, v71
	v_mov_b32_e32 v71, v62
	v_mov_b32_e32 v79, v64
	v_mov_b32_e32 v83, v77
	v_pk_add_f32 v[76:77], v[62:63], v[64:65]
	v_pk_mul_f32 v[64:65], v[62:63], v[64:65]
	v_and_b32_e32 v62, 64, v169
	v_xor_b32_e32 v61, 16, v169
	v_add_u32_e32 v62, 64, v62
	v_mov_b32_e32 v70, v74
	v_pk_mul_f32 v[78:79], v[78:79], v[78:79]
	v_mul_f32_e32 v56, v58, v58
	v_cmp_lt_i32_e32 vcc, v61, v62
	v_pk_fma_f32 v[70:71], v[70:71], v[70:71], v[78:79]
	v_pk_fma_f32 v[78:79], v[58:59], v[58:59], v[56:57] op_sel_hi:[1,1,0]
	v_mul_f32_e32 v56, v52, v52
	v_mov_b32_e32 v77, v65
	v_mul_f32_e32 v65, v73, v73
	v_mul_f32_e32 v85, v57, v57
	v_pk_mul_f32 v[86:87], v[54:55], v[54:55]
	v_pk_mul_f32 v[50:51], v[50:51], v[50:51]
	v_cndmask_b32_e32 v61, v169, v61, vcc
	v_mov_b32_e32 v64, v58
	v_mov_b32_e32 v84, v59
	v_pk_fma_f32 v[80:81], v[52:53], v[52:53], v[56:57] op_sel_hi:[1,1,0]
	v_mov_b32_e32 v72, v75
	v_mov_b32_e32 v56, v63
	v_lshlrev_b32_e32 v63, 2, v61
	v_mov_b32_e32 v61, v86
	v_pk_mov_b32 v[50:51], v[54:55], v[50:51] op_sel:[1,0]
	v_pk_add_f32 v[54:55], v[82:83], v[76:77]
	v_pk_add_f32 v[58:59], v[64:65], v[84:85]
	v_pk_add_f32 v[56:57], v[72:73], v[56:57]
	v_pk_add_f32 v[50:51], v[60:61], v[50:51]
	v_pk_add_f32 v[54:55], v[54:55], v[58:59]
	v_mul_f32_e32 v88, v60, v60
	v_pk_add_f32 v[70:71], v[70:71], v[70:71] op_sel_hi:[0,1]
	v_pk_add_f32 v[50:51], v[54:55], v[50:51]
	v_pk_add_f32 v[54:55], v[56:57], v[56:57] op_sel:[0,1] op_sel_hi:[1,0]
	v_mov_b32_e32 v70, v52
	v_mov_b32_e32 v78, v53
	v_mov_b32_e32 v55, v88
	v_mov_b32_e32 v80, v131
	v_pk_add_f32 v[52:53], v[70:71], v[78:79]
	v_pk_add_f32 v[54:55], v[54:55], v[68:69]
	v_pk_add_f32 v[50:51], v[50:51], v[80:81]
	v_pk_add_f32 v[52:53], v[54:55], v[52:53]
	v_xor_b32_e32 v54, 32, v169
	v_pk_add_f32 v[50:51], v[52:53], v[50:51]
	ds_bpermute_b32 v52, v63, v50
	ds_bpermute_b32 v53, v63, v51
	v_cmp_lt_i32_e32 vcc, v54, v62
	s_waitcnt lgkmcnt(0)
	v_pk_add_f32 v[50:51], v[50:51], v[52:53]
	v_cndmask_b32_e32 v54, v169, v54, vcc
	v_lshlrev_b32_e32 v54, 2, v54
	ds_bpermute_b32 v52, v54, v50
	ds_bpermute_b32 v53, v54, v51
	s_and_saveexec_b64 s[0:1], s[6:7]
	s_cbranch_execz .LBB0_265
	s_waitcnt lgkmcnt(0)
	v_pk_add_f32 v[50:51], v[50:51], v[52:53]
	v_lshlrev_b64 v[52:53], 7, v[66:67]
	v_lshl_add_u64 v[52:53], s[12:13], 0, v[52:53]
	global_store_dwordx2 v[52:53], v[50:51], off sc1

; __device__ __forceinline__ unsigned cvt_pk_bf16(float lo, float hi) { f32x2 v = {lo, hi}; bf16x2_t b = __builtin_convertvector(v, bf16x2_t); return __builtin_bit_cast(unsigned, b); }
; __device__ __forceinline__ f32x2 gelu_pk(f32x2 v) {
;     const f32x2 av = __builtin_elementwise_abs(v), d = av * 0.2316418882f + 1.0f;
;     f32x2 t; t.x = __builtin_amdgcn_rcpf(d.x); t.y = __builtin_amdgcn_rcpf(d.y);
;     f32x2 q = t * 0.5307027145f + (-0.7265760135f); q = q * t + 0.7107068705f; q = q * t + (-0.142248368f); q = q * t + 0.127414796f; q = q * t;
;     const f32x2 s = (v * v) * (-0.72134752044f);
;     f32x2 e; e.x = __builtin_amdgcn_exp2f(s.x); e.y = __builtin_amdgcn_exp2f(s.y);
;     const f32x2 m = v * (q * e), r = v - m;
;     f32x2 o; o.x = v.x < 0.f ? m.x : r.x; o.y = v.y < 0.f ? m.y : r.y; return o;
; }
; __device__ __forceinline__ f32x4 gelu4(f32x4 v) { f32x2 a = gelu_pk((f32x2){v[0], v[1]}), b = gelu_pk((f32x2){v[2], v[3]}); return (f32x4){a.x, a.y, b.x, b.y}; }
;     __device__ __forceinline__ void operator()(const AccT& acc, const pg8::Unit& u, int wr, int wc, int fr, int fq) const {
;     ...
;                 for (int m = 0; m < 4; ++m) { const int row = row0 + ai * 128 + m * 16; float s = 0.f, q = 0.f;
; #pragma unroll
;                     for (int bj = 0; bj < 2; ++bj) { const f32x4 v0 = gelu4(acc[ai][bj][m][0]), v1 = gelu4(acc[ai][bj][m][1]);
;                         s += (v0[0] + v0[1]) + (v0[2] + v0[3]) + (v1[0] + v1[1]) + (v1[2] + v1[3]);
;                         q += (v0[0] * v0[0] + v0[1] * v0[1]) + (v0[2] * v0[2] + v0[3] * v0[3]) + (v1[0] * v1[0] + v1[1] * v1[1]) + (v1[2] * v1[2] + v1[3] * v1[3]);
;                         u32x4 w; w.x = cvt_pk_bf16(v0[0], v0[1]); w.y = cvt_pk_bf16(v0[2], v0[3]); w.z = cvt_pk_bf16(v1[0], v1[1]); w.w = cvt_pk_bf16(v1[2], v1[3]);
;                         *(u32x4*)(dst + (size_t)row * GW + col0 + bj * 128) = w; }
.LBB0_266:
	s_waitcnt lgkmcnt(0)
	v_and_b32_e32 v53, 0x7fffffff, v47
	v_and_b32_e32 v52, 0x7fffffff, v46
	v_pk_fma_f32 v[52:53], v[52:53], s[28:29], 1.0 op_sel_hi:[1,0,0]
	v_mov_b64_e32 v[54:55], s[34:35]
	v_rcp_f32_e32 v56, v52
	v_rcp_f32_e32 v57, v53
	v_pk_mul_f32 v[60:61], v[46:47], v[46:47]
	v_and_b32_e32 v63, 0x7fffffff, v49
	v_pk_mul_f32 v[60:61], v[60:61], s[42:43] op_sel_hi:[1,0]
	v_pk_fma_f32 v[58:59], v[56:57], s[30:31], v[54:55] op_sel_hi:[1,0,0]
	v_and_b32_e32 v62, 0x7fffffff, v48
	v_pk_fma_f32 v[58:59], v[56:57], v[58:59], s[36:37] op_sel_hi:[1,1,0]
	v_exp_f32_e32 v60, v60
	v_exp_f32_e32 v61, v61
	v_pk_fma_f32 v[62:63], v[62:63], s[28:29], 1.0 op_sel_hi:[1,0,0]
	v_pk_fma_f32 v[58:59], v[56:57], v[58:59], s[38:39] op_sel_hi:[1,1,0]
	v_rcp_f32_e32 v62, v62
	v_rcp_f32_e32 v63, v63
	v_pk_fma_f32 v[58:59], v[56:57], v[58:59], s[40:41] op_sel_hi:[1,1,0]
	v_and_b32_e32 v65, 0x7fffffff, v45
	v_pk_mul_f32 v[56:57], v[56:57], v[58:59]
	v_pk_mul_f32 v[58:59], v[48:49], v[48:49]
	v_pk_mul_f32 v[56:57], v[60:61], v[56:57]
	v_pk_mul_f32 v[58:59], v[58:59], s[42:43] op_sel_hi:[1,0]
	v_pk_mul_f32 v[60:61], v[46:47], v[56:57]
	v_pk_fma_f32 v[66:67], v[46:47], v[56:57], v[46:47] neg_lo:[1,0,0] neg_hi:[1,0,0]
	v_pk_fma_f32 v[56:57], v[62:63], s[30:31], v[54:55] op_sel_hi:[1,0,0]
	v_exp_f32_e32 v58, v58
	v_pk_fma_f32 v[56:57], v[62:63], v[56:57], s[36:37] op_sel_hi:[1,1,0]
	v_exp_f32_e32 v59, v59
	v_pk_fma_f32 v[56:57], v[62:63], v[56:57], s[38:39] op_sel_hi:[1,1,0]
	v_and_b32_e32 v64, 0x7fffffff, v44
	v_pk_fma_f32 v[56:57], v[62:63], v[56:57], s[40:41] op_sel_hi:[1,1,0]
	v_pk_fma_f32 v[64:65], v[64:65], s[28:29], 1.0 op_sel_hi:[1,0,0]
	v_pk_mul_f32 v[56:57], v[62:63], v[56:57]
	v_and_b32_e32 v63, 0x7fffffff, v43
	v_and_b32_e32 v62, 0x7fffffff, v42
	v_pk_fma_f32 v[62:63], v[62:63], s[28:29], 1.0 op_sel_hi:[1,0,0]
	v_pk_mul_f32 v[56:57], v[58:59], v[56:57]
	v_rcp_f32_e32 v62, v62
	v_rcp_f32_e32 v63, v63
	v_pk_mul_f32 v[58:59], v[42:43], v[42:43]
	v_pk_mul_f32 v[68:69], v[48:49], v[56:57]
	v_pk_fma_f32 v[70:71], v[48:49], v[56:57], v[48:49] neg_lo:[1,0,0] neg_hi:[1,0,0]
	v_pk_fma_f32 v[56:57], v[62:63], s[30:31], v[54:55] op_sel_hi:[1,0,0]
	v_pk_mul_f32 v[58:59], v[58:59], s[42:43] op_sel_hi:[1,0]
	v_pk_fma_f32 v[56:57], v[62:63], v[56:57], s[36:37] op_sel_hi:[1,1,0]
	v_exp_f32_e32 v58, v58
	v_exp_f32_e32 v59, v59
	v_pk_fma_f32 v[56:57], v[62:63], v[56:57], s[38:39] op_sel_hi:[1,1,0]
	v_rcp_f32_e32 v64, v64
	v_pk_fma_f32 v[56:57], v[62:63], v[56:57], s[40:41] op_sel_hi:[1,1,0]
	v_rcp_f32_e32 v65, v65
	v_pk_mul_f32 v[56:57], v[62:63], v[56:57]
	v_cmp_gt_f32_e32 vcc, 0, v43
	v_pk_mul_f32 v[56:57], v[58:59], v[56:57]
	v_pk_mul_f32 v[62:63], v[44:45], v[44:45]
	v_pk_mul_f32 v[58:59], v[42:43], v[56:57]
	v_pk_fma_f32 v[56:57], v[42:43], v[56:57], v[42:43] neg_lo:[1,0,0] neg_hi:[1,0,0]
	v_pk_mul_f32 v[72:73], v[38:39], v[38:39]
	v_cndmask_b32_e32 v43, v57, v59, vcc
	v_cmp_gt_f32_e32 vcc, 0, v42
	v_pk_mul_f32 v[72:73], v[72:73], s[42:43] op_sel_hi:[1,0]
	v_and_b32_e32 v75, 0x7fffffff, v41
	v_cndmask_b32_e32 v42, v56, v58, vcc
	v_pk_fma_f32 v[56:57], v[64:65], s[30:31], v[54:55] op_sel_hi:[1,0,0]
	v_pk_mul_f32 v[58:59], v[62:63], s[42:43] op_sel_hi:[1,0]
	v_pk_fma_f32 v[56:57], v[64:65], v[56:57], s[36:37] op_sel_hi:[1,1,0]
	v_exp_f32_e32 v58, v58
	v_exp_f32_e32 v59, v59
	v_pk_fma_f32 v[56:57], v[64:65], v[56:57], s[38:39] op_sel_hi:[1,1,0]
	v_and_b32_e32 v74, 0x7fffffff, v40
	v_pk_fma_f32 v[56:57], v[64:65], v[56:57], s[40:41] op_sel_hi:[1,1,0]
	v_exp_f32_e32 v72, v72
	v_pk_mul_f32 v[56:57], v[64:65], v[56:57]
	v_exp_f32_e32 v73, v73
	v_pk_mul_f32 v[56:57], v[58:59], v[56:57]
	v_pk_fma_f32 v[74:75], v[74:75], s[28:29], 1.0 op_sel_hi:[1,0,0]
	v_pk_mul_f32 v[62:63], v[44:45], v[56:57]
	v_pk_fma_f32 v[64:65], v[44:45], v[56:57], v[44:45] neg_lo:[1,0,0] neg_hi:[1,0,0]
	v_and_b32_e32 v57, 0x7fffffff, v39
	v_and_b32_e32 v56, 0x7fffffff, v38
	v_pk_fma_f32 v[56:57], v[56:57], s[28:29], 1.0 op_sel_hi:[1,0,0]
	v_rcp_f32_e32 v74, v74
	v_rcp_f32_e32 v56, v56
	v_rcp_f32_e32 v57, v57
	v_rcp_f32_e32 v75, v75
	v_cmp_gt_f32_e32 vcc, 0, v44
	v_add_u32_e32 v50, 0x90, v142
	v_pk_fma_f32 v[58:59], v[56:57], s[30:31], v[54:55] op_sel_hi:[1,0,0]
	v_cndmask_b32_e32 v44, v64, v62, vcc
	v_pk_fma_f32 v[58:59], v[56:57], v[58:59], s[36:37] op_sel_hi:[1,1,0]
	v_cmp_gt_f32_e32 vcc, 0, v40
	v_pk_fma_f32 v[58:59], v[56:57], v[58:59], s[38:39] op_sel_hi:[1,1,0]
	v_ashrrev_i32_e32 v51, 31, v50
	v_pk_fma_f32 v[58:59], v[56:57], v[58:59], s[40:41] op_sel_hi:[1,1,0]
	v_lshlrev_b64 v[52:53], 11, v[50:51]
	v_pk_mul_f32 v[56:57], v[56:57], v[58:59]
	v_pk_mul_f32 v[58:59], v[40:41], v[40:41]
	v_pk_mul_f32 v[56:57], v[72:73], v[56:57]
	v_pk_mul_f32 v[58:59], v[58:59], s[42:43] op_sel_hi:[1,0]
	v_pk_mul_f32 v[72:73], v[38:39], v[56:57]
	v_pk_fma_f32 v[76:77], v[38:39], v[56:57], v[38:39] neg_lo:[1,0,0] neg_hi:[1,0,0]
	v_pk_fma_f32 v[56:57], v[74:75], s[30:31], v[54:55] op_sel_hi:[1,0,0]
	v_exp_f32_e32 v58, v58
	v_pk_fma_f32 v[56:57], v[74:75], v[56:57], s[36:37] op_sel_hi:[1,1,0]
	v_exp_f32_e32 v59, v59
	v_pk_fma_f32 v[56:57], v[74:75], v[56:57], s[38:39] op_sel_hi:[1,1,0]
	v_lshl_add_u64 v[52:53], v[144:145], 0, v[52:53]
	v_pk_fma_f32 v[56:57], v[74:75], v[56:57], s[40:41] op_sel_hi:[1,1,0]
	v_cvt_pk_bf16_f32 v64, v42, v43
	v_pk_mul_f32 v[56:57], v[74:75], v[56:57]
	s_nop 0
	v_pk_mul_f32 v[56:57], v[58:59], v[56:57]
	s_nop 0
	v_pk_mul_f32 v[58:59], v[40:41], v[56:57]
	v_pk_fma_f32 v[74:75], v[40:41], v[56:57], v[40:41] neg_lo:[1,0,0] neg_hi:[1,0,0]
	v_and_b32_e32 v57, 0x7fffffff, v35
	v_and_b32_e32 v56, 0x7fffffff, v34
; __device__ __forceinline__ unsigned cvt_pk_bf16(float lo, float hi) { f32x2 v = {lo, hi}; bf16x2_t b = __builtin_convertvector(v, bf16x2_t); return __builtin_bit_cast(unsigned, b); }
; __device__ __forceinline__ f32x4 gelu4(f32x4 v) { f32x2 a = gelu_pk((f32x2){v[0], v[1]}), b = gelu_pk((f32x2){v[2], v[3]}); return (f32x4){a.x, a.y, b.x, b.y}; }
;     __device__ __forceinline__ void operator()(const AccT& acc, const pg8::Unit& u, int wr, int wc, int fr, int fq) const {
;     ...
;                 for (int m = 0; m < 4; ++m) { const int row = row0 + ai * 128 + m * 16; float s = 0.f, q = 0.f;
; #pragma unroll
;                     for (int bj = 0; bj < 2; ++bj) { const f32x4 v0 = gelu4(acc[ai][bj][m][0]), v1 = gelu4(acc[ai][bj][m][1]);
;                         s += (v0[0] + v0[1]) + (v0[2] + v0[3]) + (v1[0] + v1[1]) + (v1[2] + v1[3]);
;                         q += (v0[0] * v0[0] + v0[1] * v0[1]) + (v0[2] * v0[2] + v0[3] * v0[3]) + (v1[0] * v1[0] + v1[1] * v1[1]) + (v1[2] * v1[2] + v1[3] * v1[3]);
;                         u32x4 w; w.x = cvt_pk_bf16(v0[0], v0[1]); w.y = cvt_pk_bf16(v0[2], v0[3]); w.z = cvt_pk_bf16(v1[0], v1[1]); w.w = cvt_pk_bf16(v1[2], v1[3]);
;                         *(u32x4*)(dst + (size_t)row * GW + col0 + bj * 128) = w; }
;                     if (pn >= 4) { s += __shfl_xor(s, 16); s += __shfl_xor(s, 32); q += __shfl_xor(q, 16); q += __shfl_xor(q, 32);
;                         if (fq == 0) *(f32x2*)(vstat + (size_t)row * 32 + ((pn - 4) * 4 + wc) * 2) = (f32x2){s, q}; } }
	v_pk_fma_f32 v[56:57], v[56:57], s[28:29], 1.0 op_sel_hi:[1,0,0]
	s_nop 0
	v_rcp_f32_e32 v78, v56
	v_rcp_f32_e32 v79, v57
	v_cndmask_b32_e32 v57, v74, v58, vcc
	v_cmp_gt_f32_e32 vcc, 0, v41
	s_nop 1
	v_cndmask_b32_e32 v41, v75, v59, vcc
	v_pk_mul_f32 v[74:75], v[34:35], v[34:35]
	v_pk_fma_f32 v[58:59], v[78:79], s[30:31], v[54:55] op_sel_hi:[1,0,0]
	v_pk_mul_f32 v[74:75], v[74:75], s[42:43] op_sel_hi:[1,0]
	v_pk_fma_f32 v[58:59], v[78:79], v[58:59], s[36:37] op_sel_hi:[1,1,0]
	v_exp_f32_e32 v74, v74
	v_exp_f32_e32 v75, v75
	v_pk_fma_f32 v[58:59], v[78:79], v[58:59], s[38:39] op_sel_hi:[1,1,0]
	v_cmp_gt_f32_e32 vcc, 0, v46
	v_pk_fma_f32 v[58:59], v[78:79], v[58:59], s[40:41] op_sel_hi:[1,1,0]
	s_nop 0
	v_pk_mul_f32 v[58:59], v[78:79], v[58:59]
	v_pk_mul_f32 v[78:79], v[36:37], v[36:37]
	v_pk_mul_f32 v[58:59], v[74:75], v[58:59]
	s_nop 0
	v_pk_mul_f32 v[74:75], v[34:35], v[58:59]
	v_pk_fma_f32 v[80:81], v[34:35], v[58:59], v[34:35] neg_lo:[1,0,0] neg_hi:[1,0,0]
	v_cndmask_b32_e32 v58, v66, v60, vcc
	v_cmp_gt_f32_e32 vcc, 0, v38
	v_and_b32_e32 v66, 0x7fffffff, v36
	s_nop 0
	v_cndmask_b32_e32 v59, v76, v72, vcc
	v_cmp_gt_f32_e32 vcc, 0, v47
	s_nop 1
	v_cndmask_b32_e32 v60, v67, v61, vcc
	v_cmp_gt_f32_e32 vcc, 0, v48
	v_and_b32_e32 v67, 0x7fffffff, v37
	v_pk_fma_f32 v[66:67], v[66:67], s[28:29], 1.0 op_sel_hi:[1,0,0]
	v_cndmask_b32_e32 v46, v70, v68, vcc
	v_cmp_gt_f32_e32 vcc, 0, v39
	v_rcp_f32_e32 v66, v66
	v_rcp_f32_e32 v67, v67
	v_cndmask_b32_e32 v47, v77, v73, vcc
	v_cmp_gt_f32_e32 vcc, 0, v49
	v_cvt_pk_bf16_f32 v62, v58, v60
	v_pk_fma_f32 v[54:55], v[66:67], s[30:31], v[54:55] op_sel_hi:[1,0,0]
	v_cndmask_b32_e32 v48, v71, v69, vcc
	v_cmp_gt_f32_e32 vcc, 0, v34
	v_pk_fma_f32 v[54:55], v[66:67], v[54:55], s[36:37] op_sel_hi:[1,1,0]
	s_nop 0
	v_cndmask_b32_e32 v38, v80, v74, vcc
	v_cmp_gt_f32_e32 vcc, 0, v45
	v_pk_fma_f32 v[54:55], v[66:67], v[54:55], s[38:39] op_sel_hi:[1,1,0]
	s_nop 0
	v_cndmask_b32_e32 v39, v65, v63, vcc
	v_cvt_pk_bf16_f32 v63, v46, v48
	v_cvt_pk_bf16_f32 v65, v44, v39
	global_store_dwordx4 v[52:53], v[62:65], off sc1
	v_pk_fma_f32 v[54:55], v[66:67], v[54:55], s[40:41] op_sel_hi:[1,1,0]
	v_cmp_gt_f32_e32 vcc, 0, v35
	v_pk_mul_f32 v[62:63], v[78:79], s[42:43] op_sel_hi:[1,0]
	v_pk_mul_f32 v[54:55], v[66:67], v[54:55]
	v_exp_f32_e32 v62, v62
	v_exp_f32_e32 v63, v63
	v_cndmask_b32_e32 v34, v81, v75, vcc
	v_cmp_gt_f32_e32 vcc, 0, v37
	v_cvt_pk_bf16_f32 v64, v38, v34
	v_pk_mul_f32 v[54:55], v[62:63], v[54:55]
	s_nop 0
	v_pk_mul_f32 v[62:63], v[36:37], v[54:55]
	v_pk_fma_f32 v[54:55], v[36:37], v[54:55], v[36:37] neg_lo:[1,0,0] neg_hi:[1,0,0]
	s_nop 0
	v_cndmask_b32_e32 v37, v55, v63, vcc
	v_cmp_gt_f32_e32 vcc, 0, v36
	v_cvt_pk_bf16_f32 v63, v57, v41
	s_nop 0
	v_cndmask_b32_e32 v36, v54, v62, vcc
	v_cvt_pk_bf16_f32 v62, v59, v47
	v_cvt_pk_bf16_f32 v65, v36, v37
	s_and_b64 vcc, exec, s[10:11]
	global_store_dwordx4 v[52:53], v[62:65], off offset:256 sc1
	s_cbranch_vccnz .LBB0_270
	v_mov_b32_e32 v61, v59
	v_mov_b32_e32 v35, v39
	v_mov_b32_e32 v49, v47
	v_pk_add_f32 v[52:53], v[38:39], v[34:35]
	v_pk_mul_f32 v[54:55], v[38:39], v[34:35]
	v_mov_b32_e32 v62, v60
	v_pk_add_f32 v[66:67], v[58:59], v[60:61]
	v_pk_mul_f32 v[60:61], v[58:59], v[60:61]
	v_mov_b32_e32 v53, v55
	v_mov_b32_e32 v55, v46
	v_mov_b32_e32 v63, v48
	v_mov_b32_e32 v67, v61
	v_pk_add_f32 v[60:61], v[46:47], v[48:49]
	v_pk_mul_f32 v[48:49], v[46:47], v[48:49]
	v_and_b32_e32 v46, 64, v169
	v_xor_b32_e32 v45, 16, v169
	v_add_u32_e32 v46, 64, v46
	v_mov_b32_e32 v54, v58
	v_pk_mul_f32 v[62:63], v[62:63], v[62:63]
	v_mul_f32_e32 v40, v42, v42
	v_cmp_lt_i32_e32 vcc, v45, v46
	v_pk_fma_f32 v[54:55], v[54:55], v[54:55], v[62:63]
	v_pk_fma_f32 v[62:63], v[42:43], v[42:43], v[40:41] op_sel_hi:[1,1,0]
	v_mul_f32_e32 v40, v36, v36
	v_mov_b32_e32 v61, v49
	v_mul_f32_e32 v49, v57, v57
	v_mul_f32_e32 v69, v41, v41
	v_pk_mul_f32 v[70:71], v[38:39], v[38:39]
	v_pk_mul_f32 v[34:35], v[34:35], v[34:35]
	v_cndmask_b32_e32 v45, v169, v45, vcc
	v_mov_b32_e32 v48, v42
	v_mov_b32_e32 v68, v43
	v_pk_fma_f32 v[64:65], v[36:37], v[36:37], v[40:41] op_sel_hi:[1,1,0]
	v_mov_b32_e32 v56, v59
	v_mov_b32_e32 v40, v47
	v_lshlrev_b32_e32 v47, 2, v45
	v_mov_b32_e32 v45, v70
	v_pk_mov_b32 v[34:35], v[38:39], v[34:35] op_sel:[1,0]
	v_pk_add_f32 v[38:39], v[66:67], v[60:61]
	v_pk_add_f32 v[42:43], v[48:49], v[68:69]
	v_pk_add_f32 v[40:41], v[56:57], v[40:41]
	v_pk_add_f32 v[34:35], v[44:45], v[34:35]
	v_pk_add_f32 v[38:39], v[38:39], v[42:43]
	v_mul_f32_e32 v72, v44, v44
	v_pk_add_f32 v[54:55], v[54:55], v[54:55] op_sel_hi:[0,1]
	v_pk_add_f32 v[34:35], v[38:39], v[34:35]
	v_pk_add_f32 v[38:39], v[40:41], v[40:41] op_sel:[0,1] op_sel_hi:[1,0]
	v_mov_b32_e32 v54, v36
	v_mov_b32_e32 v62, v37
	v_mov_b32_e32 v39, v72
	v_mov_b32_e32 v64, v131
	v_pk_add_f32 v[36:37], v[54:55], v[62:63]
	v_pk_add_f32 v[38:39], v[38:39], v[52:53]
	v_pk_add_f32 v[34:35], v[34:35], v[64:65]
	v_pk_add_f32 v[36:37], v[38:39], v[36:37]
	v_xor_b32_e32 v38, 32, v169
	v_pk_add_f32 v[34:35], v[36:37], v[34:35]
	ds_bpermute_b32 v36, v47, v34
	ds_bpermute_b32 v37, v47, v35
	v_cmp_lt_i32_e32 vcc, v38, v46
	s_waitcnt lgkmcnt(0)
	v_pk_add_f32 v[34:35], v[34:35], v[36:37]
	v_cndmask_b32_e32 v38, v169, v38, vcc
	v_lshlrev_b32_e32 v38, 2, v38
	ds_bpermute_b32 v36, v38, v34
	ds_bpermute_b32 v37, v38, v35
	s_and_saveexec_b64 s[0:1], s[6:7]
	s_cbranch_execz .LBB0_269
	s_waitcnt lgkmcnt(0)
	v_pk_add_f32 v[34:35], v[34:35], v[36:37]
	v_lshlrev_b64 v[36:37], 7, v[50:51]
	v_lshl_add_u64 v[36:37], s[12:13], 0, v[36:37]
	global_store_dwordx2 v[36:37], v[34:35], off sc1

; __device__ __forceinline__ unsigned cvt_pk_bf16(float lo, float hi) { f32x2 v = {lo, hi}; bf16x2_t b = __builtin_convertvector(v, bf16x2_t); return __builtin_bit_cast(unsigned, b); }
; __device__ __forceinline__ f32x2 gelu_pk(f32x2 v) {
;     const f32x2 av = __builtin_elementwise_abs(v), d = av * 0.2316418882f + 1.0f;
;     f32x2 t; t.x = __builtin_amdgcn_rcpf(d.x); t.y = __builtin_amdgcn_rcpf(d.y);
;     f32x2 q = t * 0.5307027145f + (-0.7265760135f); q = q * t + 0.7107068705f; q = q * t + (-0.142248368f); q = q * t + 0.127414796f; q = q * t;
;     const f32x2 s = (v * v) * (-0.72134752044f);
;     f32x2 e; e.x = __builtin_amdgcn_exp2f(s.x); e.y = __builtin_amdgcn_exp2f(s.y);
;     const f32x2 m = v * (q * e), r = v - m;
;     f32x2 o; o.x = v.x < 0.f ? m.x : r.x; o.y = v.y < 0.f ? m.y : r.y; return o;
; }
; __device__ __forceinline__ f32x4 gelu4(f32x4 v) { f32x2 a = gelu_pk((f32x2){v[0], v[1]}), b = gelu_pk((f32x2){v[2], v[3]}); return (f32x4){a.x, a.y, b.x, b.y}; }
;     __device__ __forceinline__ void operator()(const AccT& acc, const pg8::Unit& u, int wr, int wc, int fr, int fq) const {
;     ...
;                 for (int m = 0; m < 4; ++m) { const int row = row0 + ai * 128 + m * 16; float s = 0.f, q = 0.f;
; #pragma unroll
;                     for (int bj = 0; bj < 2; ++bj) { const f32x4 v0 = gelu4(acc[ai][bj][m][0]), v1 = gelu4(acc[ai][bj][m][1]);
;                         s += (v0[0] + v0[1]) + (v0[2] + v0[3]) + (v1[0] + v1[1]) + (v1[2] + v1[3]);
;                         q += (v0[0] * v0[0] + v0[1] * v0[1]) + (v0[2] * v0[2] + v0[3] * v0[3]) + (v1[0] * v1[0] + v1[1] * v1[1]) + (v1[2] * v1[2] + v1[3] * v1[3]);
;                         u32x4 w; w.x = cvt_pk_bf16(v0[0], v0[1]); w.y = cvt_pk_bf16(v0[2], v0[3]); w.z = cvt_pk_bf16(v1[0], v1[1]); w.w = cvt_pk_bf16(v1[2], v1[3]);
;                         *(u32x4*)(dst + (size_t)row * GW + col0 + bj * 128) = w; }
.LBB0_270:
	s_waitcnt lgkmcnt(0)
	v_and_b32_e32 v37, 0x7fffffff, v31
	v_and_b32_e32 v36, 0x7fffffff, v30
	v_pk_fma_f32 v[36:37], v[36:37], s[28:29], 1.0 op_sel_hi:[1,0,0]
	v_mov_b64_e32 v[38:39], s[34:35]
	v_rcp_f32_e32 v40, v36
	v_rcp_f32_e32 v41, v37
	v_pk_mul_f32 v[44:45], v[30:31], v[30:31]
	v_and_b32_e32 v47, 0x7fffffff, v33
	v_pk_mul_f32 v[44:45], v[44:45], s[42:43] op_sel_hi:[1,0]
	v_pk_fma_f32 v[42:43], v[40:41], s[30:31], v[38:39] op_sel_hi:[1,0,0]
	v_and_b32_e32 v46, 0x7fffffff, v32
	v_pk_fma_f32 v[42:43], v[40:41], v[42:43], s[36:37] op_sel_hi:[1,1,0]
	v_exp_f32_e32 v44, v44
	v_exp_f32_e32 v45, v45
	v_pk_fma_f32 v[46:47], v[46:47], s[28:29], 1.0 op_sel_hi:[1,0,0]
	v_pk_fma_f32 v[42:43], v[40:41], v[42:43], s[38:39] op_sel_hi:[1,1,0]
	v_rcp_f32_e32 v46, v46
	v_rcp_f32_e32 v47, v47
	v_pk_fma_f32 v[42:43], v[40:41], v[42:43], s[40:41] op_sel_hi:[1,1,0]
	v_and_b32_e32 v49, 0x7fffffff, v29
	v_pk_mul_f32 v[40:41], v[40:41], v[42:43]
	v_pk_mul_f32 v[42:43], v[32:33], v[32:33]
	v_pk_mul_f32 v[40:41], v[44:45], v[40:41]
	v_pk_mul_f32 v[42:43], v[42:43], s[42:43] op_sel_hi:[1,0]
	v_pk_mul_f32 v[44:45], v[30:31], v[40:41]
	v_pk_fma_f32 v[50:51], v[30:31], v[40:41], v[30:31] neg_lo:[1,0,0] neg_hi:[1,0,0]
	v_pk_fma_f32 v[40:41], v[46:47], s[30:31], v[38:39] op_sel_hi:[1,0,0]
	v_exp_f32_e32 v42, v42
	v_pk_fma_f32 v[40:41], v[46:47], v[40:41], s[36:37] op_sel_hi:[1,1,0]
	v_exp_f32_e32 v43, v43
	v_pk_fma_f32 v[40:41], v[46:47], v[40:41], s[38:39] op_sel_hi:[1,1,0]
	v_and_b32_e32 v48, 0x7fffffff, v28
	v_pk_fma_f32 v[40:41], v[46:47], v[40:41], s[40:41] op_sel_hi:[1,1,0]
	v_pk_fma_f32 v[48:49], v[48:49], s[28:29], 1.0 op_sel_hi:[1,0,0]
	v_pk_mul_f32 v[40:41], v[46:47], v[40:41]
	v_and_b32_e32 v47, 0x7fffffff, v27
	v_and_b32_e32 v46, 0x7fffffff, v26
	v_pk_fma_f32 v[46:47], v[46:47], s[28:29], 1.0 op_sel_hi:[1,0,0]
	v_pk_mul_f32 v[40:41], v[42:43], v[40:41]
	v_rcp_f32_e32 v46, v46
	v_rcp_f32_e32 v47, v47
	v_pk_mul_f32 v[42:43], v[26:27], v[26:27]
	v_pk_mul_f32 v[52:53], v[32:33], v[40:41]
	v_pk_fma_f32 v[54:55], v[32:33], v[40:41], v[32:33] neg_lo:[1,0,0] neg_hi:[1,0,0]
	v_pk_fma_f32 v[40:41], v[46:47], s[30:31], v[38:39] op_sel_hi:[1,0,0]
	v_pk_mul_f32 v[42:43], v[42:43], s[42:43] op_sel_hi:[1,0]
	v_pk_fma_f32 v[40:41], v[46:47], v[40:41], s[36:37] op_sel_hi:[1,1,0]
	v_exp_f32_e32 v42, v42
	v_exp_f32_e32 v43, v43
	v_pk_fma_f32 v[40:41], v[46:47], v[40:41], s[38:39] op_sel_hi:[1,1,0]
	v_rcp_f32_e32 v48, v48
	v_pk_fma_f32 v[40:41], v[46:47], v[40:41], s[40:41] op_sel_hi:[1,1,0]
	v_rcp_f32_e32 v49, v49
	v_pk_mul_f32 v[40:41], v[46:47], v[40:41]
	v_cmp_gt_f32_e32 vcc, 0, v27
	v_pk_mul_f32 v[40:41], v[42:43], v[40:41]
	v_pk_mul_f32 v[46:47], v[28:29], v[28:29]
	v_pk_mul_f32 v[42:43], v[26:27], v[40:41]
	v_pk_fma_f32 v[40:41], v[26:27], v[40:41], v[26:27] neg_lo:[1,0,0] neg_hi:[1,0,0]
	v_pk_mul_f32 v[56:57], v[22:23], v[22:23]
	v_cndmask_b32_e32 v27, v41, v43, vcc
	v_cmp_gt_f32_e32 vcc, 0, v26
	v_pk_mul_f32 v[56:57], v[56:57], s[42:43] op_sel_hi:[1,0]
	v_and_b32_e32 v59, 0x7fffffff, v25
	v_cndmask_b32_e32 v26, v40, v42, vcc
	v_pk_fma_f32 v[40:41], v[48:49], s[30:31], v[38:39] op_sel_hi:[1,0,0]
	v_pk_mul_f32 v[42:43], v[46:47], s[42:43] op_sel_hi:[1,0]
	v_pk_fma_f32 v[40:41], v[48:49], v[40:41], s[36:37] op_sel_hi:[1,1,0]
	v_exp_f32_e32 v42, v42
	v_exp_f32_e32 v43, v43
	v_pk_fma_f32 v[40:41], v[48:49], v[40:41], s[38:39] op_sel_hi:[1,1,0]
	v_and_b32_e32 v58, 0x7fffffff, v24
	v_pk_fma_f32 v[40:41], v[48:49], v[40:41], s[40:41] op_sel_hi:[1,1,0]
	v_exp_f32_e32 v56, v56
	v_pk_mul_f32 v[40:41], v[48:49], v[40:41]
	v_exp_f32_e32 v57, v57
	v_pk_mul_f32 v[40:41], v[42:43], v[40:41]
	v_pk_fma_f32 v[58:59], v[58:59], s[28:29], 1.0 op_sel_hi:[1,0,0]
	v_pk_mul_f32 v[46:47], v[28:29], v[40:41]
	v_pk_fma_f32 v[48:49], v[28:29], v[40:41], v[28:29] neg_lo:[1,0,0] neg_hi:[1,0,0]
	v_and_b32_e32 v41, 0x7fffffff, v23
	v_and_b32_e32 v40, 0x7fffffff, v22
	v_pk_fma_f32 v[40:41], v[40:41], s[28:29], 1.0 op_sel_hi:[1,0,0]
	v_rcp_f32_e32 v58, v58
	v_rcp_f32_e32 v40, v40
	v_rcp_f32_e32 v41, v41
	v_rcp_f32_e32 v59, v59
	v_cmp_gt_f32_e32 vcc, 0, v28
	v_add_u32_e32 v34, 0xa0, v142
	v_pk_fma_f32 v[42:43], v[40:41], s[30:31], v[38:39] op_sel_hi:[1,0,0]
	v_cndmask_b32_e32 v28, v48, v46, vcc
	v_pk_fma_f32 v[42:43], v[40:41], v[42:43], s[36:37] op_sel_hi:[1,1,0]
	v_cmp_gt_f32_e32 vcc, 0, v24
	v_pk_fma_f32 v[42:43], v[40:41], v[42:43], s[38:39] op_sel_hi:[1,1,0]
	v_ashrrev_i32_e32 v35, 31, v34
	v_pk_fma_f32 v[42:43], v[40:41], v[42:43], s[40:41] op_sel_hi:[1,1,0]
	v_lshlrev_b64 v[36:37], 11, v[34:35]
	v_pk_mul_f32 v[40:41], v[40:41], v[42:43]
	v_pk_mul_f32 v[42:43], v[24:25], v[24:25]
	v_pk_mul_f32 v[40:41], v[56:57], v[40:41]
	v_pk_mul_f32 v[42:43], v[42:43], s[42:43] op_sel_hi:[1,0]
	v_pk_mul_f32 v[56:57], v[22:23], v[40:41]
	v_pk_fma_f32 v[60:61], v[22:23], v[40:41], v[22:23] neg_lo:[1,0,0] neg_hi:[1,0,0]
	v_pk_fma_f32 v[40:41], v[58:59], s[30:31], v[38:39] op_sel_hi:[1,0,0]
	v_exp_f32_e32 v42, v42
	v_pk_fma_f32 v[40:41], v[58:59], v[40:41], s[36:37] op_sel_hi:[1,1,0]
	v_exp_f32_e32 v43, v43
	v_pk_fma_f32 v[40:41], v[58:59], v[40:41], s[38:39] op_sel_hi:[1,1,0]
	v_lshl_add_u64 v[36:37], v[144:145], 0, v[36:37]
	v_pk_fma_f32 v[40:41], v[58:59], v[40:41], s[40:41] op_sel_hi:[1,1,0]
	v_cvt_pk_bf16_f32 v48, v26, v27
	v_pk_mul_f32 v[40:41], v[58:59], v[40:41]
	s_nop 0
	v_pk_mul_f32 v[40:41], v[42:43], v[40:41]
	s_nop 0
	v_pk_mul_f32 v[42:43], v[24:25], v[40:41]
	v_pk_fma_f32 v[58:59], v[24:25], v[40:41], v[24:25] neg_lo:[1,0,0] neg_hi:[1,0,0]
	v_and_b32_e32 v41, 0x7fffffff, v19
	v_and_b32_e32 v40, 0x7fffffff, v18
; __device__ __forceinline__ unsigned cvt_pk_bf16(float lo, float hi) { f32x2 v = {lo, hi}; bf16x2_t b = __builtin_convertvector(v, bf16x2_t); return __builtin_bit_cast(unsigned, b); }
; __device__ __forceinline__ f32x4 gelu4(f32x4 v) { f32x2 a = gelu_pk((f32x2){v[0], v[1]}), b = gelu_pk((f32x2){v[2], v[3]}); return (f32x4){a.x, a.y, b.x, b.y}; }
;     __device__ __forceinline__ void operator()(const AccT& acc, const pg8::Unit& u, int wr, int wc, int fr, int fq) const {
;     ...
;                 for (int m = 0; m < 4; ++m) { const int row = row0 + ai * 128 + m * 16; float s = 0.f, q = 0.f;
; #pragma unroll
;                     for (int bj = 0; bj < 2; ++bj) { const f32x4 v0 = gelu4(acc[ai][bj][m][0]), v1 = gelu4(acc[ai][bj][m][1]);
;                         s += (v0[0] + v0[1]) + (v0[2] + v0[3]) + (v1[0] + v1[1]) + (v1[2] + v1[3]);
;                         q += (v0[0] * v0[0] + v0[1] * v0[1]) + (v0[2] * v0[2] + v0[3] * v0[3]) + (v1[0] * v1[0] + v1[1] * v1[1]) + (v1[2] * v1[2] + v1[3] * v1[3]);
;                         u32x4 w; w.x = cvt_pk_bf16(v0[0], v0[1]); w.y = cvt_pk_bf16(v0[2], v0[3]); w.z = cvt_pk_bf16(v1[0], v1[1]); w.w = cvt_pk_bf16(v1[2], v1[3]);
;                         *(u32x4*)(dst + (size_t)row * GW + col0 + bj * 128) = w; }
;                     if (pn >= 4) { s += __shfl_xor(s, 16); s += __shfl_xor(s, 32); q += __shfl_xor(q, 16); q += __shfl_xor(q, 32);
;                         if (fq == 0) *(f32x2*)(vstat + (size_t)row * 32 + ((pn - 4) * 4 + wc) * 2) = (f32x2){s, q}; } }
	v_pk_fma_f32 v[40:41], v[40:41], s[28:29], 1.0 op_sel_hi:[1,0,0]
	s_nop 0
	v_rcp_f32_e32 v62, v40
	v_rcp_f32_e32 v63, v41
	v_cndmask_b32_e32 v41, v58, v42, vcc
	v_cmp_gt_f32_e32 vcc, 0, v25
	s_nop 1
	v_cndmask_b32_e32 v25, v59, v43, vcc
	v_pk_mul_f32 v[58:59], v[18:19], v[18:19]
	v_pk_fma_f32 v[42:43], v[62:63], s[30:31], v[38:39] op_sel_hi:[1,0,0]
	v_pk_mul_f32 v[58:59], v[58:59], s[42:43] op_sel_hi:[1,0]
	v_pk_fma_f32 v[42:43], v[62:63], v[42:43], s[36:37] op_sel_hi:[1,1,0]
	v_exp_f32_e32 v58, v58
	v_exp_f32_e32 v59, v59
	v_pk_fma_f32 v[42:43], v[62:63], v[42:43], s[38:39] op_sel_hi:[1,1,0]
	v_cmp_gt_f32_e32 vcc, 0, v30
	v_pk_fma_f32 v[42:43], v[62:63], v[42:43], s[40:41] op_sel_hi:[1,1,0]
	s_nop 0
	v_pk_mul_f32 v[42:43], v[62:63], v[42:43]
	v_pk_mul_f32 v[62:63], v[20:21], v[20:21]
	v_pk_mul_f32 v[42:43], v[58:59], v[42:43]
	s_nop 0
	v_pk_mul_f32 v[58:59], v[18:19], v[42:43]
	v_pk_fma_f32 v[64:65], v[18:19], v[42:43], v[18:19] neg_lo:[1,0,0] neg_hi:[1,0,0]
	v_cndmask_b32_e32 v42, v50, v44, vcc
	v_cmp_gt_f32_e32 vcc, 0, v22
	v_and_b32_e32 v50, 0x7fffffff, v20
	s_nop 0
	v_cndmask_b32_e32 v43, v60, v56, vcc
	v_cmp_gt_f32_e32 vcc, 0, v31
	s_nop 1
	v_cndmask_b32_e32 v44, v51, v45, vcc
	v_cmp_gt_f32_e32 vcc, 0, v32
	v_and_b32_e32 v51, 0x7fffffff, v21
	v_pk_fma_f32 v[50:51], v[50:51], s[28:29], 1.0 op_sel_hi:[1,0,0]
	v_cndmask_b32_e32 v30, v54, v52, vcc
	v_cmp_gt_f32_e32 vcc, 0, v23
	v_rcp_f32_e32 v50, v50
	v_rcp_f32_e32 v51, v51
	v_cndmask_b32_e32 v31, v61, v57, vcc
	v_cmp_gt_f32_e32 vcc, 0, v33
	v_cvt_pk_bf16_f32 v46, v42, v44
	v_pk_fma_f32 v[38:39], v[50:51], s[30:31], v[38:39] op_sel_hi:[1,0,0]
	v_cndmask_b32_e32 v32, v55, v53, vcc
	v_cmp_gt_f32_e32 vcc, 0, v18
	v_pk_fma_f32 v[38:39], v[50:51], v[38:39], s[36:37] op_sel_hi:[1,1,0]
	s_nop 0
	v_cndmask_b32_e32 v22, v64, v58, vcc
	v_cmp_gt_f32_e32 vcc, 0, v29
	v_pk_fma_f32 v[38:39], v[50:51], v[38:39], s[38:39] op_sel_hi:[1,1,0]
	s_nop 0
	v_cndmask_b32_e32 v23, v49, v47, vcc
	v_cvt_pk_bf16_f32 v47, v30, v32
	v_cvt_pk_bf16_f32 v49, v28, v23
	global_store_dwordx4 v[36:37], v[46:49], off sc1
	v_pk_fma_f32 v[38:39], v[50:51], v[38:39], s[40:41] op_sel_hi:[1,1,0]
	v_cmp_gt_f32_e32 vcc, 0, v19
	v_pk_mul_f32 v[46:47], v[62:63], s[42:43] op_sel_hi:[1,0]
	v_pk_mul_f32 v[38:39], v[50:51], v[38:39]
	v_exp_f32_e32 v46, v46
	v_exp_f32_e32 v47, v47
	v_cndmask_b32_e32 v18, v65, v59, vcc
	v_cmp_gt_f32_e32 vcc, 0, v21
	v_cvt_pk_bf16_f32 v48, v22, v18
	v_pk_mul_f32 v[38:39], v[46:47], v[38:39]
	s_nop 0
	v_pk_mul_f32 v[46:47], v[20:21], v[38:39]
	v_pk_fma_f32 v[38:39], v[20:21], v[38:39], v[20:21] neg_lo:[1,0,0] neg_hi:[1,0,0]
	s_nop 0
	v_cndmask_b32_e32 v21, v39, v47, vcc
	v_cmp_gt_f32_e32 vcc, 0, v20
	v_cvt_pk_bf16_f32 v47, v41, v25
	s_nop 0
	v_cndmask_b32_e32 v20, v38, v46, vcc
	v_cvt_pk_bf16_f32 v46, v43, v31
	v_cvt_pk_bf16_f32 v49, v20, v21
	s_and_b64 vcc, exec, s[10:11]
	global_store_dwordx4 v[36:37], v[46:49], off offset:256 sc1
	s_cbranch_vccnz .LBB0_274
	v_mov_b32_e32 v45, v43
	v_mov_b32_e32 v19, v23
	v_mov_b32_e32 v33, v31
	v_pk_add_f32 v[36:37], v[22:23], v[18:19]
	v_pk_mul_f32 v[38:39], v[22:23], v[18:19]
	v_mov_b32_e32 v46, v44
	v_pk_add_f32 v[50:51], v[42:43], v[44:45]
	v_pk_mul_f32 v[44:45], v[42:43], v[44:45]
	v_mov_b32_e32 v37, v39
	v_mov_b32_e32 v39, v30
	v_mov_b32_e32 v47, v32
	v_mov_b32_e32 v51, v45
	v_pk_add_f32 v[44:45], v[30:31], v[32:33]
	v_pk_mul_f32 v[32:33], v[30:31], v[32:33]
	v_and_b32_e32 v30, 64, v169
	v_xor_b32_e32 v29, 16, v169
	v_add_u32_e32 v30, 64, v30
	v_mov_b32_e32 v38, v42
	v_pk_mul_f32 v[46:47], v[46:47], v[46:47]
	v_mul_f32_e32 v24, v26, v26
	v_cmp_lt_i32_e32 vcc, v29, v30
	v_pk_fma_f32 v[38:39], v[38:39], v[38:39], v[46:47]
	v_pk_fma_f32 v[46:47], v[26:27], v[26:27], v[24:25] op_sel_hi:[1,1,0]
	v_mul_f32_e32 v24, v20, v20
	v_mov_b32_e32 v45, v33
	v_mul_f32_e32 v33, v41, v41
	v_mul_f32_e32 v53, v25, v25
	v_pk_mul_f32 v[54:55], v[22:23], v[22:23]
	v_pk_mul_f32 v[18:19], v[18:19], v[18:19]
	v_cndmask_b32_e32 v29, v169, v29, vcc
	v_mov_b32_e32 v32, v26
	v_mov_b32_e32 v52, v27
	v_pk_fma_f32 v[48:49], v[20:21], v[20:21], v[24:25] op_sel_hi:[1,1,0]
	v_mov_b32_e32 v40, v43
	v_mov_b32_e32 v24, v31
	v_lshlrev_b32_e32 v31, 2, v29
	v_mov_b32_e32 v29, v54
	v_pk_mov_b32 v[18:19], v[22:23], v[18:19] op_sel:[1,0]
	v_pk_add_f32 v[22:23], v[50:51], v[44:45]
	v_pk_add_f32 v[26:27], v[32:33], v[52:53]
	v_pk_add_f32 v[24:25], v[40:41], v[24:25]
	v_pk_add_f32 v[18:19], v[28:29], v[18:19]
	v_pk_add_f32 v[22:23], v[22:23], v[26:27]
	v_mul_f32_e32 v56, v28, v28
	v_pk_add_f32 v[38:39], v[38:39], v[38:39] op_sel_hi:[0,1]
	v_pk_add_f32 v[18:19], v[22:23], v[18:19]
	v_pk_add_f32 v[22:23], v[24:25], v[24:25] op_sel:[0,1] op_sel_hi:[1,0]
	v_mov_b32_e32 v38, v20
	v_mov_b32_e32 v46, v21
	v_mov_b32_e32 v23, v56
	v_mov_b32_e32 v48, v131
	v_pk_add_f32 v[20:21], v[38:39], v[46:47]
	v_pk_add_f32 v[22:23], v[22:23], v[36:37]
	v_pk_add_f32 v[18:19], v[18:19], v[48:49]
	v_pk_add_f32 v[20:21], v[22:23], v[20:21]
	v_xor_b32_e32 v22, 32, v169
	v_pk_add_f32 v[18:19], v[20:21], v[18:19]
	ds_bpermute_b32 v20, v31, v18
	ds_bpermute_b32 v21, v31, v19
	v_cmp_lt_i32_e32 vcc, v22, v30
	s_waitcnt lgkmcnt(0)
	v_pk_add_f32 v[18:19], v[18:19], v[20:21]
	v_cndmask_b32_e32 v22, v169, v22, vcc
	v_lshlrev_b32_e32 v22, 2, v22
	ds_bpermute_b32 v20, v22, v18
	ds_bpermute_b32 v21, v22, v19
	s_and_saveexec_b64 s[0:1], s[6:7]
	s_cbranch_execz .LBB0_273
	s_waitcnt lgkmcnt(0)
	v_pk_add_f32 v[18:19], v[18:19], v[20:21]
	v_lshlrev_b64 v[20:21], 7, v[34:35]
	v_lshl_add_u64 v[20:21], s[12:13], 0, v[20:21]
	global_store_dwordx2 v[20:21], v[18:19], off sc1

; __device__ __forceinline__ unsigned cvt_pk_bf16(float lo, float hi) { f32x2 v = {lo, hi}; bf16x2_t b = __builtin_convertvector(v, bf16x2_t); return __builtin_bit_cast(unsigned, b); }
; __device__ __forceinline__ f32x2 gelu_pk(f32x2 v) {
;     const f32x2 av = __builtin_elementwise_abs(v), d = av * 0.2316418882f + 1.0f;
;     f32x2 t; t.x = __builtin_amdgcn_rcpf(d.x); t.y = __builtin_amdgcn_rcpf(d.y);
;     f32x2 q = t * 0.5307027145f + (-0.7265760135f); q = q * t + 0.7107068705f; q = q * t + (-0.142248368f); q = q * t + 0.127414796f; q = q * t;
;     const f32x2 s = (v * v) * (-0.72134752044f);
;     f32x2 e; e.x = __builtin_amdgcn_exp2f(s.x); e.y = __builtin_amdgcn_exp2f(s.y);
;     const f32x2 m = v * (q * e), r = v - m;
;     f32x2 o; o.x = v.x < 0.f ? m.x : r.x; o.y = v.y < 0.f ? m.y : r.y; return o;
; }
; __device__ __forceinline__ f32x4 gelu4(f32x4 v) { f32x2 a = gelu_pk((f32x2){v[0], v[1]}), b = gelu_pk((f32x2){v[2], v[3]}); return (f32x4){a.x, a.y, b.x, b.y}; }
;     __device__ __forceinline__ void operator()(const AccT& acc, const pg8::Unit& u, int wr, int wc, int fr, int fq) const {
;     ...
;                 for (int m = 0; m < 4; ++m) { const int row = row0 + ai * 128 + m * 16; float s = 0.f, q = 0.f;
; #pragma unroll
;                     for (int bj = 0; bj < 2; ++bj) { const f32x4 v0 = gelu4(acc[ai][bj][m][0]), v1 = gelu4(acc[ai][bj][m][1]);
;                         s += (v0[0] + v0[1]) + (v0[2] + v0[3]) + (v1[0] + v1[1]) + (v1[2] + v1[3]);
;                         q += (v0[0] * v0[0] + v0[1] * v0[1]) + (v0[2] * v0[2] + v0[3] * v0[3]) + (v1[0] * v1[0] + v1[1] * v1[1]) + (v1[2] * v1[2] + v1[3] * v1[3]);
;                         u32x4 w; w.x = cvt_pk_bf16(v0[0], v0[1]); w.y = cvt_pk_bf16(v0[2], v0[3]); w.z = cvt_pk_bf16(v1[0], v1[1]); w.w = cvt_pk_bf16(v1[2], v1[3]);
;                         *(u32x4*)(dst + (size_t)row * GW + col0 + bj * 128) = w; }
.LBB0_274:
	s_waitcnt lgkmcnt(0)
	v_and_b32_e32 v21, 0x7fffffff, v15
	v_and_b32_e32 v20, 0x7fffffff, v14
	v_pk_fma_f32 v[20:21], v[20:21], s[28:29], 1.0 op_sel_hi:[1,0,0]
	v_mov_b64_e32 v[22:23], s[34:35]
	v_rcp_f32_e32 v24, v20
	v_rcp_f32_e32 v25, v21
	v_pk_mul_f32 v[28:29], v[14:15], v[14:15]
	v_and_b32_e32 v31, 0x7fffffff, v17
	v_pk_mul_f32 v[28:29], v[28:29], s[42:43] op_sel_hi:[1,0]
	v_pk_fma_f32 v[26:27], v[24:25], s[30:31], v[22:23] op_sel_hi:[1,0,0]
	v_and_b32_e32 v30, 0x7fffffff, v16
	v_pk_fma_f32 v[26:27], v[24:25], v[26:27], s[36:37] op_sel_hi:[1,1,0]
	v_exp_f32_e32 v28, v28
	v_exp_f32_e32 v29, v29
	v_pk_fma_f32 v[30:31], v[30:31], s[28:29], 1.0 op_sel_hi:[1,0,0]
	v_pk_fma_f32 v[26:27], v[24:25], v[26:27], s[38:39] op_sel_hi:[1,1,0]
	v_rcp_f32_e32 v30, v30
	v_rcp_f32_e32 v31, v31
	v_pk_fma_f32 v[26:27], v[24:25], v[26:27], s[40:41] op_sel_hi:[1,1,0]
	v_and_b32_e32 v33, 0x7fffffff, v13
	v_pk_mul_f32 v[24:25], v[24:25], v[26:27]
	v_pk_mul_f32 v[26:27], v[16:17], v[16:17]
	v_pk_mul_f32 v[24:25], v[28:29], v[24:25]
	v_pk_mul_f32 v[26:27], v[26:27], s[42:43] op_sel_hi:[1,0]
	v_pk_mul_f32 v[28:29], v[14:15], v[24:25]
	v_pk_fma_f32 v[34:35], v[14:15], v[24:25], v[14:15] neg_lo:[1,0,0] neg_hi:[1,0,0]
	v_pk_fma_f32 v[24:25], v[30:31], s[30:31], v[22:23] op_sel_hi:[1,0,0]
	v_exp_f32_e32 v26, v26
	v_pk_fma_f32 v[24:25], v[30:31], v[24:25], s[36:37] op_sel_hi:[1,1,0]
	v_exp_f32_e32 v27, v27
	v_pk_fma_f32 v[24:25], v[30:31], v[24:25], s[38:39] op_sel_hi:[1,1,0]
	v_and_b32_e32 v32, 0x7fffffff, v12
	v_pk_fma_f32 v[24:25], v[30:31], v[24:25], s[40:41] op_sel_hi:[1,1,0]
	v_pk_fma_f32 v[32:33], v[32:33], s[28:29], 1.0 op_sel_hi:[1,0,0]
	v_pk_mul_f32 v[24:25], v[30:31], v[24:25]
	v_and_b32_e32 v31, 0x7fffffff, v11
	v_and_b32_e32 v30, 0x7fffffff, v10
	v_pk_fma_f32 v[30:31], v[30:31], s[28:29], 1.0 op_sel_hi:[1,0,0]
	v_pk_mul_f32 v[24:25], v[26:27], v[24:25]
	v_rcp_f32_e32 v30, v30
	v_rcp_f32_e32 v31, v31
	v_pk_mul_f32 v[26:27], v[10:11], v[10:11]
	v_pk_mul_f32 v[36:37], v[16:17], v[24:25]
	v_pk_fma_f32 v[38:39], v[16:17], v[24:25], v[16:17] neg_lo:[1,0,0] neg_hi:[1,0,0]
	v_pk_fma_f32 v[24:25], v[30:31], s[30:31], v[22:23] op_sel_hi:[1,0,0]
	v_pk_mul_f32 v[26:27], v[26:27], s[42:43] op_sel_hi:[1,0]
	v_pk_fma_f32 v[24:25], v[30:31], v[24:25], s[36:37] op_sel_hi:[1,1,0]
	v_exp_f32_e32 v26, v26
	v_exp_f32_e32 v27, v27
	v_pk_fma_f32 v[24:25], v[30:31], v[24:25], s[38:39] op_sel_hi:[1,1,0]
	v_rcp_f32_e32 v32, v32
	v_pk_fma_f32 v[24:25], v[30:31], v[24:25], s[40:41] op_sel_hi:[1,1,0]
	v_rcp_f32_e32 v33, v33
	v_pk_mul_f32 v[24:25], v[30:31], v[24:25]
	v_cmp_gt_f32_e32 vcc, 0, v11
	v_pk_mul_f32 v[24:25], v[26:27], v[24:25]
	v_pk_mul_f32 v[30:31], v[12:13], v[12:13]
	v_pk_mul_f32 v[26:27], v[10:11], v[24:25]
	v_pk_fma_f32 v[24:25], v[10:11], v[24:25], v[10:11] neg_lo:[1,0,0] neg_hi:[1,0,0]
	v_pk_mul_f32 v[40:41], v[6:7], v[6:7]
	v_cndmask_b32_e32 v11, v25, v27, vcc
	v_cmp_gt_f32_e32 vcc, 0, v10
	v_pk_mul_f32 v[40:41], v[40:41], s[42:43] op_sel_hi:[1,0]
	v_and_b32_e32 v43, 0x7fffffff, v9
	v_cndmask_b32_e32 v10, v24, v26, vcc
	v_pk_fma_f32 v[24:25], v[32:33], s[30:31], v[22:23] op_sel_hi:[1,0,0]
	v_pk_mul_f32 v[26:27], v[30:31], s[42:43] op_sel_hi:[1,0]
	v_pk_fma_f32 v[24:25], v[32:33], v[24:25], s[36:37] op_sel_hi:[1,1,0]
	v_exp_f32_e32 v26, v26
	v_exp_f32_e32 v27, v27
	v_pk_fma_f32 v[24:25], v[32:33], v[24:25], s[38:39] op_sel_hi:[1,1,0]
	v_and_b32_e32 v42, 0x7fffffff, v8
	v_pk_fma_f32 v[24:25], v[32:33], v[24:25], s[40:41] op_sel_hi:[1,1,0]
	v_exp_f32_e32 v40, v40
	v_pk_mul_f32 v[24:25], v[32:33], v[24:25]
	v_exp_f32_e32 v41, v41
	v_pk_mul_f32 v[24:25], v[26:27], v[24:25]
	v_pk_fma_f32 v[42:43], v[42:43], s[28:29], 1.0 op_sel_hi:[1,0,0]
	v_pk_mul_f32 v[30:31], v[12:13], v[24:25]
	v_pk_fma_f32 v[32:33], v[12:13], v[24:25], v[12:13] neg_lo:[1,0,0] neg_hi:[1,0,0]
	v_and_b32_e32 v25, 0x7fffffff, v7
	v_and_b32_e32 v24, 0x7fffffff, v6
	v_pk_fma_f32 v[24:25], v[24:25], s[28:29], 1.0 op_sel_hi:[1,0,0]
	v_rcp_f32_e32 v42, v42
	v_rcp_f32_e32 v24, v24
	v_rcp_f32_e32 v25, v25
	v_rcp_f32_e32 v43, v43
	v_cmp_gt_f32_e32 vcc, 0, v12
	v_add_u32_e32 v18, 0xb0, v142
	v_pk_fma_f32 v[26:27], v[24:25], s[30:31], v[22:23] op_sel_hi:[1,0,0]
	v_cndmask_b32_e32 v12, v32, v30, vcc
	v_pk_fma_f32 v[26:27], v[24:25], v[26:27], s[36:37] op_sel_hi:[1,1,0]
	v_cmp_gt_f32_e32 vcc, 0, v8
	v_pk_fma_f32 v[26:27], v[24:25], v[26:27], s[38:39] op_sel_hi:[1,1,0]
	v_ashrrev_i32_e32 v19, 31, v18
	v_pk_fma_f32 v[26:27], v[24:25], v[26:27], s[40:41] op_sel_hi:[1,1,0]
	v_lshlrev_b64 v[20:21], 11, v[18:19]
	v_pk_mul_f32 v[24:25], v[24:25], v[26:27]
	v_pk_mul_f32 v[26:27], v[8:9], v[8:9]
	v_pk_mul_f32 v[24:25], v[40:41], v[24:25]
	v_pk_mul_f32 v[26:27], v[26:27], s[42:43] op_sel_hi:[1,0]
	v_pk_mul_f32 v[40:41], v[6:7], v[24:25]
	v_pk_fma_f32 v[44:45], v[6:7], v[24:25], v[6:7] neg_lo:[1,0,0] neg_hi:[1,0,0]
	v_pk_fma_f32 v[24:25], v[42:43], s[30:31], v[22:23] op_sel_hi:[1,0,0]
	v_exp_f32_e32 v26, v26
	v_pk_fma_f32 v[24:25], v[42:43], v[24:25], s[36:37] op_sel_hi:[1,1,0]
	v_exp_f32_e32 v27, v27
	v_pk_fma_f32 v[24:25], v[42:43], v[24:25], s[38:39] op_sel_hi:[1,1,0]
	v_lshl_add_u64 v[20:21], v[144:145], 0, v[20:21]
	v_pk_fma_f32 v[24:25], v[42:43], v[24:25], s[40:41] op_sel_hi:[1,1,0]
	v_cvt_pk_bf16_f32 v32, v10, v11
	v_pk_mul_f32 v[24:25], v[42:43], v[24:25]
	s_nop 0
	v_pk_mul_f32 v[24:25], v[26:27], v[24:25]
	s_nop 0
	v_pk_mul_f32 v[26:27], v[8:9], v[24:25]
	v_pk_fma_f32 v[42:43], v[8:9], v[24:25], v[8:9] neg_lo:[1,0,0] neg_hi:[1,0,0]
; __device__ __forceinline__ unsigned cvt_pk_bf16(float lo, float hi) { f32x2 v = {lo, hi}; bf16x2_t b = __builtin_convertvector(v, bf16x2_t); return __builtin_bit_cast(unsigned, b); }
; __device__ __forceinline__ f32x4 gelu4(f32x4 v) { f32x2 a = gelu_pk((f32x2){v[0], v[1]}), b = gelu_pk((f32x2){v[2], v[3]}); return (f32x4){a.x, a.y, b.x, b.y}; }
;     __device__ __forceinline__ void operator()(const AccT& acc, const pg8::Unit& u, int wr, int wc, int fr, int fq) const {
;     ...
;                 for (int m = 0; m < 4; ++m) { const int row = row0 + ai * 128 + m * 16; float s = 0.f, q = 0.f;
; #pragma unroll
;                     for (int bj = 0; bj < 2; ++bj) { const f32x4 v0 = gelu4(acc[ai][bj][m][0]), v1 = gelu4(acc[ai][bj][m][1]);
;                         s += (v0[0] + v0[1]) + (v0[2] + v0[3]) + (v1[0] + v1[1]) + (v1[2] + v1[3]);
;                         q += (v0[0] * v0[0] + v0[1] * v0[1]) + (v0[2] * v0[2] + v0[3] * v0[3]) + (v1[0] * v1[0] + v1[1] * v1[1]) + (v1[2] * v1[2] + v1[3] * v1[3]);
;                         u32x4 w; w.x = cvt_pk_bf16(v0[0], v0[1]); w.y = cvt_pk_bf16(v0[2], v0[3]); w.z = cvt_pk_bf16(v1[0], v1[1]); w.w = cvt_pk_bf16(v1[2], v1[3]);
;                         *(u32x4*)(dst + (size_t)row * GW + col0 + bj * 128) = w; }
;                     if (pn >= 4) { s += __shfl_xor(s, 16); s += __shfl_xor(s, 32); q += __shfl_xor(q, 16); q += __shfl_xor(q, 32);
;                         if (fq == 0) *(f32x2*)(vstat + (size_t)row * 32 + ((pn - 4) * 4 + wc) * 2) = (f32x2){s, q}; } }
	v_and_b32_e32 v25, 0x7fffffff, v3
	v_and_b32_e32 v24, 0x7fffffff, v2
	v_pk_fma_f32 v[24:25], v[24:25], s[28:29], 1.0 op_sel_hi:[1,0,0]
	s_nop 0
	v_rcp_f32_e32 v46, v24
	v_rcp_f32_e32 v47, v25
	v_cndmask_b32_e32 v25, v42, v26, vcc
	v_cmp_gt_f32_e32 vcc, 0, v9
	s_nop 1
	v_cndmask_b32_e32 v9, v43, v27, vcc
	v_pk_mul_f32 v[42:43], v[2:3], v[2:3]
	v_pk_fma_f32 v[26:27], v[46:47], s[30:31], v[22:23] op_sel_hi:[1,0,0]
	v_pk_mul_f32 v[42:43], v[42:43], s[42:43] op_sel_hi:[1,0]
	v_pk_fma_f32 v[26:27], v[46:47], v[26:27], s[36:37] op_sel_hi:[1,1,0]
	v_exp_f32_e32 v42, v42
	v_exp_f32_e32 v43, v43
	v_pk_fma_f32 v[26:27], v[46:47], v[26:27], s[38:39] op_sel_hi:[1,1,0]
	v_cmp_gt_f32_e32 vcc, 0, v14
	v_pk_fma_f32 v[26:27], v[46:47], v[26:27], s[40:41] op_sel_hi:[1,1,0]
	s_nop 0
	v_pk_mul_f32 v[26:27], v[46:47], v[26:27]
	v_pk_mul_f32 v[46:47], v[4:5], v[4:5]
	v_pk_mul_f32 v[26:27], v[42:43], v[26:27]
	s_nop 0
	v_pk_mul_f32 v[42:43], v[2:3], v[26:27]
	v_pk_fma_f32 v[48:49], v[2:3], v[26:27], v[2:3] neg_lo:[1,0,0] neg_hi:[1,0,0]
	v_cndmask_b32_e32 v26, v34, v28, vcc
	v_cmp_gt_f32_e32 vcc, 0, v6
	v_and_b32_e32 v34, 0x7fffffff, v4
	s_nop 0
	v_cndmask_b32_e32 v27, v44, v40, vcc
	v_cmp_gt_f32_e32 vcc, 0, v15
	s_nop 1
	v_cndmask_b32_e32 v28, v35, v29, vcc
	v_cmp_gt_f32_e32 vcc, 0, v16
	v_and_b32_e32 v35, 0x7fffffff, v5
	v_pk_fma_f32 v[34:35], v[34:35], s[28:29], 1.0 op_sel_hi:[1,0,0]
	v_cndmask_b32_e32 v14, v38, v36, vcc
	v_cmp_gt_f32_e32 vcc, 0, v7
	v_rcp_f32_e32 v34, v34
	v_rcp_f32_e32 v35, v35
	v_cndmask_b32_e32 v15, v45, v41, vcc
	v_cmp_gt_f32_e32 vcc, 0, v17
	v_cvt_pk_bf16_f32 v30, v26, v28
	v_pk_fma_f32 v[22:23], v[34:35], s[30:31], v[22:23] op_sel_hi:[1,0,0]
	v_cndmask_b32_e32 v16, v39, v37, vcc
	v_cmp_gt_f32_e32 vcc, 0, v2
	v_pk_fma_f32 v[22:23], v[34:35], v[22:23], s[36:37] op_sel_hi:[1,1,0]
	s_nop 0
	v_cndmask_b32_e32 v6, v48, v42, vcc
	v_cmp_gt_f32_e32 vcc, 0, v13
	v_pk_fma_f32 v[22:23], v[34:35], v[22:23], s[38:39] op_sel_hi:[1,1,0]
	s_nop 0
	v_cndmask_b32_e32 v7, v33, v31, vcc
	v_cvt_pk_bf16_f32 v31, v14, v16
	v_cvt_pk_bf16_f32 v33, v12, v7
	global_store_dwordx4 v[20:21], v[30:33], off sc1
	v_pk_fma_f32 v[22:23], v[34:35], v[22:23], s[40:41] op_sel_hi:[1,1,0]
	v_cmp_gt_f32_e32 vcc, 0, v3
	v_pk_mul_f32 v[30:31], v[46:47], s[42:43] op_sel_hi:[1,0]
	v_pk_mul_f32 v[22:23], v[34:35], v[22:23]
	v_exp_f32_e32 v30, v30
	v_exp_f32_e32 v31, v31
	v_cndmask_b32_e32 v2, v49, v43, vcc
	v_cmp_gt_f32_e32 vcc, 0, v5
	v_cvt_pk_bf16_f32 v32, v6, v2
	v_pk_mul_f32 v[22:23], v[30:31], v[22:23]
	s_nop 0
	v_pk_mul_f32 v[30:31], v[4:5], v[22:23]
	v_pk_fma_f32 v[22:23], v[4:5], v[22:23], v[4:5] neg_lo:[1,0,0] neg_hi:[1,0,0]
	s_nop 0
	v_cndmask_b32_e32 v5, v23, v31, vcc
	v_cmp_gt_f32_e32 vcc, 0, v4
	v_cvt_pk_bf16_f32 v31, v25, v9
	s_nop 0
	v_cndmask_b32_e32 v4, v22, v30, vcc
	v_cvt_pk_bf16_f32 v30, v27, v15
	v_cvt_pk_bf16_f32 v33, v4, v5
	s_and_b64 vcc, exec, s[10:11]
	global_store_dwordx4 v[20:21], v[30:33], off offset:256 sc1
	s_cbranch_vccnz .LBB0_278
	v_mov_b32_e32 v29, v27
	v_mov_b32_e32 v3, v7
	v_mov_b32_e32 v17, v15
	v_pk_add_f32 v[20:21], v[6:7], v[2:3]
	v_pk_mul_f32 v[22:23], v[6:7], v[2:3]
	v_mov_b32_e32 v30, v28
	v_pk_add_f32 v[34:35], v[26:27], v[28:29]
	v_pk_mul_f32 v[28:29], v[26:27], v[28:29]
	v_mov_b32_e32 v21, v23
	v_mov_b32_e32 v23, v14
	v_mov_b32_e32 v31, v16
	v_mov_b32_e32 v35, v29
	v_pk_add_f32 v[28:29], v[14:15], v[16:17]
	v_pk_mul_f32 v[16:17], v[14:15], v[16:17]
	v_and_b32_e32 v14, 64, v169
	v_xor_b32_e32 v13, 16, v169
	v_add_u32_e32 v14, 64, v14
	v_mov_b32_e32 v22, v26
	v_pk_mul_f32 v[30:31], v[30:31], v[30:31]
	v_mul_f32_e32 v8, v10, v10
	v_cmp_lt_i32_e32 vcc, v13, v14
	v_pk_fma_f32 v[22:23], v[22:23], v[22:23], v[30:31]
	v_pk_fma_f32 v[30:31], v[10:11], v[10:11], v[8:9] op_sel_hi:[1,1,0]
	v_mul_f32_e32 v8, v4, v4
	v_mov_b32_e32 v29, v17
	v_mul_f32_e32 v17, v25, v25
	v_mul_f32_e32 v37, v9, v9
	v_pk_mul_f32 v[38:39], v[6:7], v[6:7]
	v_pk_mul_f32 v[2:3], v[2:3], v[2:3]
	v_cndmask_b32_e32 v13, v169, v13, vcc
	v_mov_b32_e32 v16, v10
	v_mov_b32_e32 v36, v11
	v_pk_fma_f32 v[32:33], v[4:5], v[4:5], v[8:9] op_sel_hi:[1,1,0]
	v_mov_b32_e32 v24, v27
	v_mov_b32_e32 v8, v15
	v_lshlrev_b32_e32 v15, 2, v13
	v_mov_b32_e32 v13, v38
	v_pk_mov_b32 v[2:3], v[6:7], v[2:3] op_sel:[1,0]
	v_pk_add_f32 v[6:7], v[34:35], v[28:29]
	v_pk_add_f32 v[10:11], v[16:17], v[36:37]
	v_pk_add_f32 v[8:9], v[24:25], v[8:9]
	v_pk_add_f32 v[2:3], v[12:13], v[2:3]
	v_pk_add_f32 v[6:7], v[6:7], v[10:11]
	v_mul_f32_e32 v40, v12, v12
	v_pk_add_f32 v[22:23], v[22:23], v[22:23] op_sel_hi:[0,1]
	v_pk_add_f32 v[2:3], v[6:7], v[2:3]
	v_pk_add_f32 v[6:7], v[8:9], v[8:9] op_sel:[0,1] op_sel_hi:[1,0]
	v_mov_b32_e32 v22, v4
	v_mov_b32_e32 v30, v5
	v_mov_b32_e32 v7, v40
	v_mov_b32_e32 v32, v131
	v_pk_add_f32 v[4:5], v[22:23], v[30:31]
	v_pk_add_f32 v[6:7], v[6:7], v[20:21]
	v_pk_add_f32 v[2:3], v[2:3], v[32:33]
	v_pk_add_f32 v[4:5], v[6:7], v[4:5]
	v_xor_b32_e32 v6, 32, v169
	v_pk_add_f32 v[2:3], v[4:5], v[2:3]
	ds_bpermute_b32 v4, v15, v2
	ds_bpermute_b32 v5, v15, v3
	v_cmp_lt_i32_e32 vcc, v6, v14
	s_waitcnt lgkmcnt(0)
	v_pk_add_f32 v[2:3], v[2:3], v[4:5]
	v_cndmask_b32_e32 v6, v169, v6, vcc
	v_lshlrev_b32_e32 v6, 2, v6
	ds_bpermute_b32 v4, v6, v2
	ds_bpermute_b32 v5, v6, v3
	s_and_saveexec_b64 s[0:1], s[6:7]
	s_cbranch_execz .LBB0_277
	s_waitcnt lgkmcnt(0)
	v_pk_add_f32 v[2:3], v[2:3], v[4:5]
	v_lshlrev_b64 v[4:5], 7, v[18:19]
	v_lshl_add_u64 v[4:5], s[12:13], 0, v[4:5]
	global_store_dwordx2 v[4:5], v[2:3], off sc1

; #define LAS __attribute__((address_space(3)))
; __device__ __forceinline__ unsigned cvt_pk_bf16(float lo, float hi) { f32x2 v = {lo, hi}; bf16x2_t b = __builtin_convertvector(v, bf16x2_t); return __builtin_bit_cast(unsigned, b); }
; __device__ __forceinline__ float bf_lo(unsigned w) { return __uint_as_float(w << 16); }
; __device__ __forceinline__ float bf_hi(unsigned w) { return __uint_as_float(w & 0xffff0000u); }
; __device__ __forceinline__ void spatial_unit(Frame& F, const Args& a, int n, int g) {
;     ...
;     {
;         LAS unsigned char* MT = F.lds + 66560;
;         const int t = 16 * w + (lane & 15); const float bias = a.in[6][g * 128 + t];
; #pragma unroll
;         for (int c = 0; c < 8; ++c) *(LAS f32x4*)(MT + t * 528 + (16 * c + 4 * (lane >> 4)) * 4) = acc[c] + bias;
;         __syncthreads();
;         u32x4 uu[4];
; #pragma unroll
;         for (int i = 0; i < 4; ++i) uu[i] = __builtin_nontemporal_load((const u32x4*)(U + (size_t)(t0 + (tid >> 4) + 32 * i) * GW + ch0 + 8 * (tid & 15)));
; #pragma unroll
;         for (int i = 0; i < 4; ++i) { const int tt = (tid >> 4) + 32 * i, ch = tid & 15;
;             const f32x4 m0 = *(const LAS f32x4*)(MT + tt * 528 + ch * 32), m1 = *(const LAS f32x4*)(MT + tt * 528 + ch * 32 + 16);
;             const u32x4 u4 = uu[i];
;             u32x4 r; r.x = cvt_pk_bf16(bf_lo(u4.x) * m0[0], bf_hi(u4.x) * m0[1]); r.y = cvt_pk_bf16(bf_lo(u4.y) * m0[2], bf_hi(u4.y) * m0[3]);
;             r.z = cvt_pk_bf16(bf_lo(u4.z) * m1[0], bf_hi(u4.z) * m1[1]); r.w = cvt_pk_bf16(bf_lo(u4.w) * m1[2], bf_hi(u4.w) * m1[3]);
;             *(u32x4*)(SG + (size_t)(t0 + tt) * GW + ch0 + 8 * ch) = r; }
;     }
;     __syncthreads();
.LBB0_339:
	v_add_u32_e32 v132, s0, v105
	v_ashrrev_i32_e32 v133, 31, v132
	v_lshl_add_u64 v[132:133], v[132:133], 2, s[78:79]
	global_load_dword v132, v[132:133], off
	s_lshl_b32 s76, s0, 1
	s_add_i32 s92, s92, s4
	s_add_i32 s91, s91, s90
	s_cmpk_lt_i32 s92, 0x400
	s_waitcnt vmcnt(0)
	v_pk_add_f32 v[6:7], v[6:7], v[132:133] op_sel_hi:[1,0]
	v_pk_add_f32 v[4:5], v[4:5], v[132:133] op_sel_hi:[1,0]
	ds_write_b128 v114, v[4:7] offset:448
	v_lshl_add_u64 v[4:5], v[54:55], 0, s[76:77]
	v_pk_add_f32 v[34:35], v[34:35], v[132:133] op_sel_hi:[1,0]
	v_pk_add_f32 v[32:33], v[32:33], v[132:133] op_sel_hi:[1,0]
	v_pk_add_f32 v[30:31], v[30:31], v[132:133] op_sel_hi:[1,0]
	v_pk_add_f32 v[28:29], v[28:29], v[132:133] op_sel_hi:[1,0]
	v_pk_add_f32 v[26:27], v[26:27], v[132:133] op_sel_hi:[1,0]
	v_pk_add_f32 v[24:25], v[24:25], v[132:133] op_sel_hi:[1,0]
	v_pk_add_f32 v[22:23], v[22:23], v[132:133] op_sel_hi:[1,0]
	v_pk_add_f32 v[20:21], v[20:21], v[132:133] op_sel_hi:[1,0]
	v_pk_add_f32 v[18:19], v[18:19], v[132:133] op_sel_hi:[1,0]
	v_pk_add_f32 v[16:17], v[16:17], v[132:133] op_sel_hi:[1,0]
	v_pk_add_f32 v[14:15], v[14:15], v[132:133] op_sel_hi:[1,0]
	v_pk_add_f32 v[12:13], v[12:13], v[132:133] op_sel_hi:[1,0]
	v_pk_add_f32 v[10:11], v[10:11], v[132:133] op_sel_hi:[1,0]
	v_pk_add_f32 v[8:9], v[8:9], v[132:133] op_sel_hi:[1,0]
	v_lshl_add_u64 v[6:7], v[4:5], 0, v[58:59]
	ds_write_b128 v114, v[32:35]
	ds_write_b128 v114, v[28:31] offset:64
	ds_write_b128 v114, v[24:27] offset:128
	ds_write_b128 v114, v[20:23] offset:192
	ds_write_b128 v114, v[16:19] offset:256
	ds_write_b128 v114, v[12:15] offset:320
	ds_write_b128 v114, v[8:11] offset:384
	s_waitcnt lgkmcnt(0)
	s_barrier
	global_load_dwordx4 v[10:13], v[6:7], off nt
	v_lshl_add_u64 v[6:7], v[4:5], 0, v[60:61]
	global_load_dwordx4 v[14:17], v[6:7], off nt
	v_lshl_add_u64 v[6:7], v[4:5], 0, v[62:63]
	global_load_dwordx4 v[18:21], v[6:7], off nt
	v_lshl_add_u64 v[4:5], v[4:5], 0, v[64:65]
	global_load_dwordx4 v[4:7], v[4:5], off nt
	ds_read_b128 v[22:25], v115
	ds_read_b128 v[26:29], v115 offset:16
	v_lshl_add_u64 v[8:9], v[56:57], 0, s[76:77]
	s_waitcnt vmcnt(3)
	v_lshlrev_b32_e32 v30, 16, v10
	v_and_b32_e32 v31, 0xffff0000, v10
	s_waitcnt lgkmcnt(1)
	v_pk_mul_f32 v[22:23], v[22:23], v[30:31]
	s_nop 0
	v_cvt_pk_bf16_f32 v10, v22, v23
	v_lshlrev_b32_e32 v22, 16, v11
	v_and_b32_e32 v23, 0xffff0000, v11
	v_pk_mul_f32 v[22:23], v[24:25], v[22:23]
	s_nop 0
	v_cvt_pk_bf16_f32 v11, v22, v23
	v_lshlrev_b32_e32 v22, 16, v12
	v_and_b32_e32 v23, 0xffff0000, v12
	s_waitcnt lgkmcnt(0)
	v_pk_mul_f32 v[22:23], v[26:27], v[22:23]
	s_waitcnt vmcnt(2)
	v_lshlrev_b32_e32 v26, 16, v14
	v_cvt_pk_bf16_f32 v12, v22, v23
	v_lshlrev_b32_e32 v22, 16, v13
	v_and_b32_e32 v23, 0xffff0000, v13
	v_pk_mul_f32 v[22:23], v[28:29], v[22:23]
	v_and_b32_e32 v27, 0xffff0000, v14
	v_cvt_pk_bf16_f32 v13, v22, v23
	v_lshl_add_u64 v[22:23], v[8:9], 0, v[58:59]
	global_store_dwordx4 v[22:23], v[10:13], off sc1
	ds_read_b128 v[10:13], v115 offset:16896
	ds_read_b128 v[22:25], v115 offset:16912
	v_lshlrev_b32_e32 v14, 16, v15
	v_and_b32_e32 v15, 0xffff0000, v15
	s_waitcnt lgkmcnt(1)
	v_pk_mul_f32 v[10:11], v[10:11], v[26:27]
	v_pk_mul_f32 v[12:13], v[12:13], v[14:15]
	v_cvt_pk_bf16_f32 v10, v10, v11
	v_cvt_pk_bf16_f32 v11, v12, v13
	v_lshlrev_b32_e32 v12, 16, v16
	v_and_b32_e32 v13, 0xffff0000, v16
	v_lshlrev_b32_e32 v14, 16, v17
	v_and_b32_e32 v15, 0xffff0000, v17
	s_waitcnt lgkmcnt(0)
	v_pk_mul_f32 v[12:13], v[22:23], v[12:13]
	v_pk_mul_f32 v[14:15], v[24:25], v[14:15]
	v_cvt_pk_bf16_f32 v12, v12, v13
	v_cvt_pk_bf16_f32 v13, v14, v15
	v_add_u32_e32 v14, s93, v84
	v_ashrrev_i32_e32 v15, 31, v14
	v_lshlrev_b64 v[14:15], 11, v[14:15]
	v_lshl_add_u64 v[14:15], v[8:9], 0, v[14:15]
	global_store_dwordx4 v[14:15], v[10:13], off sc1
	ds_read_b128 v[10:13], v115 offset:33792
	ds_read_b128 v[14:17], v115 offset:33808
	s_waitcnt vmcnt(3)
	v_lshlrev_b32_e32 v22, 16, v18
	v_and_b32_e32 v23, 0xffff0000, v18
	v_lshlrev_b32_e32 v18, 16, v19
	v_and_b32_e32 v19, 0xffff0000, v19
	s_waitcnt lgkmcnt(1)
	v_pk_mul_f32 v[10:11], v[10:11], v[22:23]
	v_pk_mul_f32 v[12:13], v[12:13], v[18:19]
	v_cvt_pk_bf16_f32 v10, v10, v11
	v_cvt_pk_bf16_f32 v11, v12, v13
	v_lshlrev_b32_e32 v12, 16, v20
	v_and_b32_e32 v13, 0xffff0000, v20
	s_waitcnt lgkmcnt(0)
	v_pk_mul_f32 v[12:13], v[14:15], v[12:13]
	v_lshlrev_b32_e32 v14, 16, v21
	v_and_b32_e32 v15, 0xffff0000, v21
	v_pk_mul_f32 v[14:15], v[16:17], v[14:15]
	v_cvt_pk_bf16_f32 v12, v12, v13
	v_cvt_pk_bf16_f32 v13, v14, v15
	v_add_u32_e32 v14, s93, v83
	v_ashrrev_i32_e32 v15, 31, v14
	v_lshlrev_b64 v[14:15], 11, v[14:15]
	v_lshl_add_u64 v[14:15], v[8:9], 0, v[14:15]
	global_store_dwordx4 v[14:15], v[10:13], off sc1
	ds_read_b128 v[10:13], v115 offset:50688
	ds_read_b128 v[14:17], v115 offset:50704
	s_waitcnt vmcnt(3)
	v_lshlrev_b32_e32 v18, 16, v4
	v_and_b32_e32 v19, 0xffff0000, v4
	s_waitcnt lgkmcnt(1)
	v_pk_mul_f32 v[10:11], v[10:11], v[18:19]
	s_nop 0
	v_cvt_pk_bf16_f32 v4, v10, v11
	v_lshlrev_b32_e32 v10, 16, v5
	v_and_b32_e32 v11, 0xffff0000, v5
	v_pk_mul_f32 v[10:11], v[12:13], v[10:11]
	s_nop 0
	v_cvt_pk_bf16_f32 v5, v10, v11
	v_lshlrev_b32_e32 v10, 16, v6
	v_and_b32_e32 v11, 0xffff0000, v6
	s_waitcnt lgkmcnt(0)
	v_pk_mul_f32 v[10:11], v[14:15], v[10:11]
	s_nop 0
	v_cvt_pk_bf16_f32 v6, v10, v11
	v_lshlrev_b32_e32 v10, 16, v7
	v_and_b32_e32 v11, 0xffff0000, v7
	v_pk_mul_f32 v[10:11], v[16:17], v[10:11]
	s_nop 0
	v_cvt_pk_bf16_f32 v7, v10, v11
	v_add_u32_e32 v10, s93, v82
	v_ashrrev_i32_e32 v11, 31, v10
	v_lshlrev_b64 v[10:11], 11, v[10:11]
	v_lshl_add_u64 v[8:9], v[8:9], 0, v[10:11]
	global_store_dwordx4 v[8:9], v[4:7], off sc1
	s_barrier
	s_cbranch_scc0 .LBB0_350

; #define LAS __attribute__((address_space(3)))
; __device__ __forceinline__ unsigned cvt_pk_bf16(float lo, float hi) { f32x2 v = {lo, hi}; bf16x2_t b = __builtin_convertvector(v, bf16x2_t); return __builtin_bit_cast(unsigned, b); }
; __device__ __forceinline__ float bf_lo(unsigned w) { return __uint_as_float(w << 16); }
; __device__ __forceinline__ float bf_hi(unsigned w) { return __uint_as_float(w & 0xffff0000u); }
; __device__ __forceinline__ void kv_unit(Frame& F, const Args& a, int c, int h) {
;     LAS unsigned char* Kimg = F.lds; LAS unsigned char* Vimg = F.lds + 32768;
;     const int t0 = c * 128, tid = F.tid, lane = F.lane, w = F.wave;
;     const bf16_t* Kb = (const bf16_t*)(F.ws + WS_K); const bf16_t* RV = (const bf16_t*)(F.ws + WS_RV); float* KV = (float*)(F.ws + WS_KV);
;     const float l2g = a.l2g[h];
;     {
;         u32x4 kx[4], vx[8];
; #pragma unroll
;         for (int i = 0; i < 4; ++i) kx[i] = __builtin_nontemporal_load((const u32x4*)(Kb + (size_t)(t0 + (tid >> 4) + 32 * i) * QKW + h * 128 + 8 * (tid & 15)));
; #pragma unroll
;         for (int i = 0; i < 8; ++i) vx[i] = __builtin_nontemporal_load((const u32x4*)(RV + (size_t)(t0 + (tid >> 5) + 16 * i) * D + h * 256 + 8 * (tid & 31)));
; #pragma unroll
;         for (int i = 0; i < 4; ++i) *(LAS u32x4*)(Kimg + off_b((tid >> 4) + 32 * i, tid & 15)) = kx[i];
; #pragma unroll
;         for (int i = 0; i < 8; ++i) { const int s = (tid >> 5) + 16 * i, ch = tid & 31; const u32x4 x = vx[i]; const float z = exp2f((float)(127 - s) * l2g);
;             u32x4 o; o.x = cvt_pk_bf16(bf_lo(x.x) * z, bf_hi(x.x) * z); o.y = cvt_pk_bf16(bf_lo(x.y) * z, bf_hi(x.y) * z); o.z = cvt_pk_bf16(bf_lo(x.z) * z, bf_hi(x.z) * z); o.w = cvt_pk_bf16(bf_lo(x.w) * z, bf_hi(x.w) * z);
;             *(LAS u32x4*)(Vimg + (ch >> 4) * 32768 + off_b(s, ch & 15)) = o; }
.LBB0_351:
	s_and_b32 s17, s33, 0xffffff80
	s_and_b32 s16, s15, 7
	v_add_u32_e32 v2, s17, v1
	s_lshl_b32 s0, s16, 8
	v_ashrrev_i32_e32 v3, 31, v2
	v_add_u32_e32 v6, s17, v32
	v_lshl_add_u64 v[4:5], v[10:11], 0, s[0:1]
	v_lshlrev_b64 v[2:3], 11, v[2:3]
	s_lshl_b32 s0, s16, 9
	v_ashrrev_i32_e32 v7, 31, v6
	v_lshl_add_u64 v[2:3], v[4:5], 0, v[2:3]
	v_lshl_add_u64 v[8:9], v[12:13], 0, s[0:1]
	v_lshlrev_b64 v[6:7], 12, v[6:7]
	v_add_co_u32_e32 v4, vcc, s3, v2
	v_lshl_add_u64 v[6:7], v[8:9], 0, v[6:7]
	s_nop 0
	v_addc_co_u32_e32 v5, vcc, 0, v3, vcc
	global_load_dwordx4 v[68:71], v[2:3], off nt
	global_load_dwordx4 v[72:75], v[4:5], off nt
	global_load_dwordx4 v[76:79], v[6:7], off nt
	v_add_co_u32_e32 v4, vcc, s8, v2
	s_lshl_b32 s0, s16, 2
	s_nop 0
	v_addc_co_u32_e32 v5, vcc, 0, v3, vcc
	v_add_co_u32_e32 v2, vcc, s9, v2
	s_nop 1
	v_addc_co_u32_e32 v3, vcc, 0, v3, vcc
	global_load_dwordx4 v[80:83], v[4:5], off nt
	global_load_dwordx4 v[84:87], v[2:3], off nt
	v_add_co_u32_e32 v2, vcc, s3, v6
	s_load_dword s0, s[96:97], s0 offset:0xa0
	s_nop 0
	v_addc_co_u32_e32 v3, vcc, 0, v7, vcc
	global_load_dwordx4 v[88:91], v[2:3], off nt
	v_add_co_u32_e32 v2, vcc, s8, v6
	s_nop 1
	v_addc_co_u32_e32 v3, vcc, 0, v7, vcc
	global_load_dwordx4 v[92:95], v[2:3], off nt
	v_add_co_u32_e32 v4, vcc, s9, v6
	s_nop 1
	v_addc_co_u32_e32 v5, vcc, 0, v7, vcc
	v_add_co_u32_e32 v2, vcc, s10, v6
	s_nop 1
	v_addc_co_u32_e32 v3, vcc, 0, v7, vcc
	v_add_co_u32_e32 v8, vcc, s11, v6
	s_nop 1
	v_addc_co_u32_e32 v9, vcc, 0, v7, vcc
	global_load_dwordx4 v[96:99], v[4:5], off nt
	global_load_dwordx4 v[100:103], v[2:3], off nt
	global_load_dwordx4 v[104:107], v[8:9], off nt
	v_add_co_u32_e32 v108, vcc, s12, v6
	s_waitcnt lgkmcnt(0)
	v_mul_f32_e32 v2, s0, v33
	v_addc_co_u32_e32 v109, vcc, 0, v7, vcc
	v_add_co_u32_e32 v110, vcc, s13, v6
	s_nop 1
	v_addc_co_u32_e32 v111, vcc, 0, v7, vcc
	v_cmp_gt_f32_e32 vcc, s14, v2
	s_nop 1
	v_cndmask_b32_e32 v2, 0, v65, vcc
	v_fmac_f32_e32 v2, s0, v33
	v_exp_f32_e32 v112, v2
	global_load_dwordx4 v[6:9], v[108:109], off nt
	global_load_dwordx4 v[2:5], v[110:111], off nt
	v_cndmask_b32_e32 v108, 0, v67, vcc
	v_ldexp_f32 v108, v112, v108
	s_waitcnt vmcnt(11)
	ds_write_b128 v66, v[68:71]
	s_waitcnt vmcnt(10)
	ds_write_b128 v36, v[72:75]
	s_waitcnt vmcnt(9)
	v_lshlrev_b32_e32 v68, 16, v76
	v_and_b32_e32 v69, 0xffff0000, v76
	v_lshlrev_b32_e32 v70, 16, v77
	v_and_b32_e32 v71, 0xffff0000, v77
	v_pk_mul_f32 v[68:69], v[108:109], v[68:69] op_sel_hi:[0,1]
	v_pk_mul_f32 v[70:71], v[108:109], v[70:71] op_sel_hi:[0,1]
	v_cvt_pk_bf16_f32 v68, v68, v69
	v_cvt_pk_bf16_f32 v69, v70, v71
	v_lshlrev_b32_e32 v70, 16, v78
	v_and_b32_e32 v71, 0xffff0000, v78
	v_pk_mul_f32 v[70:71], v[108:109], v[70:71] op_sel_hi:[0,1]
	v_cvt_pk_bf16_f32 v70, v70, v71
	v_mul_f32_e32 v71, s0, v34
	v_cmp_gt_f32_e32 vcc, s14, v71
	v_lshlrev_b32_e32 v72, 16, v79
	v_and_b32_e32 v73, 0xffff0000, v79
	v_cndmask_b32_e32 v71, 0, v65, vcc
	v_fmac_f32_e32 v71, s0, v34
	v_exp_f32_e32 v74, v71
	v_pk_mul_f32 v[72:73], v[108:109], v[72:73] op_sel_hi:[0,1]
	v_cvt_pk_bf16_f32 v71, v72, v73
	s_waitcnt vmcnt(8)
	ds_write_b128 v37, v[80:83]
	s_waitcnt vmcnt(7)
	ds_write_b128 v38, v[84:87]
	ds_write_b128 v39, v[68:71] offset:32768
	v_cndmask_b32_e32 v68, 0, v67, vcc
	v_ldexp_f32 v72, v74, v68
	s_waitcnt vmcnt(6)
	v_lshlrev_b32_e32 v68, 16, v88
	v_and_b32_e32 v69, 0xffff0000, v88
	v_lshlrev_b32_e32 v70, 16, v89
	v_and_b32_e32 v71, 0xffff0000, v89
	v_pk_mul_f32 v[68:69], v[72:73], v[68:69] op_sel_hi:[0,1]
	v_pk_mul_f32 v[70:71], v[72:73], v[70:71] op_sel_hi:[0,1]
	v_cvt_pk_bf16_f32 v68, v68, v69
	v_cvt_pk_bf16_f32 v69, v70, v71
	v_lshlrev_b32_e32 v70, 16, v90
	v_and_b32_e32 v71, 0xffff0000, v90
	v_pk_mul_f32 v[70:71], v[72:73], v[70:71] op_sel_hi:[0,1]
	v_cvt_pk_bf16_f32 v70, v70, v71
	v_mul_f32_e32 v71, s0, v35
	v_cmp_gt_f32_e32 vcc, s14, v71
	v_lshlrev_b32_e32 v74, 16, v91
	v_and_b32_e32 v75, 0xffff0000, v91
	v_cndmask_b32_e32 v71, 0, v65, vcc
	v_fmac_f32_e32 v71, s0, v35
	v_pk_mul_f32 v[72:73], v[72:73], v[74:75] op_sel_hi:[0,1]
	v_exp_f32_e32 v74, v71
	v_cvt_pk_bf16_f32 v71, v72, v73
	ds_write_b128 v40, v[68:71] offset:32768
	v_cndmask_b32_e32 v68, 0, v67, vcc
	v_ldexp_f32 v72, v74, v68
	s_waitcnt vmcnt(5)
	v_lshlrev_b32_e32 v68, 16, v92
	v_and_b32_e32 v69, 0xffff0000, v92
	v_lshlrev_b32_e32 v70, 16, v93
	v_and_b32_e32 v71, 0xffff0000, v93
	v_pk_mul_f32 v[68:69], v[72:73], v[68:69] op_sel_hi:[0,1]
	v_pk_mul_f32 v[70:71], v[72:73], v[70:71] op_sel_hi:[0,1]
	v_cvt_pk_bf16_f32 v68, v68, v69
	v_cvt_pk_bf16_f32 v69, v70, v71
	v_lshlrev_b32_e32 v70, 16, v94
	v_and_b32_e32 v71, 0xffff0000, v94
	v_pk_mul_f32 v[70:71], v[72:73], v[70:71] op_sel_hi:[0,1]
	v_cvt_pk_bf16_f32 v70, v70, v71
	v_mul_f32_e32 v71, s0, v46
	v_cmp_gt_f32_e32 vcc, s14, v71
	v_lshlrev_b32_e32 v74, 16, v95
	v_and_b32_e32 v75, 0xffff0000, v95
	v_cndmask_b32_e32 v71, 0, v65, vcc
	v_fmac_f32_e32 v71, s0, v46
	v_pk_mul_f32 v[72:73], v[72:73], v[74:75] op_sel_hi:[0,1]
	v_exp_f32_e32 v74, v71
	v_cvt_pk_bf16_f32 v71, v72, v73
	ds_write_b128 v41, v[68:71] offset:32768
	v_cndmask_b32_e32 v68, 0, v67, vcc
	v_ldexp_f32 v72, v74, v68
	s_waitcnt vmcnt(4)
	v_lshlrev_b32_e32 v68, 16, v96
	v_and_b32_e32 v69, 0xffff0000, v96
	v_lshlrev_b32_e32 v70, 16, v97
	v_and_b32_e32 v71, 0xffff0000, v97
	v_pk_mul_f32 v[68:69], v[72:73], v[68:69] op_sel_hi:[0,1]
	v_pk_mul_f32 v[70:71], v[72:73], v[70:71] op_sel_hi:[0,1]
	v_cvt_pk_bf16_f32 v68, v68, v69
	v_cvt_pk_bf16_f32 v69, v70, v71
	v_lshlrev_b32_e32 v70, 16, v98
	v_and_b32_e32 v71, 0xffff0000, v98
	v_pk_mul_f32 v[70:71], v[72:73], v[70:71] op_sel_hi:[0,1]
	v_cvt_pk_bf16_f32 v70, v70, v71
	v_mul_f32_e32 v71, s0, v47
	v_cmp_gt_f32_e32 vcc, s14, v71
	v_lshlrev_b32_e32 v74, 16, v99
	v_and_b32_e32 v75, 0xffff0000, v99
	v_cndmask_b32_e32 v71, 0, v65, vcc
	v_fmac_f32_e32 v71, s0, v47
	v_pk_mul_f32 v[72:73], v[72:73], v[74:75] op_sel_hi:[0,1]
	v_exp_f32_e32 v74, v71
	v_cvt_pk_bf16_f32 v71, v72, v73
	ds_write_b128 v42, v[68:71] offset:32768
	v_cndmask_b32_e32 v68, 0, v67, vcc
	v_ldexp_f32 v72, v74, v68
	s_waitcnt vmcnt(3)
; #define LAS __attribute__((address_space(3)))
; __device__ __forceinline__ unsigned cvt_pk_bf16(float lo, float hi) { f32x2 v = {lo, hi}; bf16x2_t b = __builtin_convertvector(v, bf16x2_t); return __builtin_bit_cast(unsigned, b); }
; __device__ __forceinline__ float bf_lo(unsigned w) { return __uint_as_float(w << 16); }
; __device__ __forceinline__ float bf_hi(unsigned w) { return __uint_as_float(w & 0xffff0000u); }
; #define MFMA16(a, b, c) __builtin_amdgcn_mfma_f32_16x16x32_bf16(a, b, c, 0, 0, 0)
; __device__ __forceinline__ unsigned tr_base(unsigned lane, unsigned c, unsigned t) { return tr_addr16(lane, c, 0, t); }
; __device__ __forceinline__ void kv_unit(Frame& F, const Args& a, int c, int h) {
;     ...
;         for (int i = 0; i < 8; ++i) { const int s = (tid >> 5) + 16 * i, ch = tid & 31; const u32x4 x = vx[i]; const float z = exp2f((float)(127 - s) * l2g);
;             u32x4 o; o.x = cvt_pk_bf16(bf_lo(x.x) * z, bf_hi(x.x) * z); o.y = cvt_pk_bf16(bf_lo(x.y) * z, bf_hi(x.y) * z); o.z = cvt_pk_bf16(bf_lo(x.z) * z, bf_hi(x.z) * z); o.w = cvt_pk_bf16(bf_lo(x.w) * z, bf_hi(x.w) * z);
;             *(LAS u32x4*)(Vimg + (ch >> 4) * 32768 + off_b(s, ch & 15)) = o; }
;     }
;     __syncthreads();
;     f32x4 acc[2][8];
; #pragma unroll
;     for (int j = 0; j < 2; ++j)
; #pragma unroll
;         for (int cd = 0; cd < 8; ++cd) acc[j][cd] = (f32x4){0.f, 0.f, 0.f, 0.f};
;     LAS unsigned char* vi = Vimg + (w >> 2) * 32768; const int cimg = (2 * w) & 7;
;     {
;         unsigned kb[8][2], vb[2][2];
; #pragma unroll
;         for (int cd = 0; cd < 8; ++cd) { kb[cd][0] = tr_base(lane, cd, 0); kb[cd][1] = tr_base(lane, cd, 1); }
; #pragma unroll
;         for (int j = 0; j < 2; ++j) { vb[j][0] = tr_base(lane, cimg + j, 0); vb[j][1] = tr_base(lane, cimg + j, 1); }
; #pragma unroll
;         for (int ks = 0; ks < 4; ++ks) {
;             const bf16x8 y0 = trf(vi, vb[0][0], vb[0][1], 8192 * ks), y1 = trf(vi, vb[1][0], vb[1][1], 8192 * ks);
;             bf16x8 xf[8];
; #pragma unroll
;             for (int cd = 0; cd < 8; ++cd) xf[cd] = trf(Kimg, kb[cd][0], kb[cd][1], 8192 * ks);
;             __builtin_amdgcn_sched_barrier(0);
; #pragma unroll
;             for (int cd = 0; cd < 8; ++cd) { acc[0][cd] = MFMA16(xf[cd], y0, acc[0][cd]); acc[1][cd] = MFMA16(xf[cd], y1, acc[1][cd]); }
	v_lshlrev_b32_e32 v68, 16, v100
	v_and_b32_e32 v69, 0xffff0000, v100
	v_lshlrev_b32_e32 v70, 16, v101
	v_and_b32_e32 v71, 0xffff0000, v101
	v_pk_mul_f32 v[68:69], v[72:73], v[68:69] op_sel_hi:[0,1]
	v_pk_mul_f32 v[70:71], v[72:73], v[70:71] op_sel_hi:[0,1]
	v_cvt_pk_bf16_f32 v68, v68, v69
	v_cvt_pk_bf16_f32 v69, v70, v71
	v_lshlrev_b32_e32 v70, 16, v102
	v_and_b32_e32 v71, 0xffff0000, v102
	v_pk_mul_f32 v[70:71], v[72:73], v[70:71] op_sel_hi:[0,1]
	v_cvt_pk_bf16_f32 v70, v70, v71
	v_mul_f32_e32 v71, s0, v48
	v_cmp_gt_f32_e32 vcc, s14, v71
	v_lshlrev_b32_e32 v74, 16, v103
	v_and_b32_e32 v75, 0xffff0000, v103
	v_cndmask_b32_e32 v71, 0, v65, vcc
	v_fmac_f32_e32 v71, s0, v48
	v_pk_mul_f32 v[72:73], v[72:73], v[74:75] op_sel_hi:[0,1]
	v_exp_f32_e32 v74, v71
	v_cvt_pk_bf16_f32 v71, v72, v73
	ds_write_b128 v43, v[68:71] offset:32768
	v_cndmask_b32_e32 v68, 0, v67, vcc
	v_ldexp_f32 v72, v74, v68
	s_waitcnt vmcnt(2)
	v_lshlrev_b32_e32 v68, 16, v104
	v_and_b32_e32 v69, 0xffff0000, v104
	v_lshlrev_b32_e32 v70, 16, v105
	v_and_b32_e32 v71, 0xffff0000, v105
	v_pk_mul_f32 v[68:69], v[72:73], v[68:69] op_sel_hi:[0,1]
	v_pk_mul_f32 v[70:71], v[72:73], v[70:71] op_sel_hi:[0,1]
	v_cvt_pk_bf16_f32 v68, v68, v69
	v_cvt_pk_bf16_f32 v69, v70, v71
	v_lshlrev_b32_e32 v70, 16, v106
	v_and_b32_e32 v71, 0xffff0000, v106
	v_pk_mul_f32 v[70:71], v[72:73], v[70:71] op_sel_hi:[0,1]
	v_cvt_pk_bf16_f32 v70, v70, v71
	v_mul_f32_e32 v71, s0, v49
	v_cmp_gt_f32_e32 vcc, s14, v71
	v_lshlrev_b32_e32 v74, 16, v107
	v_and_b32_e32 v75, 0xffff0000, v107
	v_cndmask_b32_e32 v71, 0, v65, vcc
	v_fmac_f32_e32 v71, s0, v49
	v_pk_mul_f32 v[72:73], v[72:73], v[74:75] op_sel_hi:[0,1]
	v_exp_f32_e32 v74, v71
	v_cvt_pk_bf16_f32 v71, v72, v73
	ds_write_b128 v44, v[68:71] offset:32768
	v_cndmask_b32_e32 v68, 0, v67, vcc
	v_ldexp_f32 v68, v74, v68
	s_waitcnt vmcnt(1)
	v_lshlrev_b32_e32 v70, 16, v6
	v_and_b32_e32 v71, 0xffff0000, v6
	v_pk_mul_f32 v[70:71], v[68:69], v[70:71] op_sel_hi:[0,1]
	v_cvt_pk_bf16_f32 v6, v70, v71
	v_lshlrev_b32_e32 v70, 16, v7
	v_and_b32_e32 v71, 0xffff0000, v7
	v_pk_mul_f32 v[70:71], v[68:69], v[70:71] op_sel_hi:[0,1]
	v_cvt_pk_bf16_f32 v7, v70, v71
	v_lshlrev_b32_e32 v70, 16, v8
	v_and_b32_e32 v71, 0xffff0000, v8
	v_pk_mul_f32 v[70:71], v[68:69], v[70:71] op_sel_hi:[0,1]
	v_cvt_pk_bf16_f32 v8, v70, v71
	v_lshlrev_b32_e32 v70, 16, v9
	v_and_b32_e32 v71, 0xffff0000, v9
	v_mul_f32_e32 v9, s0, v50
	v_cmp_gt_f32_e32 vcc, s14, v9
	v_pk_mul_f32 v[68:69], v[68:69], v[70:71] op_sel_hi:[0,1]
	s_nop 0
	v_cndmask_b32_e32 v9, 0, v65, vcc
	v_fmac_f32_e32 v9, s0, v50
	v_exp_f32_e32 v70, v9
	v_cvt_pk_bf16_f32 v9, v68, v69
	ds_write_b128 v45, v[6:9] offset:32768
	v_cndmask_b32_e32 v6, 0, v67, vcc
	v_ldexp_f32 v6, v70, v6
	s_waitcnt vmcnt(0)
	v_lshlrev_b32_e32 v8, 16, v2
	v_and_b32_e32 v9, 0xffff0000, v2
	v_pk_mul_f32 v[8:9], v[6:7], v[8:9] op_sel_hi:[0,1]
	v_cvt_pk_bf16_f32 v2, v8, v9
	v_lshlrev_b32_e32 v8, 16, v3
	v_and_b32_e32 v9, 0xffff0000, v3
	v_pk_mul_f32 v[8:9], v[6:7], v[8:9] op_sel_hi:[0,1]
	v_cvt_pk_bf16_f32 v3, v8, v9
	v_lshlrev_b32_e32 v8, 16, v4
	v_and_b32_e32 v9, 0xffff0000, v4
	v_pk_mul_f32 v[8:9], v[6:7], v[8:9] op_sel_hi:[0,1]
	v_cvt_pk_bf16_f32 v4, v8, v9
	v_lshlrev_b32_e32 v8, 16, v5
	v_and_b32_e32 v9, 0xffff0000, v5
	v_pk_mul_f32 v[6:7], v[6:7], v[8:9] op_sel_hi:[0,1]
	v_cvt_pk_bf16_f32 v5, v6, v7
	ds_write_b128 v51, v[2:5] offset:32768
	s_waitcnt lgkmcnt(0)
	s_barrier
	ds_read_b64_tr_b16 v[2:3], v52 offset:32768
	ds_read_b64_tr_b16 v[4:5], v53 offset:32768
	ds_read_b64_tr_b16 v[6:7], v54 offset:32768
	ds_read_b64_tr_b16 v[8:9], v55 offset:32768
	ds_read_b64_tr_b16 v[68:69], v116
	ds_read_b64_tr_b16 v[70:71], v117
	ds_read_b64_tr_b16 v[72:73], v118
	ds_read_b64_tr_b16 v[74:75], v119
	ds_read_b64_tr_b16 v[76:77], v120
	ds_read_b64_tr_b16 v[78:79], v121
	ds_read_b64_tr_b16 v[80:81], v122
	ds_read_b64_tr_b16 v[82:83], v123
	ds_read_b64_tr_b16 v[84:85], v124
	ds_read_b64_tr_b16 v[86:87], v125
	ds_read_b64_tr_b16 v[88:89], v126
	ds_read_b64_tr_b16 v[90:91], v127
	ds_read_b64_tr_b16 v[92:93], v128
	ds_read_b64_tr_b16 v[94:95], v129
	ds_read_b64_tr_b16 v[96:97], v130
	ds_read_b64_tr_b16 v[98:99], v131
	s_waitcnt lgkmcnt(14)
	v_mfma_f32_16x16x32_bf16 v[100:103], v[68:71], v[2:5], 0
	v_mfma_f32_16x16x32_bf16 v[68:71], v[68:71], v[6:9], 0
	s_waitcnt lgkmcnt(12)
	v_mfma_f32_16x16x32_bf16 v[104:107], v[72:75], v[2:5], 0
	v_mfma_f32_16x16x32_bf16 v[72:75], v[72:75], v[6:9], 0
	s_waitcnt lgkmcnt(10)
	v_mfma_f32_16x16x32_bf16 v[108:111], v[76:79], v[2:5], 0
	v_mfma_f32_16x16x32_bf16 v[76:79], v[76:79], v[6:9], 0
	s_waitcnt lgkmcnt(8)
	v_mfma_f32_16x16x32_bf16 v[112:115], v[80:83], v[2:5], 0
	v_mfma_f32_16x16x32_bf16 v[80:83], v[80:83], v[6:9], 0
	s_waitcnt lgkmcnt(6)
	v_mfma_f32_16x16x32_bf16 v[132:135], v[84:87], v[2:5], 0
	v_mfma_f32_16x16x32_bf16 v[84:87], v[84:87], v[6:9], 0
	s_waitcnt lgkmcnt(4)
	v_mfma_f32_16x16x32_bf16 v[136:139], v[88:91], v[2:5], 0
	v_mfma_f32_16x16x32_bf16 v[88:91], v[88:91], v[6:9], 0
	s_waitcnt lgkmcnt(2)
	v_mfma_f32_16x16x32_bf16 v[140:143], v[92:95], v[2:5], 0
	v_mfma_f32_16x16x32_bf16 v[92:95], v[92:95], v[6:9], 0
	s_waitcnt lgkmcnt(0)
; #define MFMA16(a, b, c) __builtin_amdgcn_mfma_f32_16x16x32_bf16(a, b, c, 0, 0, 0)
; __device__ __forceinline__ void kv_unit(Frame& F, const Args& a, int c, int h) {
;     ...
; #pragma unroll
;         for (int ks = 0; ks < 4; ++ks) {
;             const bf16x8 y0 = trf(vi, vb[0][0], vb[0][1], 8192 * ks), y1 = trf(vi, vb[1][0], vb[1][1], 8192 * ks);
;             bf16x8 xf[8];
; #pragma unroll
;             for (int cd = 0; cd < 8; ++cd) xf[cd] = trf(Kimg, kb[cd][0], kb[cd][1], 8192 * ks);
;             __builtin_amdgcn_sched_barrier(0);
; #pragma unroll
;             for (int cd = 0; cd < 8; ++cd) { acc[0][cd] = MFMA16(xf[cd], y0, acc[0][cd]); acc[1][cd] = MFMA16(xf[cd], y1, acc[1][cd]); }
;             __builtin_amdgcn_sched_barrier(0);
;         }
	v_mfma_f32_16x16x32_bf16 v[2:5], v[96:99], v[2:5], 0
	v_mfma_f32_16x16x32_bf16 v[6:9], v[96:99], v[6:9], 0
	ds_read_b64_tr_b16 v[96:97], v52 offset:40960
	ds_read_b64_tr_b16 v[98:99], v53 offset:40960
	ds_read_b64_tr_b16 v[144:145], v54 offset:40960
	ds_read_b64_tr_b16 v[146:147], v55 offset:40960
	ds_read_b64_tr_b16 v[148:149], v116 offset:8192
	ds_read_b64_tr_b16 v[150:151], v117 offset:8192
	ds_read_b64_tr_b16 v[152:153], v118 offset:8192
	ds_read_b64_tr_b16 v[154:155], v119 offset:8192
	ds_read_b64_tr_b16 v[156:157], v120 offset:8192
	ds_read_b64_tr_b16 v[158:159], v121 offset:8192
	ds_read_b64_tr_b16 v[160:161], v122 offset:8192
	ds_read_b64_tr_b16 v[162:163], v123 offset:8192
	ds_read_b64_tr_b16 v[164:165], v124 offset:8192
	ds_read_b64_tr_b16 v[166:167], v125 offset:8192
	ds_read_b64_tr_b16 v[168:169], v126 offset:8192
	ds_read_b64_tr_b16 v[170:171], v127 offset:8192
	ds_read_b64_tr_b16 v[172:173], v128 offset:8192
	ds_read_b64_tr_b16 v[174:175], v129 offset:8192
	ds_read_b64_tr_b16 v[176:177], v130 offset:8192
	ds_read_b64_tr_b16 v[178:179], v131 offset:8192
	s_waitcnt lgkmcnt(14)
	v_mfma_f32_16x16x32_bf16 v[100:103], v[148:151], v[96:99], v[100:103]
	v_mfma_f32_16x16x32_bf16 v[68:71], v[148:151], v[144:147], v[68:71]
	s_waitcnt lgkmcnt(12)
	v_mfma_f32_16x16x32_bf16 v[104:107], v[152:155], v[96:99], v[104:107]
	v_mfma_f32_16x16x32_bf16 v[72:75], v[152:155], v[144:147], v[72:75]
	s_waitcnt lgkmcnt(10)
	v_mfma_f32_16x16x32_bf16 v[108:111], v[156:159], v[96:99], v[108:111]
	v_mfma_f32_16x16x32_bf16 v[76:79], v[156:159], v[144:147], v[76:79]
	s_waitcnt lgkmcnt(8)
	v_mfma_f32_16x16x32_bf16 v[112:115], v[160:163], v[96:99], v[112:115]
	v_mfma_f32_16x16x32_bf16 v[80:83], v[160:163], v[144:147], v[80:83]
	s_waitcnt lgkmcnt(6)
	v_mfma_f32_16x16x32_bf16 v[132:135], v[164:167], v[96:99], v[132:135]
	v_mfma_f32_16x16x32_bf16 v[84:87], v[164:167], v[144:147], v[84:87]
	s_waitcnt lgkmcnt(4)
	v_mfma_f32_16x16x32_bf16 v[136:139], v[168:171], v[96:99], v[136:139]
	v_mfma_f32_16x16x32_bf16 v[88:91], v[168:171], v[144:147], v[88:91]
	s_waitcnt lgkmcnt(2)
	v_mfma_f32_16x16x32_bf16 v[140:143], v[172:175], v[96:99], v[140:143]
	v_mfma_f32_16x16x32_bf16 v[92:95], v[172:175], v[144:147], v[92:95]
	s_waitcnt lgkmcnt(0)
	v_mfma_f32_16x16x32_bf16 v[2:5], v[176:179], v[96:99], v[2:5]
	v_mfma_f32_16x16x32_bf16 v[6:9], v[176:179], v[144:147], v[6:9]
	ds_read_b64_tr_b16 v[96:97], v52 offset:49152
	ds_read_b64_tr_b16 v[98:99], v53 offset:49152
	ds_read_b64_tr_b16 v[144:145], v54 offset:49152
	ds_read_b64_tr_b16 v[146:147], v55 offset:49152
	ds_read_b64_tr_b16 v[148:149], v116 offset:16384
	ds_read_b64_tr_b16 v[150:151], v117 offset:16384
	ds_read_b64_tr_b16 v[152:153], v118 offset:16384
	ds_read_b64_tr_b16 v[154:155], v119 offset:16384
	ds_read_b64_tr_b16 v[156:157], v120 offset:16384
	ds_read_b64_tr_b16 v[158:159], v121 offset:16384
	ds_read_b64_tr_b16 v[160:161], v122 offset:16384
	ds_read_b64_tr_b16 v[162:163], v123 offset:16384
	ds_read_b64_tr_b16 v[164:165], v124 offset:16384
	ds_read_b64_tr_b16 v[166:167], v125 offset:16384
	ds_read_b64_tr_b16 v[168:169], v126 offset:16384
	ds_read_b64_tr_b16 v[170:171], v127 offset:16384
	ds_read_b64_tr_b16 v[172:173], v128 offset:16384
	ds_read_b64_tr_b16 v[174:175], v129 offset:16384
	ds_read_b64_tr_b16 v[176:177], v130 offset:16384
	ds_read_b64_tr_b16 v[178:179], v131 offset:16384
	s_waitcnt lgkmcnt(14)
	v_mfma_f32_16x16x32_bf16 v[100:103], v[148:151], v[96:99], v[100:103]
	v_mfma_f32_16x16x32_bf16 v[68:71], v[148:151], v[144:147], v[68:71]
	s_waitcnt lgkmcnt(12)
	v_mfma_f32_16x16x32_bf16 v[104:107], v[152:155], v[96:99], v[104:107]
	v_mfma_f32_16x16x32_bf16 v[72:75], v[152:155], v[144:147], v[72:75]
	s_waitcnt lgkmcnt(10)
	v_mfma_f32_16x16x32_bf16 v[108:111], v[156:159], v[96:99], v[108:111]
	v_mfma_f32_16x16x32_bf16 v[76:79], v[156:159], v[144:147], v[76:79]
	s_waitcnt lgkmcnt(8)
	v_mfma_f32_16x16x32_bf16 v[112:115], v[160:163], v[96:99], v[112:115]
	v_mfma_f32_16x16x32_bf16 v[80:83], v[160:163], v[144:147], v[80:83]
	s_waitcnt lgkmcnt(6)
	v_mfma_f32_16x16x32_bf16 v[132:135], v[164:167], v[96:99], v[132:135]
	v_mfma_f32_16x16x32_bf16 v[84:87], v[164:167], v[144:147], v[84:87]
	s_waitcnt lgkmcnt(4)
	v_mfma_f32_16x16x32_bf16 v[136:139], v[168:171], v[96:99], v[136:139]
	v_mfma_f32_16x16x32_bf16 v[88:91], v[168:171], v[144:147], v[88:91]
	s_waitcnt lgkmcnt(2)
	v_mfma_f32_16x16x32_bf16 v[140:143], v[172:175], v[96:99], v[140:143]
	v_mfma_f32_16x16x32_bf16 v[92:95], v[172:175], v[144:147], v[92:95]
	s_waitcnt lgkmcnt(0)
; #define LAS __attribute__((address_space(3)))
; __device__ __forceinline__ unsigned cvt_pk_bf16(float lo, float hi) { f32x2 v = {lo, hi}; bf16x2_t b = __builtin_convertvector(v, bf16x2_t); return __builtin_bit_cast(unsigned, b); }
; #define MFMA16(a, b, c) __builtin_amdgcn_mfma_f32_16x16x32_bf16(a, b, c, 0, 0, 0)
; __device__ __forceinline__ void kv_unit(Frame& F, const Args& a, int c, int h) {
;     ...
;             __builtin_amdgcn_sched_barrier(0);
; #pragma unroll
;             for (int cd = 0; cd < 8; ++cd) { acc[0][cd] = MFMA16(xf[cd], y0, acc[0][cd]); acc[1][cd] = MFMA16(xf[cd], y1, acc[1][cd]); }
;             __builtin_amdgcn_sched_barrier(0);
;         }
;     }
;     bf16_t* out = (bf16_t*)KV + (size_t)(c * 8 + h) * 32768;
;     __syncthreads();
;     LAS unsigned char* KT = F.lds;
; #pragma unroll
;     for (int j = 0; j < 2; ++j)
; #pragma unroll
;         for (int cd = 0; cd < 8; ++cd) { const int e = 16 * (2 * w + j) + (lane & 15), d = 16 * cd + 4 * (lane >> 4);
;             u32x2 o; o.x = cvt_pk_bf16(acc[j][cd][0], acc[j][cd][1]); o.y = cvt_pk_bf16(acc[j][cd][2], acc[j][cd][3]); *(LAS u32x2*)(KT + e * 272 + d * 2) = o; }
;     __syncthreads();
; #pragma unroll
;     for (int i = 0; i < 8; ++i) { const int id = tid + 512 * i, e = id >> 4, ch = id & 15;
;         *(u32x4*)(out + e * 128 + 8 * ch) = *(const LAS u32x4*)(KT + e * 272 + 16 * ch); }
;     __syncthreads();
; }
	v_mfma_f32_16x16x32_bf16 v[2:5], v[176:179], v[96:99], v[2:5]
	v_mfma_f32_16x16x32_bf16 v[6:9], v[176:179], v[144:147], v[6:9]
	ds_read_b64_tr_b16 v[96:97], v52 offset:57344
	ds_read_b64_tr_b16 v[98:99], v53 offset:57344
	ds_read_b64_tr_b16 v[144:145], v54 offset:57344
	ds_read_b64_tr_b16 v[146:147], v55 offset:57344
	ds_read_b64_tr_b16 v[148:149], v116 offset:24576
	ds_read_b64_tr_b16 v[150:151], v117 offset:24576
	ds_read_b64_tr_b16 v[152:153], v118 offset:24576
	ds_read_b64_tr_b16 v[154:155], v119 offset:24576
	ds_read_b64_tr_b16 v[156:157], v120 offset:24576
	ds_read_b64_tr_b16 v[158:159], v121 offset:24576
	ds_read_b64_tr_b16 v[160:161], v122 offset:24576
	ds_read_b64_tr_b16 v[162:163], v123 offset:24576
	ds_read_b64_tr_b16 v[164:165], v124 offset:24576
	ds_read_b64_tr_b16 v[166:167], v125 offset:24576
	ds_read_b64_tr_b16 v[168:169], v126 offset:24576
	ds_read_b64_tr_b16 v[170:171], v127 offset:24576
	ds_read_b64_tr_b16 v[172:173], v128 offset:24576
	ds_read_b64_tr_b16 v[174:175], v129 offset:24576
	ds_read_b64_tr_b16 v[176:177], v130 offset:24576
	ds_read_b64_tr_b16 v[178:179], v131 offset:24576
	s_waitcnt lgkmcnt(14)
	v_mfma_f32_16x16x32_bf16 v[100:103], v[148:151], v[96:99], v[100:103]
	v_mfma_f32_16x16x32_bf16 v[68:71], v[148:151], v[144:147], v[68:71]
	s_waitcnt lgkmcnt(12)
	v_mfma_f32_16x16x32_bf16 v[104:107], v[152:155], v[96:99], v[104:107]
	v_mfma_f32_16x16x32_bf16 v[72:75], v[152:155], v[144:147], v[72:75]
	s_waitcnt lgkmcnt(10)
	v_mfma_f32_16x16x32_bf16 v[108:111], v[156:159], v[96:99], v[108:111]
	v_mfma_f32_16x16x32_bf16 v[76:79], v[156:159], v[144:147], v[76:79]
	s_waitcnt lgkmcnt(8)
	v_mfma_f32_16x16x32_bf16 v[112:115], v[160:163], v[96:99], v[112:115]
	v_mfma_f32_16x16x32_bf16 v[80:83], v[160:163], v[144:147], v[80:83]
	s_waitcnt lgkmcnt(6)
	v_mfma_f32_16x16x32_bf16 v[132:135], v[164:167], v[96:99], v[132:135]
	v_mfma_f32_16x16x32_bf16 v[84:87], v[164:167], v[144:147], v[84:87]
	s_waitcnt lgkmcnt(4)
	v_mfma_f32_16x16x32_bf16 v[136:139], v[168:171], v[96:99], v[136:139]
	v_mfma_f32_16x16x32_bf16 v[88:91], v[168:171], v[144:147], v[88:91]
	s_waitcnt lgkmcnt(2)
	v_mfma_f32_16x16x32_bf16 v[140:143], v[172:175], v[96:99], v[140:143]
	v_mfma_f32_16x16x32_bf16 v[92:95], v[172:175], v[144:147], v[92:95]
	s_waitcnt lgkmcnt(0)
	v_mfma_f32_16x16x32_bf16 v[2:5], v[176:179], v[96:99], v[2:5]
	v_mfma_f32_16x16x32_bf16 v[6:9], v[176:179], v[144:147], v[6:9]
	v_cvt_pk_bf16_f32 v96, v100, v101
	v_cvt_pk_bf16_f32 v97, v102, v103
	v_cvt_pk_bf16_f32 v98, v104, v105
	v_cvt_pk_bf16_f32 v99, v106, v107
	s_nop 2
	v_cvt_pk_bf16_f32 v2, v2, v3
	v_cvt_pk_bf16_f32 v3, v4, v5
	v_cvt_pk_bf16_f32 v4, v68, v69
	v_cvt_pk_bf16_f32 v5, v70, v71
	v_cvt_pk_bf16_f32 v68, v72, v73
	v_cvt_pk_bf16_f32 v69, v74, v75
	v_cvt_pk_bf16_f32 v70, v76, v77
	v_cvt_pk_bf16_f32 v71, v78, v79
	v_cvt_pk_bf16_f32 v72, v80, v81
	v_cvt_pk_bf16_f32 v73, v82, v83
	v_cvt_pk_bf16_f32 v74, v84, v85
	v_cvt_pk_bf16_f32 v75, v86, v87
	v_cvt_pk_bf16_f32 v76, v88, v89
	v_cvt_pk_bf16_f32 v77, v90, v91
	v_cvt_pk_bf16_f32 v78, v92, v93
	v_cvt_pk_bf16_f32 v79, v94, v95
	v_cvt_pk_bf16_f32 v6, v6, v7
	v_cvt_pk_bf16_f32 v7, v8, v9
	s_barrier
	v_cvt_pk_bf16_f32 v100, v108, v109
	v_cvt_pk_bf16_f32 v101, v110, v111
	v_cvt_pk_bf16_f32 v102, v112, v113
	v_cvt_pk_bf16_f32 v103, v114, v115
	v_cvt_pk_bf16_f32 v104, v132, v133
	v_cvt_pk_bf16_f32 v105, v134, v135
	v_cvt_pk_bf16_f32 v106, v136, v137
	v_cvt_pk_bf16_f32 v107, v138, v139
	v_cvt_pk_bf16_f32 v108, v140, v141
	v_cvt_pk_bf16_f32 v109, v142, v143
	v_add_u32_e32 v138, 0x1000, v56
	ds_write2_b64 v56, v[96:97], v[98:99] offset1:4
	ds_write2_b64 v56, v[100:101], v[102:103] offset0:8 offset1:12
	ds_write2_b64 v56, v[104:105], v[106:107] offset0:16 offset1:20
	ds_write2_b64 v56, v[108:109], v[2:3] offset0:24 offset1:28
	ds_write2_b64 v138, v[4:5], v[68:69] offset0:32 offset1:36
	ds_write2_b64 v138, v[70:71], v[72:73] offset0:40 offset1:44
	ds_write2_b64 v138, v[74:75], v[76:77] offset0:48 offset1:52
	ds_write2_b64 v138, v[78:79], v[6:7] offset0:56 offset1:60
	s_waitcnt lgkmcnt(0)
	s_barrier
	ds_read_b128 v[2:5], v57
	ds_read_b128 v[6:9], v58
	ds_read_b128 v[68:71], v59
	ds_read_b128 v[72:75], v60
	ds_read_b128 v[76:79], v61
	ds_read_b128 v[80:83], v62
	ds_read_b128 v[84:87], v63
	ds_read_b128 v[88:91], v64
	s_add_i32 s15, s15, s4
	s_add_i32 s33, s33, s90
	v_lshl_add_u64 v[92:93], v[16:17], 0, v[14:15]
	v_lshl_add_u64 v[94:95], v[16:17], 0, v[18:19]
	v_lshl_add_u64 v[110:111], v[16:17], 0, v[20:21]
	v_lshl_add_u64 v[112:113], v[16:17], 0, v[22:23]
	v_lshl_add_u64 v[114:115], v[16:17], 0, v[24:25]
	v_lshl_add_u64 v[132:133], v[16:17], 0, v[26:27]
	v_lshl_add_u64 v[134:135], v[16:17], 0, v[28:29]
	v_lshl_add_u64 v[136:137], v[16:17], 0, v[30:31]
	v_lshl_add_u64 v[16:17], v[16:17], 0, s[6:7]
	s_cmpk_lt_i32 s15, 0x400
	s_waitcnt lgkmcnt(7)
	global_store_dwordx4 v[92:93], v[2:5], off sc1
	s_waitcnt lgkmcnt(6)
	global_store_dwordx4 v[94:95], v[6:9], off sc1
	s_waitcnt lgkmcnt(5)
	global_store_dwordx4 v[110:111], v[68:71], off sc1
	s_waitcnt lgkmcnt(4)
	global_store_dwordx4 v[112:113], v[72:75], off sc1
	s_waitcnt lgkmcnt(3)
	global_store_dwordx4 v[114:115], v[76:79], off sc1
	s_waitcnt lgkmcnt(2)
	global_store_dwordx4 v[132:133], v[80:83], off sc1
	s_waitcnt lgkmcnt(1)
	global_store_dwordx4 v[134:135], v[84:87], off sc1
	s_waitcnt lgkmcnt(0)
	global_store_dwordx4 v[136:137], v[88:91], off sc1
	s_barrier
	s_cbranch_scc1 .LBB0_351
	s_load_dwordx2 s[88:89], s[96:97], 0xc0
	s_mov_b32 s2, s4
	v_readlane_b32 s4, v254, 10
	v_readlane_b32 s5, v254, 11

; #define LAS __attribute__((address_space(3)))
; __device__ __forceinline__ unsigned cvt_pk_bf16(float lo, float hi) { f32x2 v = {lo, hi}; bf16x2_t b = __builtin_convertvector(v, bf16x2_t); return __builtin_bit_cast(unsigned, b); }
; __device__ __forceinline__ void ret_unit(Frame& F, const Args& a, int c, int h) {
;     ...
;     __syncthreads();
;     {
;         LAS unsigned char* OT = F.lds;
; #pragma unroll
;         for (int ct = 0; ct < 8; ++ct) { const int tt = 16 * ct + (lane & 15); const float mean = stats[2 * tt], rstd = stats[2 * tt + 1];
; #pragma unroll
;             for (int j = 0; j < 2; ++j) { const f32x4 v = (acc[j][ct] - mean) * rstd; u32x2 r; r.x = cvt_pk_bf16(v[0], v[1]); r.y = cvt_pk_bf16(v[2], v[3]);
;                 *(LAS u32x2*)(OT + tt * 528 + (16 * (2 * w + j) + 4 * (lane >> 4)) * 2) = r; } }
;         __syncthreads();
.LBB0_469:
	s_or_b64 exec, exec, s[4:5]
	s_add_i32 s0, 0, 0x22000
	v_add_u32_e32 v66, s0, v183
	s_waitcnt lgkmcnt(0)
	s_barrier
	ds_read_b64 v[66:67], v66
	s_lshl_b32 s14, s46, 1
	s_add_i32 s44, s44, s2
	s_add_i32 s3, s3, s41
	s_cmpk_lt_i32 s44, 0x400
	s_waitcnt lgkmcnt(0)
	v_sub_f32_e32 v63, v63, v66
	v_sub_f32_e32 v62, v62, v66
	v_sub_f32_e32 v65, v65, v66
	v_sub_f32_e32 v64, v64, v66
	v_sub_f32_e32 v59, v59, v66
	v_sub_f32_e32 v58, v58, v66
	v_sub_f32_e32 v61, v61, v66
	v_sub_f32_e32 v60, v60, v66
	v_pk_mul_f32 v[64:65], v[66:67], v[64:65] op_sel:[1,0]
	v_pk_mul_f32 v[62:63], v[66:67], v[62:63] op_sel:[1,0]
	v_pk_mul_f32 v[60:61], v[66:67], v[60:61] op_sel:[1,0]
	v_pk_mul_f32 v[58:59], v[66:67], v[58:59] op_sel:[1,0]
	v_cvt_pk_bf16_f32 v62, v62, v63
	v_cvt_pk_bf16_f32 v63, v64, v65
	v_add_u32_e32 v64, s40, v184
	v_cvt_pk_bf16_f32 v58, v58, v59
	v_cvt_pk_bf16_f32 v59, v60, v61
	ds_write2_b64 v64, v[62:63], v[58:59] offset1:4
	v_or_b32_e32 v58, 0x80, v183
	v_add_u32_e32 v58, s0, v58
	ds_read_b64 v[58:59], v58
	v_lshl_add_u64 v[96:97], v[96:97], 0, s[30:31]
	s_waitcnt lgkmcnt(0)
	v_sub_f32_e32 v55, v55, v58
	v_sub_f32_e32 v54, v54, v58
	v_sub_f32_e32 v57, v57, v58
	v_sub_f32_e32 v56, v56, v58
	v_sub_f32_e32 v51, v51, v58
	v_sub_f32_e32 v50, v50, v58
	v_sub_f32_e32 v53, v53, v58
	v_sub_f32_e32 v52, v52, v58
	v_pk_mul_f32 v[56:57], v[58:59], v[56:57] op_sel:[1,0]
	v_pk_mul_f32 v[54:55], v[58:59], v[54:55] op_sel:[1,0]
	v_pk_mul_f32 v[52:53], v[58:59], v[52:53] op_sel:[1,0]
	v_pk_mul_f32 v[50:51], v[58:59], v[50:51] op_sel:[1,0]
	v_cvt_pk_bf16_f32 v54, v54, v55
	v_cvt_pk_bf16_f32 v55, v56, v57
	v_cvt_pk_bf16_f32 v50, v50, v51
	v_cvt_pk_bf16_f32 v51, v52, v53
	ds_write2_b64 v222, v[54:55], v[50:51] offset1:4
	v_or_b32_e32 v50, 0x100, v183
	v_add_u32_e32 v50, s0, v50
	ds_read_b64 v[50:51], v50
	s_waitcnt lgkmcnt(0)
	v_sub_f32_e32 v47, v47, v50
	v_sub_f32_e32 v46, v46, v50
	v_sub_f32_e32 v49, v49, v50
	v_sub_f32_e32 v48, v48, v50
	v_sub_f32_e32 v43, v43, v50
	v_sub_f32_e32 v42, v42, v50
	v_sub_f32_e32 v45, v45, v50
	v_sub_f32_e32 v44, v44, v50
	v_pk_mul_f32 v[48:49], v[50:51], v[48:49] op_sel:[1,0]
	v_pk_mul_f32 v[46:47], v[50:51], v[46:47] op_sel:[1,0]
	v_pk_mul_f32 v[44:45], v[50:51], v[44:45] op_sel:[1,0]
	v_pk_mul_f32 v[42:43], v[50:51], v[42:43] op_sel:[1,0]
	v_cvt_pk_bf16_f32 v46, v46, v47
	v_cvt_pk_bf16_f32 v47, v48, v49
	v_cvt_pk_bf16_f32 v42, v42, v43
	v_cvt_pk_bf16_f32 v43, v44, v45
	ds_write2_b64 v223, v[46:47], v[42:43] offset1:4
	v_or_b32_e32 v42, 0x180, v183
	v_add_u32_e32 v42, s0, v42
	ds_read_b64 v[42:43], v42
	s_waitcnt lgkmcnt(0)
	v_sub_f32_e32 v39, v39, v42
	v_sub_f32_e32 v38, v38, v42
	v_sub_f32_e32 v41, v41, v42
	v_sub_f32_e32 v40, v40, v42
	v_sub_f32_e32 v35, v35, v42
	v_sub_f32_e32 v34, v34, v42
	v_sub_f32_e32 v37, v37, v42
	v_sub_f32_e32 v36, v36, v42
	v_pk_mul_f32 v[40:41], v[42:43], v[40:41] op_sel:[1,0]
	v_pk_mul_f32 v[38:39], v[42:43], v[38:39] op_sel:[1,0]
	v_pk_mul_f32 v[36:37], v[42:43], v[36:37] op_sel:[1,0]
	v_pk_mul_f32 v[34:35], v[42:43], v[34:35] op_sel:[1,0]
	v_cvt_pk_bf16_f32 v38, v38, v39
	v_cvt_pk_bf16_f32 v39, v40, v41
	v_cvt_pk_bf16_f32 v34, v34, v35
	v_cvt_pk_bf16_f32 v35, v36, v37
	ds_write2_b64 v224, v[38:39], v[34:35] offset1:4
	v_or_b32_e32 v34, 0x200, v183
	v_add_u32_e32 v34, s0, v34
	ds_read_b64 v[34:35], v34
	s_waitcnt lgkmcnt(0)
	v_sub_f32_e32 v31, v31, v34
	v_sub_f32_e32 v30, v30, v34
	v_sub_f32_e32 v33, v33, v34
	v_sub_f32_e32 v32, v32, v34
	v_sub_f32_e32 v27, v27, v34
	v_sub_f32_e32 v26, v26, v34
	v_sub_f32_e32 v29, v29, v34
	v_sub_f32_e32 v28, v28, v34
	v_pk_mul_f32 v[32:33], v[34:35], v[32:33] op_sel:[1,0]
	v_pk_mul_f32 v[30:31], v[34:35], v[30:31] op_sel:[1,0]
	v_pk_mul_f32 v[28:29], v[34:35], v[28:29] op_sel:[1,0]
	v_pk_mul_f32 v[26:27], v[34:35], v[26:27] op_sel:[1,0]
	v_cvt_pk_bf16_f32 v30, v30, v31
	v_cvt_pk_bf16_f32 v31, v32, v33
	v_cvt_pk_bf16_f32 v26, v26, v27
	v_cvt_pk_bf16_f32 v27, v28, v29
	ds_write2_b64 v225, v[30:31], v[26:27] offset1:4
	v_or_b32_e32 v26, 0x280, v183
	v_add_u32_e32 v26, s0, v26
	ds_read_b64 v[26:27], v26
	s_waitcnt lgkmcnt(0)
	v_sub_f32_e32 v23, v23, v26
	v_sub_f32_e32 v22, v22, v26
	v_sub_f32_e32 v25, v25, v26
	v_sub_f32_e32 v24, v24, v26
	v_sub_f32_e32 v19, v19, v26
	v_sub_f32_e32 v18, v18, v26
	v_sub_f32_e32 v21, v21, v26
	v_sub_f32_e32 v20, v20, v26
	v_pk_mul_f32 v[24:25], v[26:27], v[24:25] op_sel:[1,0]
	v_pk_mul_f32 v[22:23], v[26:27], v[22:23] op_sel:[1,0]
	v_pk_mul_f32 v[20:21], v[26:27], v[20:21] op_sel:[1,0]
	v_pk_mul_f32 v[18:19], v[26:27], v[18:19] op_sel:[1,0]
	v_cvt_pk_bf16_f32 v22, v22, v23
	v_cvt_pk_bf16_f32 v23, v24, v25
	v_cvt_pk_bf16_f32 v18, v18, v19
	v_cvt_pk_bf16_f32 v19, v20, v21
	ds_write2_b64 v226, v[22:23], v[18:19] offset1:4
	v_or_b32_e32 v18, 0x300, v183
	v_add_u32_e32 v18, s0, v18
	ds_read_b64 v[18:19], v18
	v_lshl_add_u64 v[22:23], v[94:95], 0, s[14:15]
	s_waitcnt lgkmcnt(0)
	v_sub_f32_e32 v15, v15, v18
	v_sub_f32_e32 v14, v14, v18
	v_sub_f32_e32 v17, v17, v18
	v_sub_f32_e32 v16, v16, v18
	v_sub_f32_e32 v11, v11, v18
	v_sub_f32_e32 v10, v10, v18
	v_sub_f32_e32 v13, v13, v18
	v_sub_f32_e32 v12, v12, v18
	v_pk_mul_f32 v[16:17], v[18:19], v[16:17] op_sel:[1,0]
	v_pk_mul_f32 v[14:15], v[18:19], v[14:15] op_sel:[1,0]
	v_pk_mul_f32 v[12:13], v[18:19], v[12:13] op_sel:[1,0]
	v_pk_mul_f32 v[10:11], v[18:19], v[10:11] op_sel:[1,0]
	v_cvt_pk_bf16_f32 v14, v14, v15
	v_cvt_pk_bf16_f32 v15, v16, v17
	v_cvt_pk_bf16_f32 v10, v10, v11
	v_cvt_pk_bf16_f32 v11, v12, v13
	ds_write2_b64 v227, v[14:15], v[10:11] offset1:4
	v_or_b32_e32 v10, 0x380, v183
	v_add_u32_e32 v10, s0, v10
	ds_read_b64 v[10:11], v10
	s_waitcnt lgkmcnt(0)
	v_sub_f32_e32 v7, v7, v10
	v_sub_f32_e32 v6, v6, v10
	v_sub_f32_e32 v9, v9, v10
	v_sub_f32_e32 v8, v8, v10
	v_sub_f32_e32 v3, v3, v10
	v_sub_f32_e32 v2, v2, v10
	v_sub_f32_e32 v5, v5, v10
	v_sub_f32_e32 v4, v4, v10
	v_pk_mul_f32 v[8:9], v[10:11], v[8:9] op_sel:[1,0]
	v_pk_mul_f32 v[6:7], v[10:11], v[6:7] op_sel:[1,0]
	v_pk_mul_f32 v[4:5], v[10:11], v[4:5] op_sel:[1,0]
	v_pk_mul_f32 v[2:3], v[10:11], v[2:3] op_sel:[1,0]
	v_cvt_pk_bf16_f32 v6, v6, v7
	v_cvt_pk_bf16_f32 v7, v8, v9
	v_cvt_pk_bf16_f32 v2, v2, v3
	v_cvt_pk_bf16_f32 v3, v4, v5
	ds_write2_b64 v228, v[6:7], v[2:3] offset1:4
	v_lshl_add_u64 v[2:3], v[92:93], 0, s[14:15]
	v_lshl_add_u64 v[4:5], v[2:3], 0, v[98:99]
	s_waitcnt lgkmcnt(0)
	s_barrier
; #define LAS __attribute__((address_space(3)))
; __device__ __forceinline__ unsigned cvt_pk_bf16(float lo, float hi) { f32x2 v = {lo, hi}; bf16x2_t b = __builtin_convertvector(v, bf16x2_t); return __builtin_bit_cast(unsigned, b); }
; __device__ __forceinline__ float bf_lo(unsigned w) { return __uint_as_float(w << 16); }
; __device__ __forceinline__ float bf_hi(unsigned w) { return __uint_as_float(w & 0xffff0000u); }
; __device__ __forceinline__ void ret_unit(Frame& F, const Args& a, int c, int h) {
;     ...
;         __syncthreads();
;         u32x4 gx[8];
; #pragma unroll
;         for (int i = 0; i < 8; ++i) gx[i] = __builtin_nontemporal_load((const u32x4*)(RG + (size_t)(t0 + (tid >> 5) + 16 * i) * D + h * 256 + 8 * (tid & 31)));
; #pragma unroll
;         for (int i = 0; i < 8; ++i) { const int tt = (tid >> 5) + 16 * i, ch = tid & 31;
;             const u32x4 v = *(const LAS u32x4*)(OT + tt * 528 + ch * 16); const u32x4 g = gx[i];
;             u32x4 r; r.x = cvt_pk_bf16(bf_lo(v.x) * bf_lo(g.x), bf_hi(v.x) * bf_hi(g.x)); r.y = cvt_pk_bf16(bf_lo(v.y) * bf_lo(g.y), bf_hi(v.y) * bf_hi(g.y));
;             r.z = cvt_pk_bf16(bf_lo(v.z) * bf_lo(g.z), bf_hi(v.z) * bf_hi(g.z)); r.w = cvt_pk_bf16(bf_lo(v.w) * bf_lo(g.w), bf_hi(v.w) * bf_hi(g.w));
;             *(u32x4*)(RO + (size_t)(t0 + tt) * D + h * 256 + 8 * ch) = r; }
	global_load_dwordx4 v[24:27], v[4:5], off nt
	v_lshl_add_u64 v[4:5], v[2:3], 0, v[100:101]
	global_load_dwordx4 v[28:31], v[4:5], off nt
	v_lshl_add_u64 v[4:5], v[2:3], 0, v[102:103]
	global_load_dwordx4 v[32:35], v[4:5], off nt
	v_lshl_add_u64 v[4:5], v[2:3], 0, v[104:105]
	global_load_dwordx4 v[18:21], v[4:5], off nt
	v_lshl_add_u64 v[4:5], v[2:3], 0, v[106:107]
	v_lshl_add_u64 v[6:7], v[2:3], 0, v[108:109]
	global_load_dwordx4 v[14:17], v[4:5], off nt
	global_load_dwordx4 v[10:13], v[6:7], off nt
	v_lshl_add_u64 v[4:5], v[2:3], 0, v[110:111]
	v_lshl_add_u64 v[2:3], v[2:3], 0, v[112:113]
	ds_read_b128 v[36:39], v229
	global_load_dwordx4 v[6:9], v[4:5], off nt
	s_nop 0
	global_load_dwordx4 v[2:5], v[2:3], off nt
	ds_read_b128 v[40:43], v229 offset:8448
	s_waitcnt lgkmcnt(1)
	v_lshlrev_b32_e32 v44, 16, v36
	v_and_b32_e32 v45, 0xffff0000, v36
	v_lshlrev_b32_e32 v36, 16, v37
	v_and_b32_e32 v37, 0xffff0000, v37
	s_waitcnt vmcnt(7)
	v_lshlrev_b32_e32 v46, 16, v24
	v_and_b32_e32 v47, 0xffff0000, v24
	v_pk_mul_f32 v[44:45], v[46:47], v[44:45]
	s_nop 0
	v_cvt_pk_bf16_f32 v24, v44, v45
	v_lshlrev_b32_e32 v44, 16, v25
	v_and_b32_e32 v45, 0xffff0000, v25
	v_pk_mul_f32 v[36:37], v[44:45], v[36:37]
	v_lshlrev_b32_e32 v44, 16, v26
	v_cvt_pk_bf16_f32 v25, v36, v37
	v_lshlrev_b32_e32 v36, 16, v38
	v_and_b32_e32 v37, 0xffff0000, v38
	v_and_b32_e32 v45, 0xffff0000, v26
	v_pk_mul_f32 v[36:37], v[44:45], v[36:37]
	v_lshlrev_b32_e32 v38, 16, v27
	v_cvt_pk_bf16_f32 v26, v36, v37
	v_lshlrev_b32_e32 v36, 16, v39
	v_and_b32_e32 v37, 0xffff0000, v39
	v_and_b32_e32 v39, 0xffff0000, v27
	v_pk_mul_f32 v[36:37], v[38:39], v[36:37]
	s_waitcnt vmcnt(5)
	v_lshlrev_b32_e32 v38, 16, v32
	v_cvt_pk_bf16_f32 v27, v36, v37
	v_lshl_add_u64 v[36:37], v[22:23], 0, v[98:99]
	global_store_dwordx4 v[36:37], v[24:27], off sc1
	v_add_u32_e32 v36, s45, v132
	v_ashrrev_i32_e32 v37, 31, v36
	s_waitcnt lgkmcnt(0)
	v_lshlrev_b32_e32 v24, 16, v40
	v_and_b32_e32 v25, 0xffff0000, v40
	v_lshlrev_b32_e32 v26, 16, v28
	v_and_b32_e32 v27, 0xffff0000, v28
	v_pk_mul_f32 v[24:25], v[26:27], v[24:25]
	v_lshlrev_b32_e32 v26, 16, v41
	v_and_b32_e32 v27, 0xffff0000, v41
	v_lshlrev_b32_e32 v28, 16, v29
	v_and_b32_e32 v29, 0xffff0000, v29
	v_pk_mul_f32 v[26:27], v[28:29], v[26:27]
	v_cvt_pk_bf16_f32 v24, v24, v25
	v_cvt_pk_bf16_f32 v25, v26, v27
	v_lshlrev_b32_e32 v26, 16, v42
	v_and_b32_e32 v27, 0xffff0000, v42
	v_lshlrev_b32_e32 v28, 16, v30
	v_and_b32_e32 v29, 0xffff0000, v30
	v_pk_mul_f32 v[26:27], v[28:29], v[26:27]
	v_lshlrev_b32_e32 v28, 16, v43
	v_and_b32_e32 v29, 0xffff0000, v43
	v_lshlrev_b32_e32 v30, 16, v31
	v_and_b32_e32 v31, 0xffff0000, v31
	v_pk_mul_f32 v[28:29], v[30:31], v[28:29]
	v_cvt_pk_bf16_f32 v26, v26, v27
	v_cvt_pk_bf16_f32 v27, v28, v29
	ds_read_b128 v[28:31], v229 offset:16896
	v_lshlrev_b64 v[36:37], 12, v[36:37]
	v_lshl_add_u64 v[36:37], v[22:23], 0, v[36:37]
	global_store_dwordx4 v[36:37], v[24:27], off sc1
	ds_read_b128 v[24:27], v229 offset:25344
	s_waitcnt lgkmcnt(1)
	v_lshlrev_b32_e32 v36, 16, v28
	v_and_b32_e32 v37, 0xffff0000, v28
	v_and_b32_e32 v39, 0xffff0000, v32
	v_pk_mul_f32 v[36:37], v[38:39], v[36:37]
	v_lshlrev_b32_e32 v32, 16, v33
	v_cvt_pk_bf16_f32 v28, v36, v37
	v_lshlrev_b32_e32 v36, 16, v29
	v_and_b32_e32 v37, 0xffff0000, v29
	v_and_b32_e32 v33, 0xffff0000, v33
	v_pk_mul_f32 v[32:33], v[32:33], v[36:37]
	v_lshlrev_b32_e32 v36, 16, v34
	v_cvt_pk_bf16_f32 v29, v32, v33
	v_lshlrev_b32_e32 v32, 16, v30
	v_and_b32_e32 v33, 0xffff0000, v30
	v_and_b32_e32 v37, 0xffff0000, v34
	v_pk_mul_f32 v[32:33], v[36:37], v[32:33]
	v_lshlrev_b32_e32 v34, 16, v35
	v_cvt_pk_bf16_f32 v30, v32, v33
	v_lshlrev_b32_e32 v32, 16, v31
	v_and_b32_e32 v33, 0xffff0000, v31
	v_and_b32_e32 v35, 0xffff0000, v35
	v_pk_mul_f32 v[32:33], v[34:35], v[32:33]
	s_nop 0
	v_cvt_pk_bf16_f32 v31, v32, v33
	v_add_u32_e32 v32, s45, v133
	v_ashrrev_i32_e32 v33, 31, v32
	v_lshlrev_b64 v[32:33], 12, v[32:33]
	v_lshl_add_u64 v[32:33], v[22:23], 0, v[32:33]
	global_store_dwordx4 v[32:33], v[28:31], off sc1
	s_waitcnt lgkmcnt(0)
	s_nop 0
	v_lshlrev_b32_e32 v28, 16, v24
	v_and_b32_e32 v29, 0xffff0000, v24
	s_waitcnt vmcnt(7)
	v_lshlrev_b32_e32 v30, 16, v18
	v_and_b32_e32 v31, 0xffff0000, v18
	v_pk_mul_f32 v[28:29], v[30:31], v[28:29]
	v_lshlrev_b32_e32 v24, 16, v25
	v_cvt_pk_bf16_f32 v18, v28, v29
	v_and_b32_e32 v25, 0xffff0000, v25
	v_lshlrev_b32_e32 v28, 16, v19
	v_and_b32_e32 v29, 0xffff0000, v19
	v_pk_mul_f32 v[24:25], v[28:29], v[24:25]
	v_lshlrev_b32_e32 v28, 16, v20
	v_cvt_pk_bf16_f32 v19, v24, v25
	v_lshlrev_b32_e32 v24, 16, v26
	v_and_b32_e32 v25, 0xffff0000, v26
	v_and_b32_e32 v29, 0xffff0000, v20
	v_pk_mul_f32 v[24:25], v[28:29], v[24:25]
	v_lshlrev_b32_e32 v26, 16, v21
	v_cvt_pk_bf16_f32 v20, v24, v25
	v_lshlrev_b32_e32 v24, 16, v27
	v_and_b32_e32 v25, 0xffff0000, v27
	v_and_b32_e32 v27, 0xffff0000, v21
	v_pk_mul_f32 v[24:25], v[26:27], v[24:25]
	v_add_u32_e32 v28, s45, v134
	v_cvt_pk_bf16_f32 v21, v24, v25
	ds_read_b128 v[24:27], v229 offset:33792
	v_ashrrev_i32_e32 v29, 31, v28
	v_lshlrev_b64 v[28:29], 12, v[28:29]
	v_lshl_add_u64 v[28:29], v[22:23], 0, v[28:29]
	global_store_dwordx4 v[28:29], v[18:21], off sc1
	ds_read_b128 v[18:21], v229 offset:42240
	s_waitcnt lgkmcnt(1)
; #define LAS __attribute__((address_space(3)))
; __device__ __forceinline__ unsigned cvt_pk_bf16(float lo, float hi) { f32x2 v = {lo, hi}; bf16x2_t b = __builtin_convertvector(v, bf16x2_t); return __builtin_bit_cast(unsigned, b); }
; __device__ __forceinline__ float bf_lo(unsigned w) { return __uint_as_float(w << 16); }
; __device__ __forceinline__ float bf_hi(unsigned w) { return __uint_as_float(w & 0xffff0000u); }
; __device__ __forceinline__ void ret_unit(Frame& F, const Args& a, int c, int h) {
;     ...
;         for (int i = 0; i < 8; ++i) { const int tt = (tid >> 5) + 16 * i, ch = tid & 31;
;             const u32x4 v = *(const LAS u32x4*)(OT + tt * 528 + ch * 16); const u32x4 g = gx[i];
;             u32x4 r; r.x = cvt_pk_bf16(bf_lo(v.x) * bf_lo(g.x), bf_hi(v.x) * bf_hi(g.x)); r.y = cvt_pk_bf16(bf_lo(v.y) * bf_lo(g.y), bf_hi(v.y) * bf_hi(g.y));
;             r.z = cvt_pk_bf16(bf_lo(v.z) * bf_lo(g.z), bf_hi(v.z) * bf_hi(g.z)); r.w = cvt_pk_bf16(bf_lo(v.w) * bf_lo(g.w), bf_hi(v.w) * bf_hi(g.w));
;             *(u32x4*)(RO + (size_t)(t0 + tt) * D + h * 256 + 8 * ch) = r; }
;     }
;     __syncthreads();
	v_lshlrev_b32_e32 v28, 16, v24
	v_and_b32_e32 v29, 0xffff0000, v24
	s_waitcnt vmcnt(7)
	v_lshlrev_b32_e32 v30, 16, v14
	v_and_b32_e32 v31, 0xffff0000, v14
	v_pk_mul_f32 v[28:29], v[30:31], v[28:29]
	v_lshlrev_b32_e32 v24, 16, v25
	v_cvt_pk_bf16_f32 v14, v28, v29
	v_and_b32_e32 v25, 0xffff0000, v25
	v_lshlrev_b32_e32 v28, 16, v15
	v_and_b32_e32 v29, 0xffff0000, v15
	v_pk_mul_f32 v[24:25], v[28:29], v[24:25]
	v_lshlrev_b32_e32 v28, 16, v16
	v_cvt_pk_bf16_f32 v15, v24, v25
	v_lshlrev_b32_e32 v24, 16, v26
	v_and_b32_e32 v25, 0xffff0000, v26
	v_and_b32_e32 v29, 0xffff0000, v16
	v_pk_mul_f32 v[24:25], v[28:29], v[24:25]
	v_lshlrev_b32_e32 v26, 16, v17
	v_cvt_pk_bf16_f32 v16, v24, v25
	v_lshlrev_b32_e32 v24, 16, v27
	v_and_b32_e32 v25, 0xffff0000, v27
	v_and_b32_e32 v27, 0xffff0000, v17
	v_pk_mul_f32 v[24:25], v[26:27], v[24:25]
	s_nop 0
	v_cvt_pk_bf16_f32 v17, v24, v25
	v_add_u32_e32 v24, s45, v135
	v_ashrrev_i32_e32 v25, 31, v24
	v_lshlrev_b64 v[24:25], 12, v[24:25]
	v_lshl_add_u64 v[24:25], v[22:23], 0, v[24:25]
	global_store_dwordx4 v[24:25], v[14:17], off sc1
	s_waitcnt lgkmcnt(0)
	s_nop 0
	v_lshlrev_b32_e32 v14, 16, v18
	v_and_b32_e32 v15, 0xffff0000, v18
	s_waitcnt vmcnt(7)
	v_lshlrev_b32_e32 v16, 16, v10
	v_and_b32_e32 v17, 0xffff0000, v10
	v_pk_mul_f32 v[14:15], v[16:17], v[14:15]
	v_lshlrev_b32_e32 v16, 16, v11
	v_cvt_pk_bf16_f32 v10, v14, v15
	v_lshlrev_b32_e32 v14, 16, v19
	v_and_b32_e32 v15, 0xffff0000, v19
	v_and_b32_e32 v17, 0xffff0000, v11
	v_pk_mul_f32 v[14:15], v[16:17], v[14:15]
	v_lshlrev_b32_e32 v16, 16, v12
	v_cvt_pk_bf16_f32 v11, v14, v15
	v_lshlrev_b32_e32 v14, 16, v20
	v_and_b32_e32 v15, 0xffff0000, v20
	v_and_b32_e32 v17, 0xffff0000, v12
	v_pk_mul_f32 v[14:15], v[16:17], v[14:15]
	v_lshlrev_b32_e32 v16, 16, v13
	v_cvt_pk_bf16_f32 v12, v14, v15
	v_lshlrev_b32_e32 v14, 16, v21
	v_and_b32_e32 v15, 0xffff0000, v21
	v_and_b32_e32 v17, 0xffff0000, v13
	v_pk_mul_f32 v[14:15], v[16:17], v[14:15]
	v_add_u32_e32 v18, s45, v136
	v_cvt_pk_bf16_f32 v13, v14, v15
	ds_read_b128 v[14:17], v229 offset:50688
	v_ashrrev_i32_e32 v19, 31, v18
	v_lshlrev_b64 v[18:19], 12, v[18:19]
	v_lshl_add_u64 v[18:19], v[22:23], 0, v[18:19]
	global_store_dwordx4 v[18:19], v[10:13], off sc1
	ds_read_b128 v[10:13], v229 offset:59136
	s_waitcnt lgkmcnt(1)
	v_lshlrev_b32_e32 v18, 16, v14
	v_and_b32_e32 v19, 0xffff0000, v14
	s_waitcnt vmcnt(7)
	v_lshlrev_b32_e32 v20, 16, v6
	v_and_b32_e32 v21, 0xffff0000, v6
	v_pk_mul_f32 v[18:19], v[20:21], v[18:19]
	v_lshlrev_b32_e32 v14, 16, v15
	v_cvt_pk_bf16_f32 v6, v18, v19
	v_and_b32_e32 v15, 0xffff0000, v15
	v_lshlrev_b32_e32 v18, 16, v7
	v_and_b32_e32 v19, 0xffff0000, v7
	v_pk_mul_f32 v[14:15], v[18:19], v[14:15]
	v_lshlrev_b32_e32 v18, 16, v8
	v_cvt_pk_bf16_f32 v7, v14, v15
	v_lshlrev_b32_e32 v14, 16, v16
	v_and_b32_e32 v15, 0xffff0000, v16
	v_and_b32_e32 v19, 0xffff0000, v8
	v_pk_mul_f32 v[14:15], v[18:19], v[14:15]
	v_lshlrev_b32_e32 v16, 16, v9
	v_cvt_pk_bf16_f32 v8, v14, v15
	v_lshlrev_b32_e32 v14, 16, v17
	v_and_b32_e32 v15, 0xffff0000, v17
	v_and_b32_e32 v17, 0xffff0000, v9
	v_pk_mul_f32 v[14:15], v[16:17], v[14:15]
	s_nop 0
	v_cvt_pk_bf16_f32 v9, v14, v15
	v_add_u32_e32 v14, s45, v137
	v_ashrrev_i32_e32 v15, 31, v14
	v_lshlrev_b64 v[14:15], 12, v[14:15]
	v_lshl_add_u64 v[14:15], v[22:23], 0, v[14:15]
	global_store_dwordx4 v[14:15], v[6:9], off sc1
	s_waitcnt lgkmcnt(0)
	s_nop 0
	v_lshlrev_b32_e32 v6, 16, v10
	v_and_b32_e32 v7, 0xffff0000, v10
	s_waitcnt vmcnt(7)
	v_lshlrev_b32_e32 v8, 16, v2
	v_and_b32_e32 v9, 0xffff0000, v2
	v_pk_mul_f32 v[6:7], v[8:9], v[6:7]
	v_lshlrev_b32_e32 v8, 16, v3
	v_cvt_pk_bf16_f32 v2, v6, v7
	v_lshlrev_b32_e32 v6, 16, v11
	v_and_b32_e32 v7, 0xffff0000, v11
	v_and_b32_e32 v9, 0xffff0000, v3
	v_pk_mul_f32 v[6:7], v[8:9], v[6:7]
	v_lshlrev_b32_e32 v8, 16, v4
	v_cvt_pk_bf16_f32 v3, v6, v7
	v_lshlrev_b32_e32 v6, 16, v12
	v_and_b32_e32 v7, 0xffff0000, v12
	v_and_b32_e32 v9, 0xffff0000, v4
	v_pk_mul_f32 v[6:7], v[8:9], v[6:7]
	v_lshlrev_b32_e32 v8, 16, v5
	v_cvt_pk_bf16_f32 v4, v6, v7
	v_lshlrev_b32_e32 v6, 16, v13
	v_and_b32_e32 v7, 0xffff0000, v13
	v_and_b32_e32 v9, 0xffff0000, v5
	v_pk_mul_f32 v[6:7], v[8:9], v[6:7]
	s_nop 0
	v_cvt_pk_bf16_f32 v5, v6, v7
	v_add_u32_e32 v6, s45, v138
	v_ashrrev_i32_e32 v7, 31, v6
	v_lshlrev_b64 v[6:7], 12, v[6:7]
	v_lshl_add_u64 v[6:7], v[22:23], 0, v[6:7]
	global_store_dwordx4 v[6:7], v[2:5], off sc1
	s_barrier
	s_cbranch_scc0 .LBB0_504

; __device__ __forceinline__ unsigned cvt_pk_bf16(float lo, float hi) { f32x2 v = {lo, hi}; bf16x2_t b = __builtin_convertvector(v, bf16x2_t); return __builtin_bit_cast(unsigned, b); }
; __device__ __forceinline__ float bf_lo(unsigned w) { return __uint_as_float(w << 16); }
; __device__ __forceinline__ float bf_hi(unsigned w) { return __uint_as_float(w & 0xffff0000u); }
;     __device__ __forceinline__ void operator()(const AccT& acc, const pg8::Unit& u, int wr, int wc, int fr, int fq) const {
;         const int row0 = u.pm * 256 + wr * 64 + fr, col0 = u.pn * 256 + wc * 32 + 8 * fq;
;         const bf16_t* gate = (const bf16_t*)(ws + (MODE == 0 ? WS_GA : WS_GR)); bf16_t* mrg = (bf16_t*)(ws + WS_MRG);
; #pragma unroll
;         for (int ai = 0; ai < 2; ++ai) {
;             u32x4 gg[4][2], pp[4][2];
; #pragma unroll
;             for (int m = 0; m < 4; ++m)
; #pragma unroll
;                 for (int bj = 0; bj < 2; ++bj) { const size_t ro = (size_t)(row0 + ai * 128 + m * 16) * D + col0 + bj * 128; gg[m][bj] = *(const u32x4*)(gate + ro); if (MODE == 1) pp[m][bj] = *(const u32x4*)(mrg + ro); }
; #pragma unroll
;             for (int m = 0; m < 4; ++m)
; #pragma unroll
;                 for (int bj = 0; bj < 2; ++bj) { const size_t ro = (size_t)(row0 + ai * 128 + m * 16) * D + col0 + bj * 128; const u32x4 g = gg[m][bj]; const f32x4 v0 = acc[ai][bj][m][0], v1 = acc[ai][bj][m][1];
;                     float o[8] = {v0[0] * bf_lo(g.x), v0[1] * bf_hi(g.x), v0[2] * bf_lo(g.y), v0[3] * bf_hi(g.y), v1[0] * bf_lo(g.z), v1[1] * bf_hi(g.z), v1[2] * bf_lo(g.w), v1[3] * bf_hi(g.w)};
;                     if (MODE == 1) { const u32x4 p = pp[m][bj];
;                         o[0] += bf_lo(p.x); o[1] += bf_hi(p.x); o[2] += bf_lo(p.y); o[3] += bf_hi(p.y); o[4] += bf_lo(p.z); o[5] += bf_hi(p.z); o[6] += bf_lo(p.w); o[7] += bf_hi(p.w); }
;                     u32x4 w; w.x = cvt_pk_bf16(o[0], o[1]); w.y = cvt_pk_bf16(o[2], o[3]); w.z = cvt_pk_bf16(o[4], o[5]); w.w = cvt_pk_bf16(o[6], o[7]);
;                     *(u32x4*)(mrg + ro) = w; } }
.LBB0_584:
	v_lshl_or_b32 v130, s71, 8, v165
	v_lshl_add_u32 v134, s36, 8, v164
	v_ashrrev_i32_e32 v131, 31, v130
	v_lshlrev_b64 v[136:137], 1, v[130:131]
	v_ashrrev_i32_e32 v135, 31, v134
	v_lshl_add_u64 v[152:153], s[16:17], 0, v[136:137]
	v_lshlrev_b64 v[154:155], 12, v[134:135]
	v_lshl_add_u64 v[130:131], v[152:153], 0, v[154:155]
	global_load_dwordx4 v[170:173], v[130:131], off
	global_load_dwordx4 v[174:177], v[130:131], off offset:256
	v_or_b32_e32 v130, 16, v134
	v_ashrrev_i32_e32 v131, 31, v130
	v_lshlrev_b64 v[138:139], 12, v[130:131]
	v_lshl_add_u64 v[130:131], v[152:153], 0, v[138:139]
	global_load_dwordx4 v[178:181], v[130:131], off
	global_load_dwordx4 v[182:185], v[130:131], off offset:256
	v_or_b32_e32 v130, 32, v134
	v_ashrrev_i32_e32 v131, 31, v130
	v_lshlrev_b64 v[186:187], 12, v[130:131]
	v_lshl_add_u64 v[140:141], v[152:153], 0, v[186:187]
	global_load_dwordx4 v[130:133], v[140:141], off
	v_or_b32_e32 v134, 48, v134
	v_ashrrev_i32_e32 v135, 31, v134
	v_lshlrev_b64 v[156:157], 12, v[134:135]
	v_lshl_add_u64 v[150:151], s[8:9], 0, v[136:137]
	v_lshl_add_u64 v[134:135], v[152:153], 0, v[156:157]
	v_lshl_add_u64 v[190:191], v[150:151], 0, v[138:139]
	global_load_dwordx4 v[142:145], v[140:141], off offset:256
	s_nop 0
	global_load_dwordx4 v[138:141], v[134:135], off
	s_nop 0
	global_load_dwordx4 v[134:137], v[134:135], off offset:256
	v_lshl_add_u64 v[188:189], v[150:151], 0, v[154:155]
	s_and_b64 vcc, exec, s[6:7]
	s_mov_b64 s[6:7], -1
	s_waitcnt vmcnt(7)
	v_lshlrev_b32_e32 v192, 16, v170
	v_and_b32_e32 v193, 0xffff0000, v170
	v_lshlrev_b32_e32 v170, 16, v171
	v_and_b32_e32 v171, 0xffff0000, v171
	v_lshlrev_b32_e32 v194, 16, v172
	v_and_b32_e32 v195, 0xffff0000, v172
	v_lshlrev_b32_e32 v172, 16, v173
	v_and_b32_e32 v173, 0xffff0000, v173
	s_waitcnt vmcnt(6)
	v_lshlrev_b32_e32 v196, 16, v174
	v_and_b32_e32 v197, 0xffff0000, v174
	v_lshlrev_b32_e32 v174, 16, v175
	v_and_b32_e32 v175, 0xffff0000, v175
	v_lshlrev_b32_e32 v198, 16, v176
	v_and_b32_e32 v199, 0xffff0000, v176
	v_lshlrev_b32_e32 v176, 16, v177
	v_and_b32_e32 v177, 0xffff0000, v177
	s_waitcnt vmcnt(5)
	v_lshlrev_b32_e32 v200, 16, v178
	v_and_b32_e32 v201, 0xffff0000, v178
	v_lshlrev_b32_e32 v178, 16, v179
	v_and_b32_e32 v179, 0xffff0000, v179
	v_lshlrev_b32_e32 v202, 16, v180
	v_and_b32_e32 v203, 0xffff0000, v180
	v_lshlrev_b32_e32 v180, 16, v181
	v_and_b32_e32 v181, 0xffff0000, v181
	v_pk_mul_f32 v[114:115], v[114:115], v[192:193]
	v_pk_mul_f32 v[116:117], v[116:117], v[170:171]
	v_pk_mul_f32 v[110:111], v[110:111], v[194:195]
	v_pk_mul_f32 v[112:113], v[112:113], v[172:173]
	s_waitcnt vmcnt(4)
	v_lshlrev_b32_e32 v206, 16, v184
	v_pk_mul_f32 v[126:127], v[126:127], v[196:197]
	v_pk_mul_f32 v[128:129], v[128:129], v[174:175]
	v_pk_mul_f32 v[122:123], v[122:123], v[198:199]
	v_pk_mul_f32 v[124:125], v[124:125], v[176:177]
	v_pk_mul_f32 v[170:171], v[106:107], v[200:201]
	v_pk_mul_f32 v[172:173], v[108:109], v[178:179]
	v_pk_mul_f32 v[174:175], v[102:103], v[202:203]
	v_pk_mul_f32 v[176:177], v[104:105], v[180:181]
	v_cvt_pk_bf16_f32 v102, v114, v115
	v_cvt_pk_bf16_f32 v103, v116, v117
	v_cvt_pk_bf16_f32 v104, v110, v111
	v_cvt_pk_bf16_f32 v105, v112, v113
	v_and_b32_e32 v207, 0xffff0000, v184
	v_lshlrev_b32_e32 v204, 16, v182
	v_and_b32_e32 v205, 0xffff0000, v182
	v_lshlrev_b32_e32 v182, 16, v183
	v_and_b32_e32 v183, 0xffff0000, v183
	v_cvt_pk_bf16_f32 v106, v126, v127
	v_cvt_pk_bf16_f32 v107, v128, v129
	v_cvt_pk_bf16_f32 v108, v122, v123
	v_cvt_pk_bf16_f32 v109, v124, v125
	v_cvt_pk_bf16_f32 v110, v170, v171
	v_cvt_pk_bf16_f32 v111, v172, v173
	v_cvt_pk_bf16_f32 v112, v174, v175
	v_cvt_pk_bf16_f32 v113, v176, v177
	global_store_dwordx4 v[188:189], v[102:105], off sc1
	global_store_dwordx4 v[188:189], v[106:109], off offset:256 sc1
	global_store_dwordx4 v[190:191], v[110:113], off sc1
	v_pk_mul_f32 v[102:103], v[98:99], v[206:207]
	v_lshlrev_b32_e32 v98, 16, v185
	v_and_b32_e32 v99, 0xffff0000, v185
	v_pk_mul_f32 v[118:119], v[118:119], v[204:205]
	v_pk_mul_f32 v[120:121], v[120:121], v[182:183]
	v_pk_mul_f32 v[104:105], v[100:101], v[98:99]
	v_cvt_pk_bf16_f32 v98, v118, v119
	v_cvt_pk_bf16_f32 v99, v120, v121
	v_cvt_pk_bf16_f32 v100, v102, v103
	v_cvt_pk_bf16_f32 v101, v104, v105
	v_lshl_add_u64 v[106:107], v[154:155], 0, s[20:21]
	global_store_dwordx4 v[190:191], v[98:101], off offset:256 sc1
	s_waitcnt vmcnt(7)
	v_lshlrev_b32_e32 v104, 16, v131
	v_lshl_add_u64 v[108:109], v[152:153], 0, v[106:107]
	v_lshlrev_b32_e32 v98, 16, v130
	v_and_b32_e32 v99, 0xffff0000, v130
	v_and_b32_e32 v105, 0xffff0000, v131
	v_pk_mul_f32 v[94:95], v[94:95], v[98:99]
	global_load_dwordx4 v[98:101], v[108:109], off
	v_pk_mul_f32 v[96:97], v[96:97], v[104:105]
	v_lshlrev_b32_e32 v104, 16, v132
	v_and_b32_e32 v105, 0xffff0000, v132
	v_pk_mul_f32 v[104:105], v[86:87], v[104:105]
	v_lshlrev_b32_e32 v86, 16, v133
	v_and_b32_e32 v87, 0xffff0000, v133
	v_pk_mul_f32 v[110:111], v[88:89], v[86:87]
	v_lshl_add_u64 v[102:103], v[150:151], 0, v[186:187]
	v_cvt_pk_bf16_f32 v86, v94, v95
	v_cvt_pk_bf16_f32 v87, v96, v97
	v_cvt_pk_bf16_f32 v88, v104, v105
	v_cvt_pk_bf16_f32 v89, v110, v111
	global_store_dwordx4 v[102:103], v[86:89], off sc1
	s_waitcnt vmcnt(8)
	v_lshlrev_b32_e32 v94, 16, v143
	v_and_b32_e32 v95, 0xffff0000, v143
	v_lshlrev_b32_e32 v86, 16, v142
	v_and_b32_e32 v87, 0xffff0000, v142
	v_pk_mul_f32 v[90:91], v[90:91], v[86:87]
	global_load_dwordx4 v[86:89], v[108:109], off offset:256
	v_pk_mul_f32 v[92:93], v[92:93], v[94:95]
	v_lshlrev_b32_e32 v94, 16, v144
	v_and_b32_e32 v95, 0xffff0000, v144
	v_pk_mul_f32 v[94:95], v[82:83], v[94:95]
	v_lshlrev_b32_e32 v82, 16, v145
	v_and_b32_e32 v83, 0xffff0000, v145
	v_pk_mul_f32 v[96:97], v[84:85], v[82:83]
	v_cvt_pk_bf16_f32 v84, v94, v95
	v_lshl_add_u64 v[94:95], v[154:155], 0, s[22:23]
	v_cvt_pk_bf16_f32 v82, v90, v91
	v_cvt_pk_bf16_f32 v83, v92, v93
	v_cvt_pk_bf16_f32 v85, v96, v97
	v_lshl_add_u64 v[92:93], v[152:153], 0, v[94:95]
	global_store_dwordx4 v[102:103], v[82:85], off offset:256 sc1
	global_load_dwordx4 v[82:85], v[92:93], off
	s_waitcnt vmcnt(10)
; __device__ __forceinline__ unsigned cvt_pk_bf16(float lo, float hi) { f32x2 v = {lo, hi}; bf16x2_t b = __builtin_convertvector(v, bf16x2_t); return __builtin_bit_cast(unsigned, b); }
; __device__ __forceinline__ float bf_lo(unsigned w) { return __uint_as_float(w << 16); }
; __device__ __forceinline__ float bf_hi(unsigned w) { return __uint_as_float(w & 0xffff0000u); }
;     __device__ __forceinline__ void operator()(const AccT& acc, const pg8::Unit& u, int wr, int wc, int fr, int fq) const {
;     ...
;                 for (int bj = 0; bj < 2; ++bj) { const size_t ro = (size_t)(row0 + ai * 128 + m * 16) * D + col0 + bj * 128; gg[m][bj] = *(const u32x4*)(gate + ro); if (MODE == 1) pp[m][bj] = *(const u32x4*)(mrg + ro); }
; #pragma unroll
;             for (int m = 0; m < 4; ++m)
; #pragma unroll
;                 for (int bj = 0; bj < 2; ++bj) { const size_t ro = (size_t)(row0 + ai * 128 + m * 16) * D + col0 + bj * 128; const u32x4 g = gg[m][bj]; const f32x4 v0 = acc[ai][bj][m][0], v1 = acc[ai][bj][m][1];
;                     float o[8] = {v0[0] * bf_lo(g.x), v0[1] * bf_hi(g.x), v0[2] * bf_lo(g.y), v0[3] * bf_hi(g.y), v1[0] * bf_lo(g.z), v1[1] * bf_hi(g.z), v1[2] * bf_lo(g.w), v1[3] * bf_hi(g.w)};
;                     if (MODE == 1) { const u32x4 p = pp[m][bj];
;                         o[0] += bf_lo(p.x); o[1] += bf_hi(p.x); o[2] += bf_lo(p.y); o[3] += bf_hi(p.y); o[4] += bf_lo(p.z); o[5] += bf_hi(p.z); o[6] += bf_lo(p.w); o[7] += bf_hi(p.w); }
;                     u32x4 w; w.x = cvt_pk_bf16(o[0], o[1]); w.y = cvt_pk_bf16(o[2], o[3]); w.z = cvt_pk_bf16(o[4], o[5]); w.w = cvt_pk_bf16(o[6], o[7]);
;                     *(u32x4*)(mrg + ro) = w; } }
	v_lshlrev_b32_e32 v96, 16, v138
	v_and_b32_e32 v97, 0xffff0000, v138
	v_pk_mul_f32 v[70:71], v[70:71], v[96:97]
	v_lshlrev_b32_e32 v96, 16, v139
	v_and_b32_e32 v97, 0xffff0000, v139
	v_pk_mul_f32 v[72:73], v[72:73], v[96:97]
	v_lshlrev_b32_e32 v96, 16, v140
	v_and_b32_e32 v97, 0xffff0000, v140
	v_pk_mul_f32 v[96:97], v[58:59], v[96:97]
	v_lshlrev_b32_e32 v58, 16, v141
	v_and_b32_e32 v59, 0xffff0000, v141
	v_pk_mul_f32 v[102:103], v[60:61], v[58:59]
	v_cvt_pk_bf16_f32 v58, v70, v71
	v_cvt_pk_bf16_f32 v59, v72, v73
	global_load_dwordx4 v[70:73], v[92:93], off offset:256
	v_lshl_add_u64 v[90:91], v[150:151], 0, v[156:157]
	v_cvt_pk_bf16_f32 v60, v96, v97
	v_cvt_pk_bf16_f32 v61, v102, v103
	global_store_dwordx4 v[90:91], v[58:61], off sc1
	v_lshl_add_u64 v[96:97], v[154:155], 0, s[24:25]
	v_lshl_add_u64 v[92:93], v[152:153], 0, v[96:97]
	s_waitcnt vmcnt(11)
	v_lshlrev_b32_e32 v58, 16, v134
	v_and_b32_e32 v59, 0xffff0000, v134
	v_pk_mul_f32 v[58:59], v[66:67], v[58:59]
	v_lshlrev_b32_e32 v60, 16, v135
	v_and_b32_e32 v61, 0xffff0000, v135
	v_lshlrev_b32_e32 v66, 16, v136
	v_and_b32_e32 v67, 0xffff0000, v136
	v_pk_mul_f32 v[60:61], v[68:69], v[60:61]
	v_pk_mul_f32 v[66:67], v[54:55], v[66:67]
	v_lshlrev_b32_e32 v54, 16, v137
	v_and_b32_e32 v55, 0xffff0000, v137
	v_pk_mul_f32 v[68:69], v[56:57], v[54:55]
	v_cvt_pk_bf16_f32 v54, v58, v59
	v_cvt_pk_bf16_f32 v55, v60, v61
	global_load_dwordx4 v[58:61], v[92:93], off
	v_cvt_pk_bf16_f32 v56, v66, v67
	v_cvt_pk_bf16_f32 v57, v68, v69
	global_load_dwordx4 v[66:69], v[92:93], off offset:256
	v_lshl_add_u64 v[102:103], v[154:155], 0, s[26:27]
	global_store_dwordx4 v[90:91], v[54:57], off offset:256 sc1
	v_lshl_add_u64 v[104:105], v[150:151], 0, v[106:107]
	s_waitcnt vmcnt(9)
	v_lshlrev_b32_e32 v106, 16, v98
	v_lshl_add_u64 v[54:55], v[152:153], 0, v[102:103]
	global_load_dwordx4 v[90:93], v[54:55], off
	s_nop 0
	global_load_dwordx4 v[54:57], v[54:55], off offset:256
	v_and_b32_e32 v107, 0xffff0000, v98
	v_lshlrev_b32_e32 v98, 16, v99
	v_and_b32_e32 v99, 0xffff0000, v99
	v_pk_mul_f32 v[80:81], v[80:81], v[98:99]
	v_lshlrev_b32_e32 v98, 16, v100
	v_and_b32_e32 v99, 0xffff0000, v100
	v_pk_mul_f32 v[98:99], v[74:75], v[98:99]
	v_lshlrev_b32_e32 v74, 16, v101
	v_and_b32_e32 v75, 0xffff0000, v101
	v_pk_mul_f32 v[78:79], v[78:79], v[106:107]
	v_pk_mul_f32 v[100:101], v[76:77], v[74:75]
	v_cvt_pk_bf16_f32 v74, v78, v79
	v_cvt_pk_bf16_f32 v75, v80, v81
	v_cvt_pk_bf16_f32 v76, v98, v99
	v_cvt_pk_bf16_f32 v77, v100, v101
	global_store_dwordx4 v[104:105], v[74:77], off sc1
	s_waitcnt vmcnt(10)
	s_nop 0
	v_lshlrev_b32_e32 v74, 16, v86
	v_and_b32_e32 v75, 0xffff0000, v86
	v_pk_mul_f32 v[62:63], v[62:63], v[74:75]
	v_lshlrev_b32_e32 v74, 16, v87
	v_and_b32_e32 v75, 0xffff0000, v87
	v_pk_mul_f32 v[64:65], v[64:65], v[74:75]
	v_lshlrev_b32_e32 v74, 16, v88
	v_and_b32_e32 v75, 0xffff0000, v88
	v_pk_mul_f32 v[74:75], v[50:51], v[74:75]
	v_lshlrev_b32_e32 v50, 16, v89
	v_and_b32_e32 v51, 0xffff0000, v89
	v_pk_mul_f32 v[76:77], v[52:53], v[50:51]
	v_cvt_pk_bf16_f32 v50, v62, v63
	v_cvt_pk_bf16_f32 v51, v64, v65
	v_cvt_pk_bf16_f32 v52, v74, v75
	v_cvt_pk_bf16_f32 v53, v76, v77
	global_store_dwordx4 v[104:105], v[50:53], off offset:256 sc1
	s_waitcnt vmcnt(9)
	s_nop 0
	v_lshlrev_b32_e32 v52, 16, v82
	v_and_b32_e32 v53, 0xffff0000, v82
	v_pk_mul_f32 v[46:47], v[46:47], v[52:53]
	v_lshlrev_b32_e32 v52, 16, v83
	v_and_b32_e32 v53, 0xffff0000, v83
	v_pk_mul_f32 v[48:49], v[48:49], v[52:53]
	v_lshlrev_b32_e32 v52, 16, v84
	v_and_b32_e32 v53, 0xffff0000, v84
	v_pk_mul_f32 v[52:53], v[42:43], v[52:53]
	v_lshlrev_b32_e32 v42, 16, v85
	v_and_b32_e32 v43, 0xffff0000, v85
	v_pk_mul_f32 v[62:63], v[44:45], v[42:43]
	v_lshl_add_u64 v[50:51], v[150:151], 0, v[94:95]
	v_cvt_pk_bf16_f32 v42, v46, v47
	v_cvt_pk_bf16_f32 v43, v48, v49
	v_cvt_pk_bf16_f32 v44, v52, v53
	v_cvt_pk_bf16_f32 v45, v62, v63
	global_store_dwordx4 v[50:51], v[42:45], off sc1
	s_waitcnt vmcnt(9)
; __device__ __forceinline__ unsigned cvt_pk_bf16(float lo, float hi) { f32x2 v = {lo, hi}; bf16x2_t b = __builtin_convertvector(v, bf16x2_t); return __builtin_bit_cast(unsigned, b); }
; __device__ __forceinline__ float bf_lo(unsigned w) { return __uint_as_float(w << 16); }
; __device__ __forceinline__ float bf_hi(unsigned w) { return __uint_as_float(w & 0xffff0000u); }
;     __device__ __forceinline__ void operator()(const AccT& acc, const pg8::Unit& u, int wr, int wc, int fr, int fq) const {
;     ...
;                 for (int bj = 0; bj < 2; ++bj) { const size_t ro = (size_t)(row0 + ai * 128 + m * 16) * D + col0 + bj * 128; gg[m][bj] = *(const u32x4*)(gate + ro); if (MODE == 1) pp[m][bj] = *(const u32x4*)(mrg + ro); }
; #pragma unroll
;             for (int m = 0; m < 4; ++m)
; #pragma unroll
;                 for (int bj = 0; bj < 2; ++bj) { const size_t ro = (size_t)(row0 + ai * 128 + m * 16) * D + col0 + bj * 128; const u32x4 g = gg[m][bj]; const f32x4 v0 = acc[ai][bj][m][0], v1 = acc[ai][bj][m][1];
;                     float o[8] = {v0[0] * bf_lo(g.x), v0[1] * bf_hi(g.x), v0[2] * bf_lo(g.y), v0[3] * bf_hi(g.y), v1[0] * bf_lo(g.z), v1[1] * bf_hi(g.z), v1[2] * bf_lo(g.w), v1[3] * bf_hi(g.w)};
;                     if (MODE == 1) { const u32x4 p = pp[m][bj];
;                         o[0] += bf_lo(p.x); o[1] += bf_hi(p.x); o[2] += bf_lo(p.y); o[3] += bf_hi(p.y); o[4] += bf_lo(p.z); o[5] += bf_hi(p.z); o[6] += bf_lo(p.w); o[7] += bf_hi(p.w); }
;                     u32x4 w; w.x = cvt_pk_bf16(o[0], o[1]); w.y = cvt_pk_bf16(o[2], o[3]); w.z = cvt_pk_bf16(o[4], o[5]); w.w = cvt_pk_bf16(o[6], o[7]);
;                     *(u32x4*)(mrg + ro) = w; } }
	s_nop 0
	v_lshlrev_b32_e32 v42, 16, v70
	v_and_b32_e32 v43, 0xffff0000, v70
	v_pk_mul_f32 v[38:39], v[38:39], v[42:43]
	v_lshlrev_b32_e32 v42, 16, v71
	v_and_b32_e32 v43, 0xffff0000, v71
	v_pk_mul_f32 v[40:41], v[40:41], v[42:43]
	v_lshlrev_b32_e32 v42, 16, v72
	v_and_b32_e32 v43, 0xffff0000, v72
	v_pk_mul_f32 v[42:43], v[34:35], v[42:43]
	v_lshlrev_b32_e32 v34, 16, v73
	v_and_b32_e32 v35, 0xffff0000, v73
	v_pk_mul_f32 v[44:45], v[36:37], v[34:35]
	v_cvt_pk_bf16_f32 v34, v38, v39
	v_cvt_pk_bf16_f32 v35, v40, v41
	v_cvt_pk_bf16_f32 v36, v42, v43
	v_cvt_pk_bf16_f32 v37, v44, v45
	global_store_dwordx4 v[50:51], v[34:37], off offset:256 sc1
	s_waitcnt vmcnt(8)
	s_nop 0
	v_lshlrev_b32_e32 v36, 16, v58
	v_and_b32_e32 v37, 0xffff0000, v58
	v_pk_mul_f32 v[30:31], v[30:31], v[36:37]
	v_lshlrev_b32_e32 v36, 16, v59
	v_and_b32_e32 v37, 0xffff0000, v59
	v_pk_mul_f32 v[32:33], v[32:33], v[36:37]
	v_lshlrev_b32_e32 v36, 16, v60
	v_and_b32_e32 v37, 0xffff0000, v60
	v_pk_mul_f32 v[36:37], v[26:27], v[36:37]
	v_lshlrev_b32_e32 v26, 16, v61
	v_and_b32_e32 v27, 0xffff0000, v61
	v_pk_mul_f32 v[38:39], v[28:29], v[26:27]
	v_lshl_add_u64 v[34:35], v[150:151], 0, v[96:97]
	v_cvt_pk_bf16_f32 v26, v30, v31
	v_cvt_pk_bf16_f32 v27, v32, v33
	v_cvt_pk_bf16_f32 v28, v36, v37
	v_cvt_pk_bf16_f32 v29, v38, v39
	global_store_dwordx4 v[34:35], v[26:29], off sc1
	s_waitcnt vmcnt(8)
	s_nop 0
	v_lshlrev_b32_e32 v26, 16, v66
	v_and_b32_e32 v27, 0xffff0000, v66
	v_pk_mul_f32 v[22:23], v[22:23], v[26:27]
	v_lshlrev_b32_e32 v26, 16, v67
	v_and_b32_e32 v27, 0xffff0000, v67
	v_pk_mul_f32 v[24:25], v[24:25], v[26:27]
	v_lshlrev_b32_e32 v26, 16, v68
	v_and_b32_e32 v27, 0xffff0000, v68
	v_pk_mul_f32 v[26:27], v[18:19], v[26:27]
	v_lshlrev_b32_e32 v18, 16, v69
	v_and_b32_e32 v19, 0xffff0000, v69
	v_pk_mul_f32 v[28:29], v[20:21], v[18:19]
	v_cvt_pk_bf16_f32 v18, v22, v23
	v_cvt_pk_bf16_f32 v19, v24, v25
	v_cvt_pk_bf16_f32 v20, v26, v27
	v_cvt_pk_bf16_f32 v21, v28, v29
	global_store_dwordx4 v[34:35], v[18:21], off offset:256 sc1
	s_waitcnt vmcnt(7)
	s_nop 0
	v_lshlrev_b32_e32 v20, 16, v90
	v_and_b32_e32 v21, 0xffff0000, v90
	v_pk_mul_f32 v[14:15], v[14:15], v[20:21]
	v_lshlrev_b32_e32 v20, 16, v91
	v_and_b32_e32 v21, 0xffff0000, v91
	v_pk_mul_f32 v[16:17], v[16:17], v[20:21]
	v_lshlrev_b32_e32 v20, 16, v92
	v_and_b32_e32 v21, 0xffff0000, v92
	v_pk_mul_f32 v[20:21], v[10:11], v[20:21]
	v_lshlrev_b32_e32 v10, 16, v93
	v_and_b32_e32 v11, 0xffff0000, v93
	v_pk_mul_f32 v[22:23], v[12:13], v[10:11]
	v_lshl_add_u64 v[18:19], v[150:151], 0, v[102:103]
	v_cvt_pk_bf16_f32 v10, v14, v15
	v_cvt_pk_bf16_f32 v11, v16, v17
	v_cvt_pk_bf16_f32 v12, v20, v21
	v_cvt_pk_bf16_f32 v13, v22, v23
	global_store_dwordx4 v[18:19], v[10:13], off sc1
	s_waitcnt vmcnt(7)
	s_nop 0
	v_lshlrev_b32_e32 v10, 16, v54
	v_and_b32_e32 v11, 0xffff0000, v54
	v_pk_mul_f32 v[6:7], v[6:7], v[10:11]
	v_lshlrev_b32_e32 v10, 16, v55
	v_and_b32_e32 v11, 0xffff0000, v55
	v_pk_mul_f32 v[8:9], v[8:9], v[10:11]
	v_lshlrev_b32_e32 v10, 16, v56
	v_and_b32_e32 v11, 0xffff0000, v56
	v_pk_mul_f32 v[10:11], v[2:3], v[10:11]
	v_lshlrev_b32_e32 v2, 16, v57
	v_and_b32_e32 v3, 0xffff0000, v57
	v_pk_mul_f32 v[12:13], v[4:5], v[2:3]
	v_cvt_pk_bf16_f32 v2, v6, v7
	v_cvt_pk_bf16_f32 v3, v8, v9
	v_cvt_pk_bf16_f32 v4, v10, v11
	v_cvt_pk_bf16_f32 v5, v12, v13
	global_store_dwordx4 v[18:19], v[2:5], off offset:256 sc1
	s_cbranch_vccnz .LBB0_565
	s_andn2_b64 vcc, exec, s[14:15]
	s_cbranch_vccnz .LBB0_564
	s_barrier
	s_branch .LBB0_564

; __device__ __forceinline__ unsigned cvt_pk_bf16(float lo, float hi) { f32x2 v = {lo, hi}; bf16x2_t b = __builtin_convertvector(v, bf16x2_t); return __builtin_bit_cast(unsigned, b); }
; __device__ __forceinline__ float bf_lo(unsigned w) { return __uint_as_float(w << 16); }
; __device__ __forceinline__ float bf_hi(unsigned w) { return __uint_as_float(w & 0xffff0000u); }
;     __device__ __forceinline__ void operator()(const AccT& acc, const pg8::Unit& u, int wr, int wc, int fr, int fq) const {
;     ...
;                 for (int bj = 0; bj < 2; ++bj) { const size_t ro = (size_t)(row0 + ai * 128 + m * 16) * D + col0 + bj * 128; gg[m][bj] = *(const u32x4*)(gate + ro); if (MODE == 1) pp[m][bj] = *(const u32x4*)(mrg + ro); }
; #pragma unroll
;             for (int m = 0; m < 4; ++m)
; #pragma unroll
;                 for (int bj = 0; bj < 2; ++bj) { const size_t ro = (size_t)(row0 + ai * 128 + m * 16) * D + col0 + bj * 128; const u32x4 g = gg[m][bj]; const f32x4 v0 = acc[ai][bj][m][0], v1 = acc[ai][bj][m][1];
;                     float o[8] = {v0[0] * bf_lo(g.x), v0[1] * bf_hi(g.x), v0[2] * bf_lo(g.y), v0[3] * bf_hi(g.y), v1[0] * bf_lo(g.z), v1[1] * bf_hi(g.z), v1[2] * bf_lo(g.w), v1[3] * bf_hi(g.w)};
;                     if (MODE == 1) { const u32x4 p = pp[m][bj];
;                         o[0] += bf_lo(p.x); o[1] += bf_hi(p.x); o[2] += bf_lo(p.y); o[3] += bf_hi(p.y); o[4] += bf_lo(p.z); o[5] += bf_hi(p.z); o[6] += bf_lo(p.w); o[7] += bf_hi(p.w); }
;                     u32x4 w; w.x = cvt_pk_bf16(o[0], o[1]); w.y = cvt_pk_bf16(o[2], o[3]); w.z = cvt_pk_bf16(o[4], o[5]); w.w = cvt_pk_bf16(o[6], o[7]);
;                     *(u32x4*)(mrg + ro) = w; } }
.LBB0_614:
	v_lshl_add_u32 v166, s22, 8, v177
	v_lshl_or_b32 v164, s56, 8, v178
	v_ashrrev_i32_e32 v167, 31, v166
	v_ashrrev_i32_e32 v165, 31, v164
	v_lshlrev_b64 v[130:131], 11, v[166:167]
	v_lshl_add_u64 v[130:131], v[130:131], 0, v[164:165]
	v_lshlrev_b64 v[130:131], 1, v[130:131]
	v_lshl_add_u64 v[132:133], s[12:13], 0, v[130:131]
	v_lshl_add_u64 v[162:163], v[164:165], 1, s[8:9]
	global_load_dwordx4 v[184:187], v[132:133], off
	v_lshlrev_b64 v[132:133], 12, v[166:167]
	v_lshl_add_u64 v[158:159], v[162:163], 0, v[132:133]
	global_load_dwordx4 v[188:191], v[158:159], off
	v_or_b32_e32 v130, 0x100, v130
	v_lshl_add_u64 v[132:133], s[12:13], 0, v[130:131]
	v_lshl_add_u64 v[130:131], s[8:9], 0, v[130:131]
	global_load_dwordx4 v[192:195], v[132:133], off
	global_load_dwordx4 v[196:199], v[130:131], off
	v_or_b32_e32 v130, 16, v166
	v_ashrrev_i32_e32 v131, 31, v130
	v_lshlrev_b64 v[136:137], 11, v[130:131]
	v_lshl_add_u64 v[136:137], v[136:137], 0, v[164:165]
	v_lshlrev_b64 v[130:131], 12, v[130:131]
	v_lshlrev_b64 v[136:137], 1, v[136:137]
	v_lshl_add_u64 v[142:143], s[12:13], 0, v[136:137]
	v_lshl_add_u64 v[220:221], v[162:163], 0, v[130:131]
	global_load_dwordx4 v[200:203], v[142:143], off
	global_load_dwordx4 v[204:207], v[220:221], off
	v_or_b32_e32 v132, 32, v166
	v_or_b32_e32 v134, 48, v166
	v_ashrrev_i32_e32 v133, 31, v132
	v_ashrrev_i32_e32 v135, 31, v134
	v_lshlrev_b64 v[138:139], 11, v[132:133]
	v_lshlrev_b64 v[132:133], 12, v[132:133]
	v_lshlrev_b64 v[140:141], 11, v[134:135]
	v_lshl_add_u64 v[130:131], v[138:139], 0, v[164:165]
	v_lshl_add_u64 v[170:171], v[162:163], 0, v[132:133]
	v_lshl_add_u64 v[132:133], v[140:141], 0, v[164:165]
	v_lshlrev_b64 v[134:135], 12, v[134:135]
	v_lshlrev_b64 v[130:131], 1, v[130:131]
	v_lshlrev_b64 v[132:133], 1, v[132:133]
	v_lshl_add_u64 v[168:169], v[162:163], 0, v[134:135]
	v_or_b32_e32 v136, 0x100, v136
	v_lshl_add_u64 v[134:135], s[12:13], 0, v[130:131]
	v_or_b32_e32 v130, 0x100, v130
	v_lshl_add_u64 v[138:139], s[12:13], 0, v[132:133]
	v_or_b32_e32 v132, 0x100, v132
	v_lshl_add_u64 v[146:147], s[12:13], 0, v[136:137]
	v_lshl_add_u64 v[136:137], s[8:9], 0, v[136:137]
	global_load_dwordx4 v[208:211], v[134:135], off
	global_load_dwordx4 v[154:157], v[170:171], off
	v_lshl_add_u64 v[134:135], s[12:13], 0, v[130:131]
	v_lshl_add_u64 v[130:131], s[8:9], 0, v[130:131]
	v_lshl_add_u64 v[222:223], s[12:13], 0, v[132:133]
	v_lshl_add_u64 v[132:133], s[8:9], 0, v[132:133]
	global_load_dwordx4 v[142:145], v[138:139], off
	s_nop 0
	global_load_dwordx4 v[138:141], v[168:169], off
	global_load_dwordx4 v[212:215], v[146:147], off
	global_load_dwordx4 v[216:219], v[136:137], off
	global_load_dwordx4 v[150:153], v[134:135], off
	s_nop 0
	global_load_dwordx4 v[146:149], v[130:131], off
	global_load_dwordx4 v[134:137], v[222:223], off
	s_nop 0
	global_load_dwordx4 v[130:133], v[132:133], off
	s_and_b64 vcc, exec, s[6:7]
	s_mov_b64 s[6:7], -1
	s_waitcnt vmcnt(15)
	v_lshlrev_b32_e32 v222, 16, v184
	v_and_b32_e32 v223, 0xffff0000, v184
	v_lshlrev_b32_e32 v184, 16, v185
	s_waitcnt vmcnt(14)
	v_lshlrev_b32_e32 v224, 16, v188
	v_and_b32_e32 v225, 0xffff0000, v188
	v_and_b32_e32 v185, 0xffff0000, v185
	v_lshlrev_b32_e32 v188, 16, v189
	v_and_b32_e32 v189, 0xffff0000, v189
	v_lshlrev_b32_e32 v226, 16, v186
	v_and_b32_e32 v227, 0xffff0000, v186
	v_lshlrev_b32_e32 v228, 16, v190
	v_and_b32_e32 v229, 0xffff0000, v190
	v_lshlrev_b32_e32 v186, 16, v187
	v_and_b32_e32 v187, 0xffff0000, v187
	v_lshlrev_b32_e32 v190, 16, v191
	v_and_b32_e32 v191, 0xffff0000, v191
	v_pk_fma_f32 v[126:127], v[126:127], v[222:223], v[224:225]
	v_pk_fma_f32 v[128:129], v[128:129], v[184:185], v[188:189]
	v_pk_fma_f32 v[184:185], v[122:123], v[226:227], v[228:229]
	v_pk_fma_f32 v[186:187], v[124:125], v[186:187], v[190:191]
	v_cvt_pk_bf16_f32 v122, v126, v127
	v_cvt_pk_bf16_f32 v123, v128, v129
	v_cvt_pk_bf16_f32 v124, v184, v185
	v_cvt_pk_bf16_f32 v125, v186, v187
	s_waitcnt vmcnt(13)
	v_lshlrev_b32_e32 v188, 16, v192
	v_and_b32_e32 v189, 0xffff0000, v192
	global_store_dwordx4 v[158:159], v[122:125], off sc1
	s_waitcnt vmcnt(13)
	s_nop 0
	v_lshlrev_b32_e32 v122, 16, v196
	v_and_b32_e32 v123, 0xffff0000, v196
	v_pk_fma_f32 v[118:119], v[118:119], v[188:189], v[122:123]
	v_lshlrev_b32_e32 v122, 16, v193
	v_and_b32_e32 v123, 0xffff0000, v193
	v_lshlrev_b32_e32 v124, 16, v197
	v_and_b32_e32 v125, 0xffff0000, v197
	v_pk_fma_f32 v[120:121], v[120:121], v[122:123], v[124:125]
	v_lshlrev_b32_e32 v122, 16, v194
	v_and_b32_e32 v123, 0xffff0000, v194
	v_lshlrev_b32_e32 v124, 16, v198
	v_and_b32_e32 v125, 0xffff0000, v198
	v_pk_fma_f32 v[122:123], v[114:115], v[122:123], v[124:125]
	v_lshlrev_b32_e32 v114, 16, v195
	v_and_b32_e32 v115, 0xffff0000, v195
	v_lshlrev_b32_e32 v124, 16, v199
	v_and_b32_e32 v125, 0xffff0000, v199
	v_pk_fma_f32 v[124:125], v[116:117], v[114:115], v[124:125]
	v_cvt_pk_bf16_f32 v114, v118, v119
	v_cvt_pk_bf16_f32 v115, v120, v121
	v_cvt_pk_bf16_f32 v116, v122, v123
	v_cvt_pk_bf16_f32 v117, v124, v125
	global_store_dwordx4 v[158:159], v[114:117], off offset:256 sc1
	s_waitcnt vmcnt(13)
	s_nop 0
	v_lshlrev_b32_e32 v114, 16, v200
	v_and_b32_e32 v115, 0xffff0000, v200
	s_waitcnt vmcnt(12)
; __device__ __forceinline__ unsigned cvt_pk_bf16(float lo, float hi) { f32x2 v = {lo, hi}; bf16x2_t b = __builtin_convertvector(v, bf16x2_t); return __builtin_bit_cast(unsigned, b); }
; __device__ __forceinline__ float bf_lo(unsigned w) { return __uint_as_float(w << 16); }
; __device__ __forceinline__ float bf_hi(unsigned w) { return __uint_as_float(w & 0xffff0000u); }
;     __device__ __forceinline__ void operator()(const AccT& acc, const pg8::Unit& u, int wr, int wc, int fr, int fq) const {
;     ...
;                 for (int bj = 0; bj < 2; ++bj) { const size_t ro = (size_t)(row0 + ai * 128 + m * 16) * D + col0 + bj * 128; gg[m][bj] = *(const u32x4*)(gate + ro); if (MODE == 1) pp[m][bj] = *(const u32x4*)(mrg + ro); }
; #pragma unroll
;             for (int m = 0; m < 4; ++m)
; #pragma unroll
;                 for (int bj = 0; bj < 2; ++bj) { const size_t ro = (size_t)(row0 + ai * 128 + m * 16) * D + col0 + bj * 128; const u32x4 g = gg[m][bj]; const f32x4 v0 = acc[ai][bj][m][0], v1 = acc[ai][bj][m][1];
;                     float o[8] = {v0[0] * bf_lo(g.x), v0[1] * bf_hi(g.x), v0[2] * bf_lo(g.y), v0[3] * bf_hi(g.y), v1[0] * bf_lo(g.z), v1[1] * bf_hi(g.z), v1[2] * bf_lo(g.w), v1[3] * bf_hi(g.w)};
;                     if (MODE == 1) { const u32x4 p = pp[m][bj];
;                         o[0] += bf_lo(p.x); o[1] += bf_hi(p.x); o[2] += bf_lo(p.y); o[3] += bf_hi(p.y); o[4] += bf_lo(p.z); o[5] += bf_hi(p.z); o[6] += bf_lo(p.w); o[7] += bf_hi(p.w); }
;                     u32x4 w; w.x = cvt_pk_bf16(o[0], o[1]); w.y = cvt_pk_bf16(o[2], o[3]); w.z = cvt_pk_bf16(o[4], o[5]); w.w = cvt_pk_bf16(o[6], o[7]);
;                     *(u32x4*)(mrg + ro) = w; } }
	v_lshlrev_b32_e32 v116, 16, v204
	v_and_b32_e32 v117, 0xffff0000, v204
	v_pk_fma_f32 v[110:111], v[110:111], v[114:115], v[116:117]
	v_lshlrev_b32_e32 v114, 16, v201
	v_and_b32_e32 v115, 0xffff0000, v201
	v_lshlrev_b32_e32 v116, 16, v205
	v_and_b32_e32 v117, 0xffff0000, v205
	v_pk_fma_f32 v[112:113], v[112:113], v[114:115], v[116:117]
	v_lshlrev_b32_e32 v114, 16, v202
	v_and_b32_e32 v115, 0xffff0000, v202
	v_lshlrev_b32_e32 v116, 16, v206
	v_and_b32_e32 v117, 0xffff0000, v206
	v_pk_fma_f32 v[114:115], v[106:107], v[114:115], v[116:117]
	v_lshlrev_b32_e32 v106, 16, v203
	v_and_b32_e32 v107, 0xffff0000, v203
	v_lshlrev_b32_e32 v116, 16, v207
	v_and_b32_e32 v117, 0xffff0000, v207
	v_pk_fma_f32 v[116:117], v[108:109], v[106:107], v[116:117]
	v_cvt_pk_bf16_f32 v106, v110, v111
	v_cvt_pk_bf16_f32 v107, v112, v113
	v_cvt_pk_bf16_f32 v108, v114, v115
	v_cvt_pk_bf16_f32 v109, v116, v117
	global_store_dwordx4 v[220:221], v[106:109], off sc1
	s_waitcnt vmcnt(8)
	s_nop 0
	v_lshlrev_b32_e32 v106, 16, v212
	v_and_b32_e32 v107, 0xffff0000, v212
	s_waitcnt vmcnt(7)
	v_lshlrev_b32_e32 v108, 16, v216
	v_and_b32_e32 v109, 0xffff0000, v216
	v_pk_fma_f32 v[102:103], v[102:103], v[106:107], v[108:109]
	v_lshlrev_b32_e32 v106, 16, v213
	v_and_b32_e32 v107, 0xffff0000, v213
	v_lshlrev_b32_e32 v108, 16, v217
	v_and_b32_e32 v109, 0xffff0000, v217
	v_pk_fma_f32 v[104:105], v[104:105], v[106:107], v[108:109]
	v_lshlrev_b32_e32 v106, 16, v214
	v_and_b32_e32 v107, 0xffff0000, v214
	v_lshlrev_b32_e32 v108, 16, v218
	v_and_b32_e32 v109, 0xffff0000, v218
	v_pk_fma_f32 v[106:107], v[98:99], v[106:107], v[108:109]
	v_lshlrev_b32_e32 v98, 16, v215
	v_and_b32_e32 v99, 0xffff0000, v215
	v_lshlrev_b32_e32 v108, 16, v219
	v_and_b32_e32 v109, 0xffff0000, v219
	v_pk_fma_f32 v[108:109], v[100:101], v[98:99], v[108:109]
	v_cvt_pk_bf16_f32 v98, v102, v103
	v_cvt_pk_bf16_f32 v99, v104, v105
	v_cvt_pk_bf16_f32 v100, v106, v107
	v_cvt_pk_bf16_f32 v101, v108, v109
	global_store_dwordx4 v[220:221], v[98:101], off offset:256 sc1
	s_nop 1
	v_lshlrev_b32_e32 v98, 16, v208
	v_and_b32_e32 v99, 0xffff0000, v208
	v_lshlrev_b32_e32 v100, 16, v154
	v_and_b32_e32 v101, 0xffff0000, v154
	v_pk_fma_f32 v[94:95], v[94:95], v[98:99], v[100:101]
	v_lshlrev_b32_e32 v98, 16, v209
	v_and_b32_e32 v99, 0xffff0000, v209
	v_lshlrev_b32_e32 v100, 16, v155
	v_and_b32_e32 v101, 0xffff0000, v155
	v_pk_fma_f32 v[96:97], v[96:97], v[98:99], v[100:101]
	v_lshlrev_b32_e32 v98, 16, v210
	v_and_b32_e32 v99, 0xffff0000, v210
	v_lshlrev_b32_e32 v100, 16, v156
	v_and_b32_e32 v101, 0xffff0000, v156
	v_pk_fma_f32 v[98:99], v[90:91], v[98:99], v[100:101]
	v_lshlrev_b32_e32 v90, 16, v211
	v_and_b32_e32 v91, 0xffff0000, v211
	v_lshlrev_b32_e32 v100, 16, v157
	v_and_b32_e32 v101, 0xffff0000, v157
	v_pk_fma_f32 v[100:101], v[92:93], v[90:91], v[100:101]
	v_cvt_pk_bf16_f32 v90, v94, v95
	v_cvt_pk_bf16_f32 v91, v96, v97
	v_cvt_pk_bf16_f32 v92, v98, v99
	v_cvt_pk_bf16_f32 v93, v100, v101
	global_store_dwordx4 v[170:171], v[90:93], off sc1
	s_waitcnt vmcnt(8)
	s_nop 0
	v_lshlrev_b32_e32 v90, 16, v150
	v_and_b32_e32 v91, 0xffff0000, v150
	s_waitcnt vmcnt(7)
	v_lshlrev_b32_e32 v92, 16, v146
	v_and_b32_e32 v93, 0xffff0000, v146
	v_pk_fma_f32 v[86:87], v[86:87], v[90:91], v[92:93]
	v_lshlrev_b32_e32 v90, 16, v151
	v_and_b32_e32 v91, 0xffff0000, v151
	v_lshlrev_b32_e32 v92, 16, v147
	v_and_b32_e32 v93, 0xffff0000, v147
	v_pk_fma_f32 v[88:89], v[88:89], v[90:91], v[92:93]
	v_lshlrev_b32_e32 v90, 16, v152
	v_and_b32_e32 v91, 0xffff0000, v152
	v_lshlrev_b32_e32 v92, 16, v148
	v_and_b32_e32 v93, 0xffff0000, v148
	v_pk_fma_f32 v[90:91], v[82:83], v[90:91], v[92:93]
	v_lshlrev_b32_e32 v82, 16, v153
	v_and_b32_e32 v83, 0xffff0000, v153
	v_lshlrev_b32_e32 v92, 16, v149
	v_and_b32_e32 v93, 0xffff0000, v149
	v_pk_fma_f32 v[92:93], v[84:85], v[82:83], v[92:93]
	v_cvt_pk_bf16_f32 v82, v86, v87
	v_cvt_pk_bf16_f32 v83, v88, v89
	v_cvt_pk_bf16_f32 v84, v90, v91
	v_cvt_pk_bf16_f32 v85, v92, v93
	global_store_dwordx4 v[170:171], v[82:85], off offset:256 sc1
	s_nop 1
	v_lshlrev_b32_e32 v82, 16, v142
	v_and_b32_e32 v83, 0xffff0000, v142
	v_lshlrev_b32_e32 v84, 16, v138
	v_and_b32_e32 v85, 0xffff0000, v138
	v_pk_fma_f32 v[78:79], v[78:79], v[82:83], v[84:85]
	v_lshlrev_b32_e32 v82, 16, v143
	v_and_b32_e32 v83, 0xffff0000, v143
	v_lshlrev_b32_e32 v84, 16, v139
	v_and_b32_e32 v85, 0xffff0000, v139
	v_pk_fma_f32 v[80:81], v[80:81], v[82:83], v[84:85]
	v_lshlrev_b32_e32 v82, 16, v144
	v_and_b32_e32 v83, 0xffff0000, v144
	v_lshlrev_b32_e32 v84, 16, v140
	v_and_b32_e32 v85, 0xffff0000, v140
	v_pk_fma_f32 v[82:83], v[74:75], v[82:83], v[84:85]
	v_lshlrev_b32_e32 v74, 16, v145
	v_and_b32_e32 v75, 0xffff0000, v145
	v_lshlrev_b32_e32 v84, 16, v141
	v_and_b32_e32 v85, 0xffff0000, v141
	v_pk_fma_f32 v[84:85], v[76:77], v[74:75], v[84:85]
	v_cvt_pk_bf16_f32 v74, v78, v79
	v_cvt_pk_bf16_f32 v75, v80, v81
	v_cvt_pk_bf16_f32 v76, v82, v83
	v_cvt_pk_bf16_f32 v77, v84, v85
	global_store_dwordx4 v[168:169], v[74:77], off sc1
	s_waitcnt vmcnt(8)
	s_nop 0
	v_lshlrev_b32_e32 v74, 16, v134
	v_and_b32_e32 v75, 0xffff0000, v134
	s_waitcnt vmcnt(7)
; __device__ __forceinline__ unsigned cvt_pk_bf16(float lo, float hi) { f32x2 v = {lo, hi}; bf16x2_t b = __builtin_convertvector(v, bf16x2_t); return __builtin_bit_cast(unsigned, b); }
; __device__ __forceinline__ float bf_lo(unsigned w) { return __uint_as_float(w << 16); }
; __device__ __forceinline__ float bf_hi(unsigned w) { return __uint_as_float(w & 0xffff0000u); }
;     __device__ __forceinline__ void operator()(const AccT& acc, const pg8::Unit& u, int wr, int wc, int fr, int fq) const {
;     ...
;                 for (int bj = 0; bj < 2; ++bj) { const size_t ro = (size_t)(row0 + ai * 128 + m * 16) * D + col0 + bj * 128; gg[m][bj] = *(const u32x4*)(gate + ro); if (MODE == 1) pp[m][bj] = *(const u32x4*)(mrg + ro); }
; #pragma unroll
;             for (int m = 0; m < 4; ++m)
; #pragma unroll
;                 for (int bj = 0; bj < 2; ++bj) { const size_t ro = (size_t)(row0 + ai * 128 + m * 16) * D + col0 + bj * 128; const u32x4 g = gg[m][bj]; const f32x4 v0 = acc[ai][bj][m][0], v1 = acc[ai][bj][m][1];
;                     float o[8] = {v0[0] * bf_lo(g.x), v0[1] * bf_hi(g.x), v0[2] * bf_lo(g.y), v0[3] * bf_hi(g.y), v1[0] * bf_lo(g.z), v1[1] * bf_hi(g.z), v1[2] * bf_lo(g.w), v1[3] * bf_hi(g.w)};
;                     if (MODE == 1) { const u32x4 p = pp[m][bj];
;                         o[0] += bf_lo(p.x); o[1] += bf_hi(p.x); o[2] += bf_lo(p.y); o[3] += bf_hi(p.y); o[4] += bf_lo(p.z); o[5] += bf_hi(p.z); o[6] += bf_lo(p.w); o[7] += bf_hi(p.w); }
;                     u32x4 w; w.x = cvt_pk_bf16(o[0], o[1]); w.y = cvt_pk_bf16(o[2], o[3]); w.z = cvt_pk_bf16(o[4], o[5]); w.w = cvt_pk_bf16(o[6], o[7]);
;                     *(u32x4*)(mrg + ro) = w; } }
	v_lshlrev_b32_e32 v76, 16, v130
	v_and_b32_e32 v77, 0xffff0000, v130
	v_pk_fma_f32 v[70:71], v[70:71], v[74:75], v[76:77]
	v_lshlrev_b32_e32 v74, 16, v135
	v_and_b32_e32 v75, 0xffff0000, v135
	v_lshlrev_b32_e32 v76, 16, v131
	v_and_b32_e32 v77, 0xffff0000, v131
	v_pk_fma_f32 v[72:73], v[72:73], v[74:75], v[76:77]
	v_lshlrev_b32_e32 v74, 16, v136
	v_and_b32_e32 v75, 0xffff0000, v136
	v_lshlrev_b32_e32 v76, 16, v132
	v_and_b32_e32 v77, 0xffff0000, v132
	v_pk_fma_f32 v[74:75], v[66:67], v[74:75], v[76:77]
	v_lshlrev_b32_e32 v66, 16, v137
	v_and_b32_e32 v67, 0xffff0000, v137
	v_lshlrev_b32_e32 v76, 16, v133
	v_and_b32_e32 v77, 0xffff0000, v133
	v_pk_fma_f32 v[76:77], v[68:69], v[66:67], v[76:77]
	v_cvt_pk_bf16_f32 v66, v70, v71
	v_cvt_pk_bf16_f32 v67, v72, v73
	v_cvt_pk_bf16_f32 v68, v74, v75
	v_cvt_pk_bf16_f32 v69, v76, v77
	global_store_dwordx4 v[168:169], v[66:69], off offset:256 sc1
	s_nop 1
	v_add_u32_e32 v66, 0x80, v166
	v_ashrrev_i32_e32 v67, 31, v66
	v_lshlrev_b64 v[68:69], 11, v[66:67]
	v_lshl_add_u64 v[68:69], v[68:69], 0, v[164:165]
	v_lshlrev_b64 v[68:69], 1, v[68:69]
	v_lshlrev_b64 v[66:67], 12, v[66:67]
	v_lshl_add_u64 v[70:71], s[12:13], 0, v[68:69]
	v_lshl_add_u64 v[134:135], v[162:163], 0, v[66:67]
	global_load_dwordx4 v[102:105], v[70:71], off
	global_load_dwordx4 v[106:109], v[134:135], off
	v_or_b32_e32 v68, 0x100, v68
	v_lshl_add_u64 v[66:67], s[12:13], 0, v[68:69]
	global_load_dwordx4 v[110:113], v[66:67], off
	v_lshl_add_u64 v[66:67], s[8:9], 0, v[68:69]
	global_load_dwordx4 v[114:117], v[66:67], off
	v_add_u32_e32 v66, 0x90, v166
	v_ashrrev_i32_e32 v67, 31, v66
	v_lshlrev_b64 v[68:69], 11, v[66:67]
	v_lshl_add_u64 v[68:69], v[68:69], 0, v[164:165]
	v_lshlrev_b64 v[68:69], 1, v[68:69]
	v_lshl_add_u64 v[70:71], s[12:13], 0, v[68:69]
	v_lshlrev_b64 v[66:67], 12, v[66:67]
	v_lshl_add_u64 v[136:137], v[162:163], 0, v[66:67]
	global_load_dwordx4 v[118:121], v[70:71], off
	global_load_dwordx4 v[122:125], v[136:137], off
	v_or_b32_e32 v68, 0x100, v68
	v_lshl_add_u64 v[66:67], s[12:13], 0, v[68:69]
	v_lshl_add_u64 v[68:69], s[8:9], 0, v[68:69]
	global_load_dwordx4 v[126:129], v[66:67], off
	global_load_dwordx4 v[130:133], v[68:69], off
	v_add_u32_e32 v66, 0xa0, v166
	v_ashrrev_i32_e32 v67, 31, v66
	v_lshlrev_b64 v[68:69], 11, v[66:67]
	v_lshl_add_u64 v[68:69], v[68:69], 0, v[164:165]
	v_lshlrev_b64 v[68:69], 1, v[68:69]
	v_lshl_add_u64 v[70:71], s[12:13], 0, v[68:69]
	v_lshlrev_b64 v[66:67], 12, v[66:67]
	v_lshl_add_u64 v[100:101], v[162:163], 0, v[66:67]
	global_load_dwordx4 v[94:97], v[70:71], off
	global_load_dwordx4 v[90:93], v[100:101], off
	v_or_b32_e32 v68, 0x100, v68
	v_lshl_add_u64 v[66:67], s[12:13], 0, v[68:69]
	v_lshl_add_u64 v[68:69], s[8:9], 0, v[68:69]
	global_load_dwordx4 v[86:89], v[66:67], off
	global_load_dwordx4 v[82:85], v[68:69], off
	v_add_u32_e32 v66, 0xb0, v166
	v_ashrrev_i32_e32 v67, 31, v66
	v_lshlrev_b64 v[68:69], 11, v[66:67]
	v_lshl_add_u64 v[68:69], v[68:69], 0, v[164:165]
	v_lshlrev_b64 v[68:69], 1, v[68:69]
	v_lshl_add_u64 v[70:71], s[12:13], 0, v[68:69]
	v_lshlrev_b64 v[66:67], 12, v[66:67]
	v_lshl_add_u64 v[98:99], v[162:163], 0, v[66:67]
	global_load_dwordx4 v[78:81], v[70:71], off
	global_load_dwordx4 v[74:77], v[98:99], off
	v_or_b32_e32 v68, 0x100, v68
	v_lshl_add_u64 v[66:67], s[12:13], 0, v[68:69]
	v_lshl_add_u64 v[68:69], s[8:9], 0, v[68:69]
	global_load_dwordx4 v[70:73], v[66:67], off
	s_nop 0
	global_load_dwordx4 v[66:69], v[68:69], off
	s_waitcnt vmcnt(15)
	v_lshlrev_b32_e32 v138, 16, v102
	v_and_b32_e32 v139, 0xffff0000, v102
	s_waitcnt vmcnt(14)
	v_lshlrev_b32_e32 v140, 16, v106
	v_and_b32_e32 v141, 0xffff0000, v106
	v_lshlrev_b32_e32 v102, 16, v103
	v_and_b32_e32 v103, 0xffff0000, v103
	v_lshlrev_b32_e32 v106, 16, v107
	v_and_b32_e32 v107, 0xffff0000, v107
	v_pk_fma_f32 v[64:65], v[64:65], v[102:103], v[106:107]
	v_lshlrev_b32_e32 v102, 16, v104
	v_and_b32_e32 v103, 0xffff0000, v104
	v_lshlrev_b32_e32 v106, 16, v108
	v_and_b32_e32 v107, 0xffff0000, v108
	v_pk_fma_f32 v[102:103], v[58:59], v[102:103], v[106:107]
	v_lshlrev_b32_e32 v58, 16, v105
	v_and_b32_e32 v59, 0xffff0000, v105
	v_lshlrev_b32_e32 v104, 16, v109
	v_and_b32_e32 v105, 0xffff0000, v109
	v_pk_fma_f32 v[62:63], v[62:63], v[138:139], v[140:141]
	v_pk_fma_f32 v[104:105], v[60:61], v[58:59], v[104:105]
	v_cvt_pk_bf16_f32 v58, v62, v63
	v_cvt_pk_bf16_f32 v59, v64, v65
	v_cvt_pk_bf16_f32 v60, v102, v103
	v_cvt_pk_bf16_f32 v61, v104, v105
	global_store_dwordx4 v[134:135], v[58:61], off sc1
	s_waitcnt vmcnt(14)
	s_nop 0
	v_lshlrev_b32_e32 v58, 16, v110
	v_and_b32_e32 v59, 0xffff0000, v110
	s_waitcnt vmcnt(13)
	v_lshlrev_b32_e32 v60, 16, v114
	v_and_b32_e32 v61, 0xffff0000, v114
	v_pk_fma_f32 v[54:55], v[54:55], v[58:59], v[60:61]
	v_lshlrev_b32_e32 v58, 16, v111
	v_and_b32_e32 v59, 0xffff0000, v111
	v_lshlrev_b32_e32 v60, 16, v115
	v_and_b32_e32 v61, 0xffff0000, v115
	v_pk_fma_f32 v[56:57], v[56:57], v[58:59], v[60:61]
	v_lshlrev_b32_e32 v58, 16, v112
	v_and_b32_e32 v59, 0xffff0000, v112
	v_lshlrev_b32_e32 v60, 16, v116
	v_and_b32_e32 v61, 0xffff0000, v116
	v_pk_fma_f32 v[58:59], v[50:51], v[58:59], v[60:61]
	v_lshlrev_b32_e32 v50, 16, v113
	v_and_b32_e32 v51, 0xffff0000, v113
	v_lshlrev_b32_e32 v60, 16, v117
	v_and_b32_e32 v61, 0xffff0000, v117
	v_pk_fma_f32 v[60:61], v[52:53], v[50:51], v[60:61]
	v_cvt_pk_bf16_f32 v50, v54, v55
	v_cvt_pk_bf16_f32 v51, v56, v57
	v_cvt_pk_bf16_f32 v52, v58, v59
	v_cvt_pk_bf16_f32 v53, v60, v61
	global_store_dwordx4 v[134:135], v[50:53], off offset:256 sc1
	s_waitcnt vmcnt(13)
	s_nop 0
	v_lshlrev_b32_e32 v50, 16, v118
	v_and_b32_e32 v51, 0xffff0000, v118
	s_waitcnt vmcnt(12)
; __device__ __forceinline__ unsigned cvt_pk_bf16(float lo, float hi) { f32x2 v = {lo, hi}; bf16x2_t b = __builtin_convertvector(v, bf16x2_t); return __builtin_bit_cast(unsigned, b); }
; __device__ __forceinline__ float bf_lo(unsigned w) { return __uint_as_float(w << 16); }
; __device__ __forceinline__ float bf_hi(unsigned w) { return __uint_as_float(w & 0xffff0000u); }
;     __device__ __forceinline__ void operator()(const AccT& acc, const pg8::Unit& u, int wr, int wc, int fr, int fq) const {
;     ...
;                 for (int bj = 0; bj < 2; ++bj) { const size_t ro = (size_t)(row0 + ai * 128 + m * 16) * D + col0 + bj * 128; gg[m][bj] = *(const u32x4*)(gate + ro); if (MODE == 1) pp[m][bj] = *(const u32x4*)(mrg + ro); }
; #pragma unroll
;             for (int m = 0; m < 4; ++m)
; #pragma unroll
;                 for (int bj = 0; bj < 2; ++bj) { const size_t ro = (size_t)(row0 + ai * 128 + m * 16) * D + col0 + bj * 128; const u32x4 g = gg[m][bj]; const f32x4 v0 = acc[ai][bj][m][0], v1 = acc[ai][bj][m][1];
;                     float o[8] = {v0[0] * bf_lo(g.x), v0[1] * bf_hi(g.x), v0[2] * bf_lo(g.y), v0[3] * bf_hi(g.y), v1[0] * bf_lo(g.z), v1[1] * bf_hi(g.z), v1[2] * bf_lo(g.w), v1[3] * bf_hi(g.w)};
;                     if (MODE == 1) { const u32x4 p = pp[m][bj];
;                         o[0] += bf_lo(p.x); o[1] += bf_hi(p.x); o[2] += bf_lo(p.y); o[3] += bf_hi(p.y); o[4] += bf_lo(p.z); o[5] += bf_hi(p.z); o[6] += bf_lo(p.w); o[7] += bf_hi(p.w); }
;                     u32x4 w; w.x = cvt_pk_bf16(o[0], o[1]); w.y = cvt_pk_bf16(o[2], o[3]); w.z = cvt_pk_bf16(o[4], o[5]); w.w = cvt_pk_bf16(o[6], o[7]);
;                     *(u32x4*)(mrg + ro) = w; } }
	v_lshlrev_b32_e32 v52, 16, v122
	v_and_b32_e32 v53, 0xffff0000, v122
	v_pk_fma_f32 v[46:47], v[46:47], v[50:51], v[52:53]
	v_lshlrev_b32_e32 v50, 16, v119
	v_and_b32_e32 v51, 0xffff0000, v119
	v_lshlrev_b32_e32 v52, 16, v123
	v_and_b32_e32 v53, 0xffff0000, v123
	v_pk_fma_f32 v[48:49], v[48:49], v[50:51], v[52:53]
	v_lshlrev_b32_e32 v50, 16, v120
	v_and_b32_e32 v51, 0xffff0000, v120
	v_lshlrev_b32_e32 v52, 16, v124
	v_and_b32_e32 v53, 0xffff0000, v124
	v_pk_fma_f32 v[50:51], v[42:43], v[50:51], v[52:53]
	v_lshlrev_b32_e32 v42, 16, v121
	v_and_b32_e32 v43, 0xffff0000, v121
	v_lshlrev_b32_e32 v52, 16, v125
	v_and_b32_e32 v53, 0xffff0000, v125
	v_pk_fma_f32 v[52:53], v[44:45], v[42:43], v[52:53]
	v_cvt_pk_bf16_f32 v42, v46, v47
	v_cvt_pk_bf16_f32 v43, v48, v49
	v_cvt_pk_bf16_f32 v44, v50, v51
	v_cvt_pk_bf16_f32 v45, v52, v53
	global_store_dwordx4 v[136:137], v[42:45], off sc1
	s_waitcnt vmcnt(12)
	s_nop 0
	v_lshlrev_b32_e32 v42, 16, v126
	v_and_b32_e32 v43, 0xffff0000, v126
	s_waitcnt vmcnt(11)
	v_lshlrev_b32_e32 v44, 16, v130
	v_and_b32_e32 v45, 0xffff0000, v130
	v_pk_fma_f32 v[38:39], v[38:39], v[42:43], v[44:45]
	v_lshlrev_b32_e32 v42, 16, v127
	v_and_b32_e32 v43, 0xffff0000, v127
	v_lshlrev_b32_e32 v44, 16, v131
	v_and_b32_e32 v45, 0xffff0000, v131
	v_pk_fma_f32 v[40:41], v[40:41], v[42:43], v[44:45]
	v_lshlrev_b32_e32 v42, 16, v128
	v_and_b32_e32 v43, 0xffff0000, v128
	v_lshlrev_b32_e32 v44, 16, v132
	v_and_b32_e32 v45, 0xffff0000, v132
	v_pk_fma_f32 v[42:43], v[34:35], v[42:43], v[44:45]
	v_lshlrev_b32_e32 v34, 16, v129
	v_and_b32_e32 v35, 0xffff0000, v129
	v_lshlrev_b32_e32 v44, 16, v133
	v_and_b32_e32 v45, 0xffff0000, v133
	v_pk_fma_f32 v[44:45], v[36:37], v[34:35], v[44:45]
	v_cvt_pk_bf16_f32 v34, v38, v39
	v_cvt_pk_bf16_f32 v35, v40, v41
	v_cvt_pk_bf16_f32 v36, v42, v43
	v_cvt_pk_bf16_f32 v37, v44, v45
	global_store_dwordx4 v[136:137], v[34:37], off offset:256 sc1
	s_waitcnt vmcnt(11)
	s_nop 0
	v_lshlrev_b32_e32 v34, 16, v94
	v_and_b32_e32 v35, 0xffff0000, v94
	s_waitcnt vmcnt(10)
	v_lshlrev_b32_e32 v36, 16, v90
	v_and_b32_e32 v37, 0xffff0000, v90
	v_pk_fma_f32 v[30:31], v[30:31], v[34:35], v[36:37]
	v_lshlrev_b32_e32 v34, 16, v95
	v_and_b32_e32 v35, 0xffff0000, v95
	v_lshlrev_b32_e32 v36, 16, v91
	v_and_b32_e32 v37, 0xffff0000, v91
	v_pk_fma_f32 v[32:33], v[32:33], v[34:35], v[36:37]
	v_lshlrev_b32_e32 v34, 16, v96
	v_and_b32_e32 v35, 0xffff0000, v96
	v_lshlrev_b32_e32 v36, 16, v92
	v_and_b32_e32 v37, 0xffff0000, v92
	v_pk_fma_f32 v[34:35], v[26:27], v[34:35], v[36:37]
	v_lshlrev_b32_e32 v26, 16, v97
	v_and_b32_e32 v27, 0xffff0000, v97
	v_lshlrev_b32_e32 v36, 16, v93
	v_and_b32_e32 v37, 0xffff0000, v93
	v_pk_fma_f32 v[36:37], v[28:29], v[26:27], v[36:37]
	v_cvt_pk_bf16_f32 v26, v30, v31
	v_cvt_pk_bf16_f32 v27, v32, v33
	v_cvt_pk_bf16_f32 v28, v34, v35
	v_cvt_pk_bf16_f32 v29, v36, v37
	global_store_dwordx4 v[100:101], v[26:29], off sc1
	s_waitcnt vmcnt(10)
	s_nop 0
	v_lshlrev_b32_e32 v26, 16, v86
	v_and_b32_e32 v27, 0xffff0000, v86
	s_waitcnt vmcnt(9)
	v_lshlrev_b32_e32 v28, 16, v82
	v_and_b32_e32 v29, 0xffff0000, v82
	v_pk_fma_f32 v[22:23], v[22:23], v[26:27], v[28:29]
	v_lshlrev_b32_e32 v26, 16, v87
	v_and_b32_e32 v27, 0xffff0000, v87
	v_lshlrev_b32_e32 v28, 16, v83
	v_and_b32_e32 v29, 0xffff0000, v83
	v_pk_fma_f32 v[24:25], v[24:25], v[26:27], v[28:29]
	v_lshlrev_b32_e32 v26, 16, v88
	v_and_b32_e32 v27, 0xffff0000, v88
	v_lshlrev_b32_e32 v28, 16, v84
	v_and_b32_e32 v29, 0xffff0000, v84
	v_pk_fma_f32 v[26:27], v[18:19], v[26:27], v[28:29]
	v_lshlrev_b32_e32 v18, 16, v89
	v_and_b32_e32 v19, 0xffff0000, v89
	v_lshlrev_b32_e32 v28, 16, v85
	v_and_b32_e32 v29, 0xffff0000, v85
	v_pk_fma_f32 v[28:29], v[20:21], v[18:19], v[28:29]
	v_cvt_pk_bf16_f32 v18, v22, v23
	v_cvt_pk_bf16_f32 v19, v24, v25
	v_cvt_pk_bf16_f32 v20, v26, v27
	v_cvt_pk_bf16_f32 v21, v28, v29
	global_store_dwordx4 v[100:101], v[18:21], off offset:256 sc1
	s_waitcnt vmcnt(9)
	s_nop 0
	v_lshlrev_b32_e32 v18, 16, v78
	v_and_b32_e32 v19, 0xffff0000, v78
	s_waitcnt vmcnt(8)
	v_lshlrev_b32_e32 v20, 16, v74
	v_and_b32_e32 v21, 0xffff0000, v74
	v_pk_fma_f32 v[14:15], v[14:15], v[18:19], v[20:21]
	v_lshlrev_b32_e32 v18, 16, v79
	v_and_b32_e32 v19, 0xffff0000, v79
	v_lshlrev_b32_e32 v20, 16, v75
	v_and_b32_e32 v21, 0xffff0000, v75
	v_pk_fma_f32 v[16:17], v[16:17], v[18:19], v[20:21]
	v_lshlrev_b32_e32 v18, 16, v80
	v_and_b32_e32 v19, 0xffff0000, v80
	v_lshlrev_b32_e32 v20, 16, v76
	v_and_b32_e32 v21, 0xffff0000, v76
	v_pk_fma_f32 v[18:19], v[10:11], v[18:19], v[20:21]
	v_lshlrev_b32_e32 v10, 16, v81
	v_and_b32_e32 v11, 0xffff0000, v81
	v_lshlrev_b32_e32 v20, 16, v77
	v_and_b32_e32 v21, 0xffff0000, v77
	v_pk_fma_f32 v[20:21], v[12:13], v[10:11], v[20:21]
	v_cvt_pk_bf16_f32 v10, v14, v15
	v_cvt_pk_bf16_f32 v11, v16, v17
	v_cvt_pk_bf16_f32 v12, v18, v19
	v_cvt_pk_bf16_f32 v13, v20, v21
	global_store_dwordx4 v[98:99], v[10:13], off sc1
	s_waitcnt vmcnt(8)
	s_nop 0
	v_lshlrev_b32_e32 v10, 16, v70
	v_and_b32_e32 v11, 0xffff0000, v70
	s_waitcnt vmcnt(7)
	v_lshlrev_b32_e32 v12, 16, v66
	v_and_b32_e32 v13, 0xffff0000, v66
	v_pk_fma_f32 v[6:7], v[6:7], v[10:11], v[12:13]
	v_lshlrev_b32_e32 v10, 16, v71
	v_and_b32_e32 v11, 0xffff0000, v71
	v_lshlrev_b32_e32 v12, 16, v67
	v_and_b32_e32 v13, 0xffff0000, v67
	v_pk_fma_f32 v[8:9], v[8:9], v[10:11], v[12:13]
	v_lshlrev_b32_e32 v10, 16, v72
	v_and_b32_e32 v11, 0xffff0000, v72
	v_lshlrev_b32_e32 v12, 16, v68
	v_and_b32_e32 v13, 0xffff0000, v68
	v_pk_fma_f32 v[10:11], v[2:3], v[10:11], v[12:13]
	v_lshlrev_b32_e32 v2, 16, v73
	v_and_b32_e32 v3, 0xffff0000, v73
	v_lshlrev_b32_e32 v12, 16, v69
	v_and_b32_e32 v13, 0xffff0000, v69
	v_pk_fma_f32 v[12:13], v[4:5], v[2:3], v[12:13]
	v_cvt_pk_bf16_f32 v2, v6, v7
	v_cvt_pk_bf16_f32 v3, v8, v9
	v_cvt_pk_bf16_f32 v4, v10, v11
	v_cvt_pk_bf16_f32 v5, v12, v13
	global_store_dwordx4 v[98:99], v[2:5], off offset:256 sc1
	s_cbranch_vccnz .LBB0_595
	s_andn2_b64 vcc, exec, s[10:11]
	s_cbranch_vccnz .LBB0_594
	s_barrier
	s_branch .LBB0_594

;     __device__ __forceinline__ void operator()(const AccT& acc, const pg8::Unit& u, int wr, int wc, int fr, int fq) const {
;         const int row0 = u.pm * 256 + wr * 64 + fr, col0 = u.pn * 256 + wc * 32 + 4 * fq;
;         float* x1 = (float*)(ws + WS_X1); float* ss = (float*)(ws + WS_SS);
; #pragma unroll
;         for (int ai = 0; ai < 2; ++ai) {
;             f32x4 xx[4][2][2];
; #pragma unroll
;             for (int m = 0; m < 4; ++m)
; #pragma unroll
;                 for (int bj = 0; bj < 2; ++bj)
; #pragma unroll
;                     for (int n = 0; n < 2; ++n) xx[m][bj][n] = *(const f32x4*)(x + (size_t)(row0 + ai * 128 + m * 16) * D + col0 + bj * 128 + n * 16);
; #pragma unroll
;             for (int m = 0; m < 4; ++m) { const int row = row0 + ai * 128 + m * 16; const size_t ro = (size_t)row * D + col0; float q = 0.f;
; #pragma unroll
;                 for (int bj = 0; bj < 2; ++bj)
; #pragma unroll
;                     for (int n = 0; n < 2; ++n) { const f32x4 o = xx[m][bj][n] + acc[ai][bj][m][n];
;                         q += (o[0] * o[0] + o[1] * o[1]) + (o[2] * o[2] + o[3] * o[3]);
;                         *(f32x4*)(x1 + ro + bj * 128 + n * 16) = o; }
;                 q += __shfl_xor(q, 16); q += __shfl_xor(q, 32);
;                 if (fq == 0) ss[(size_t)row * 32 + u.pn * 4 + wc] = q; } }
.LBB0_701:
	v_lshl_or_b32 v130, s24, 8, v206
	v_lshl_add_u32 v184, s26, 8, v205
	v_ashrrev_i32_e32 v131, 31, v130
	v_lshlrev_b64 v[178:179], 2, v[130:131]
	v_ashrrev_i32_e32 v185, 31, v184
	v_lshl_add_u64 v[186:187], s[10:11], 0, v[178:179]
	v_lshlrev_b64 v[230:231], 13, v[184:185]
	v_lshl_add_u64 v[130:131], v[186:187], 0, v[230:231]
	global_load_dwordx4 v[214:217], v[130:131], off
	global_load_dwordx4 v[218:221], v[130:131], off offset:64
	global_load_dwordx4 v[222:225], v[130:131], off offset:512
	global_load_dwordx4 v[226:229], v[130:131], off offset:576
	v_or_b32_e32 v196, 16, v184
	v_or_b32_e32 v192, 32, v184
	v_or_b32_e32 v188, 48, v184
	v_ashrrev_i32_e32 v197, 31, v196
	v_ashrrev_i32_e32 v193, 31, v192
	v_ashrrev_i32_e32 v189, 31, v188
	v_lshlrev_b64 v[198:199], 13, v[196:197]
	v_lshlrev_b64 v[194:195], 13, v[192:193]
	v_lshlrev_b64 v[190:191], 13, v[188:189]
	v_lshl_add_u64 v[130:131], v[186:187], 0, v[198:199]
	v_lshl_add_u64 v[132:133], v[186:187], 0, v[194:195]
	v_lshl_add_u64 v[182:183], v[186:187], 0, v[190:191]
	global_load_dwordx4 v[174:177], v[130:131], off
	global_load_dwordx4 v[170:173], v[130:131], off offset:64
	global_load_dwordx4 v[166:169], v[130:131], off offset:512
	global_load_dwordx4 v[162:165], v[130:131], off offset:576
	global_load_dwordx4 v[158:161], v[132:133], off
	global_load_dwordx4 v[154:157], v[132:133], off offset:64
	global_load_dwordx4 v[150:153], v[132:133], off offset:512
	global_load_dwordx4 v[146:149], v[132:133], off offset:576
	global_load_dwordx4 v[142:145], v[182:183], off
	global_load_dwordx4 v[138:141], v[182:183], off offset:64
	global_load_dwordx4 v[134:137], v[182:183], off offset:512
	s_nop 0
	global_load_dwordx4 v[130:133], v[182:183], off offset:576
	v_and_b32_e32 v183, 64, v211
	v_xor_b32_e32 v182, 16, v211
	v_add_u32_e32 v183, 64, v183
	v_xor_b32_e32 v212, 32, v211
	v_cmp_lt_i32_e32 vcc, v182, v183
	s_lshl_b32 s24, s24, 2
	s_ashr_i32 s25, s24, 31
	v_cndmask_b32_e32 v213, v211, v182, vcc
	v_cmp_lt_i32_e32 vcc, v212, v183
	v_lshl_add_u64 v[182:183], s[14:15], 0, v[178:179]
	v_lshlrev_b32_e32 v213, 2, v213
	v_cndmask_b32_e32 v212, v211, v212, vcc
	v_lshlrev_b32_e32 v212, 2, v212
	s_lshl_b64 s[24:25], s[24:25], 2
	s_add_u32 s24, s60, s24
	s_addc_u32 s25, s61, s25
	s_waitcnt vmcnt(15)
	v_pk_add_f32 v[128:129], v[128:129], v[216:217]
	v_pk_add_f32 v[126:127], v[126:127], v[214:215]
	s_waitcnt vmcnt(14)
	v_pk_add_f32 v[120:121], v[120:121], v[220:221]
	v_pk_add_f32 v[118:119], v[118:119], v[218:219]
	s_waitcnt vmcnt(13)
	v_pk_add_f32 v[124:125], v[124:125], v[224:225]
	v_pk_add_f32 v[122:123], v[122:123], v[222:223]
	s_waitcnt vmcnt(12)
	v_pk_add_f32 v[216:217], v[116:117], v[228:229]
	v_pk_add_f32 v[214:215], v[114:115], v[226:227]
	v_mul_f32_e32 v114, v127, v127
	v_mul_f32_e32 v115, v129, v129
	v_mul_f32_e32 v116, v119, v119
	v_mul_f32_e32 v117, v121, v121
	v_mul_f32_e32 v178, v123, v123
	v_mul_f32_e32 v179, v125, v125
	v_fmac_f32_e32 v114, v126, v126
	v_fmac_f32_e32 v115, v128, v128
	v_fmac_f32_e32 v116, v118, v118
	v_fmac_f32_e32 v117, v120, v120
	v_mul_f32_e32 v218, v215, v215
	v_mul_f32_e32 v219, v217, v217
	v_fmac_f32_e32 v178, v122, v122
	v_fmac_f32_e32 v179, v124, v124
	v_add_f32_e32 v114, v114, v115
	v_add_f32_e32 v115, v116, v117
	v_fmac_f32_e32 v218, v214, v214
	v_fmac_f32_e32 v219, v216, v216
	v_add_f32_e32 v116, v178, v179
	v_add_f32_e32 v114, v114, v115
	v_add_f32_e32 v114, v114, v116
	v_add_f32_e32 v115, v218, v219
	v_add_f32_e32 v114, v114, v115
	ds_bpermute_b32 v115, v213, v114
	v_lshl_add_u64 v[116:117], v[182:183], 0, v[230:231]
	global_store_dwordx4 v[116:117], v[126:129], off sc1
	global_store_dwordx4 v[116:117], v[118:121], off offset:64 sc1
	global_store_dwordx4 v[116:117], v[122:125], off offset:512 sc1
	global_store_dwordx4 v[116:117], v[214:217], off offset:576 sc1
	s_waitcnt lgkmcnt(0)
	v_add_f32_e32 v114, v114, v115
	ds_bpermute_b32 v115, v212, v114
	s_and_saveexec_b64 s[26:27], s[6:7]
	s_cbranch_execz .LBB0_703
	v_lshlrev_b64 v[116:117], 7, v[184:185]
	v_lshl_add_u64 v[116:117], s[24:25], 0, v[116:117]
	s_waitcnt lgkmcnt(0)
	v_add_f32_e32 v114, v114, v115
	global_store_dword v[116:117], v114, off
.LBB0_703:
	s_or_b64 exec, exec, s[26:27]
	s_waitcnt vmcnt(15)
	v_pk_add_f32 v[112:113], v[112:113], v[176:177]
	v_pk_add_f32 v[110:111], v[110:111], v[174:175]
	s_waitcnt lgkmcnt(0)
	v_mul_f32_e32 v115, v113, v113
	v_mul_f32_e32 v114, v111, v111
	v_fmac_f32_e32 v114, v110, v110
	v_fmac_f32_e32 v115, v112, v112
	s_waitcnt vmcnt(14)
	v_pk_add_f32 v[104:105], v[104:105], v[172:173]
	v_pk_add_f32 v[102:103], v[102:103], v[170:171]
	v_add_f32_e32 v114, v114, v115
	v_mul_f32_e32 v115, v103, v103
	v_mul_f32_e32 v116, v105, v105
	v_fmac_f32_e32 v115, v102, v102
	v_fmac_f32_e32 v116, v104, v104
	v_add_f32_e32 v115, v115, v116
	s_waitcnt vmcnt(13)
	v_pk_add_f32 v[108:109], v[108:109], v[168:169]
	v_pk_add_f32 v[106:107], v[106:107], v[166:167]
	v_add_f32_e32 v114, v114, v115
	v_mul_f32_e32 v115, v107, v107
	v_mul_f32_e32 v116, v109, v109
	v_fmac_f32_e32 v115, v106, v106
	v_fmac_f32_e32 v116, v108, v108
	v_add_f32_e32 v115, v115, v116
	v_add_f32_e32 v118, v114, v115
	s_waitcnt vmcnt(12)
	v_pk_add_f32 v[116:117], v[100:101], v[164:165]
	v_pk_add_f32 v[114:115], v[98:99], v[162:163]
	v_mul_f32_e32 v99, v117, v117
	v_mul_f32_e32 v98, v115, v115
	v_fmac_f32_e32 v98, v114, v114
	v_fmac_f32_e32 v99, v116, v116
	v_add_f32_e32 v98, v98, v99
	v_add_f32_e32 v98, v118, v98
	ds_bpermute_b32 v99, v213, v98
	v_lshl_add_u64 v[100:101], v[182:183], 0, v[198:199]
	global_store_dwordx4 v[100:101], v[110:113], off sc1
	global_store_dwordx4 v[100:101], v[102:105], off offset:64 sc1
	global_store_dwordx4 v[100:101], v[106:109], off offset:512 sc1
	global_store_dwordx4 v[100:101], v[114:117], off offset:576 sc1
	s_waitcnt lgkmcnt(0)
	v_add_f32_e32 v98, v98, v99
	ds_bpermute_b32 v99, v212, v98
	s_and_saveexec_b64 s[26:27], s[6:7]
	s_cbranch_execz .LBB0_705
	v_lshlrev_b64 v[100:101], 7, v[196:197]
	v_lshl_add_u64 v[100:101], s[24:25], 0, v[100:101]
	s_waitcnt lgkmcnt(0)
	v_add_f32_e32 v98, v98, v99
	global_store_dword v[100:101], v98, off
;     __device__ __forceinline__ void operator()(const AccT& acc, const pg8::Unit& u, int wr, int wc, int fr, int fq) const {
;     ...
; #pragma unroll
;         for (int ai = 0; ai < 2; ++ai) {
;             f32x4 xx[4][2][2];
; #pragma unroll
;             for (int m = 0; m < 4; ++m)
; #pragma unroll
;                 for (int bj = 0; bj < 2; ++bj)
; #pragma unroll
;                     for (int n = 0; n < 2; ++n) xx[m][bj][n] = *(const f32x4*)(x + (size_t)(row0 + ai * 128 + m * 16) * D + col0 + bj * 128 + n * 16);
; #pragma unroll
;             for (int m = 0; m < 4; ++m) { const int row = row0 + ai * 128 + m * 16; const size_t ro = (size_t)row * D + col0; float q = 0.f;
; #pragma unroll
;                 for (int bj = 0; bj < 2; ++bj)
; #pragma unroll
;                     for (int n = 0; n < 2; ++n) { const f32x4 o = xx[m][bj][n] + acc[ai][bj][m][n];
;                         q += (o[0] * o[0] + o[1] * o[1]) + (o[2] * o[2] + o[3] * o[3]);
;                         *(f32x4*)(x1 + ro + bj * 128 + n * 16) = o; }
;                 q += __shfl_xor(q, 16); q += __shfl_xor(q, 32);
;                 if (fq == 0) ss[(size_t)row * 32 + u.pn * 4 + wc] = q; } }
.LBB0_705:
	s_or_b64 exec, exec, s[26:27]
	s_waitcnt vmcnt(15)
	v_pk_add_f32 v[96:97], v[96:97], v[160:161]
	v_pk_add_f32 v[94:95], v[94:95], v[158:159]
	s_waitcnt lgkmcnt(0)
	v_mul_f32_e32 v99, v97, v97
	v_mul_f32_e32 v98, v95, v95
	v_fmac_f32_e32 v98, v94, v94
	v_fmac_f32_e32 v99, v96, v96
	s_waitcnt vmcnt(14)
	v_pk_add_f32 v[88:89], v[88:89], v[156:157]
	v_pk_add_f32 v[86:87], v[86:87], v[154:155]
	v_add_f32_e32 v98, v98, v99
	v_mul_f32_e32 v99, v87, v87
	v_mul_f32_e32 v100, v89, v89
	v_fmac_f32_e32 v99, v86, v86
	v_fmac_f32_e32 v100, v88, v88
	v_add_f32_e32 v99, v99, v100
	s_waitcnt vmcnt(13)
	v_pk_add_f32 v[92:93], v[92:93], v[152:153]
	v_pk_add_f32 v[90:91], v[90:91], v[150:151]
	v_add_f32_e32 v98, v98, v99
	v_mul_f32_e32 v99, v91, v91
	v_mul_f32_e32 v100, v93, v93
	v_fmac_f32_e32 v99, v90, v90
	v_fmac_f32_e32 v100, v92, v92
	v_add_f32_e32 v99, v99, v100
	v_add_f32_e32 v102, v98, v99
	s_waitcnt vmcnt(12)
	v_pk_add_f32 v[100:101], v[84:85], v[148:149]
	v_pk_add_f32 v[98:99], v[82:83], v[146:147]
	v_mul_f32_e32 v83, v101, v101
	v_mul_f32_e32 v82, v99, v99
	v_fmac_f32_e32 v82, v98, v98
	v_fmac_f32_e32 v83, v100, v100
	v_add_f32_e32 v82, v82, v83
	v_add_f32_e32 v82, v102, v82
	ds_bpermute_b32 v83, v213, v82
	v_lshl_add_u64 v[84:85], v[182:183], 0, v[194:195]
	global_store_dwordx4 v[84:85], v[94:97], off sc1
	global_store_dwordx4 v[84:85], v[86:89], off offset:64 sc1
	global_store_dwordx4 v[84:85], v[90:93], off offset:512 sc1
	global_store_dwordx4 v[84:85], v[98:101], off offset:576 sc1
	s_waitcnt lgkmcnt(0)
	v_add_f32_e32 v82, v82, v83
	ds_bpermute_b32 v83, v212, v82
	s_and_saveexec_b64 s[26:27], s[6:7]
	s_cbranch_execz .LBB0_707
	v_lshlrev_b64 v[84:85], 7, v[192:193]
	v_lshl_add_u64 v[84:85], s[24:25], 0, v[84:85]
	s_waitcnt lgkmcnt(0)
	v_add_f32_e32 v82, v82, v83
	global_store_dword v[84:85], v82, off
.LBB0_707:
	s_or_b64 exec, exec, s[26:27]
	s_waitcnt vmcnt(15)
	v_pk_add_f32 v[80:81], v[80:81], v[144:145]
	v_pk_add_f32 v[78:79], v[78:79], v[142:143]
	s_waitcnt lgkmcnt(0)
	v_mul_f32_e32 v83, v81, v81
	v_mul_f32_e32 v82, v79, v79
	v_fmac_f32_e32 v82, v78, v78
	v_fmac_f32_e32 v83, v80, v80
	s_waitcnt vmcnt(14)
	v_pk_add_f32 v[72:73], v[72:73], v[140:141]
	v_pk_add_f32 v[70:71], v[70:71], v[138:139]
	v_add_f32_e32 v82, v82, v83
	v_mul_f32_e32 v83, v71, v71
	v_mul_f32_e32 v84, v73, v73
	v_fmac_f32_e32 v83, v70, v70
	v_fmac_f32_e32 v84, v72, v72
	v_add_f32_e32 v83, v83, v84
	s_waitcnt vmcnt(13)
	v_pk_add_f32 v[76:77], v[76:77], v[136:137]
	v_pk_add_f32 v[74:75], v[74:75], v[134:135]
	v_add_f32_e32 v82, v82, v83
	v_mul_f32_e32 v83, v75, v75
	v_mul_f32_e32 v84, v77, v77
	v_fmac_f32_e32 v83, v74, v74
	v_fmac_f32_e32 v84, v76, v76
	v_add_f32_e32 v83, v83, v84
	v_add_f32_e32 v86, v82, v83
	s_waitcnt vmcnt(12)
	v_pk_add_f32 v[84:85], v[68:69], v[132:133]
	v_pk_add_f32 v[82:83], v[66:67], v[130:131]
	v_mul_f32_e32 v67, v85, v85
	v_mul_f32_e32 v66, v83, v83
	v_fmac_f32_e32 v66, v82, v82
	v_fmac_f32_e32 v67, v84, v84
	v_add_f32_e32 v66, v66, v67
	v_add_f32_e32 v66, v86, v66
	ds_bpermute_b32 v67, v213, v66
	v_lshl_add_u64 v[68:69], v[182:183], 0, v[190:191]
	global_store_dwordx4 v[68:69], v[78:81], off sc1
	global_store_dwordx4 v[68:69], v[70:73], off offset:64 sc1
	global_store_dwordx4 v[68:69], v[74:77], off offset:512 sc1
	global_store_dwordx4 v[68:69], v[82:85], off offset:576 sc1
	s_waitcnt lgkmcnt(0)
	v_add_f32_e32 v66, v66, v67
	ds_bpermute_b32 v67, v212, v66
	s_and_saveexec_b64 s[26:27], s[6:7]
	s_cbranch_execz .LBB0_709
	v_lshlrev_b64 v[68:69], 7, v[188:189]
	v_lshl_add_u64 v[68:69], s[24:25], 0, v[68:69]
	s_waitcnt lgkmcnt(0)
	v_add_f32_e32 v66, v66, v67
	global_store_dword v[68:69], v66, off
.LBB0_709:
	s_or_b64 exec, exec, s[26:27]
	v_add_u32_e32 v126, 0x80, v184
	v_ashrrev_i32_e32 v127, 31, v126
	v_lshlrev_b64 v[144:145], 13, v[126:127]
	s_waitcnt lgkmcnt(0)
	v_lshl_add_u64 v[66:67], v[186:187], 0, v[144:145]
	global_load_dwordx4 v[128:131], v[66:67], off
	global_load_dwordx4 v[132:135], v[66:67], off offset:64
	global_load_dwordx4 v[136:139], v[66:67], off offset:512
	global_load_dwordx4 v[140:143], v[66:67], off offset:576
	v_add_u32_e32 v122, 0x90, v184
	v_add_u32_e32 v118, 0xa0, v184
	v_add_u32_e32 v114, 0xb0, v184
	v_ashrrev_i32_e32 v123, 31, v122
	v_ashrrev_i32_e32 v119, 31, v118
	v_ashrrev_i32_e32 v115, 31, v114
	v_lshlrev_b64 v[124:125], 13, v[122:123]
	v_lshlrev_b64 v[120:121], 13, v[118:119]
	v_lshlrev_b64 v[116:117], 13, v[114:115]
	v_lshl_add_u64 v[66:67], v[186:187], 0, v[124:125]
	v_lshl_add_u64 v[68:69], v[186:187], 0, v[120:121]
	v_lshl_add_u64 v[146:147], v[186:187], 0, v[116:117]
	global_load_dwordx4 v[110:113], v[66:67], off
	global_load_dwordx4 v[106:109], v[66:67], off offset:64
	global_load_dwordx4 v[102:105], v[66:67], off offset:512
	global_load_dwordx4 v[98:101], v[66:67], off offset:576
	global_load_dwordx4 v[94:97], v[68:69], off
	global_load_dwordx4 v[90:93], v[68:69], off offset:64
	global_load_dwordx4 v[86:89], v[68:69], off offset:512
	global_load_dwordx4 v[82:85], v[68:69], off offset:576
	global_load_dwordx4 v[78:81], v[146:147], off
	global_load_dwordx4 v[74:77], v[146:147], off offset:64
	global_load_dwordx4 v[70:73], v[146:147], off offset:512
	s_nop 0
	global_load_dwordx4 v[66:69], v[146:147], off offset:576
	s_waitcnt vmcnt(15)
	v_pk_add_f32 v[64:65], v[64:65], v[130:131]
	v_pk_add_f32 v[62:63], v[62:63], v[128:129]
	s_waitcnt vmcnt(14)
	v_pk_add_f32 v[56:57], v[56:57], v[134:135]
	v_pk_add_f32 v[54:55], v[54:55], v[132:133]
	s_waitcnt vmcnt(13)
	v_pk_add_f32 v[60:61], v[60:61], v[138:139]
	v_pk_add_f32 v[58:59], v[58:59], v[136:137]
	s_waitcnt vmcnt(12)
	v_pk_add_f32 v[130:131], v[52:53], v[142:143]
	v_pk_add_f32 v[128:129], v[50:51], v[140:141]
	v_mul_f32_e32 v50, v63, v63
	v_mul_f32_e32 v51, v65, v65
	v_mul_f32_e32 v52, v55, v55
	v_mul_f32_e32 v53, v57, v57
	v_mul_f32_e32 v132, v59, v59
	v_mul_f32_e32 v133, v61, v61
	v_fmac_f32_e32 v50, v62, v62
	v_fmac_f32_e32 v51, v64, v64
	v_fmac_f32_e32 v52, v54, v54
	v_fmac_f32_e32 v53, v56, v56
	v_mul_f32_e32 v134, v129, v129
	v_mul_f32_e32 v135, v131, v131
	v_fmac_f32_e32 v132, v58, v58
	v_fmac_f32_e32 v133, v60, v60
	v_add_f32_e32 v50, v50, v51
	v_add_f32_e32 v51, v52, v53
	v_fmac_f32_e32 v134, v128, v128
	v_fmac_f32_e32 v135, v130, v130
	v_add_f32_e32 v52, v132, v133
	v_add_f32_e32 v50, v50, v51
	v_add_f32_e32 v50, v50, v52
	v_add_f32_e32 v51, v134, v135
	v_add_f32_e32 v50, v50, v51
	ds_bpermute_b32 v51, v213, v50
	v_lshl_add_u64 v[52:53], v[182:183], 0, v[144:145]
	global_store_dwordx4 v[52:53], v[62:65], off sc1
	global_store_dwordx4 v[52:53], v[54:57], off offset:64 sc1
	global_store_dwordx4 v[52:53], v[58:61], off offset:512 sc1
	global_store_dwordx4 v[52:53], v[128:131], off offset:576 sc1
	s_waitcnt lgkmcnt(0)
	v_add_f32_e32 v50, v50, v51
	ds_bpermute_b32 v51, v212, v50
	s_and_saveexec_b64 s[26:27], s[6:7]
	s_cbranch_execz .LBB0_711
	v_lshlrev_b64 v[52:53], 7, v[126:127]
	v_lshl_add_u64 v[52:53], s[24:25], 0, v[52:53]
	s_waitcnt lgkmcnt(0)
	v_add_f32_e32 v50, v50, v51
	global_store_dword v[52:53], v50, off
;     __device__ __forceinline__ void operator()(const AccT& acc, const pg8::Unit& u, int wr, int wc, int fr, int fq) const {
;     ...
;             for (int m = 0; m < 4; ++m) { const int row = row0 + ai * 128 + m * 16; const size_t ro = (size_t)row * D + col0; float q = 0.f;
; #pragma unroll
;                 for (int bj = 0; bj < 2; ++bj)
; #pragma unroll
;                     for (int n = 0; n < 2; ++n) { const f32x4 o = xx[m][bj][n] + acc[ai][bj][m][n];
;                         q += (o[0] * o[0] + o[1] * o[1]) + (o[2] * o[2] + o[3] * o[3]);
;                         *(f32x4*)(x1 + ro + bj * 128 + n * 16) = o; }
;                 q += __shfl_xor(q, 16); q += __shfl_xor(q, 32);
;                 if (fq == 0) ss[(size_t)row * 32 + u.pn * 4 + wc] = q; } }
.LBB0_711:
	s_or_b64 exec, exec, s[26:27]
	s_waitcnt vmcnt(15)
	v_pk_add_f32 v[48:49], v[48:49], v[112:113]
	v_pk_add_f32 v[46:47], v[46:47], v[110:111]
	s_waitcnt lgkmcnt(0)
	v_mul_f32_e32 v51, v49, v49
	v_mul_f32_e32 v50, v47, v47
	v_fmac_f32_e32 v50, v46, v46
	v_fmac_f32_e32 v51, v48, v48
	s_waitcnt vmcnt(14)
	v_pk_add_f32 v[40:41], v[40:41], v[108:109]
	v_pk_add_f32 v[38:39], v[38:39], v[106:107]
	v_add_f32_e32 v50, v50, v51
	v_mul_f32_e32 v51, v39, v39
	v_mul_f32_e32 v52, v41, v41
	v_fmac_f32_e32 v51, v38, v38
	v_fmac_f32_e32 v52, v40, v40
	v_add_f32_e32 v51, v51, v52
	s_waitcnt vmcnt(13)
	v_pk_add_f32 v[44:45], v[44:45], v[104:105]
	v_pk_add_f32 v[42:43], v[42:43], v[102:103]
	v_add_f32_e32 v50, v50, v51
	v_mul_f32_e32 v51, v43, v43
	v_mul_f32_e32 v52, v45, v45
	v_fmac_f32_e32 v51, v42, v42
	v_fmac_f32_e32 v52, v44, v44
	v_add_f32_e32 v51, v51, v52
	v_add_f32_e32 v54, v50, v51
	s_waitcnt vmcnt(12)
	v_pk_add_f32 v[52:53], v[36:37], v[100:101]
	v_pk_add_f32 v[50:51], v[34:35], v[98:99]
	v_mul_f32_e32 v35, v53, v53
	v_mul_f32_e32 v34, v51, v51
	v_fmac_f32_e32 v34, v50, v50
	v_fmac_f32_e32 v35, v52, v52
	v_add_f32_e32 v34, v34, v35
	v_add_f32_e32 v34, v54, v34
	ds_bpermute_b32 v35, v213, v34
	v_lshl_add_u64 v[36:37], v[182:183], 0, v[124:125]
	global_store_dwordx4 v[36:37], v[46:49], off sc1
	global_store_dwordx4 v[36:37], v[38:41], off offset:64 sc1
	global_store_dwordx4 v[36:37], v[42:45], off offset:512 sc1
	global_store_dwordx4 v[36:37], v[50:53], off offset:576 sc1
	s_waitcnt lgkmcnt(0)
	v_add_f32_e32 v34, v34, v35
	ds_bpermute_b32 v35, v212, v34
	s_and_saveexec_b64 s[26:27], s[6:7]
	s_cbranch_execz .LBB0_713
	v_lshlrev_b64 v[36:37], 7, v[122:123]
	v_lshl_add_u64 v[36:37], s[24:25], 0, v[36:37]
	s_waitcnt lgkmcnt(0)
	v_add_f32_e32 v34, v34, v35
	global_store_dword v[36:37], v34, off
.LBB0_713:
	s_or_b64 exec, exec, s[26:27]
	s_waitcnt vmcnt(15)
	v_pk_add_f32 v[32:33], v[32:33], v[96:97]
	v_pk_add_f32 v[30:31], v[30:31], v[94:95]
	s_waitcnt lgkmcnt(0)
	v_mul_f32_e32 v35, v33, v33
	v_mul_f32_e32 v34, v31, v31
	v_fmac_f32_e32 v34, v30, v30
	v_fmac_f32_e32 v35, v32, v32
	s_waitcnt vmcnt(14)
	v_pk_add_f32 v[24:25], v[24:25], v[92:93]
	v_pk_add_f32 v[22:23], v[22:23], v[90:91]
	v_add_f32_e32 v34, v34, v35
	v_mul_f32_e32 v35, v23, v23
	v_mul_f32_e32 v36, v25, v25
	v_fmac_f32_e32 v35, v22, v22
	v_fmac_f32_e32 v36, v24, v24
	v_add_f32_e32 v35, v35, v36
	s_waitcnt vmcnt(13)
	v_pk_add_f32 v[28:29], v[28:29], v[88:89]
	v_pk_add_f32 v[26:27], v[26:27], v[86:87]
	v_add_f32_e32 v34, v34, v35
	v_mul_f32_e32 v35, v27, v27
	v_mul_f32_e32 v36, v29, v29
	v_fmac_f32_e32 v35, v26, v26
	v_fmac_f32_e32 v36, v28, v28
	v_add_f32_e32 v35, v35, v36
	v_add_f32_e32 v38, v34, v35
	s_waitcnt vmcnt(12)
	v_pk_add_f32 v[36:37], v[20:21], v[84:85]
	v_pk_add_f32 v[34:35], v[18:19], v[82:83]
	v_mul_f32_e32 v19, v37, v37
	v_mul_f32_e32 v18, v35, v35
	v_fmac_f32_e32 v18, v34, v34
	v_fmac_f32_e32 v19, v36, v36
	v_add_f32_e32 v18, v18, v19
	v_add_f32_e32 v18, v38, v18
	ds_bpermute_b32 v19, v213, v18
	v_lshl_add_u64 v[20:21], v[182:183], 0, v[120:121]
	global_store_dwordx4 v[20:21], v[30:33], off sc1
	global_store_dwordx4 v[20:21], v[22:25], off offset:64 sc1
	global_store_dwordx4 v[20:21], v[26:29], off offset:512 sc1
	global_store_dwordx4 v[20:21], v[34:37], off offset:576 sc1
	s_waitcnt lgkmcnt(0)
	v_add_f32_e32 v18, v18, v19
	ds_bpermute_b32 v19, v212, v18
	s_and_saveexec_b64 s[26:27], s[6:7]
	s_cbranch_execz .LBB0_715
	v_lshlrev_b64 v[20:21], 7, v[118:119]
	v_lshl_add_u64 v[20:21], s[24:25], 0, v[20:21]
	s_waitcnt lgkmcnt(0)
	v_add_f32_e32 v18, v18, v19
	global_store_dword v[20:21], v18, off
.LBB0_715:
	s_or_b64 exec, exec, s[26:27]
	s_waitcnt vmcnt(15)
	v_pk_add_f32 v[16:17], v[16:17], v[80:81]
	v_pk_add_f32 v[14:15], v[14:15], v[78:79]
	s_waitcnt lgkmcnt(0)
	v_mul_f32_e32 v19, v17, v17
	v_mul_f32_e32 v18, v15, v15
	v_fmac_f32_e32 v18, v14, v14
	v_fmac_f32_e32 v19, v16, v16
	s_waitcnt vmcnt(14)
	v_pk_add_f32 v[8:9], v[8:9], v[76:77]
	v_pk_add_f32 v[6:7], v[6:7], v[74:75]
	v_add_f32_e32 v18, v18, v19
	v_mul_f32_e32 v19, v7, v7
	v_mul_f32_e32 v20, v9, v9
	v_fmac_f32_e32 v19, v6, v6
	v_fmac_f32_e32 v20, v8, v8
	v_add_f32_e32 v19, v19, v20
	s_waitcnt vmcnt(13)
	v_pk_add_f32 v[12:13], v[12:13], v[72:73]
	v_pk_add_f32 v[10:11], v[10:11], v[70:71]
	v_add_f32_e32 v18, v18, v19
	v_mul_f32_e32 v19, v11, v11
	v_mul_f32_e32 v20, v13, v13
	v_fmac_f32_e32 v19, v10, v10
	v_fmac_f32_e32 v20, v12, v12
	v_add_f32_e32 v19, v19, v20
	v_add_f32_e32 v22, v18, v19
	s_waitcnt vmcnt(12)
	v_pk_add_f32 v[20:21], v[4:5], v[68:69]
	v_pk_add_f32 v[18:19], v[2:3], v[66:67]
	v_mul_f32_e32 v3, v21, v21
	v_mul_f32_e32 v2, v19, v19
	v_fmac_f32_e32 v2, v18, v18
	v_fmac_f32_e32 v3, v20, v20
	v_add_f32_e32 v2, v2, v3
	v_add_f32_e32 v2, v22, v2
	ds_bpermute_b32 v3, v213, v2
	v_lshl_add_u64 v[4:5], v[182:183], 0, v[116:117]
	global_store_dwordx4 v[4:5], v[14:17], off sc1
	global_store_dwordx4 v[4:5], v[6:9], off offset:64 sc1
	global_store_dwordx4 v[4:5], v[10:13], off offset:512 sc1
	global_store_dwordx4 v[4:5], v[18:21], off offset:576 sc1
	s_waitcnt lgkmcnt(0)
	v_add_f32_e32 v2, v2, v3
	ds_bpermute_b32 v3, v212, v2
	s_and_saveexec_b64 s[26:27], s[6:7]
	s_cbranch_execz .LBB0_717
	v_lshlrev_b64 v[4:5], 7, v[114:115]
	v_lshl_add_u64 v[4:5], s[24:25], 0, v[4:5]
	s_waitcnt lgkmcnt(0)
	v_add_f32_e32 v2, v2, v3
	global_store_dword v[4:5], v2, off

; #define LAS __attribute__((address_space(3)))
; #define RT_LOAD(sc_, X) do { const int kb_ = 512 * kq + 64 * ((sc_) >> 1) + 32 * kh + 16 * ((sc_) & 1); \
;             _Pragma("unroll") for (int q = 0; q < 4; ++q) X[q] = *(const f32x4*)(X1 + (size_t)tok * D + kb_ + 4 * q); } while (0)
; __device__ __forceinline__ void q6_block(const float (&v)[32], u32x4& lo, u32x4& hi) {
;     float amax = 0.f;
; #pragma unroll
;     for (int t = 0; t < 32; ++t) amax = fmaxf(amax, fabsf(v[t]));
;     const unsigned eb = ((__float_as_uint(amax * 0.13333334f) >> 23) & 255u) + 1u;
;     const float sc = __uint_as_float(eb << 23);
;     f32x16v a, b;
; #pragma unroll
;     for (int t = 0; t < 16; ++t) { a[t] = v[t]; b[t] = v[16 + t]; }
;     const u32x6 q = __builtin_amdgcn_cvt_scalef32_2xpk16_fp6_f32(a, b, MK_F6_SCALE_INV ? __uint_as_float((254u - eb) << 23) : sc);
;     lo = (u32x4){q[0], q[1], q[2], q[3]};
;     hi = (u32x4){q[4], q[5], eb * 0x01010101u, 0u};
; }
; __device__ __forceinline__ void router_tile(Frame& F, const Args& a, int tile) {
;     ...
;             const int kb = 512 * kq + 64 * (sc >> 1) + 32 * kh + 16 * (sc & 1);
;             f32x4 xn[4];
;             { const int sn = sc < 15 ? sc + 1 : 15; RT_LOAD(sn, xn); }
;             f32x4 gc[4]; float bc[16];
; #pragma unroll
;             for (int q = 0; q < 4; ++q) gc[q] = *(const LAS f32x4*)(g2l + kb + 4 * q);
;             { const LAS float* rwb = rwl + ((sc >> 1) & 1) * 8192 + kq * 2048 + (32 * kh + 16 * (sc & 1)) * 32 + i;
; #pragma unroll
;               for (int q = 0; q < 16; ++q) bc[q] = rwb[q * 32]; }
;             float av[16];
; #pragma unroll
;             for (int q = 0; q < 4; ++q) { av[4 * q] = xc[q][0] * rstd * gc[q][0]; av[4 * q + 1] = xc[q][1] * rstd * gc[q][1]; av[4 * q + 2] = xc[q][2] * rstd * gc[q][2]; av[4 * q + 3] = xc[q][3] * rstd * gc[q][3]; }
;             if (sc & 1) {
;                 float v32[32];
; #pragma unroll
;                 for (int q = 0; q < 16; ++q) { v32[q] = avp[q]; v32[16 + q] = av[q]; }
;                 u32x4 lo, hi; q6_block(v32, lo, hi);
;                 const int k0 = kb - 16, b32 = k0 >> 5;
;                 unsigned char* base = H2 + (size_t)tok * D + 128 * (b32 >> 2) + 16 * (b32 & 3);
;                 *(u32x4*)base = lo; *(u32x4*)(base + 64) = hi;
.LBB0_788:
	s_and_b32 s35, s36, 1
	s_lshl_b32 s37, s36, 5
	s_andn2_b32 s37, s37, 63
	s_lshl_b32 s40, s35, 4
	s_add_i32 s35, s36, 1
	s_cmp_lg_u32 s36, 15
	s_cselect_b32 s41, s35, 15
	s_lshl_b32 s42, s41, 5
	s_and_b32 s42, s42, 0x3c0
	v_add_u32_e32 v50, s42, v72
	s_lshl_b32 s41, s41, 4
	v_and_or_b32 v50, s41, 16, v50
	v_ashrrev_i32_e32 v51, 31, v50
	v_lshl_add_u64 v[50:51], v[50:51], 2, v[76:77]
	global_load_dwordx4 v[54:57], v[50:51], off offset:48
	global_load_dwordx4 v[58:61], v[50:51], off offset:32
	global_load_dwordx4 v[62:65], v[50:51], off offset:16
	global_load_dwordx4 v[66:69], v[50:51], off
	v_add_u32_e32 v50, s37, v72
	v_or_b32_e32 v113, s40, v50
	v_lshl_add_u32 v50, v113, 2, 0
	v_add_u32_e32 v50, 0x1c000, v50
	s_lshl_b32 s36, s36, 14
	ds_read_b128 v[114:117], v50
	ds_read_b128 v[118:121], v50 offset:16
	ds_read_b128 v[122:125], v50 offset:32
	ds_read_b128 v[126:129], v50 offset:48
	s_and_b32 s36, s36, 0x8000
	v_or_b32_e32 v50, s40, v106
	s_add_i32 s36, s3, s36
	v_lshlrev_b32_e32 v50, 7, v50
	v_lshlrev_b32_e32 v51, 2, v98
	v_add3_u32 v50, s36, v50, v51
	v_add_u32_e32 v51, 0xc000, v50
	v_add_u32_e32 v50, 0xc400, v50
	ds_read2_b32 v[96:97], v51 offset1:32
	ds_read2_b32 v[94:95], v51 offset0:64 offset1:96
	ds_read2_b32 v[92:93], v51 offset0:128 offset1:160
	ds_read2_b32 v[90:91], v51 offset0:192 offset1:224
	ds_read2_b32 v[88:89], v50 offset1:32
	ds_read2_b32 v[86:87], v50 offset0:64 offset1:96
	ds_read2_b32 v[84:85], v50 offset0:128 offset1:160
	ds_read2_b32 v[82:83], v50 offset0:192 offset1:224
	s_waitcnt vmcnt(4)
	v_pk_mul_f32 v[34:35], v[78:79], v[34:35]
	v_pk_mul_f32 v[36:37], v[78:79], v[36:37]
	v_pk_mul_f32 v[38:39], v[78:79], v[38:39]
	v_pk_mul_f32 v[40:41], v[78:79], v[40:41]
	v_pk_mul_f32 v[42:43], v[78:79], v[42:43]
	v_pk_mul_f32 v[44:45], v[78:79], v[44:45]
	v_pk_mul_f32 v[46:47], v[78:79], v[46:47]
	v_pk_mul_f32 v[48:49], v[78:79], v[48:49]
	s_waitcnt lgkmcnt(11)
	v_pk_mul_f32 v[34:35], v[34:35], v[114:115]
	v_pk_mul_f32 v[36:37], v[36:37], v[116:117]
	s_waitcnt lgkmcnt(10)
	v_pk_mul_f32 v[38:39], v[38:39], v[118:119]
	v_pk_mul_f32 v[40:41], v[40:41], v[120:121]
	s_waitcnt lgkmcnt(9)
	v_pk_mul_f32 v[42:43], v[42:43], v[122:123]
	v_pk_mul_f32 v[44:45], v[44:45], v[124:125]
	s_waitcnt lgkmcnt(8)
	v_pk_mul_f32 v[46:47], v[46:47], v[126:127]
	v_pk_mul_f32 v[48:49], v[48:49], v[128:129]
	s_and_b64 vcc, exec, s[0:1]
	s_cbranch_vccz .LBB0_784
	v_max3_f32 v50, |v18|, 0, |v19|
	v_max3_f32 v50, v50, |v20|, |v21|
	v_max3_f32 v50, v50, |v22|, |v23|
	v_max3_f32 v50, v50, |v24|, |v25|
	v_max3_f32 v50, v50, |v26|, |v27|
	v_max3_f32 v50, v50, |v28|, |v29|
	v_max3_f32 v50, v50, |v30|, |v31|
	v_max3_f32 v50, v50, |v32|, |v33|
	v_max3_f32 v50, v50, |v34|, |v35|
	v_max3_f32 v50, v50, |v36|, |v37|
	v_max3_f32 v50, v50, |v38|, |v39|
	v_max3_f32 v50, v50, |v40|, |v41|
	v_max3_f32 v50, v50, |v42|, |v43|
	v_max3_f32 v50, v50, |v44|, |v45|
	v_max3_f32 v50, v50, |v46|, |v47|
	v_max3_f32 v50, v50, |v48|, |v49|
	v_mul_f32_e32 v50, 0x3e088889, v50
	v_bfe_u32 v50, v50, 23, 8
	v_add_u32_e32 v50, 1, v50
	v_lshlrev_b32_e32 v51, 23, v50
	v_cvt_scalef32_2xpk16_fp6_f32 v[18:23], v[18:33], v[34:49], v51
	v_mul_lo_u32 v52, v50, s33
	v_mov_b32_e32 v50, v22
	v_add_u32_e32 v22, -16, v113
	v_lshrrev_b32_e32 v24, 1, v22
	v_and_b32_e32 v22, 0xffffff80, v22
	v_mov_b32_e32 v51, v23
	v_ashrrev_i32_e32 v23, 31, v22
	v_lshl_add_u64 v[22:23], v[80:81], 0, v[22:23]
	v_and_b32_e32 v24, 48, v24
	v_mov_b32_e32 v25, v53
	v_lshl_add_u64 v[22:23], v[22:23], 0, v[24:25]
	global_store_dwordx4 v[22:23], v[18:21], off sc1
	global_store_dwordx4 v[22:23], v[50:53], off offset:64 sc1
	s_branch .LBB0_784

; __device__ __forceinline__ void router_tile(Frame& F, const Args& a, int tile) {
;     ...
;     if (tid < 64) {
;         const int t = tile * 64 + tid;
;         int* TOKE = (int*)(F.ws + WS_TOKE); int* TOKR = (int*)(F.ws + WS_TOKR); float* TOKW = (float*)(F.ws + WS_TOKW); int* ROWTOK = (int*)(F.ws + WS_ROWTOK);
;         float ex[4], sum = 0.f;
; #pragma unroll
;         for (int k = 0; k < 4; ++k) { ex[k] = __expf(tv[k] - tv[0]); sum += ex[k]; }
;         const float inv = 1.0f / sum;
; #pragma unroll
;         for (int k = 0; k < 4; ++k) { const int rank = basel[te[k]] + lr[k]; TOKE[t * 4 + k] = te[k]; TOKR[t * 4 + k] = rank; TOKW[t * 4 + k] = ex[k] * inv; ROWTOK[te[k] * T + rank] = t * 4 + k; }
;     }
.LBB0_1038:
	s_or_b64 exec, exec, s[0:1]
	s_waitcnt lgkmcnt(0)
	s_barrier
	s_and_saveexec_b64 s[0:1], s[8:9]
	s_cbranch_execz .LBB0_780
	v_sub_f32_e32 v14, v2, v2
	v_sub_f32_e32 v6, v6, v2
	v_mul_f32_e32 v14, 0x3fb8aa3b, v14
	v_mul_f32_e32 v6, 0x3fb8aa3b, v6
	v_exp_f32_e32 v18, v14
	v_exp_f32_e32 v19, v6
	v_sub_f32_e32 v6, v8, v2
	v_mul_f32_e32 v6, 0x3fb8aa3b, v6
	v_sub_f32_e32 v2, v7, v2
	v_exp_f32_e32 v8, v6
	v_mul_f32_e32 v2, 0x3fb8aa3b, v2
	v_exp_f32_e32 v2, v2
	v_add_f32_e32 v6, 0, v18
	v_add_f32_e32 v6, v19, v6
	v_add_f32_e32 v6, v8, v6
	v_add_f32_e32 v6, v2, v6
	v_div_scale_f32 v7, s[34:35], v6, v6, 1.0
	v_rcp_f32_e32 v14, v7
	s_nop 0
	v_fma_f32 v15, -v7, v14, 1.0
	v_fmac_f32_e32 v14, v15, v14
	v_div_scale_f32 v15, vcc, 1.0, v6, 1.0
	v_mul_f32_e32 v16, v15, v14
	v_fma_f32 v17, -v7, v16, v15
	v_fmac_f32_e32 v16, v17, v14
	v_fma_f32 v7, -v7, v16, v15
	v_div_fmas_f32 v7, v7, v14, v16
	v_div_fixup_f32 v20, v7, v6, 1.0
	v_lshl_add_u32 v7, v4, 2, 0
	ds_read_b32 v7, v7 offset:41088
	v_add_lshl_u32 v6, s39, v1, 2
	v_lshl_add_u32 v14, v5, 2, 0
	v_lshl_add_u32 v15, v9, 2, 0
	v_lshl_add_u32 v16, v3, 2, 0
	s_waitcnt lgkmcnt(0)
	v_add_u32_e32 v13, v7, v13
	v_ashrrev_i32_e32 v7, 31, v6
	ds_read_b32 v21, v14 offset:41088
	ds_read_b32 v22, v15 offset:41088
	ds_read_b32 v23, v16 offset:41088
	v_lshlrev_b64 v[14:15], 2, v[6:7]
	v_lshl_add_u64 v[16:17], s[24:25], 0, v[14:15]
	global_store_dword v[16:17], v4, off
	v_lshl_add_u64 v[16:17], s[28:29], 0, v[14:15]
	v_mul_f32_e32 v7, v18, v20
	v_lshl_add_u64 v[14:15], s[26:27], 0, v[14:15]
	global_store_dword v[14:15], v7, off
	v_lshl_add_u32 v14, v4, 14, v13
	v_ashrrev_i32_e32 v15, 31, v14
	s_waitcnt lgkmcnt(2)
	v_add_u32_e32 v4, v21, v12
	v_or_b32_e32 v12, 1, v6
	global_store_dword v[16:17], v13, off
	v_lshl_add_u64 v[14:15], v[14:15], 2, s[30:31]
	v_ashrrev_i32_e32 v13, 31, v12
	global_store_dword v[14:15], v6, off
	v_lshlrev_b64 v[14:15], 2, v[12:13]
	v_lshl_add_u64 v[16:17], s[24:25], 0, v[14:15]
	global_store_dword v[16:17], v5, off
	v_lshl_add_u64 v[16:17], s[28:29], 0, v[14:15]
	global_store_dword v[16:17], v4, off
	v_lshl_add_u32 v4, v5, 14, v4
	v_ashrrev_i32_e32 v5, 31, v4
	v_lshl_add_u64 v[4:5], v[4:5], 2, s[30:31]
	global_store_dword v[4:5], v12, off
	v_or_b32_e32 v4, 2, v6
	v_ashrrev_i32_e32 v5, 31, v4
	v_mul_f32_e32 v7, v19, v20
	v_lshl_add_u64 v[14:15], s[26:27], 0, v[14:15]
	v_lshlrev_b64 v[12:13], 2, v[4:5]
	global_store_dword v[14:15], v7, off
	v_lshl_add_u64 v[14:15], s[24:25], 0, v[12:13]
	s_waitcnt lgkmcnt(1)
	v_add_u32_e32 v7, v22, v11
	global_store_dword v[14:15], v9, off
	v_lshl_add_u64 v[14:15], s[28:29], 0, v[12:13]
	global_store_dword v[14:15], v7, off
	v_lshl_add_u32 v14, v9, 14, v7
	v_ashrrev_i32_e32 v15, 31, v14
	v_lshl_add_u64 v[14:15], v[14:15], 2, s[30:31]
	global_store_dword v[14:15], v4, off
	v_or_b32_e32 v4, 3, v6
	v_ashrrev_i32_e32 v5, 31, v4
	s_waitcnt lgkmcnt(0)
	v_add_u32_e32 v14, v23, v10
	v_lshlrev_b64 v[6:7], 2, v[4:5]
	v_lshl_add_u64 v[10:11], s[24:25], 0, v[6:7]
	v_mul_f32_e32 v9, v2, v20
	v_lshl_add_u32 v2, v3, 14, v14
	global_store_dword v[10:11], v3, off
	v_ashrrev_i32_e32 v3, 31, v2
	v_mul_f32_e32 v8, v8, v20
	v_lshl_add_u64 v[12:13], s[26:27], 0, v[12:13]
	v_lshl_add_u64 v[6:7], s[28:29], 0, v[6:7]
	v_lshl_add_u64 v[2:3], v[2:3], 2, s[30:31]
	global_store_dword v[6:7], v14, off
	global_store_dwordx2 v[12:13], v[8:9], off sc1
	global_store_dword v[2:3], v4, off
	s_branch .LBB0_780

; #define LAS __attribute__((address_space(3)))
; __device__ __forceinline__ unsigned pk4_fp8(float a, float b, float c, float d) { int w = 0; w = __builtin_amdgcn_cvt_pk_fp8_f32(a, b, w, false); w = __builtin_amdgcn_cvt_pk_fp8_f32(c, d, w, true); return (unsigned)w; }
;     __device__ __forceinline__ void operator()(const AccT& acc, const pg8::Unit& u, int wr, int wc, int fr, int fq, const LAS float* bl, int nai) const {
;         const int row0 = u.pm * 256 + u.hx * 128 + wr * 64 + fr, a0 = u.pn * 128 + wc * 32 + 8 * fq;
;         unsigned char* act = (unsigned char*)(ws + WS_ACT);
;         const f32x4 bg0 = *(const LAS f32x4*)(bl + 8 * fq), bg1 = *(const LAS f32x4*)(bl + 8 * fq + 4), bu0 = *(const LAS f32x4*)(bl + 32 + 8 * fq), bu1 = *(const LAS f32x4*)(bl + 32 + 8 * fq + 4);
; #pragma unroll
;         for (int ai = 0; ai < 2; ++ai) if (ai < nai)
; #pragma unroll
;             for (int m = 0; m < 4; ++m) { const size_t ro = (size_t)(row0 + ai * 128 + m * 16) * DFF + a0; float o[8];
; #pragma unroll
;                 for (int n = 0; n < 2; ++n) {
;                     f32x4 g4 = acc[ai][0][m][n] + (n ? bg1 : bg0), u4 = acc[ai][1][m][n] + (n ? bu1 : bu0);
; #pragma unroll
;                     for (int j = 0; j < 4; ++j) { g4[j] = fminf(g4[j], 7.0f); u4[j] = __builtin_amdgcn_fmed3f(u4[j], -7.0f, 7.0f); }
;                     const f32x4 t4 = g4 * (-1.702f * 1.4426950408889634f);
;                     f32x4 e4;
; #pragma unroll
;                     for (int j = 0; j < 4; ++j) e4[j] = __builtin_amdgcn_exp2f(t4[j]);
;                     e4 = e4 + 1.0f;
;                     f32x4 r4;
; #pragma unroll
;                     for (int j = 0; j < 4; ++j) r4[j] = __builtin_amdgcn_rcpf(e4[j]);
;                     const f32x4 o4 = (u4 * A8_SCALE + A8_SCALE) * (g4 * r4);
; #pragma unroll
;                     for (int j = 0; j < 4; ++j) o[4 * n + j] = o4[j]; }
;                 u32x2 w; w.x = pk4_fp8(o[0], o[1], o[2], o[3]); w.y = pk4_fp8(o[4], o[5], o[6], o[7]);
;                 *(u32x2*)(act + ro) = w; }
.LBB0_1142:
	s_nop 15
	s_nop 15
	ds_read_b128 v[14:17], v220
	ds_read_b128 v[6:9], v220 offset:16
	ds_read_b128 v[10:13], v220 offset:128
	ds_read_b128 v[2:5], v220 offset:144
	v_lshl_or_b32 v18, s46, 7, v222
	s_waitcnt lgkmcnt(3)
	v_pk_add_f32 v[22:23], v[172:173], v[16:17]
	v_pk_add_f32 v[24:25], v[170:171], v[14:15]
	v_min_f32_e32 v22, 0x40e00000, v22
	v_min_f32_e32 v24, 0x40e00000, v24
	v_min_f32_e32 v25, 0x40e00000, v25
	v_min_f32_e32 v23, 0x40e00000, v23
	v_mul_f32_e32 v21, 0xc01d265f, v24
	v_mul_f32_e32 v31, 0xc01d265f, v22
	v_exp_f32_e32 v30, v21
	v_mul_f32_e32 v21, 0xc01d265f, v25
	v_exp_f32_e32 v32, v31
	v_mul_f32_e32 v31, 0xc01d265f, v23
	v_exp_f32_e32 v33, v31
	v_exp_f32_e32 v31, v21
	s_waitcnt lgkmcnt(1)
	v_pk_add_f32 v[28:29], v[178:179], v[10:11]
	v_pk_add_f32 v[26:27], v[180:181], v[12:13]
	v_med3_f32 v21, v28, s80, v225
	v_pk_add_f32 v[30:31], v[30:31], 1.0 op_sel_hi:[1,0]
	v_med3_f32 v34, v29, s80, v225
	v_rcp_f32_e32 v30, v30
	v_rcp_f32_e32 v31, v31
	v_pk_add_f32 v[28:29], v[32:33], 1.0 op_sel_hi:[1,0]
	v_fma_f32 v21, v21, 4.0, 4.0
	v_rcp_f32_e32 v28, v28
	v_rcp_f32_e32 v29, v29
	v_pk_mul_f32 v[24:25], v[24:25], v[30:31]
	v_med3_f32 v26, v26, s80, v225
	v_mul_f32_e32 v21, v21, v24
	v_fma_f32 v24, v34, 4.0, 4.0
	v_med3_f32 v27, v27, s80, v225
	v_pk_mul_f32 v[22:23], v[22:23], v[28:29]
	v_mul_f32_e32 v34, v24, v25
	v_fma_f32 v24, v26, 4.0, 4.0
	v_mul_f32_e32 v35, v24, v22
	v_fma_f32 v22, v27, 4.0, 4.0
	v_mul_f32_e32 v36, v22, v23
	v_pk_add_f32 v[22:23], v[168:169], v[8:9]
	v_pk_add_f32 v[24:25], v[166:167], v[6:7]
	v_min_f32_e32 v22, 0x40e00000, v22
	v_min_f32_e32 v24, 0x40e00000, v24
	v_min_f32_e32 v25, 0x40e00000, v25
	v_min_f32_e32 v23, 0x40e00000, v23
	v_mul_f32_e32 v30, 0xc01d265f, v24
	v_mul_f32_e32 v31, 0xc01d265f, v25
	v_mul_f32_e32 v32, 0xc01d265f, v22
	v_mul_f32_e32 v33, 0xc01d265f, v23
	v_exp_f32_e32 v30, v30
	v_exp_f32_e32 v32, v32
	v_exp_f32_e32 v33, v33
	v_exp_f32_e32 v31, v31
	s_waitcnt lgkmcnt(0)
	v_pk_add_f32 v[28:29], v[174:175], v[2:3]
	v_pk_add_f32 v[26:27], v[176:177], v[4:5]
	v_med3_f32 v37, v28, s80, v225
	v_med3_f32 v38, v29, s80, v225
	v_pk_add_f32 v[28:29], v[32:33], 1.0 op_sel_hi:[1,0]
	v_pk_add_f32 v[30:31], v[30:31], 1.0 op_sel_hi:[1,0]
	v_rcp_f32_e32 v28, v28
	v_rcp_f32_e32 v30, v30
	v_rcp_f32_e32 v29, v29
	v_rcp_f32_e32 v31, v31
	v_med3_f32 v26, v26, s80, v225
	v_med3_f32 v27, v27, s80, v225
	v_pk_mul_f32 v[22:23], v[22:23], v[28:29]
	v_pk_mul_f32 v[24:25], v[24:25], v[30:31]
	v_fma_f32 v28, v37, 4.0, 4.0
	v_mul_f32_e32 v28, v28, v24
	v_fma_f32 v24, v38, 4.0, 4.0
	v_mul_f32_e32 v29, v24, v25
	v_fma_f32 v24, v26, 4.0, 4.0
	v_mul_f32_e32 v22, v24, v22
	v_mov_b32_e32 v24, 0
	v_mov_b32_e32 v25, 0
	v_cvt_pk_fp8_f32 v24, v21, v34
	v_cvt_pk_fp8_f32 v25, v28, v29
	v_fma_f32 v21, v27, 4.0, 4.0
	v_mul_f32_e32 v21, v21, v23
	v_lshl_add_u32 v20, s84, 8, v219
	v_cvt_pk_fp8_f32 v24, v35, v36 op_sel:[0,0,1]
	v_cvt_pk_fp8_f32 v25, v22, v21 op_sel:[0,0,1]
	v_ashrrev_i32_e32 v19, 31, v18
	v_ashrrev_i32_e32 v21, 31, v20
	v_lshl_add_u64 v[18:19], s[28:29], 0, v[18:19]
	v_lshlrev_b64 v[22:23], 11, v[20:21]
	v_lshl_add_u64 v[22:23], v[18:19], 0, v[22:23]
	v_pk_add_f32 v[26:27], v[154:155], v[14:15]
	global_store_dwordx2 v[22:23], v[24:25], off sc1
	v_pk_add_f32 v[24:25], v[156:157], v[16:17]
	v_min_f32_e32 v26, 0x40e00000, v26
	v_min_f32_e32 v27, 0x40e00000, v27
	v_min_f32_e32 v24, 0x40e00000, v24
	v_mul_f32_e32 v21, 0xc01d265f, v26
	v_min_f32_e32 v25, 0x40e00000, v25
	v_exp_f32_e32 v32, v21
	v_mul_f32_e32 v21, 0xc01d265f, v27
	v_mul_f32_e32 v23, 0xc01d265f, v24
	v_exp_f32_e32 v34, v23
	v_mul_f32_e32 v23, 0xc01d265f, v25
	v_exp_f32_e32 v33, v21
	v_exp_f32_e32 v35, v23
	v_pk_add_f32 v[30:31], v[162:163], v[10:11]
	v_pk_add_f32 v[28:29], v[164:165], v[12:13]
	v_pk_add_f32 v[32:33], v[32:33], 1.0 op_sel_hi:[1,0]
	v_med3_f32 v21, v30, s80, v225
	v_med3_f32 v23, v31, s80, v225
	v_pk_add_f32 v[30:31], v[34:35], 1.0 op_sel_hi:[1,0]
	v_rcp_f32_e32 v32, v32
	v_rcp_f32_e32 v33, v33
	v_rcp_f32_e32 v30, v30
	v_rcp_f32_e32 v31, v31
	v_med3_f32 v28, v28, s80, v225
	v_pk_mul_f32 v[26:27], v[26:27], v[32:33]
	v_fma_f32 v21, v21, 4.0, 4.0
	v_med3_f32 v29, v29, s80, v225
	v_pk_mul_f32 v[24:25], v[24:25], v[30:31]
	v_mul_f32_e32 v21, v21, v26
	v_fma_f32 v26, v28, 4.0, 4.0
	v_fma_f32 v23, v23, 4.0, 4.0
	v_mul_f32_e32 v36, v26, v24
	v_fma_f32 v24, v29, 4.0, 4.0
	v_mul_f32_e32 v23, v23, v27
	v_mul_f32_e32 v37, v24, v25
	v_pk_add_f32 v[24:25], v[152:153], v[8:9]
	v_pk_add_f32 v[26:27], v[150:151], v[6:7]
	v_min_f32_e32 v24, 0x40e00000, v24
	v_min_f32_e32 v26, 0x40e00000, v26
	v_min_f32_e32 v27, 0x40e00000, v27
	v_min_f32_e32 v25, 0x40e00000, v25
	v_mul_f32_e32 v32, 0xc01d265f, v26
	v_mul_f32_e32 v33, 0xc01d265f, v27
	v_mul_f32_e32 v34, 0xc01d265f, v24
	v_mul_f32_e32 v35, 0xc01d265f, v25
	v_exp_f32_e32 v32, v32
	v_exp_f32_e32 v34, v34
	v_exp_f32_e32 v35, v35
	v_exp_f32_e32 v33, v33
	v_pk_add_f32 v[30:31], v[158:159], v[2:3]
	v_pk_add_f32 v[28:29], v[160:161], v[4:5]
	v_med3_f32 v38, v30, s80, v225
	v_med3_f32 v39, v31, s80, v225
	v_pk_add_f32 v[30:31], v[34:35], 1.0 op_sel_hi:[1,0]
	v_pk_add_f32 v[32:33], v[32:33], 1.0 op_sel_hi:[1,0]
	v_rcp_f32_e32 v30, v30
	v_rcp_f32_e32 v32, v32
	v_rcp_f32_e32 v31, v31
	v_rcp_f32_e32 v33, v33
	v_med3_f32 v28, v28, s80, v225
	v_med3_f32 v29, v29, s80, v225
	v_pk_mul_f32 v[24:25], v[24:25], v[30:31]
	v_pk_mul_f32 v[26:27], v[26:27], v[32:33]
	v_fma_f32 v30, v38, 4.0, 4.0
	v_mul_f32_e32 v30, v30, v26
	v_fma_f32 v26, v39, 4.0, 4.0
	v_mul_f32_e32 v31, v26, v27
	v_fma_f32 v26, v28, 4.0, 4.0
	v_mul_f32_e32 v24, v26, v24
	v_mov_b32_e32 v26, 0
	v_mov_b32_e32 v27, 0
	v_cvt_pk_fp8_f32 v26, v21, v23
; __device__ __forceinline__ unsigned pk4_fp8(float a, float b, float c, float d) { int w = 0; w = __builtin_amdgcn_cvt_pk_fp8_f32(a, b, w, false); w = __builtin_amdgcn_cvt_pk_fp8_f32(c, d, w, true); return (unsigned)w; }
;     __device__ __forceinline__ void operator()(const AccT& acc, const pg8::Unit& u, int wr, int wc, int fr, int fq, const LAS float* bl, int nai) const {
;     ...
;             for (int m = 0; m < 4; ++m) { const size_t ro = (size_t)(row0 + ai * 128 + m * 16) * DFF + a0; float o[8];
; #pragma unroll
;                 for (int n = 0; n < 2; ++n) {
;                     f32x4 g4 = acc[ai][0][m][n] + (n ? bg1 : bg0), u4 = acc[ai][1][m][n] + (n ? bu1 : bu0);
; #pragma unroll
;                     for (int j = 0; j < 4; ++j) { g4[j] = fminf(g4[j], 7.0f); u4[j] = __builtin_amdgcn_fmed3f(u4[j], -7.0f, 7.0f); }
;                     const f32x4 t4 = g4 * (-1.702f * 1.4426950408889634f);
;                     f32x4 e4;
; #pragma unroll
;                     for (int j = 0; j < 4; ++j) e4[j] = __builtin_amdgcn_exp2f(t4[j]);
;                     e4 = e4 + 1.0f;
;                     f32x4 r4;
; #pragma unroll
;                     for (int j = 0; j < 4; ++j) r4[j] = __builtin_amdgcn_rcpf(e4[j]);
;                     const f32x4 o4 = (u4 * A8_SCALE + A8_SCALE) * (g4 * r4);
; #pragma unroll
;                     for (int j = 0; j < 4; ++j) o[4 * n + j] = o4[j]; }
;                 u32x2 w; w.x = pk4_fp8(o[0], o[1], o[2], o[3]); w.y = pk4_fp8(o[4], o[5], o[6], o[7]);
;                 *(u32x2*)(act + ro) = w; }
	v_cvt_pk_fp8_f32 v27, v30, v31
	v_fma_f32 v21, v29, 4.0, 4.0
	v_mul_f32_e32 v21, v21, v25
	v_or_b32_e32 v22, 16, v20
	v_cvt_pk_fp8_f32 v26, v36, v37 op_sel:[0,0,1]
	v_cvt_pk_fp8_f32 v27, v24, v21 op_sel:[0,0,1]
	v_ashrrev_i32_e32 v23, 31, v22
	v_lshlrev_b64 v[22:23], 11, v[22:23]
	v_lshl_add_u64 v[22:23], v[18:19], 0, v[22:23]
	global_store_dwordx2 v[22:23], v[26:27], off sc1
	v_pk_add_f32 v[26:27], v[142:143], v[14:15]
	v_pk_add_f32 v[24:25], v[144:145], v[16:17]
	v_min_f32_e32 v26, 0x40e00000, v26
	v_min_f32_e32 v27, 0x40e00000, v27
	v_min_f32_e32 v24, 0x40e00000, v24
	v_mul_f32_e32 v21, 0xc01d265f, v26
	v_min_f32_e32 v25, 0x40e00000, v25
	v_exp_f32_e32 v32, v21
	v_mul_f32_e32 v21, 0xc01d265f, v27
	v_mul_f32_e32 v23, 0xc01d265f, v24
	v_exp_f32_e32 v34, v23
	v_mul_f32_e32 v23, 0xc01d265f, v25
	v_exp_f32_e32 v33, v21
	v_exp_f32_e32 v35, v23
	v_pk_add_f32 v[30:31], v[146:147], v[10:11]
	v_pk_add_f32 v[28:29], v[148:149], v[12:13]
	v_pk_add_f32 v[32:33], v[32:33], 1.0 op_sel_hi:[1,0]
	v_med3_f32 v21, v30, s80, v225
	v_med3_f32 v23, v31, s80, v225
	v_pk_add_f32 v[30:31], v[34:35], 1.0 op_sel_hi:[1,0]
	v_rcp_f32_e32 v32, v32
	v_rcp_f32_e32 v33, v33
	v_rcp_f32_e32 v30, v30
	v_rcp_f32_e32 v31, v31
	v_med3_f32 v28, v28, s80, v225
	v_pk_mul_f32 v[26:27], v[26:27], v[32:33]
	v_fma_f32 v21, v21, 4.0, 4.0
	v_med3_f32 v29, v29, s80, v225
	v_pk_mul_f32 v[24:25], v[24:25], v[30:31]
	v_mul_f32_e32 v21, v21, v26
	v_fma_f32 v26, v28, 4.0, 4.0
	v_fma_f32 v23, v23, 4.0, 4.0
	v_mul_f32_e32 v36, v26, v24
	v_fma_f32 v24, v29, 4.0, 4.0
	v_mul_f32_e32 v23, v23, v27
	v_mul_f32_e32 v37, v24, v25
	v_pk_add_f32 v[24:25], v[136:137], v[8:9]
	v_pk_add_f32 v[26:27], v[134:135], v[6:7]
	v_min_f32_e32 v24, 0x40e00000, v24
	v_min_f32_e32 v26, 0x40e00000, v26
	v_min_f32_e32 v27, 0x40e00000, v27
	v_min_f32_e32 v25, 0x40e00000, v25
	v_mul_f32_e32 v32, 0xc01d265f, v26
	v_mul_f32_e32 v33, 0xc01d265f, v27
	v_mul_f32_e32 v34, 0xc01d265f, v24
	v_mul_f32_e32 v35, 0xc01d265f, v25
	v_exp_f32_e32 v32, v32
	v_exp_f32_e32 v34, v34
	v_exp_f32_e32 v35, v35
	v_exp_f32_e32 v33, v33
	v_pk_add_f32 v[30:31], v[138:139], v[2:3]
	v_pk_add_f32 v[28:29], v[140:141], v[4:5]
	v_med3_f32 v38, v30, s80, v225
	v_med3_f32 v39, v31, s80, v225
	v_pk_add_f32 v[30:31], v[34:35], 1.0 op_sel_hi:[1,0]
	v_pk_add_f32 v[32:33], v[32:33], 1.0 op_sel_hi:[1,0]
	v_rcp_f32_e32 v30, v30
	v_rcp_f32_e32 v32, v32
	v_rcp_f32_e32 v31, v31
	v_rcp_f32_e32 v33, v33
	v_med3_f32 v28, v28, s80, v225
	v_med3_f32 v29, v29, s80, v225
	v_pk_mul_f32 v[24:25], v[24:25], v[30:31]
	v_pk_mul_f32 v[26:27], v[26:27], v[32:33]
	v_fma_f32 v30, v38, 4.0, 4.0
	v_mul_f32_e32 v30, v30, v26
	v_fma_f32 v26, v39, 4.0, 4.0
	v_mul_f32_e32 v31, v26, v27
	v_fma_f32 v26, v28, 4.0, 4.0
	v_mul_f32_e32 v24, v26, v24
	v_mov_b32_e32 v26, 0
	v_mov_b32_e32 v27, 0
	v_cvt_pk_fp8_f32 v26, v21, v23
	v_cvt_pk_fp8_f32 v27, v30, v31
	v_fma_f32 v21, v29, 4.0, 4.0
	v_mul_f32_e32 v21, v21, v25
	v_or_b32_e32 v22, 32, v20
	v_cvt_pk_fp8_f32 v26, v36, v37 op_sel:[0,0,1]
	v_cvt_pk_fp8_f32 v27, v24, v21 op_sel:[0,0,1]
	v_ashrrev_i32_e32 v23, 31, v22
	v_lshlrev_b64 v[22:23], 11, v[22:23]
	v_lshl_add_u64 v[22:23], v[18:19], 0, v[22:23]
	global_store_dwordx2 v[22:23], v[26:27], off sc1
	v_pk_add_f32 v[26:27], v[118:119], v[14:15]
	v_pk_add_f32 v[24:25], v[120:121], v[16:17]
	v_min_f32_e32 v26, 0x40e00000, v26
	v_min_f32_e32 v27, 0x40e00000, v27
	v_min_f32_e32 v24, 0x40e00000, v24
	v_mul_f32_e32 v21, 0xc01d265f, v26
	v_min_f32_e32 v25, 0x40e00000, v25
	v_exp_f32_e32 v32, v21
	v_mul_f32_e32 v21, 0xc01d265f, v27
	v_mul_f32_e32 v23, 0xc01d265f, v24
	v_exp_f32_e32 v34, v23
	v_mul_f32_e32 v23, 0xc01d265f, v25
	v_exp_f32_e32 v33, v21
	v_exp_f32_e32 v35, v23
	v_pk_add_f32 v[30:31], v[126:127], v[10:11]
	v_pk_add_f32 v[28:29], v[128:129], v[12:13]
	v_pk_add_f32 v[32:33], v[32:33], 1.0 op_sel_hi:[1,0]
	v_med3_f32 v21, v30, s80, v225
	v_med3_f32 v23, v31, s80, v225
	v_pk_add_f32 v[30:31], v[34:35], 1.0 op_sel_hi:[1,0]
	v_rcp_f32_e32 v32, v32
	v_rcp_f32_e32 v33, v33
	v_rcp_f32_e32 v30, v30
	v_rcp_f32_e32 v31, v31
	v_med3_f32 v28, v28, s80, v225
	v_pk_mul_f32 v[26:27], v[26:27], v[32:33]
	v_fma_f32 v21, v21, 4.0, 4.0
	v_med3_f32 v29, v29, s80, v225
	v_pk_mul_f32 v[24:25], v[24:25], v[30:31]
	v_mul_f32_e32 v21, v21, v26
	v_fma_f32 v26, v28, 4.0, 4.0
	v_fma_f32 v23, v23, 4.0, 4.0
	v_mul_f32_e32 v36, v26, v24
	v_fma_f32 v24, v29, 4.0, 4.0
	v_mul_f32_e32 v23, v23, v27
	v_mul_f32_e32 v37, v24, v25
	v_pk_add_f32 v[24:25], v[112:113], v[8:9]
	v_pk_add_f32 v[26:27], v[110:111], v[6:7]
	v_min_f32_e32 v24, 0x40e00000, v24
	v_min_f32_e32 v26, 0x40e00000, v26
	v_min_f32_e32 v27, 0x40e00000, v27
	v_min_f32_e32 v25, 0x40e00000, v25
	v_mul_f32_e32 v32, 0xc01d265f, v26
	v_mul_f32_e32 v33, 0xc01d265f, v27
	v_mul_f32_e32 v34, 0xc01d265f, v24
	v_mul_f32_e32 v35, 0xc01d265f, v25
	v_exp_f32_e32 v32, v32
	v_exp_f32_e32 v34, v34
	v_exp_f32_e32 v35, v35
	v_exp_f32_e32 v33, v33
	v_pk_add_f32 v[30:31], v[98:99], v[2:3]
	v_pk_add_f32 v[28:29], v[100:101], v[4:5]
	v_med3_f32 v38, v30, s80, v225
	v_med3_f32 v39, v31, s80, v225
	v_pk_add_f32 v[30:31], v[34:35], 1.0 op_sel_hi:[1,0]
	v_pk_add_f32 v[32:33], v[32:33], 1.0 op_sel_hi:[1,0]
	v_rcp_f32_e32 v30, v30
	v_rcp_f32_e32 v32, v32
	v_rcp_f32_e32 v31, v31
	v_rcp_f32_e32 v33, v33
	v_med3_f32 v28, v28, s80, v225
	v_med3_f32 v29, v29, s80, v225
	v_pk_mul_f32 v[24:25], v[24:25], v[30:31]
	v_pk_mul_f32 v[26:27], v[26:27], v[32:33]
	v_fma_f32 v30, v38, 4.0, 4.0
	v_mul_f32_e32 v30, v30, v26
	v_fma_f32 v26, v39, 4.0, 4.0
	v_mul_f32_e32 v31, v26, v27
	v_fma_f32 v26, v28, 4.0, 4.0
	v_mul_f32_e32 v24, v26, v24
	v_mov_b32_e32 v26, 0
	v_mov_b32_e32 v27, 0
	v_cvt_pk_fp8_f32 v26, v21, v23
; __device__ __forceinline__ unsigned pk4_fp8(float a, float b, float c, float d) { int w = 0; w = __builtin_amdgcn_cvt_pk_fp8_f32(a, b, w, false); w = __builtin_amdgcn_cvt_pk_fp8_f32(c, d, w, true); return (unsigned)w; }
;     __device__ __forceinline__ void operator()(const AccT& acc, const pg8::Unit& u, int wr, int wc, int fr, int fq, const LAS float* bl, int nai) const {
;     ...
;             for (int m = 0; m < 4; ++m) { const size_t ro = (size_t)(row0 + ai * 128 + m * 16) * DFF + a0; float o[8];
; #pragma unroll
;                 for (int n = 0; n < 2; ++n) {
;                     f32x4 g4 = acc[ai][0][m][n] + (n ? bg1 : bg0), u4 = acc[ai][1][m][n] + (n ? bu1 : bu0);
; #pragma unroll
;                     for (int j = 0; j < 4; ++j) { g4[j] = fminf(g4[j], 7.0f); u4[j] = __builtin_amdgcn_fmed3f(u4[j], -7.0f, 7.0f); }
;                     const f32x4 t4 = g4 * (-1.702f * 1.4426950408889634f);
;                     f32x4 e4;
; #pragma unroll
;                     for (int j = 0; j < 4; ++j) e4[j] = __builtin_amdgcn_exp2f(t4[j]);
;                     e4 = e4 + 1.0f;
;                     f32x4 r4;
; #pragma unroll
;                     for (int j = 0; j < 4; ++j) r4[j] = __builtin_amdgcn_rcpf(e4[j]);
;                     const f32x4 o4 = (u4 * A8_SCALE + A8_SCALE) * (g4 * r4);
; #pragma unroll
;                     for (int j = 0; j < 4; ++j) o[4 * n + j] = o4[j]; }
;                 u32x2 w; w.x = pk4_fp8(o[0], o[1], o[2], o[3]); w.y = pk4_fp8(o[4], o[5], o[6], o[7]);
;                 *(u32x2*)(act + ro) = w; }
	v_cvt_pk_fp8_f32 v27, v30, v31
	v_fma_f32 v21, v29, 4.0, 4.0
	v_mul_f32_e32 v21, v21, v25
	v_or_b32_e32 v22, 48, v20
	v_cvt_pk_fp8_f32 v26, v36, v37 op_sel:[0,0,1]
	v_cvt_pk_fp8_f32 v27, v24, v21 op_sel:[0,0,1]
	v_ashrrev_i32_e32 v23, 31, v22
	v_lshlrev_b64 v[22:23], 11, v[22:23]
	v_lshl_add_u64 v[22:23], v[18:19], 0, v[22:23]
	global_store_dwordx2 v[22:23], v[26:27], off sc1
	v_pk_add_f32 v[26:27], v[114:115], v[14:15]
	v_pk_add_f32 v[24:25], v[116:117], v[16:17]
	v_min_f32_e32 v26, 0x40e00000, v26
	v_min_f32_e32 v27, 0x40e00000, v27
	v_min_f32_e32 v24, 0x40e00000, v24
	v_mul_f32_e32 v21, 0xc01d265f, v26
	v_min_f32_e32 v25, 0x40e00000, v25
	v_exp_f32_e32 v32, v21
	v_mul_f32_e32 v21, 0xc01d265f, v27
	v_mul_f32_e32 v23, 0xc01d265f, v24
	v_exp_f32_e32 v34, v23
	v_mul_f32_e32 v23, 0xc01d265f, v25
	v_exp_f32_e32 v33, v21
	v_exp_f32_e32 v35, v23
	v_pk_add_f32 v[30:31], v[130:131], v[10:11]
	v_pk_add_f32 v[28:29], v[132:133], v[12:13]
	v_pk_add_f32 v[32:33], v[32:33], 1.0 op_sel_hi:[1,0]
	v_med3_f32 v21, v30, s80, v225
	v_med3_f32 v23, v31, s80, v225
	v_pk_add_f32 v[30:31], v[34:35], 1.0 op_sel_hi:[1,0]
	v_rcp_f32_e32 v32, v32
	v_rcp_f32_e32 v33, v33
	v_rcp_f32_e32 v30, v30
	v_rcp_f32_e32 v31, v31
	v_med3_f32 v28, v28, s80, v225
	v_pk_mul_f32 v[26:27], v[26:27], v[32:33]
	v_fma_f32 v21, v21, 4.0, 4.0
	v_med3_f32 v29, v29, s80, v225
	v_pk_mul_f32 v[24:25], v[24:25], v[30:31]
	v_mul_f32_e32 v21, v21, v26
	v_fma_f32 v26, v28, 4.0, 4.0
	v_fma_f32 v23, v23, 4.0, 4.0
	v_mul_f32_e32 v36, v26, v24
	v_fma_f32 v24, v29, 4.0, 4.0
	v_mul_f32_e32 v23, v23, v27
	v_mul_f32_e32 v37, v24, v25
	v_pk_add_f32 v[24:25], v[108:109], v[8:9]
	v_pk_add_f32 v[26:27], v[106:107], v[6:7]
	v_min_f32_e32 v24, 0x40e00000, v24
	v_min_f32_e32 v26, 0x40e00000, v26
	v_min_f32_e32 v27, 0x40e00000, v27
	v_min_f32_e32 v25, 0x40e00000, v25
	v_mul_f32_e32 v32, 0xc01d265f, v26
	v_mul_f32_e32 v33, 0xc01d265f, v27
	v_mul_f32_e32 v34, 0xc01d265f, v24
	v_mul_f32_e32 v35, 0xc01d265f, v25
	v_exp_f32_e32 v32, v32
	v_exp_f32_e32 v34, v34
	v_exp_f32_e32 v35, v35
	v_exp_f32_e32 v33, v33
	v_pk_add_f32 v[30:31], v[122:123], v[2:3]
	v_pk_add_f32 v[28:29], v[124:125], v[4:5]
	v_med3_f32 v38, v30, s80, v225
	v_med3_f32 v39, v31, s80, v225
	v_pk_add_f32 v[30:31], v[34:35], 1.0 op_sel_hi:[1,0]
	v_pk_add_f32 v[32:33], v[32:33], 1.0 op_sel_hi:[1,0]
	v_rcp_f32_e32 v30, v30
	v_rcp_f32_e32 v32, v32
	v_rcp_f32_e32 v31, v31
	v_rcp_f32_e32 v33, v33
	v_med3_f32 v28, v28, s80, v225
	v_med3_f32 v29, v29, s80, v225
	v_pk_mul_f32 v[24:25], v[24:25], v[30:31]
	v_pk_mul_f32 v[26:27], v[26:27], v[32:33]
	v_fma_f32 v30, v38, 4.0, 4.0
	v_mul_f32_e32 v30, v30, v26
	v_fma_f32 v26, v39, 4.0, 4.0
	v_mul_f32_e32 v31, v26, v27
	v_fma_f32 v26, v28, 4.0, 4.0
	v_mul_f32_e32 v24, v26, v24
	v_mov_b32_e32 v26, 0
	v_mov_b32_e32 v27, 0
	v_cvt_pk_fp8_f32 v26, v21, v23
	v_cvt_pk_fp8_f32 v27, v30, v31
	v_fma_f32 v21, v29, 4.0, 4.0
	v_mul_f32_e32 v21, v21, v25
	v_add_u32_e32 v22, 0x80, v20
	v_cvt_pk_fp8_f32 v26, v36, v37 op_sel:[0,0,1]
	v_cvt_pk_fp8_f32 v27, v24, v21 op_sel:[0,0,1]
	v_ashrrev_i32_e32 v23, 31, v22
	v_lshlrev_b64 v[22:23], 11, v[22:23]
	v_lshl_add_u64 v[22:23], v[18:19], 0, v[22:23]
	global_store_dwordx2 v[22:23], v[26:27], off sc1
	v_pk_add_f32 v[26:27], v[94:95], v[14:15]
	v_pk_add_f32 v[24:25], v[96:97], v[16:17]
	v_min_f32_e32 v26, 0x40e00000, v26
	v_min_f32_e32 v27, 0x40e00000, v27
	v_min_f32_e32 v24, 0x40e00000, v24
	v_mul_f32_e32 v21, 0xc01d265f, v26
	v_min_f32_e32 v25, 0x40e00000, v25
	v_exp_f32_e32 v32, v21
	v_mul_f32_e32 v21, 0xc01d265f, v27
	v_mul_f32_e32 v23, 0xc01d265f, v24
	v_exp_f32_e32 v34, v23
	v_mul_f32_e32 v23, 0xc01d265f, v25
	v_exp_f32_e32 v33, v21
	v_exp_f32_e32 v35, v23
	v_pk_add_f32 v[30:31], v[102:103], v[10:11]
	v_pk_add_f32 v[28:29], v[104:105], v[12:13]
	v_pk_add_f32 v[32:33], v[32:33], 1.0 op_sel_hi:[1,0]
	v_med3_f32 v21, v30, s80, v225
	v_med3_f32 v23, v31, s80, v225
	v_pk_add_f32 v[30:31], v[34:35], 1.0 op_sel_hi:[1,0]
	v_rcp_f32_e32 v32, v32
	v_rcp_f32_e32 v33, v33
	v_rcp_f32_e32 v30, v30
	v_rcp_f32_e32 v31, v31
	v_med3_f32 v28, v28, s80, v225
	v_pk_mul_f32 v[26:27], v[26:27], v[32:33]
	v_fma_f32 v21, v21, 4.0, 4.0
	v_med3_f32 v29, v29, s80, v225
	v_pk_mul_f32 v[24:25], v[24:25], v[30:31]
	v_mul_f32_e32 v21, v21, v26
	v_fma_f32 v26, v28, 4.0, 4.0
	v_fma_f32 v23, v23, 4.0, 4.0
	v_mul_f32_e32 v36, v26, v24
	v_fma_f32 v24, v29, 4.0, 4.0
	v_mul_f32_e32 v23, v23, v27
	v_mul_f32_e32 v37, v24, v25
	v_pk_add_f32 v[24:25], v[88:89], v[8:9]
	v_pk_add_f32 v[26:27], v[86:87], v[6:7]
	v_min_f32_e32 v24, 0x40e00000, v24
	v_min_f32_e32 v26, 0x40e00000, v26
	v_min_f32_e32 v27, 0x40e00000, v27
	v_min_f32_e32 v25, 0x40e00000, v25
	v_mul_f32_e32 v32, 0xc01d265f, v26
	v_mul_f32_e32 v33, 0xc01d265f, v27
	v_mul_f32_e32 v34, 0xc01d265f, v24
	v_mul_f32_e32 v35, 0xc01d265f, v25
	v_exp_f32_e32 v32, v32
	v_exp_f32_e32 v34, v34
	v_exp_f32_e32 v35, v35
	v_exp_f32_e32 v33, v33
	v_pk_add_f32 v[30:31], v[90:91], v[2:3]
	v_pk_add_f32 v[28:29], v[92:93], v[4:5]
	v_med3_f32 v38, v30, s80, v225
	v_med3_f32 v39, v31, s80, v225
	v_pk_add_f32 v[30:31], v[34:35], 1.0 op_sel_hi:[1,0]
	v_pk_add_f32 v[32:33], v[32:33], 1.0 op_sel_hi:[1,0]
	v_rcp_f32_e32 v30, v30
	v_rcp_f32_e32 v32, v32
	v_rcp_f32_e32 v31, v31
	v_rcp_f32_e32 v33, v33
	v_med3_f32 v28, v28, s80, v225
	v_med3_f32 v29, v29, s80, v225
	v_pk_mul_f32 v[24:25], v[24:25], v[30:31]
	v_pk_mul_f32 v[26:27], v[26:27], v[32:33]
	v_fma_f32 v30, v38, 4.0, 4.0
	v_mul_f32_e32 v30, v30, v26
	v_fma_f32 v26, v39, 4.0, 4.0
	v_mul_f32_e32 v31, v26, v27
	v_fma_f32 v26, v28, 4.0, 4.0
	v_mul_f32_e32 v24, v26, v24
	v_mov_b32_e32 v26, 0
	v_mov_b32_e32 v27, 0
	v_cvt_pk_fp8_f32 v26, v21, v23
; __device__ __forceinline__ unsigned pk4_fp8(float a, float b, float c, float d) { int w = 0; w = __builtin_amdgcn_cvt_pk_fp8_f32(a, b, w, false); w = __builtin_amdgcn_cvt_pk_fp8_f32(c, d, w, true); return (unsigned)w; }
;     __device__ __forceinline__ const char* bias_base(const pg8::Unit& u) const { return (const char*)(bgu + (size_t)u.e * 4096 + u.pn * 128); }
;     __device__ __forceinline__ unsigned bias_off(const pg8::Unit&, int wc, int lane) const { return (unsigned)(((lane >> 3) & 1) * 2048 + wc * 32 + (lane & 7) * 4) * 4u; }
;     ...
;         if (!has_next) break;
;         if constexpr (RSYNC) xcd_barrier(*rbar);
; #pragma unroll
;         for (int a = 0; a < 2; ++a)
; #pragma unroll
;             for (int b = 0; b < 2; ++b)
; #pragma unroll
;                 for (int m = 0; m < 4; ++m)
; #pragma unroll
;                     for (int n = 0; n < 2; ++n) acc[a][b][m][n] = (f32x4){0.f, 0.f, 0.f, 0.f};
;         cur = nxt; cA = nA; cB = nB; ++ui;
;         if constexpr (Epi::kBiasDMA) { if (lane < 16) glds16(E.bias_base(cur), E.bias_off(cur, wc, lane), bias_lds); }
;     __device__ __forceinline__ void operator()(const AccT& acc, const pg8::Unit& u, int wr, int wc, int fr, int fq, const LAS float* bl, int nai) const {
;     ...
;             for (int m = 0; m < 4; ++m) { const size_t ro = (size_t)(row0 + ai * 128 + m * 16) * DFF + a0; float o[8];
; #pragma unroll
;                 for (int n = 0; n < 2; ++n) {
;                     f32x4 g4 = acc[ai][0][m][n] + (n ? bg1 : bg0), u4 = acc[ai][1][m][n] + (n ? bu1 : bu0);
; #pragma unroll
;                     for (int j = 0; j < 4; ++j) { g4[j] = fminf(g4[j], 7.0f); u4[j] = __builtin_amdgcn_fmed3f(u4[j], -7.0f, 7.0f); }
;                     const f32x4 t4 = g4 * (-1.702f * 1.4426950408889634f);
;                     f32x4 e4;
; #pragma unroll
;                     for (int j = 0; j < 4; ++j) e4[j] = __builtin_amdgcn_exp2f(t4[j]);
;                     e4 = e4 + 1.0f;
;                     f32x4 r4;
; #pragma unroll
;                     for (int j = 0; j < 4; ++j) r4[j] = __builtin_amdgcn_rcpf(e4[j]);
;                     const f32x4 o4 = (u4 * A8_SCALE + A8_SCALE) * (g4 * r4);
; #pragma unroll
;                     for (int j = 0; j < 4; ++j) o[4 * n + j] = o4[j]; }
;                 u32x2 w; w.x = pk4_fp8(o[0], o[1], o[2], o[3]); w.y = pk4_fp8(o[4], o[5], o[6], o[7]);
;                 *(u32x2*)(act + ro) = w; }
	v_cvt_pk_fp8_f32 v27, v30, v31
	v_fma_f32 v21, v29, 4.0, 4.0
	v_mul_f32_e32 v21, v21, v25
	v_add_u32_e32 v22, 0x90, v20
	v_cvt_pk_fp8_f32 v26, v36, v37 op_sel:[0,0,1]
	v_cvt_pk_fp8_f32 v27, v24, v21 op_sel:[0,0,1]
	v_ashrrev_i32_e32 v23, 31, v22
	v_lshlrev_b64 v[22:23], 11, v[22:23]
	v_lshl_add_u64 v[22:23], v[18:19], 0, v[22:23]
	global_store_dwordx2 v[22:23], v[26:27], off sc1
	v_pk_add_f32 v[26:27], v[78:79], v[14:15]
	v_pk_add_f32 v[24:25], v[80:81], v[16:17]
	v_min_f32_e32 v26, 0x40e00000, v26
	v_min_f32_e32 v27, 0x40e00000, v27
	v_min_f32_e32 v24, 0x40e00000, v24
	v_mul_f32_e32 v21, 0xc01d265f, v26
	v_min_f32_e32 v25, 0x40e00000, v25
	v_exp_f32_e32 v32, v21
	v_mul_f32_e32 v21, 0xc01d265f, v27
	v_mul_f32_e32 v23, 0xc01d265f, v24
	v_exp_f32_e32 v34, v23
	v_mul_f32_e32 v23, 0xc01d265f, v25
	v_exp_f32_e32 v33, v21
	v_exp_f32_e32 v35, v23
	v_pk_add_f32 v[30:31], v[82:83], v[10:11]
	v_pk_add_f32 v[28:29], v[84:85], v[12:13]
	v_pk_add_f32 v[32:33], v[32:33], 1.0 op_sel_hi:[1,0]
	v_med3_f32 v21, v30, s80, v225
	v_med3_f32 v23, v31, s80, v225
	v_pk_add_f32 v[30:31], v[34:35], 1.0 op_sel_hi:[1,0]
	v_rcp_f32_e32 v32, v32
	v_rcp_f32_e32 v33, v33
	v_rcp_f32_e32 v30, v30
	v_rcp_f32_e32 v31, v31
	v_med3_f32 v28, v28, s80, v225
	v_pk_mul_f32 v[26:27], v[26:27], v[32:33]
	v_fma_f32 v21, v21, 4.0, 4.0
	v_med3_f32 v29, v29, s80, v225
	v_pk_mul_f32 v[24:25], v[24:25], v[30:31]
	v_mul_f32_e32 v21, v21, v26
	v_fma_f32 v26, v28, 4.0, 4.0
	v_fma_f32 v23, v23, 4.0, 4.0
	v_mul_f32_e32 v36, v26, v24
	v_fma_f32 v24, v29, 4.0, 4.0
	v_mul_f32_e32 v23, v23, v27
	v_mul_f32_e32 v37, v24, v25
	v_pk_add_f32 v[24:25], v[72:73], v[8:9]
	v_pk_add_f32 v[26:27], v[70:71], v[6:7]
	v_min_f32_e32 v24, 0x40e00000, v24
	v_min_f32_e32 v26, 0x40e00000, v26
	v_min_f32_e32 v27, 0x40e00000, v27
	v_min_f32_e32 v25, 0x40e00000, v25
	v_mul_f32_e32 v32, 0xc01d265f, v26
	v_mul_f32_e32 v33, 0xc01d265f, v27
	v_mul_f32_e32 v34, 0xc01d265f, v24
	v_mul_f32_e32 v35, 0xc01d265f, v25
	v_exp_f32_e32 v32, v32
	v_exp_f32_e32 v34, v34
	v_exp_f32_e32 v35, v35
	v_exp_f32_e32 v33, v33
	v_pk_add_f32 v[30:31], v[74:75], v[2:3]
	v_pk_add_f32 v[28:29], v[76:77], v[4:5]
	v_med3_f32 v38, v30, s80, v225
	v_med3_f32 v39, v31, s80, v225
	v_pk_add_f32 v[30:31], v[34:35], 1.0 op_sel_hi:[1,0]
	v_pk_add_f32 v[32:33], v[32:33], 1.0 op_sel_hi:[1,0]
	v_rcp_f32_e32 v30, v30
	v_rcp_f32_e32 v32, v32
	v_rcp_f32_e32 v31, v31
	v_rcp_f32_e32 v33, v33
	v_med3_f32 v28, v28, s80, v225
	v_med3_f32 v29, v29, s80, v225
	v_pk_mul_f32 v[24:25], v[24:25], v[30:31]
	v_pk_mul_f32 v[26:27], v[26:27], v[32:33]
	v_fma_f32 v30, v38, 4.0, 4.0
	v_mul_f32_e32 v30, v30, v26
	v_fma_f32 v26, v39, 4.0, 4.0
	v_mul_f32_e32 v31, v26, v27
	v_fma_f32 v26, v28, 4.0, 4.0
	v_mul_f32_e32 v24, v26, v24
	v_mov_b32_e32 v26, 0
	v_mov_b32_e32 v27, 0
	v_cvt_pk_fp8_f32 v26, v21, v23
	v_cvt_pk_fp8_f32 v27, v30, v31
	v_fma_f32 v21, v29, 4.0, 4.0
	v_mul_f32_e32 v21, v21, v25
	v_add_u32_e32 v22, 0xa0, v20
	v_cvt_pk_fp8_f32 v26, v36, v37 op_sel:[0,0,1]
	v_cvt_pk_fp8_f32 v27, v24, v21 op_sel:[0,0,1]
	v_ashrrev_i32_e32 v23, 31, v22
	v_lshlrev_b64 v[22:23], 11, v[22:23]
	v_pk_add_f32 v[16:17], v[64:65], v[16:17]
	v_pk_add_f32 v[14:15], v[62:63], v[14:15]
	v_lshl_add_u64 v[22:23], v[18:19], 0, v[22:23]
	v_min_f32_e32 v14, 0x40e00000, v14
	v_min_f32_e32 v16, 0x40e00000, v16
	global_store_dwordx2 v[22:23], v[26:27], off sc1
	v_min_f32_e32 v15, 0x40e00000, v15
	v_min_f32_e32 v17, 0x40e00000, v17
	v_mul_f32_e32 v21, 0xc01d265f, v14
	v_mul_f32_e32 v23, 0xc01d265f, v16
	v_exp_f32_e32 v22, v21
	v_mul_f32_e32 v21, 0xc01d265f, v15
	v_exp_f32_e32 v24, v23
	v_mul_f32_e32 v23, 0xc01d265f, v17
	v_exp_f32_e32 v25, v23
	v_exp_f32_e32 v23, v21
	v_pk_add_f32 v[10:11], v[66:67], v[10:11]
	v_pk_add_f32 v[12:13], v[68:69], v[12:13]
	v_med3_f32 v21, v10, s80, v225
	v_pk_add_f32 v[22:23], v[22:23], 1.0 op_sel_hi:[1,0]
	v_med3_f32 v26, v11, s80, v225
	v_rcp_f32_e32 v22, v22
	v_rcp_f32_e32 v23, v23
	v_pk_add_f32 v[10:11], v[24:25], 1.0 op_sel_hi:[1,0]
	v_med3_f32 v24, v12, s80, v225
	v_rcp_f32_e32 v10, v10
	v_rcp_f32_e32 v11, v11
	v_med3_f32 v25, v13, s80, v225
	v_pk_mul_f32 v[12:13], v[14:15], v[22:23]
	v_fma_f32 v14, v21, 4.0, 4.0
	v_mul_f32_e32 v14, v14, v12
	v_fma_f32 v12, v26, 4.0, 4.0
	v_pk_mul_f32 v[10:11], v[16:17], v[10:11]
	v_mul_f32_e32 v15, v12, v13
	v_fma_f32 v12, v24, 4.0, 4.0
	v_pk_add_f32 v[6:7], v[58:59], v[6:7]
	v_mul_f32_e32 v16, v12, v10
	v_fma_f32 v10, v25, 4.0, 4.0
	v_min_f32_e32 v6, 0x40e00000, v6
	v_min_f32_e32 v7, 0x40e00000, v7
	v_mul_f32_e32 v17, v10, v11
	v_pk_add_f32 v[8:9], v[60:61], v[8:9]
	v_mul_f32_e32 v10, 0xc01d265f, v6
	v_mul_f32_e32 v11, 0xc01d265f, v7
	v_min_f32_e32 v8, 0x40e00000, v8
	v_min_f32_e32 v9, 0x40e00000, v9
	v_exp_f32_e32 v10, v10
	v_exp_f32_e32 v11, v11
	v_mul_f32_e32 v12, 0xc01d265f, v8
	v_mul_f32_e32 v13, 0xc01d265f, v9
	v_exp_f32_e32 v12, v12
	v_exp_f32_e32 v13, v13
	v_pk_add_f32 v[10:11], v[10:11], 1.0 op_sel_hi:[1,0]
	v_pk_add_f32 v[2:3], v[54:55], v[2:3]
	v_rcp_f32_e32 v10, v10
	v_rcp_f32_e32 v11, v11
	v_med3_f32 v21, v2, s80, v225
	v_med3_f32 v22, v3, s80, v225
	v_pk_add_f32 v[2:3], v[12:13], 1.0 op_sel_hi:[1,0]
	v_pk_add_f32 v[4:5], v[56:57], v[4:5]
	v_rcp_f32_e32 v2, v2
	v_rcp_f32_e32 v3, v3
	v_med3_f32 v12, v4, s80, v225
	v_med3_f32 v13, v5, s80, v225
	v_pk_mul_f32 v[4:5], v[6:7], v[10:11]
	v_fma_f32 v6, v21, 4.0, 4.0
	v_mul_f32_e32 v6, v6, v4
	v_fma_f32 v4, v22, 4.0, 4.0
	v_pk_mul_f32 v[2:3], v[8:9], v[2:3]
	v_mul_f32_e32 v7, v4, v5
	v_fma_f32 v4, v12, 4.0, 4.0
	v_mul_f32_e32 v2, v4, v2
	v_mov_b32_e32 v4, 0
	v_mov_b32_e32 v5, 0
	v_cvt_pk_fp8_f32 v4, v14, v15
	v_cvt_pk_fp8_f32 v5, v6, v7
	v_fma_f32 v6, v13, 4.0, 4.0
	v_mul_f32_e32 v3, v6, v3
	v_add_u32_e32 v20, 0xb0, v20
	v_cvt_pk_fp8_f32 v4, v16, v17 op_sel:[0,0,1]
	v_cvt_pk_fp8_f32 v5, v2, v3 op_sel:[0,0,1]
	v_ashrrev_i32_e32 v21, 31, v20
	v_lshlrev_b64 v[2:3], 11, v[20:21]
	v_lshl_add_u64 v[2:3], v[18:19], 0, v[2:3]
	s_and_b64 vcc, exec, s[8:9]
	s_mov_b64 s[8:9], -1
	global_store_dwordx2 v[2:3], v[4:5], off sc1
	s_cbranch_vccnz .LBB0_1117
	s_and_saveexec_b64 s[8:9], s[6:7]
	s_cbranch_execz .LBB0_1145
	s_ashr_i32 s41, s40, 31
	s_lshl_b64 s[10:11], s[40:41], 14
	s_add_u32 s16, s22, s10
	s_addc_u32 s17, s23, s11
	s_lshl_b32 s10, s42, 7
	s_ashr_i32 s11, s10, 31
	s_lshl_b64 s[10:11], s[10:11], 2
	s_add_u32 s10, s16, s10
	s_addc_u32 s11, s17, s11
	s_mov_b32 s16, m0
	s_mov_b32 m0, s65
	s_nop 0
	global_load_lds_dwordx4 v221, s[10:11]
	s_mov_b32 m0, s16

; #define LAS __attribute__((address_space(3)))
; __device__ __forceinline__ unsigned pk4_fp8(float a, float b, float c, float d) { int w = 0; w = __builtin_amdgcn_cvt_pk_fp8_f32(a, b, w, false); w = __builtin_amdgcn_cvt_pk_fp8_f32(c, d, w, true); return (unsigned)w; }
;     __device__ __forceinline__ void operator()(const AccT& acc, const pg8::Unit& u, int wr, int wc, int fr, int fq, const LAS float* bl, int nai) const {
;         const int row0 = u.pm * 256 + u.hx * 128 + wr * 64 + fr, a0 = u.pn * 128 + wc * 32 + 8 * fq;
;         unsigned char* act = (unsigned char*)(ws + WS_ACT);
;         const f32x4 bg0 = *(const LAS f32x4*)(bl + 8 * fq), bg1 = *(const LAS f32x4*)(bl + 8 * fq + 4), bu0 = *(const LAS f32x4*)(bl + 32 + 8 * fq), bu1 = *(const LAS f32x4*)(bl + 32 + 8 * fq + 4);
; #pragma unroll
;         for (int ai = 0; ai < 2; ++ai) if (ai < nai)
; #pragma unroll
;             for (int m = 0; m < 4; ++m) { const size_t ro = (size_t)(row0 + ai * 128 + m * 16) * DFF + a0; float o[8];
; #pragma unroll
;                 for (int n = 0; n < 2; ++n) {
;                     f32x4 g4 = acc[ai][0][m][n] + (n ? bg1 : bg0), u4 = acc[ai][1][m][n] + (n ? bu1 : bu0);
; #pragma unroll
;                     for (int j = 0; j < 4; ++j) { g4[j] = fminf(g4[j], 7.0f); u4[j] = __builtin_amdgcn_fmed3f(u4[j], -7.0f, 7.0f); }
;                     const f32x4 t4 = g4 * (-1.702f * 1.4426950408889634f);
;                     f32x4 e4;
; #pragma unroll
;                     for (int j = 0; j < 4; ++j) e4[j] = __builtin_amdgcn_exp2f(t4[j]);
;                     e4 = e4 + 1.0f;
;                     f32x4 r4;
; #pragma unroll
;                     for (int j = 0; j < 4; ++j) r4[j] = __builtin_amdgcn_rcpf(e4[j]);
;                     const f32x4 o4 = (u4 * A8_SCALE + A8_SCALE) * (g4 * r4);
; #pragma unroll
;                     for (int j = 0; j < 4; ++j) o[4 * n + j] = o4[j]; }
;                 u32x2 w; w.x = pk4_fp8(o[0], o[1], o[2], o[3]); w.y = pk4_fp8(o[4], o[5], o[6], o[7]);
;                 *(u32x2*)(act + ro) = w; }
.LBB0_1192:
	s_nop 15
	s_nop 15
	ds_read_b128 v[14:17], v156
	ds_read_b128 v[6:9], v156 offset:16
	ds_read_b128 v[10:13], v156 offset:128
	ds_read_b128 v[2:5], v156 offset:144
	v_lshl_or_b32 v18, s44, 7, v158
	s_waitcnt lgkmcnt(3)
	v_pk_add_f32 v[22:23], v[108:109], v[16:17]
	v_pk_add_f32 v[24:25], v[106:107], v[14:15]
	v_min_f32_e32 v22, 0x40e00000, v22
	v_min_f32_e32 v24, 0x40e00000, v24
	v_min_f32_e32 v25, 0x40e00000, v25
	v_min_f32_e32 v23, 0x40e00000, v23
	v_mul_f32_e32 v21, 0xc01d265f, v24
	v_mul_f32_e32 v31, 0xc01d265f, v22
	v_exp_f32_e32 v30, v21
	v_mul_f32_e32 v21, 0xc01d265f, v25
	v_exp_f32_e32 v32, v31
	v_mul_f32_e32 v31, 0xc01d265f, v23
	v_exp_f32_e32 v33, v31
	v_exp_f32_e32 v31, v21
	s_waitcnt lgkmcnt(1)
	v_pk_add_f32 v[28:29], v[114:115], v[10:11]
	v_pk_add_f32 v[26:27], v[116:117], v[12:13]
	v_med3_f32 v21, v28, s73, v161
	v_pk_add_f32 v[30:31], v[30:31], 1.0 op_sel_hi:[1,0]
	v_med3_f32 v34, v29, s73, v161
	v_rcp_f32_e32 v30, v30
	v_rcp_f32_e32 v31, v31
	v_pk_add_f32 v[28:29], v[32:33], 1.0 op_sel_hi:[1,0]
	v_fma_f32 v21, v21, 4.0, 4.0
	v_rcp_f32_e32 v28, v28
	v_rcp_f32_e32 v29, v29
	v_pk_mul_f32 v[24:25], v[24:25], v[30:31]
	v_med3_f32 v26, v26, s73, v161
	v_mul_f32_e32 v21, v21, v24
	v_fma_f32 v24, v34, 4.0, 4.0
	v_med3_f32 v27, v27, s73, v161
	v_pk_mul_f32 v[22:23], v[22:23], v[28:29]
	v_mul_f32_e32 v34, v24, v25
	v_fma_f32 v24, v26, 4.0, 4.0
	v_mul_f32_e32 v35, v24, v22
	v_fma_f32 v22, v27, 4.0, 4.0
	v_mul_f32_e32 v36, v22, v23
	v_pk_add_f32 v[22:23], v[104:105], v[8:9]
	v_pk_add_f32 v[24:25], v[102:103], v[6:7]
	v_min_f32_e32 v22, 0x40e00000, v22
	v_min_f32_e32 v24, 0x40e00000, v24
	v_min_f32_e32 v25, 0x40e00000, v25
	v_min_f32_e32 v23, 0x40e00000, v23
	v_mul_f32_e32 v30, 0xc01d265f, v24
	v_mul_f32_e32 v31, 0xc01d265f, v25
	v_mul_f32_e32 v32, 0xc01d265f, v22
	v_mul_f32_e32 v33, 0xc01d265f, v23
	v_exp_f32_e32 v30, v30
	v_exp_f32_e32 v32, v32
	v_exp_f32_e32 v33, v33
	v_exp_f32_e32 v31, v31
	s_waitcnt lgkmcnt(0)
	v_pk_add_f32 v[28:29], v[110:111], v[2:3]
	v_pk_add_f32 v[26:27], v[112:113], v[4:5]
	v_med3_f32 v37, v28, s73, v161
	v_med3_f32 v38, v29, s73, v161
	v_pk_add_f32 v[28:29], v[32:33], 1.0 op_sel_hi:[1,0]
	v_pk_add_f32 v[30:31], v[30:31], 1.0 op_sel_hi:[1,0]
	v_rcp_f32_e32 v28, v28
	v_rcp_f32_e32 v30, v30
	v_rcp_f32_e32 v29, v29
	v_rcp_f32_e32 v31, v31
	v_med3_f32 v26, v26, s73, v161
	v_med3_f32 v27, v27, s73, v161
	v_pk_mul_f32 v[22:23], v[22:23], v[28:29]
	v_pk_mul_f32 v[24:25], v[24:25], v[30:31]
	v_fma_f32 v28, v37, 4.0, 4.0
	v_mul_f32_e32 v28, v28, v24
	v_fma_f32 v24, v38, 4.0, 4.0
	v_mul_f32_e32 v29, v24, v25
	v_fma_f32 v24, v26, 4.0, 4.0
	v_mul_f32_e32 v22, v24, v22
	v_mov_b32_e32 v24, 0
	v_mov_b32_e32 v25, 0
	v_cvt_pk_fp8_f32 v24, v21, v34
	v_cvt_pk_fp8_f32 v25, v28, v29
	v_fma_f32 v21, v27, 4.0, 4.0
	v_mul_f32_e32 v21, v21, v23
	v_lshl_add_u32 v20, s77, 8, v155
	v_cvt_pk_fp8_f32 v24, v35, v36 op_sel:[0,0,1]
	v_cvt_pk_fp8_f32 v25, v22, v21 op_sel:[0,0,1]
	v_ashrrev_i32_e32 v19, 31, v18
	v_ashrrev_i32_e32 v21, 31, v20
	v_lshl_add_u64 v[18:19], s[28:29], 0, v[18:19]
	v_lshlrev_b64 v[22:23], 11, v[20:21]
	v_lshl_add_u64 v[22:23], v[18:19], 0, v[22:23]
	v_pk_add_f32 v[26:27], v[90:91], v[14:15]
	global_store_dwordx2 v[22:23], v[24:25], off sc1
	v_pk_add_f32 v[24:25], v[92:93], v[16:17]
	v_min_f32_e32 v26, 0x40e00000, v26
	v_min_f32_e32 v27, 0x40e00000, v27
	v_min_f32_e32 v24, 0x40e00000, v24
	v_mul_f32_e32 v21, 0xc01d265f, v26
	v_min_f32_e32 v25, 0x40e00000, v25
	v_exp_f32_e32 v32, v21
	v_mul_f32_e32 v21, 0xc01d265f, v27
	v_mul_f32_e32 v23, 0xc01d265f, v24
	v_exp_f32_e32 v34, v23
	v_mul_f32_e32 v23, 0xc01d265f, v25
	v_exp_f32_e32 v33, v21
	v_exp_f32_e32 v35, v23
	v_pk_add_f32 v[30:31], v[98:99], v[10:11]
	v_pk_add_f32 v[28:29], v[100:101], v[12:13]
	v_pk_add_f32 v[32:33], v[32:33], 1.0 op_sel_hi:[1,0]
	v_med3_f32 v21, v30, s73, v161
	v_med3_f32 v23, v31, s73, v161
	v_pk_add_f32 v[30:31], v[34:35], 1.0 op_sel_hi:[1,0]
	v_rcp_f32_e32 v32, v32
	v_rcp_f32_e32 v33, v33
	v_rcp_f32_e32 v30, v30
	v_rcp_f32_e32 v31, v31
	v_med3_f32 v28, v28, s73, v161
	v_pk_mul_f32 v[26:27], v[26:27], v[32:33]
	v_fma_f32 v21, v21, 4.0, 4.0
	v_med3_f32 v29, v29, s73, v161
	v_pk_mul_f32 v[24:25], v[24:25], v[30:31]
	v_mul_f32_e32 v21, v21, v26
	v_fma_f32 v26, v28, 4.0, 4.0
	v_fma_f32 v23, v23, 4.0, 4.0
	v_mul_f32_e32 v36, v26, v24
	v_fma_f32 v24, v29, 4.0, 4.0
	v_mul_f32_e32 v23, v23, v27
	v_mul_f32_e32 v37, v24, v25
	v_pk_add_f32 v[24:25], v[88:89], v[8:9]
	v_pk_add_f32 v[26:27], v[86:87], v[6:7]
	v_min_f32_e32 v24, 0x40e00000, v24
	v_min_f32_e32 v26, 0x40e00000, v26
	v_min_f32_e32 v27, 0x40e00000, v27
	v_min_f32_e32 v25, 0x40e00000, v25
	v_mul_f32_e32 v32, 0xc01d265f, v26
	v_mul_f32_e32 v33, 0xc01d265f, v27
	v_mul_f32_e32 v34, 0xc01d265f, v24
	v_mul_f32_e32 v35, 0xc01d265f, v25
	v_exp_f32_e32 v32, v32
	v_exp_f32_e32 v34, v34
	v_exp_f32_e32 v35, v35
	v_exp_f32_e32 v33, v33
	v_pk_add_f32 v[30:31], v[94:95], v[2:3]
	v_pk_add_f32 v[28:29], v[96:97], v[4:5]
	v_med3_f32 v38, v30, s73, v161
	v_med3_f32 v39, v31, s73, v161
	v_pk_add_f32 v[30:31], v[34:35], 1.0 op_sel_hi:[1,0]
	v_pk_add_f32 v[32:33], v[32:33], 1.0 op_sel_hi:[1,0]
	v_rcp_f32_e32 v30, v30
	v_rcp_f32_e32 v32, v32
	v_rcp_f32_e32 v31, v31
	v_rcp_f32_e32 v33, v33
	v_med3_f32 v28, v28, s73, v161
	v_med3_f32 v29, v29, s73, v161
	v_pk_mul_f32 v[24:25], v[24:25], v[30:31]
	v_pk_mul_f32 v[26:27], v[26:27], v[32:33]
	v_fma_f32 v30, v38, 4.0, 4.0
	v_mul_f32_e32 v30, v30, v26
	v_fma_f32 v26, v39, 4.0, 4.0
	v_mul_f32_e32 v31, v26, v27
	v_fma_f32 v26, v28, 4.0, 4.0
	v_mul_f32_e32 v24, v26, v24
	v_mov_b32_e32 v26, 0
	v_mov_b32_e32 v27, 0
	v_cvt_pk_fp8_f32 v26, v21, v23
	v_cvt_pk_fp8_f32 v27, v30, v31
; __device__ __forceinline__ unsigned pk4_fp8(float a, float b, float c, float d) { int w = 0; w = __builtin_amdgcn_cvt_pk_fp8_f32(a, b, w, false); w = __builtin_amdgcn_cvt_pk_fp8_f32(c, d, w, true); return (unsigned)w; }
;     __device__ __forceinline__ const char* bias_base(const pg8::Unit& u) const { return (const char*)(bgu + (size_t)u.e * 4096 + u.pn * 128); }
;     __device__ __forceinline__ unsigned bias_off(const pg8::Unit&, int wc, int lane) const { return (unsigned)(((lane >> 3) & 1) * 2048 + wc * 32 + (lane & 7) * 4) * 4u; }
;     ...
;         if (!has_next) break;
;         if constexpr (RSYNC) xcd_barrier(*rbar);
; #pragma unroll
;         for (int a = 0; a < 2; ++a)
; #pragma unroll
;             for (int b = 0; b < 2; ++b)
; #pragma unroll
;                 for (int m = 0; m < 4; ++m)
; #pragma unroll
;                     for (int n = 0; n < 2; ++n) acc[a][b][m][n] = (f32x4){0.f, 0.f, 0.f, 0.f};
;         cur = nxt; cA = nA; cB = nB; ++ui;
;         if constexpr (Epi::kBiasDMA) { if (lane < 16) glds16(E.bias_base(cur), E.bias_off(cur, wc, lane), bias_lds); }
;     __device__ __forceinline__ void operator()(const AccT& acc, const pg8::Unit& u, int wr, int wc, int fr, int fq, const LAS float* bl, int nai) const {
;     ...
;             for (int m = 0; m < 4; ++m) { const size_t ro = (size_t)(row0 + ai * 128 + m * 16) * DFF + a0; float o[8];
; #pragma unroll
;                 for (int n = 0; n < 2; ++n) {
;                     f32x4 g4 = acc[ai][0][m][n] + (n ? bg1 : bg0), u4 = acc[ai][1][m][n] + (n ? bu1 : bu0);
; #pragma unroll
;                     for (int j = 0; j < 4; ++j) { g4[j] = fminf(g4[j], 7.0f); u4[j] = __builtin_amdgcn_fmed3f(u4[j], -7.0f, 7.0f); }
;                     const f32x4 t4 = g4 * (-1.702f * 1.4426950408889634f);
;                     f32x4 e4;
; #pragma unroll
;                     for (int j = 0; j < 4; ++j) e4[j] = __builtin_amdgcn_exp2f(t4[j]);
;                     e4 = e4 + 1.0f;
;                     f32x4 r4;
; #pragma unroll
;                     for (int j = 0; j < 4; ++j) r4[j] = __builtin_amdgcn_rcpf(e4[j]);
;                     const f32x4 o4 = (u4 * A8_SCALE + A8_SCALE) * (g4 * r4);
; #pragma unroll
;                     for (int j = 0; j < 4; ++j) o[4 * n + j] = o4[j]; }
;                 u32x2 w; w.x = pk4_fp8(o[0], o[1], o[2], o[3]); w.y = pk4_fp8(o[4], o[5], o[6], o[7]);
;                 *(u32x2*)(act + ro) = w; }
	v_fma_f32 v21, v29, 4.0, 4.0
	v_mul_f32_e32 v21, v21, v25
	v_or_b32_e32 v22, 16, v20
	v_cvt_pk_fp8_f32 v26, v36, v37 op_sel:[0,0,1]
	v_cvt_pk_fp8_f32 v27, v24, v21 op_sel:[0,0,1]
	v_ashrrev_i32_e32 v23, 31, v22
	v_lshlrev_b64 v[22:23], 11, v[22:23]
	v_lshl_add_u64 v[22:23], v[18:19], 0, v[22:23]
	global_store_dwordx2 v[22:23], v[26:27], off sc1
	v_pk_add_f32 v[26:27], v[78:79], v[14:15]
	v_pk_add_f32 v[24:25], v[80:81], v[16:17]
	v_min_f32_e32 v26, 0x40e00000, v26
	v_min_f32_e32 v27, 0x40e00000, v27
	v_min_f32_e32 v24, 0x40e00000, v24
	v_mul_f32_e32 v21, 0xc01d265f, v26
	v_min_f32_e32 v25, 0x40e00000, v25
	v_exp_f32_e32 v32, v21
	v_mul_f32_e32 v21, 0xc01d265f, v27
	v_mul_f32_e32 v23, 0xc01d265f, v24
	v_exp_f32_e32 v34, v23
	v_mul_f32_e32 v23, 0xc01d265f, v25
	v_exp_f32_e32 v33, v21
	v_exp_f32_e32 v35, v23
	v_pk_add_f32 v[30:31], v[82:83], v[10:11]
	v_pk_add_f32 v[28:29], v[84:85], v[12:13]
	v_pk_add_f32 v[32:33], v[32:33], 1.0 op_sel_hi:[1,0]
	v_med3_f32 v21, v30, s73, v161
	v_med3_f32 v23, v31, s73, v161
	v_pk_add_f32 v[30:31], v[34:35], 1.0 op_sel_hi:[1,0]
	v_rcp_f32_e32 v32, v32
	v_rcp_f32_e32 v33, v33
	v_rcp_f32_e32 v30, v30
	v_rcp_f32_e32 v31, v31
	v_med3_f32 v28, v28, s73, v161
	v_pk_mul_f32 v[26:27], v[26:27], v[32:33]
	v_fma_f32 v21, v21, 4.0, 4.0
	v_med3_f32 v29, v29, s73, v161
	v_pk_mul_f32 v[24:25], v[24:25], v[30:31]
	v_mul_f32_e32 v21, v21, v26
	v_fma_f32 v26, v28, 4.0, 4.0
	v_fma_f32 v23, v23, 4.0, 4.0
	v_mul_f32_e32 v36, v26, v24
	v_fma_f32 v24, v29, 4.0, 4.0
	v_mul_f32_e32 v23, v23, v27
	v_mul_f32_e32 v37, v24, v25
	v_pk_add_f32 v[24:25], v[72:73], v[8:9]
	v_pk_add_f32 v[26:27], v[70:71], v[6:7]
	v_min_f32_e32 v24, 0x40e00000, v24
	v_min_f32_e32 v26, 0x40e00000, v26
	v_min_f32_e32 v27, 0x40e00000, v27
	v_min_f32_e32 v25, 0x40e00000, v25
	v_mul_f32_e32 v32, 0xc01d265f, v26
	v_mul_f32_e32 v33, 0xc01d265f, v27
	v_mul_f32_e32 v34, 0xc01d265f, v24
	v_mul_f32_e32 v35, 0xc01d265f, v25
	v_exp_f32_e32 v32, v32
	v_exp_f32_e32 v34, v34
	v_exp_f32_e32 v35, v35
	v_exp_f32_e32 v33, v33
	v_pk_add_f32 v[30:31], v[74:75], v[2:3]
	v_pk_add_f32 v[28:29], v[76:77], v[4:5]
	v_med3_f32 v38, v30, s73, v161
	v_med3_f32 v39, v31, s73, v161
	v_pk_add_f32 v[30:31], v[34:35], 1.0 op_sel_hi:[1,0]
	v_pk_add_f32 v[32:33], v[32:33], 1.0 op_sel_hi:[1,0]
	v_rcp_f32_e32 v30, v30
	v_rcp_f32_e32 v32, v32
	v_rcp_f32_e32 v31, v31
	v_rcp_f32_e32 v33, v33
	v_med3_f32 v28, v28, s73, v161
	v_med3_f32 v29, v29, s73, v161
	v_pk_mul_f32 v[24:25], v[24:25], v[30:31]
	v_pk_mul_f32 v[26:27], v[26:27], v[32:33]
	v_fma_f32 v30, v38, 4.0, 4.0
	v_mul_f32_e32 v30, v30, v26
	v_fma_f32 v26, v39, 4.0, 4.0
	v_mul_f32_e32 v31, v26, v27
	v_fma_f32 v26, v28, 4.0, 4.0
	v_mul_f32_e32 v24, v26, v24
	v_mov_b32_e32 v26, 0
	v_mov_b32_e32 v27, 0
	v_cvt_pk_fp8_f32 v26, v21, v23
	v_cvt_pk_fp8_f32 v27, v30, v31
	v_fma_f32 v21, v29, 4.0, 4.0
	v_mul_f32_e32 v21, v21, v25
	v_or_b32_e32 v22, 32, v20
	v_cvt_pk_fp8_f32 v26, v36, v37 op_sel:[0,0,1]
	v_cvt_pk_fp8_f32 v27, v24, v21 op_sel:[0,0,1]
	v_ashrrev_i32_e32 v23, 31, v22
	v_lshlrev_b64 v[22:23], 11, v[22:23]
	v_pk_add_f32 v[16:17], v[64:65], v[16:17]
	v_pk_add_f32 v[14:15], v[62:63], v[14:15]
	v_lshl_add_u64 v[22:23], v[18:19], 0, v[22:23]
	v_min_f32_e32 v14, 0x40e00000, v14
	v_min_f32_e32 v16, 0x40e00000, v16
	global_store_dwordx2 v[22:23], v[26:27], off sc1
	v_min_f32_e32 v15, 0x40e00000, v15
	v_min_f32_e32 v17, 0x40e00000, v17
	v_mul_f32_e32 v21, 0xc01d265f, v14
	v_mul_f32_e32 v23, 0xc01d265f, v16
	v_exp_f32_e32 v22, v21
	v_mul_f32_e32 v21, 0xc01d265f, v15
	v_exp_f32_e32 v24, v23
	v_mul_f32_e32 v23, 0xc01d265f, v17
	v_exp_f32_e32 v25, v23
	v_exp_f32_e32 v23, v21
	v_pk_add_f32 v[10:11], v[66:67], v[10:11]
	v_pk_add_f32 v[12:13], v[68:69], v[12:13]
	v_med3_f32 v21, v10, s73, v161
	v_pk_add_f32 v[22:23], v[22:23], 1.0 op_sel_hi:[1,0]
	v_med3_f32 v26, v11, s73, v161
	v_rcp_f32_e32 v22, v22
	v_rcp_f32_e32 v23, v23
	v_pk_add_f32 v[10:11], v[24:25], 1.0 op_sel_hi:[1,0]
	v_med3_f32 v24, v12, s73, v161
	v_rcp_f32_e32 v10, v10
	v_rcp_f32_e32 v11, v11
	v_med3_f32 v25, v13, s73, v161
	v_pk_mul_f32 v[12:13], v[14:15], v[22:23]
	v_fma_f32 v14, v21, 4.0, 4.0
	v_mul_f32_e32 v14, v14, v12
	v_fma_f32 v12, v26, 4.0, 4.0
	v_pk_mul_f32 v[10:11], v[16:17], v[10:11]
	v_mul_f32_e32 v15, v12, v13
	v_fma_f32 v12, v24, 4.0, 4.0
	v_pk_add_f32 v[6:7], v[58:59], v[6:7]
	v_mul_f32_e32 v16, v12, v10
	v_fma_f32 v10, v25, 4.0, 4.0
	v_min_f32_e32 v6, 0x40e00000, v6
	v_min_f32_e32 v7, 0x40e00000, v7
	v_mul_f32_e32 v17, v10, v11
	v_pk_add_f32 v[8:9], v[60:61], v[8:9]
	v_mul_f32_e32 v10, 0xc01d265f, v6
	v_mul_f32_e32 v11, 0xc01d265f, v7
	v_min_f32_e32 v8, 0x40e00000, v8
	v_min_f32_e32 v9, 0x40e00000, v9
	v_exp_f32_e32 v10, v10
	v_exp_f32_e32 v11, v11
	v_mul_f32_e32 v12, 0xc01d265f, v8
	v_mul_f32_e32 v13, 0xc01d265f, v9
	v_exp_f32_e32 v12, v12
	v_exp_f32_e32 v13, v13
	v_pk_add_f32 v[10:11], v[10:11], 1.0 op_sel_hi:[1,0]
	v_pk_add_f32 v[2:3], v[54:55], v[2:3]
	v_rcp_f32_e32 v10, v10
	v_rcp_f32_e32 v11, v11
	v_med3_f32 v21, v2, s73, v161
	v_med3_f32 v22, v3, s73, v161
	v_pk_add_f32 v[2:3], v[12:13], 1.0 op_sel_hi:[1,0]
	v_pk_add_f32 v[4:5], v[56:57], v[4:5]
	v_rcp_f32_e32 v2, v2
	v_rcp_f32_e32 v3, v3
	v_med3_f32 v12, v4, s73, v161
	v_med3_f32 v13, v5, s73, v161
	v_pk_mul_f32 v[4:5], v[6:7], v[10:11]
	v_fma_f32 v6, v21, 4.0, 4.0
	v_mul_f32_e32 v6, v6, v4
	v_fma_f32 v4, v22, 4.0, 4.0
	v_pk_mul_f32 v[2:3], v[8:9], v[2:3]
	v_mul_f32_e32 v7, v4, v5
	v_fma_f32 v4, v12, 4.0, 4.0
	v_mul_f32_e32 v2, v4, v2
	v_mov_b32_e32 v4, 0
	v_mov_b32_e32 v5, 0
	v_cvt_pk_fp8_f32 v4, v14, v15
	v_cvt_pk_fp8_f32 v5, v6, v7
	v_fma_f32 v6, v13, 4.0, 4.0
	v_mul_f32_e32 v3, v6, v3
	v_or_b32_e32 v20, 48, v20
	v_cvt_pk_fp8_f32 v4, v16, v17 op_sel:[0,0,1]
	v_cvt_pk_fp8_f32 v5, v2, v3 op_sel:[0,0,1]
	v_ashrrev_i32_e32 v21, 31, v20
	v_lshlrev_b64 v[2:3], 11, v[20:21]
	v_lshl_add_u64 v[2:3], v[18:19], 0, v[2:3]
	s_and_b64 vcc, exec, s[8:9]
	s_mov_b64 s[8:9], -1
	global_store_dwordx2 v[2:3], v[4:5], off sc1
	s_cbranch_vccnz .LBB0_1165
	s_and_saveexec_b64 s[8:9], s[6:7]
	s_cbranch_execz .LBB0_1195
	s_ashr_i32 s39, s38, 31
	s_lshl_b64 s[10:11], s[38:39], 14
	s_add_u32 s39, s22, s10
	s_addc_u32 s41, s23, s11
	s_lshl_b32 s10, s40, 7
	s_ashr_i32 s11, s10, 31
	s_lshl_b64 s[10:11], s[10:11], 2
	s_add_u32 s10, s39, s10
	s_addc_u32 s11, s41, s11
	s_mov_b32 s39, m0
	s_mov_b32 m0, s59
	s_nop 0
	global_load_lds_dwordx4 v157, s[10:11]
	s_mov_b32 m0, s39

; __device__ __forceinline__ unsigned pk4_fp8(float a, float b, float c, float d) { int w = 0; w = __builtin_amdgcn_cvt_pk_fp8_f32(a, b, w, false); w = __builtin_amdgcn_cvt_pk_fp8_f32(c, d, w, true); return (unsigned)w; }
;     __device__ __forceinline__ void operator()(const AccT& acc, const pg8::Unit& u, int wr, int wc, int fr, int fq, const LAS float* bl, const LAS int* rid, int nai) const {
;     ...
;             for (int m = 0; m < 4; ++m) { const int rl = u.hx * 128 + ai * 128 + wr * 64 + m * 16 + fr; const int dst = rid[ai * 64 + m * 16 + fr];
;                 if (rl < nvalid) { const size_t ro = (size_t)dst * D + col0; unsigned wv[4];
; #pragma unroll
;                     for (int bj = 0; bj < 2; ++bj) { const f32x4 v0 = acc[ai][bj][m][0] * Y8_SCALE + bv[bj][0], v1 = acc[ai][bj][m][1] * Y8_SCALE + bv[bj][1];
;                         wv[2 * bj] = pk4_fp8(v0[0], v0[1], v0[2], v0[3]); wv[2 * bj + 1] = pk4_fp8(v1[0], v1[1], v1[2], v1[3]); }
;                     *(u32x4*)(y + ro) = (u32x4){wv[0], wv[1], wv[2], wv[3]}; } }
.LBB0_1302:
	v_pk_fma_f32 v[22:23], v[158:159], s[22:23], v[18:19] op_sel_hi:[1,0,1]
	v_pk_fma_f32 v[26:27], v[154:155], s[22:23], v[16:17] op_sel_hi:[1,0,1]
	v_mov_b32_e32 v20, 0
	v_mov_b32_e32 v21, 0
	v_cvt_pk_fp8_f32 v20, v22, v23
	v_cvt_pk_fp8_f32 v21, v26, v27
	v_pk_fma_f32 v[22:23], v[160:161], s[22:23], v[8:9] op_sel_hi:[1,0,1]
	v_pk_fma_f32 v[26:27], v[156:157], s[22:23], v[14:15] op_sel_hi:[1,0,1]
	v_cvt_pk_fp8_f32 v20, v22, v23 op_sel:[0,0,1]
	v_cvt_pk_fp8_f32 v21, v26, v27 op_sel:[0,0,1]
	v_pk_fma_f32 v[26:27], v[150:151], s[22:23], v[12:13] op_sel_hi:[1,0,1]
	v_pk_fma_f32 v[28:29], v[146:147], s[22:23], v[10:11] op_sel_hi:[1,0,1]
	v_mov_b32_e32 v22, 0
	v_mov_b32_e32 v23, 0
	ds_read_b32 v24, v173
	v_cvt_pk_fp8_f32 v22, v26, v27
	v_cvt_pk_fp8_f32 v23, v28, v29
	v_pk_fma_f32 v[26:27], v[152:153], s[22:23], v[2:3] op_sel_hi:[1,0,1]
	v_pk_fma_f32 v[28:29], v[148:149], s[22:23], v[6:7] op_sel_hi:[1,0,1]
	v_cvt_pk_fp8_f32 v22, v26, v27 op_sel:[0,0,1]
	v_cvt_pk_fp8_f32 v23, v28, v29 op_sel:[0,0,1]
	s_waitcnt lgkmcnt(0)
	v_ashrrev_i32_e32 v25, 31, v24
	v_lshlrev_b64 v[24:25], 11, v[24:25]
	v_lshl_add_u64 v[24:25], v[4:5], 0, v[24:25]
	global_store_dwordx4 v[24:25], v[20:23], off sc1
	s_or_b64 exec, exec, s[34:35]
	v_cmp_gt_i32_e32 vcc, s25, v174
	s_and_saveexec_b64 s[34:35], vcc
	s_cbranch_execz .LBB0_1295
.LBB0_1303:
	v_pk_fma_f32 v[22:23], v[142:143], s[22:23], v[18:19] op_sel_hi:[1,0,1]
	v_pk_fma_f32 v[26:27], v[138:139], s[22:23], v[16:17] op_sel_hi:[1,0,1]
	v_mov_b32_e32 v20, 0
	v_mov_b32_e32 v21, 0
	v_cvt_pk_fp8_f32 v20, v22, v23
	v_cvt_pk_fp8_f32 v21, v26, v27
	v_pk_fma_f32 v[22:23], v[144:145], s[22:23], v[8:9] op_sel_hi:[1,0,1]
	v_pk_fma_f32 v[26:27], v[140:141], s[22:23], v[14:15] op_sel_hi:[1,0,1]
	v_cvt_pk_fp8_f32 v20, v22, v23 op_sel:[0,0,1]
	v_cvt_pk_fp8_f32 v21, v26, v27 op_sel:[0,0,1]
	v_pk_fma_f32 v[26:27], v[134:135], s[22:23], v[12:13] op_sel_hi:[1,0,1]
	v_pk_fma_f32 v[28:29], v[130:131], s[22:23], v[10:11] op_sel_hi:[1,0,1]
	v_mov_b32_e32 v22, 0
	v_mov_b32_e32 v23, 0
	ds_read_b32 v24, v173 offset:64
	v_cvt_pk_fp8_f32 v22, v26, v27
	v_cvt_pk_fp8_f32 v23, v28, v29
	v_pk_fma_f32 v[26:27], v[136:137], s[22:23], v[2:3] op_sel_hi:[1,0,1]
	v_pk_fma_f32 v[28:29], v[132:133], s[22:23], v[6:7] op_sel_hi:[1,0,1]
	v_cvt_pk_fp8_f32 v22, v26, v27 op_sel:[0,0,1]
	v_cvt_pk_fp8_f32 v23, v28, v29 op_sel:[0,0,1]
	s_waitcnt lgkmcnt(0)
	v_ashrrev_i32_e32 v25, 31, v24
	v_lshlrev_b64 v[24:25], 11, v[24:25]
	v_lshl_add_u64 v[24:25], v[4:5], 0, v[24:25]
	global_store_dwordx4 v[24:25], v[20:23], off sc1
	s_or_b64 exec, exec, s[34:35]
	v_cmp_gt_i32_e32 vcc, s25, v175
	s_and_saveexec_b64 s[34:35], vcc
	s_cbranch_execz .LBB0_1296
.LBB0_1304:
	v_pk_fma_f32 v[22:23], v[126:127], s[22:23], v[18:19] op_sel_hi:[1,0,1]
	v_pk_fma_f32 v[26:27], v[122:123], s[22:23], v[16:17] op_sel_hi:[1,0,1]
	v_mov_b32_e32 v20, 0
	v_mov_b32_e32 v21, 0
	v_cvt_pk_fp8_f32 v20, v22, v23
	v_cvt_pk_fp8_f32 v21, v26, v27
	v_pk_fma_f32 v[22:23], v[128:129], s[22:23], v[8:9] op_sel_hi:[1,0,1]
	v_pk_fma_f32 v[26:27], v[124:125], s[22:23], v[14:15] op_sel_hi:[1,0,1]
	v_cvt_pk_fp8_f32 v20, v22, v23 op_sel:[0,0,1]
	v_cvt_pk_fp8_f32 v21, v26, v27 op_sel:[0,0,1]
	v_pk_fma_f32 v[26:27], v[118:119], s[22:23], v[12:13] op_sel_hi:[1,0,1]
	v_pk_fma_f32 v[28:29], v[114:115], s[22:23], v[10:11] op_sel_hi:[1,0,1]
	v_mov_b32_e32 v22, 0
	v_mov_b32_e32 v23, 0
	ds_read_b32 v24, v173 offset:128
	v_cvt_pk_fp8_f32 v22, v26, v27
	v_cvt_pk_fp8_f32 v23, v28, v29
	v_pk_fma_f32 v[26:27], v[120:121], s[22:23], v[2:3] op_sel_hi:[1,0,1]
	v_pk_fma_f32 v[28:29], v[116:117], s[22:23], v[6:7] op_sel_hi:[1,0,1]
	v_cvt_pk_fp8_f32 v22, v26, v27 op_sel:[0,0,1]
	v_cvt_pk_fp8_f32 v23, v28, v29 op_sel:[0,0,1]
	s_waitcnt lgkmcnt(0)
	v_ashrrev_i32_e32 v25, 31, v24
	v_lshlrev_b64 v[24:25], 11, v[24:25]
	v_lshl_add_u64 v[24:25], v[4:5], 0, v[24:25]
	global_store_dwordx4 v[24:25], v[20:23], off sc1
	s_or_b64 exec, exec, s[34:35]
	v_cmp_gt_i32_e32 vcc, s25, v176
	s_and_saveexec_b64 s[34:35], vcc
	s_cbranch_execz .LBB0_1297
.LBB0_1305:
	v_pk_fma_f32 v[22:23], v[110:111], s[22:23], v[18:19] op_sel_hi:[1,0,1]
	v_pk_fma_f32 v[26:27], v[106:107], s[22:23], v[16:17] op_sel_hi:[1,0,1]
	v_mov_b32_e32 v20, 0
	v_mov_b32_e32 v21, 0
	v_cvt_pk_fp8_f32 v20, v22, v23
	v_cvt_pk_fp8_f32 v21, v26, v27
	v_pk_fma_f32 v[22:23], v[112:113], s[22:23], v[8:9] op_sel_hi:[1,0,1]
	v_pk_fma_f32 v[26:27], v[108:109], s[22:23], v[14:15] op_sel_hi:[1,0,1]
	v_cvt_pk_fp8_f32 v20, v22, v23 op_sel:[0,0,1]
	v_cvt_pk_fp8_f32 v21, v26, v27 op_sel:[0,0,1]
	v_pk_fma_f32 v[26:27], v[102:103], s[22:23], v[12:13] op_sel_hi:[1,0,1]
	v_pk_fma_f32 v[28:29], v[98:99], s[22:23], v[10:11] op_sel_hi:[1,0,1]
	v_mov_b32_e32 v22, 0
	v_mov_b32_e32 v23, 0
	ds_read_b32 v24, v173 offset:192
	v_cvt_pk_fp8_f32 v22, v26, v27
	v_cvt_pk_fp8_f32 v23, v28, v29
	v_pk_fma_f32 v[26:27], v[104:105], s[22:23], v[2:3] op_sel_hi:[1,0,1]
	v_pk_fma_f32 v[28:29], v[100:101], s[22:23], v[6:7] op_sel_hi:[1,0,1]
	v_cvt_pk_fp8_f32 v22, v26, v27 op_sel:[0,0,1]
	v_cvt_pk_fp8_f32 v23, v28, v29 op_sel:[0,0,1]
	s_waitcnt lgkmcnt(0)
	v_ashrrev_i32_e32 v25, 31, v24
	v_lshlrev_b64 v[24:25], 11, v[24:25]
	v_lshl_add_u64 v[24:25], v[4:5], 0, v[24:25]
	global_store_dwordx4 v[24:25], v[20:23], off sc1
	s_or_b64 exec, exec, s[34:35]
	v_cmp_gt_i32_e32 vcc, s25, v177
	s_and_saveexec_b64 s[34:35], vcc
	s_cbranch_execz .LBB0_1298
; __device__ __forceinline__ unsigned pk4_fp8(float a, float b, float c, float d) { int w = 0; w = __builtin_amdgcn_cvt_pk_fp8_f32(a, b, w, false); w = __builtin_amdgcn_cvt_pk_fp8_f32(c, d, w, true); return (unsigned)w; }
;     __device__ __forceinline__ void operator()(const AccT& acc, const pg8::Unit& u, int wr, int wc, int fr, int fq, const LAS float* bl, const LAS int* rid, int nai) const {
;     ...
;             for (int m = 0; m < 4; ++m) { const int rl = u.hx * 128 + ai * 128 + wr * 64 + m * 16 + fr; const int dst = rid[ai * 64 + m * 16 + fr];
;                 if (rl < nvalid) { const size_t ro = (size_t)dst * D + col0; unsigned wv[4];
; #pragma unroll
;                     for (int bj = 0; bj < 2; ++bj) { const f32x4 v0 = acc[ai][bj][m][0] * Y8_SCALE + bv[bj][0], v1 = acc[ai][bj][m][1] * Y8_SCALE + bv[bj][1];
;                         wv[2 * bj] = pk4_fp8(v0[0], v0[1], v0[2], v0[3]); wv[2 * bj + 1] = pk4_fp8(v1[0], v1[1], v1[2], v1[3]); }
;                     *(u32x4*)(y + ro) = (u32x4){wv[0], wv[1], wv[2], wv[3]}; } }
.LBB0_1306:
	v_pk_fma_f32 v[22:23], v[94:95], s[22:23], v[18:19] op_sel_hi:[1,0,1]
	v_pk_fma_f32 v[26:27], v[90:91], s[22:23], v[16:17] op_sel_hi:[1,0,1]
	v_mov_b32_e32 v20, 0
	v_mov_b32_e32 v21, 0
	v_cvt_pk_fp8_f32 v20, v22, v23
	v_cvt_pk_fp8_f32 v21, v26, v27
	v_pk_fma_f32 v[22:23], v[96:97], s[22:23], v[8:9] op_sel_hi:[1,0,1]
	v_pk_fma_f32 v[26:27], v[92:93], s[22:23], v[14:15] op_sel_hi:[1,0,1]
	v_cvt_pk_fp8_f32 v20, v22, v23 op_sel:[0,0,1]
	v_cvt_pk_fp8_f32 v21, v26, v27 op_sel:[0,0,1]
	v_pk_fma_f32 v[26:27], v[86:87], s[22:23], v[12:13] op_sel_hi:[1,0,1]
	v_pk_fma_f32 v[28:29], v[82:83], s[22:23], v[10:11] op_sel_hi:[1,0,1]
	v_mov_b32_e32 v22, 0
	v_mov_b32_e32 v23, 0
	ds_read_b32 v24, v173 offset:256
	v_cvt_pk_fp8_f32 v22, v26, v27
	v_cvt_pk_fp8_f32 v23, v28, v29
	v_pk_fma_f32 v[26:27], v[88:89], s[22:23], v[2:3] op_sel_hi:[1,0,1]
	v_pk_fma_f32 v[28:29], v[84:85], s[22:23], v[6:7] op_sel_hi:[1,0,1]
	v_cvt_pk_fp8_f32 v22, v26, v27 op_sel:[0,0,1]
	v_cvt_pk_fp8_f32 v23, v28, v29 op_sel:[0,0,1]
	s_waitcnt lgkmcnt(0)
	v_ashrrev_i32_e32 v25, 31, v24
	v_lshlrev_b64 v[24:25], 11, v[24:25]
	v_lshl_add_u64 v[24:25], v[4:5], 0, v[24:25]
	global_store_dwordx4 v[24:25], v[20:23], off sc1
	s_or_b64 exec, exec, s[34:35]
	v_cmp_gt_i32_e32 vcc, s25, v178
	s_and_saveexec_b64 s[34:35], vcc
	s_cbranch_execz .LBB0_1299
.LBB0_1307:
	v_pk_fma_f32 v[22:23], v[78:79], s[22:23], v[18:19] op_sel_hi:[1,0,1]
	v_pk_fma_f32 v[26:27], v[74:75], s[22:23], v[16:17] op_sel_hi:[1,0,1]
	v_mov_b32_e32 v20, 0
	v_mov_b32_e32 v21, 0
	v_cvt_pk_fp8_f32 v20, v22, v23
	v_cvt_pk_fp8_f32 v21, v26, v27
	v_pk_fma_f32 v[22:23], v[80:81], s[22:23], v[8:9] op_sel_hi:[1,0,1]
	v_pk_fma_f32 v[26:27], v[76:77], s[22:23], v[14:15] op_sel_hi:[1,0,1]
	v_cvt_pk_fp8_f32 v20, v22, v23 op_sel:[0,0,1]
	v_cvt_pk_fp8_f32 v21, v26, v27 op_sel:[0,0,1]
	v_pk_fma_f32 v[26:27], v[70:71], s[22:23], v[12:13] op_sel_hi:[1,0,1]
	v_pk_fma_f32 v[28:29], v[66:67], s[22:23], v[10:11] op_sel_hi:[1,0,1]
	v_mov_b32_e32 v22, 0
	v_mov_b32_e32 v23, 0
	ds_read_b32 v24, v173 offset:320
	v_cvt_pk_fp8_f32 v22, v26, v27
	v_cvt_pk_fp8_f32 v23, v28, v29
	v_pk_fma_f32 v[26:27], v[72:73], s[22:23], v[2:3] op_sel_hi:[1,0,1]
	v_pk_fma_f32 v[28:29], v[68:69], s[22:23], v[6:7] op_sel_hi:[1,0,1]
	v_cvt_pk_fp8_f32 v22, v26, v27 op_sel:[0,0,1]
	v_cvt_pk_fp8_f32 v23, v28, v29 op_sel:[0,0,1]
	s_waitcnt lgkmcnt(0)
	v_ashrrev_i32_e32 v25, 31, v24
	v_lshlrev_b64 v[24:25], 11, v[24:25]
	v_lshl_add_u64 v[24:25], v[4:5], 0, v[24:25]
	global_store_dwordx4 v[24:25], v[20:23], off sc1
	s_or_b64 exec, exec, s[34:35]
	v_cmp_gt_i32_e32 vcc, s25, v179
	s_and_saveexec_b64 s[34:35], vcc
	s_cbranch_execz .LBB0_1300
.LBB0_1308:
	v_pk_fma_f32 v[22:23], v[62:63], s[22:23], v[18:19] op_sel_hi:[1,0,1]
	v_pk_fma_f32 v[26:27], v[58:59], s[22:23], v[16:17] op_sel_hi:[1,0,1]
	v_mov_b32_e32 v20, 0
	v_mov_b32_e32 v21, 0
	v_cvt_pk_fp8_f32 v20, v22, v23
	v_cvt_pk_fp8_f32 v21, v26, v27
	v_pk_fma_f32 v[22:23], v[64:65], s[22:23], v[8:9] op_sel_hi:[1,0,1]
	v_pk_fma_f32 v[26:27], v[60:61], s[22:23], v[14:15] op_sel_hi:[1,0,1]
	v_cvt_pk_fp8_f32 v20, v22, v23 op_sel:[0,0,1]
	v_cvt_pk_fp8_f32 v21, v26, v27 op_sel:[0,0,1]
	v_pk_fma_f32 v[26:27], v[54:55], s[22:23], v[12:13] op_sel_hi:[1,0,1]
	v_pk_fma_f32 v[28:29], v[50:51], s[22:23], v[10:11] op_sel_hi:[1,0,1]
	v_mov_b32_e32 v22, 0
	v_mov_b32_e32 v23, 0
	ds_read_b32 v24, v173 offset:384
	v_cvt_pk_fp8_f32 v22, v26, v27
	v_cvt_pk_fp8_f32 v23, v28, v29
	v_pk_fma_f32 v[26:27], v[56:57], s[22:23], v[2:3] op_sel_hi:[1,0,1]
	v_pk_fma_f32 v[28:29], v[52:53], s[22:23], v[6:7] op_sel_hi:[1,0,1]
	v_cvt_pk_fp8_f32 v22, v26, v27 op_sel:[0,0,1]
	v_cvt_pk_fp8_f32 v23, v28, v29 op_sel:[0,0,1]
	s_waitcnt lgkmcnt(0)
	v_ashrrev_i32_e32 v25, 31, v24
	v_lshlrev_b64 v[24:25], 11, v[24:25]
	v_lshl_add_u64 v[24:25], v[4:5], 0, v[24:25]
	global_store_dwordx4 v[24:25], v[20:23], off sc1
	s_or_b64 exec, exec, s[34:35]
	v_cmp_gt_i32_e32 vcc, s25, v180
	s_and_saveexec_b64 s[34:35], vcc
	s_cbranch_execz .LBB0_1301
.LBB0_1309:
	v_pk_fma_f32 v[18:19], v[46:47], s[22:23], v[18:19] op_sel_hi:[1,0,1]
	v_pk_fma_f32 v[22:23], v[42:43], s[22:23], v[16:17] op_sel_hi:[1,0,1]
	v_mov_b32_e32 v16, 0
	v_cvt_pk_fp8_f32 v16, v18, v19
	v_pk_fma_f32 v[8:9], v[48:49], s[22:23], v[8:9] op_sel_hi:[1,0,1]
	v_mov_b32_e32 v17, 0
	v_pk_fma_f32 v[10:11], v[34:35], s[22:23], v[10:11] op_sel_hi:[1,0,1]
	v_cvt_pk_fp8_f32 v16, v8, v9 op_sel:[0,0,1]
	v_pk_fma_f32 v[8:9], v[38:39], s[22:23], v[12:13] op_sel_hi:[1,0,1]
	v_mov_b32_e32 v18, 0
	v_mov_b32_e32 v19, 0
	ds_read_b32 v20, v173 offset:448
	v_cvt_pk_fp8_f32 v17, v22, v23
	v_cvt_pk_fp8_f32 v18, v8, v9
	v_cvt_pk_fp8_f32 v19, v10, v11
	v_pk_fma_f32 v[14:15], v[44:45], s[22:23], v[14:15] op_sel_hi:[1,0,1]
	v_pk_fma_f32 v[2:3], v[40:41], s[22:23], v[2:3] op_sel_hi:[1,0,1]
	v_pk_fma_f32 v[6:7], v[36:37], s[22:23], v[6:7] op_sel_hi:[1,0,1]
	v_cvt_pk_fp8_f32 v17, v14, v15 op_sel:[0,0,1]
	v_cvt_pk_fp8_f32 v18, v2, v3 op_sel:[0,0,1]
	v_cvt_pk_fp8_f32 v19, v6, v7 op_sel:[0,0,1]
	s_waitcnt lgkmcnt(0)
	v_ashrrev_i32_e32 v21, 31, v20
	v_lshlrev_b64 v[2:3], 11, v[20:21]
	v_lshl_add_u64 v[2:3], v[4:5], 0, v[2:3]
	global_store_dwordx4 v[2:3], v[16:19], off sc1
	s_or_b64 exec, exec, s[34:35]
	s_and_b64 vcc, exec, s[10:11]
	s_mov_b64 s[10:11], -1
	s_cbranch_vccnz .LBB0_1280

; __device__ __forceinline__ unsigned pk4_fp8(float a, float b, float c, float d) { int w = 0; w = __builtin_amdgcn_cvt_pk_fp8_f32(a, b, w, false); w = __builtin_amdgcn_cvt_pk_fp8_f32(c, d, w, true); return (unsigned)w; }
;     __device__ __forceinline__ void operator()(const AccT& acc, const pg8::Unit& u, int wr, int wc, int fr, int fq, const LAS float* bl, const LAS int* rid, int nai) const {
;     ...
;             for (int m = 0; m < 4; ++m) { const int rl = u.hx * 128 + ai * 128 + wr * 64 + m * 16 + fr; const int dst = rid[ai * 64 + m * 16 + fr];
;                 if (rl < nvalid) { const size_t ro = (size_t)dst * D + col0; unsigned wv[4];
; #pragma unroll
;                     for (int bj = 0; bj < 2; ++bj) { const f32x4 v0 = acc[ai][bj][m][0] * Y8_SCALE + bv[bj][0], v1 = acc[ai][bj][m][1] * Y8_SCALE + bv[bj][1];
;                         wv[2 * bj] = pk4_fp8(v0[0], v0[1], v0[2], v0[3]); wv[2 * bj + 1] = pk4_fp8(v1[0], v1[1], v1[2], v1[3]); }
;                     *(u32x4*)(y + ro) = (u32x4){wv[0], wv[1], wv[2], wv[3]}; } }
.LBB0_1354:
	v_pk_fma_f32 v[108:109], v[58:59], s[22:23], v[82:83] op_sel_hi:[1,0,1]
	v_mov_b32_e32 v59, 0
	v_cvt_pk_fp8_f32 v59, v108, v109
	v_pk_fma_f32 v[60:61], v[60:61], s[22:23], v[80:81] op_sel_hi:[1,0,1]
	v_pk_fma_f32 v[62:63], v[62:63], s[22:23], v[84:85] op_sel_hi:[1,0,1]
	v_mov_b32_e32 v58, 0
	v_cvt_pk_fp8_f32 v59, v60, v61 op_sel:[0,0,1]
	v_pk_fma_f32 v[54:55], v[54:55], s[22:23], v[78:79] op_sel_hi:[1,0,1]
	v_pk_fma_f32 v[50:51], v[50:51], s[22:23], v[76:77] op_sel_hi:[1,0,1]
	v_mov_b32_e32 v60, 0
	v_mov_b32_e32 v61, 0
	ds_read_b32 v106, v93
	v_cvt_pk_fp8_f32 v58, v62, v63
	v_cvt_pk_fp8_f32 v60, v54, v55
	v_cvt_pk_fp8_f32 v61, v50, v51
	v_pk_fma_f32 v[62:63], v[64:65], s[22:23], v[74:75] op_sel_hi:[1,0,1]
	v_pk_fma_f32 v[50:51], v[56:57], s[22:23], v[68:69] op_sel_hi:[1,0,1]
	v_pk_fma_f32 v[52:53], v[52:53], s[22:23], v[72:73] op_sel_hi:[1,0,1]
	v_cvt_pk_fp8_f32 v58, v62, v63 op_sel:[0,0,1]
	v_cvt_pk_fp8_f32 v60, v50, v51 op_sel:[0,0,1]
	v_cvt_pk_fp8_f32 v61, v52, v53 op_sel:[0,0,1]
	s_waitcnt lgkmcnt(0)
	v_ashrrev_i32_e32 v107, 31, v106
	v_lshlrev_b64 v[50:51], 11, v[106:107]
	v_lshl_add_u64 v[50:51], v[70:71], 0, v[50:51]
	global_store_dwordx4 v[50:51], v[58:61], off sc1
	s_or_b64 exec, exec, s[26:27]
	v_cmp_gt_i32_e32 vcc, s25, v94
	s_and_saveexec_b64 s[26:27], vcc
	s_cbranch_execz .LBB0_1351
.LBB0_1355:
	v_pk_fma_f32 v[52:53], v[42:43], s[22:23], v[82:83] op_sel_hi:[1,0,1]
	v_mov_b32_e32 v43, 0
	v_cvt_pk_fp8_f32 v43, v52, v53
	v_pk_fma_f32 v[44:45], v[44:45], s[22:23], v[80:81] op_sel_hi:[1,0,1]
	v_pk_fma_f32 v[46:47], v[46:47], s[22:23], v[84:85] op_sel_hi:[1,0,1]
	v_mov_b32_e32 v42, 0
	v_cvt_pk_fp8_f32 v43, v44, v45 op_sel:[0,0,1]
	v_pk_fma_f32 v[38:39], v[38:39], s[22:23], v[78:79] op_sel_hi:[1,0,1]
	v_pk_fma_f32 v[34:35], v[34:35], s[22:23], v[76:77] op_sel_hi:[1,0,1]
	v_mov_b32_e32 v44, 0
	v_mov_b32_e32 v45, 0
	ds_read_b32 v50, v93 offset:64
	v_cvt_pk_fp8_f32 v42, v46, v47
	v_cvt_pk_fp8_f32 v44, v38, v39
	v_cvt_pk_fp8_f32 v45, v34, v35
	v_pk_fma_f32 v[46:47], v[48:49], s[22:23], v[74:75] op_sel_hi:[1,0,1]
	v_pk_fma_f32 v[34:35], v[40:41], s[22:23], v[68:69] op_sel_hi:[1,0,1]
	v_pk_fma_f32 v[36:37], v[36:37], s[22:23], v[72:73] op_sel_hi:[1,0,1]
	v_cvt_pk_fp8_f32 v42, v46, v47 op_sel:[0,0,1]
	v_cvt_pk_fp8_f32 v44, v34, v35 op_sel:[0,0,1]
	v_cvt_pk_fp8_f32 v45, v36, v37 op_sel:[0,0,1]
	s_waitcnt lgkmcnt(0)
	v_ashrrev_i32_e32 v51, 31, v50
	v_lshlrev_b64 v[34:35], 11, v[50:51]
	v_lshl_add_u64 v[34:35], v[70:71], 0, v[34:35]
	global_store_dwordx4 v[34:35], v[42:45], off sc1
	s_or_b64 exec, exec, s[26:27]
	v_cmp_gt_i32_e32 vcc, s25, v95
	s_and_saveexec_b64 s[26:27], vcc
	s_cbranch_execz .LBB0_1352
.LBB0_1356:
	v_pk_fma_f32 v[36:37], v[26:27], s[22:23], v[82:83] op_sel_hi:[1,0,1]
	v_mov_b32_e32 v27, 0
	v_cvt_pk_fp8_f32 v27, v36, v37
	v_pk_fma_f32 v[28:29], v[28:29], s[22:23], v[80:81] op_sel_hi:[1,0,1]
	v_pk_fma_f32 v[30:31], v[30:31], s[22:23], v[84:85] op_sel_hi:[1,0,1]
	v_mov_b32_e32 v26, 0
	v_cvt_pk_fp8_f32 v27, v28, v29 op_sel:[0,0,1]
	v_pk_fma_f32 v[22:23], v[22:23], s[22:23], v[78:79] op_sel_hi:[1,0,1]
	v_pk_fma_f32 v[18:19], v[18:19], s[22:23], v[76:77] op_sel_hi:[1,0,1]
	v_mov_b32_e32 v28, 0
	v_mov_b32_e32 v29, 0
	ds_read_b32 v34, v93 offset:128
	v_cvt_pk_fp8_f32 v26, v30, v31
	v_cvt_pk_fp8_f32 v28, v22, v23
	v_cvt_pk_fp8_f32 v29, v18, v19
	v_pk_fma_f32 v[30:31], v[32:33], s[22:23], v[74:75] op_sel_hi:[1,0,1]
	v_pk_fma_f32 v[18:19], v[24:25], s[22:23], v[68:69] op_sel_hi:[1,0,1]
	v_pk_fma_f32 v[20:21], v[20:21], s[22:23], v[72:73] op_sel_hi:[1,0,1]
	v_cvt_pk_fp8_f32 v26, v30, v31 op_sel:[0,0,1]
	v_cvt_pk_fp8_f32 v28, v18, v19 op_sel:[0,0,1]
	v_cvt_pk_fp8_f32 v29, v20, v21 op_sel:[0,0,1]
	s_waitcnt lgkmcnt(0)
	v_ashrrev_i32_e32 v35, 31, v34
	v_lshlrev_b64 v[18:19], 11, v[34:35]
	v_lshl_add_u64 v[18:19], v[70:71], 0, v[18:19]
	global_store_dwordx4 v[18:19], v[26:29], off sc1
	s_or_b64 exec, exec, s[26:27]
	v_cmp_gt_i32_e32 vcc, s25, v96
	s_and_saveexec_b64 s[26:27], vcc
	s_cbranch_execz .LBB0_1353
.LBB0_1357:
	v_pk_fma_f32 v[20:21], v[10:11], s[22:23], v[82:83] op_sel_hi:[1,0,1]
	v_mov_b32_e32 v11, 0
	v_cvt_pk_fp8_f32 v11, v20, v21
	v_pk_fma_f32 v[12:13], v[12:13], s[22:23], v[80:81] op_sel_hi:[1,0,1]
	v_pk_fma_f32 v[14:15], v[14:15], s[22:23], v[84:85] op_sel_hi:[1,0,1]
	v_mov_b32_e32 v10, 0
	v_cvt_pk_fp8_f32 v11, v12, v13 op_sel:[0,0,1]
	v_pk_fma_f32 v[6:7], v[6:7], s[22:23], v[78:79] op_sel_hi:[1,0,1]
	v_pk_fma_f32 v[2:3], v[2:3], s[22:23], v[76:77] op_sel_hi:[1,0,1]
	v_mov_b32_e32 v12, 0
	v_mov_b32_e32 v13, 0
	ds_read_b32 v18, v93 offset:192
	v_cvt_pk_fp8_f32 v10, v14, v15
	v_cvt_pk_fp8_f32 v12, v6, v7
	v_cvt_pk_fp8_f32 v13, v2, v3
	v_pk_fma_f32 v[14:15], v[16:17], s[22:23], v[74:75] op_sel_hi:[1,0,1]
	v_pk_fma_f32 v[2:3], v[8:9], s[22:23], v[68:69] op_sel_hi:[1,0,1]
	v_pk_fma_f32 v[4:5], v[4:5], s[22:23], v[72:73] op_sel_hi:[1,0,1]
	v_cvt_pk_fp8_f32 v10, v14, v15 op_sel:[0,0,1]
	v_cvt_pk_fp8_f32 v12, v2, v3 op_sel:[0,0,1]
	v_cvt_pk_fp8_f32 v13, v4, v5 op_sel:[0,0,1]
	s_waitcnt lgkmcnt(0)
	v_ashrrev_i32_e32 v19, 31, v18
	v_lshlrev_b64 v[2:3], 11, v[18:19]
	v_lshl_add_u64 v[2:3], v[70:71], 0, v[2:3]
	global_store_dwordx4 v[2:3], v[10:13], off sc1
	s_or_b64 exec, exec, s[26:27]
	s_and_b64 vcc, exec, s[10:11]
	s_mov_b64 s[10:11], -1
	s_cbranch_vccnz .LBB0_1334
